# layer-0 mixer norm row loop double-buffered in registers (next row's loads in flight while the current row is reduced and stored); routing wave sums via DPP/permlane instead of ds_bpermute; unused per
# speedup vs baseline: 1.0061x; 1.0061x over previous
; __device__ __forceinline__ void phase_norm_x(const Frame& F, const float* x, const float* g, const float* modl, int ish, int isc, unsigned char* XN8) {
;     ...
;     for (int t = t0; t < t1; ++t) { const int b = t / S;
;         if (b != bcur) { bcur = b; const float* sh = modl + (size_t)b * MODW + ish * D; const float* sc = modl + (size_t)b * MODW + isc * D;
; #pragma unroll
;             for (int i = 0; i < 8; ++i) { const int d = 256 * i + 4 * F.lane; const f32x4 gv = *(const f32x4*)(g + d), s1 = *(const f32x4*)(sc + d); gs[i] = gv * (1.f + s1); shv[i] = *(const f32x4*)(sh + d); } }
;         f32x4 v[8]; float ss = 0.f;
; #pragma unroll
;         for (int i = 0; i < 8; ++i) v[i] = __builtin_nontemporal_load((const f32x4*)(x + (size_t)t * D + 256 * i + 4 * F.lane));
; #pragma unroll
;         for (int i = 0; i < 8; ++i) ss += v[i][0] * v[i][0] + v[i][1] * v[i][1] + v[i][2] * v[i][2] + v[i][3] * v[i][3];
;         const float r = rsqrtf(wave_sum(ss) * (1.f / D) + EPS);
.LBB0_218:
	global_load_dwordx4 v[100:103], v[82:83], off offset:-4096 nt
	global_load_dwordx4 v[104:107], v[82:83], off offset:-3072 nt
	global_load_dwordx4 v[108:111], v[82:83], off offset:-2048 nt
	global_load_dwordx4 v[112:115], v[82:83], off offset:-1024 nt
	global_load_dwordx4 v[116:119], v[82:83], off nt
	global_load_dwordx4 v[120:123], v[82:83], off offset:1024 nt
	global_load_dwordx4 v[124:127], v[82:83], off offset:2048 nt
	global_load_dwordx4 v[66:69], v[82:83], off offset:3072 nt
	s_add_i32 s2, s2, 1
	v_lshl_add_u64 v[82:83], v[82:83], 0, s[4:5]
	s_cmp_lt_i32 s2, s12
	s_cbranch_scc0 .Ln1_af_nopf
	s_ashr_i32 s14, s2, 12
	s_cmp_eq_u32 s14, s8
	s_cbranch_scc0 .Ln1_af_nopf
	global_load_dwordx4 v[160:163], v[82:83], off offset:-4096 nt
	global_load_dwordx4 v[164:167], v[82:83], off offset:-3072 nt
	global_load_dwordx4 v[168:171], v[82:83], off offset:-2048 nt
	global_load_dwordx4 v[172:175], v[82:83], off offset:-1024 nt
	global_load_dwordx4 v[176:179], v[82:83], off nt
	global_load_dwordx4 v[180:183], v[82:83], off offset:1024 nt
	global_load_dwordx4 v[184:187], v[82:83], off offset:2048 nt
	global_load_dwordx4 v[188:191], v[82:83], off offset:3072 nt
	s_add_i32 s2, s2, 1
	v_lshl_add_u64 v[82:83], v[82:83], 0, s[4:5]
	s_waitcnt vmcnt(8)
	s_cmp_eq_u32 s8, s8
	s_branch .Ln1_procA
.Ln1_af_nopf:
	s_waitcnt vmcnt(0)
	s_cmp_lg_u32 s8, s8
	s_branch .Ln1_procA
.Ln1_PA:
	s_cmp_lt_i32 s2, s12
	s_cbranch_scc0 .Ln1_a_nopf
	s_ashr_i32 s14, s2, 12
	s_cmp_eq_u32 s14, s8
	s_cbranch_scc0 .Ln1_a_nopf
	global_load_dwordx4 v[160:163], v[82:83], off offset:-4096 nt
	global_load_dwordx4 v[164:167], v[82:83], off offset:-3072 nt
	global_load_dwordx4 v[168:171], v[82:83], off offset:-2048 nt
	global_load_dwordx4 v[172:175], v[82:83], off offset:-1024 nt
	global_load_dwordx4 v[176:179], v[82:83], off nt
	global_load_dwordx4 v[180:183], v[82:83], off offset:1024 nt
	global_load_dwordx4 v[184:187], v[82:83], off offset:2048 nt
	global_load_dwordx4 v[188:191], v[82:83], off offset:3072 nt
	s_add_i32 s2, s2, 1
	v_lshl_add_u64 v[82:83], v[82:83], 0, s[4:5]
	s_waitcnt vmcnt(16)
	s_cmp_eq_u32 s8, s8
	s_branch .Ln1_procA
.Ln1_a_nopf:
	s_waitcnt vmcnt(8)
	s_cmp_lg_u32 s8, s8
.Ln1_procA:
	v_mul_f32_e32 v99, v101, v101
	v_mul_f32_e32 v144, v105, v105
	v_mul_f32_e32 v145, v109, v109
	v_fmac_f32_e32 v99, v100, v100
	v_fmac_f32_e32 v144, v104, v104
	v_mul_f32_e32 v146, v113, v113
	v_mov_b32_e32 v130, v117
	v_mov_b32_e32 v131, v121
	v_fmac_f32_e32 v145, v108, v108
	v_fmac_f32_e32 v99, v102, v102
	v_fmac_f32_e32 v144, v106, v106
	v_mov_b32_e32 v128, v116
	v_mov_b32_e32 v129, v120
	v_fmac_f32_e32 v146, v112, v112
	v_pk_mul_f32 v[130:131], v[130:131], v[130:131]
	v_fmac_f32_e32 v145, v110, v110
	v_fmac_f32_e32 v99, v103, v103
	v_fmac_f32_e32 v144, v107, v107
	v_mov_b32_e32 v132, v118
	v_mov_b32_e32 v133, v122
	v_mov_b32_e32 v138, v125
	v_mov_b32_e32 v139, v67
	v_fmac_f32_e32 v146, v114, v114
	v_pk_fma_f32 v[128:129], v[128:129], v[128:129], v[130:131]
	v_fmac_f32_e32 v145, v111, v111
	v_add_f32_e32 v99, v99, v144
	v_mov_b32_e32 v134, v119
	v_mov_b32_e32 v135, v123
	v_mov_b32_e32 v136, v124
	v_mov_b32_e32 v137, v66
	v_pk_mul_f32 v[138:139], v[138:139], v[138:139]
	v_fmac_f32_e32 v146, v115, v115
	v_pk_fma_f32 v[128:129], v[132:133], v[132:133], v[128:129]
	v_add_f32_e32 v99, v99, v145
	v_mov_b32_e32 v140, v126
	v_mov_b32_e32 v141, v68
	v_pk_fma_f32 v[130:131], v[136:137], v[136:137], v[138:139]
	v_pk_fma_f32 v[128:129], v[134:135], v[134:135], v[128:129]
	v_add_f32_e32 v99, v99, v146
	v_mov_b32_e32 v142, v127
	v_mov_b32_e32 v143, v69
	v_pk_fma_f32 v[130:131], v[140:141], v[140:141], v[130:131]
	v_add_f32_e32 v99, v99, v128
	v_pk_fma_f32 v[130:131], v[142:143], v[142:143], v[130:131]
	v_add_f32_e32 v99, v99, v129
	v_add_f32_e32 v99, v99, v130
	v_add_f32_e32 v99, v99, v131
	ds_bpermute_b32 v128, v1, v99
	v_mov_b32_e32 v129, 0
	v_mov_b32_e32 v133, 0
	v_mov_b32_e32 v130, 0
	v_mov_b32_e32 v134, 0
	s_waitcnt lgkmcnt(0)
	v_add_f32_e32 v99, v99, v128
	ds_bpermute_b32 v128, v84, v99
	v_mov_b32_e32 v131, 0
	v_mov_b32_e32 v132, 0
	s_waitcnt lgkmcnt(0)
	v_add_f32_e32 v99, v99, v128
	ds_bpermute_b32 v128, v85, v99
	s_waitcnt lgkmcnt(0)
	v_add_f32_e32 v99, v99, v128
	ds_bpermute_b32 v128, v86, v99
	s_waitcnt lgkmcnt(0)
	v_add_f32_e32 v99, v99, v128
	ds_bpermute_b32 v128, v87, v99
	s_waitcnt lgkmcnt(0)
	v_add_f32_e32 v99, v99, v128
	ds_bpermute_b32 v128, v88, v99
	s_waitcnt lgkmcnt(0)
; __device__ __forceinline__ unsigned pk4_fp8(float a, float b, float c, float d) {
;     a = __builtin_amdgcn_fmed3f(a, -448.f, 448.f); b = __builtin_amdgcn_fmed3f(b, -448.f, 448.f); c = __builtin_amdgcn_fmed3f(c, -448.f, 448.f); d = __builtin_amdgcn_fmed3f(d, -448.f, 448.f);
;     int r = 0; r = __builtin_amdgcn_cvt_pk_fp8_f32(a, b, r, false); r = __builtin_amdgcn_cvt_pk_fp8_f32(c, d, r, true); return (unsigned)r; }
; __device__ __forceinline__ void phase_norm_x(const Frame& F, const float* x, const float* g, const float* modl, int ish, int isc, unsigned char* XN8) {
;     ...
;         const float r = rsqrtf(wave_sum(ss) * (1.f / D) + EPS);
; #pragma unroll
;         for (int i = 0; i < 8; ++i) { const f32x4 y = v[i] * r * gs[i] + shv[i];
;             *(unsigned*)(XN8 + (size_t)t * D + 256 * i + 4 * F.lane) = pk4_fp8(y[0], y[1], y[2], y[3]); }
	v_add_f32_e32 v99, v99, v128
	v_fmamk_f32 v99, v99, 0x3a000000, v97
	v_mul_f32_e32 v128, 0x4b800000, v99
	v_cmp_gt_f32_e32 vcc, s3, v99
	s_nop 1
	v_cndmask_b32_e32 v99, v99, v128, vcc
	v_rsq_f32_e32 v99, v99
	s_nop 0
	v_mul_f32_e32 v128, 0x45800000, v99
	v_cndmask_b32_e32 v128, v99, v128, vcc
	v_pk_mul_f32 v[100:101], v[100:101], v[128:129] op_sel_hi:[1,0]
	v_pk_mul_f32 v[102:103], v[102:103], v[128:129] op_sel_hi:[1,0]
	v_pk_fma_f32 v[100:101], v[34:35], v[100:101], v[26:27]
	v_pk_mul_f32 v[104:105], v[104:105], v[128:129] op_sel_hi:[1,0]
	v_med3_f32 v99, v100, s13, v98
	v_med3_f32 v100, v101, s13, v98
	v_pk_mul_f32 v[106:107], v[106:107], v[128:129] op_sel_hi:[1,0]
	v_pk_mul_f32 v[108:109], v[108:109], v[128:129] op_sel_hi:[1,0]
	v_pk_mul_f32 v[110:111], v[110:111], v[128:129] op_sel_hi:[1,0]
	v_pk_mul_f32 v[112:113], v[112:113], v[128:129] op_sel_hi:[1,0]
	v_pk_mul_f32 v[114:115], v[114:115], v[128:129] op_sel_hi:[1,0]
	v_pk_mul_f32 v[116:117], v[116:117], v[128:129] op_sel_hi:[1,0]
	v_pk_mul_f32 v[118:119], v[118:119], v[128:129] op_sel_hi:[1,0]
	v_pk_mul_f32 v[120:121], v[120:121], v[128:129] op_sel_hi:[1,0]
	v_pk_mul_f32 v[122:123], v[122:123], v[128:129] op_sel_hi:[1,0]
	v_pk_mul_f32 v[124:125], v[124:125], v[128:129] op_sel_hi:[1,0]
	v_pk_mul_f32 v[126:127], v[126:127], v[128:129] op_sel_hi:[1,0]
	v_cvt_pk_fp8_f32 v129, v99, v100
	v_pk_fma_f32 v[102:103], v[36:37], v[102:103], v[28:29]
	v_pk_fma_f32 v[106:107], v[40:41], v[106:107], v[24:25]
	v_med3_f32 v101, v102, s13, v98
	v_med3_f32 v102, v103, s13, v98
	v_pk_fma_f32 v[104:105], v[38:39], v[104:105], v[22:23]
	v_pk_fma_f32 v[110:111], v[44:45], v[110:111], v[20:21]
	v_pk_fma_f32 v[108:109], v[42:43], v[108:109], v[18:19]
	v_pk_fma_f32 v[114:115], v[48:49], v[114:115], v[16:17]
	v_pk_fma_f32 v[112:113], v[46:47], v[112:113], v[14:15]
	v_pk_fma_f32 v[118:119], v[52:53], v[118:119], v[12:13]
	v_pk_fma_f32 v[116:117], v[50:51], v[116:117], v[10:11]
	v_pk_fma_f32 v[122:123], v[56:57], v[122:123], v[8:9]
	v_pk_fma_f32 v[120:121], v[54:55], v[120:121], v[6:7]
	v_pk_fma_f32 v[124:125], v[58:59], v[124:125], v[2:3]
	v_cvt_pk_fp8_f32 v129, v101, v102 op_sel:[0,0,1]
	v_med3_f32 v103, v104, s13, v98
	v_med3_f32 v104, v105, s13, v98
	v_med3_f32 v105, v106, s13, v98
	v_med3_f32 v106, v107, s13, v98
	v_med3_f32 v107, v108, s13, v98
	v_med3_f32 v108, v109, s13, v98
	v_med3_f32 v109, v110, s13, v98
	v_med3_f32 v110, v111, s13, v98
	v_med3_f32 v111, v112, s13, v98
	v_med3_f32 v112, v113, s13, v98
	v_med3_f32 v113, v114, s13, v98
	v_med3_f32 v114, v115, s13, v98
	v_med3_f32 v115, v116, s13, v98
	v_med3_f32 v116, v117, s13, v98
	v_med3_f32 v117, v118, s13, v98
	v_med3_f32 v118, v119, s13, v98
	v_med3_f32 v119, v120, s13, v98
	v_med3_f32 v120, v121, s13, v98
	v_med3_f32 v121, v122, s13, v98
	v_med3_f32 v122, v123, s13, v98
	v_med3_f32 v123, v124, s13, v98
	v_med3_f32 v99, v125, s13, v98
	v_mov_b32_e32 v102, 0
	v_cvt_pk_fp8_f32 v102, v123, v99
	v_cvt_pk_fp8_f32 v133, v115, v116
	v_pk_fma_f32 v[100:101], v[60:61], v[126:127], v[4:5]
	v_pk_mul_f32 v[66:67], v[66:67], v[128:129] op_sel_hi:[1,0]
	v_cvt_pk_fp8_f32 v130, v103, v104
	v_cvt_pk_fp8_f32 v134, v119, v120
	v_med3_f32 v99, v100, s13, v98
	v_med3_f32 v100, v101, s13, v98
	v_pk_fma_f32 v[66:67], v[62:63], v[66:67], v[30:31]
	v_cvt_pk_fp8_f32 v131, v107, v108
	v_cvt_pk_fp8_f32 v102, v99, v100 op_sel:[0,0,1]
	v_med3_f32 v66, v66, s13, v98
	v_med3_f32 v67, v67, s13, v98
	v_mov_b32_e32 v99, 0
	v_cvt_pk_fp8_f32 v132, v111, v112
	v_cvt_pk_fp8_f32 v99, v66, v67
	v_cvt_pk_fp8_f32 v133, v117, v118 op_sel:[0,0,1]
	v_pk_mul_f32 v[68:69], v[68:69], v[128:129] op_sel_hi:[1,0]
	v_cvt_pk_fp8_f32 v130, v105, v106 op_sel:[0,0,1]
	v_cvt_pk_fp8_f32 v134, v121, v122 op_sel:[0,0,1]
	v_pk_fma_f32 v[66:67], v[64:65], v[68:69], v[32:33]
	v_cvt_pk_fp8_f32 v131, v109, v110 op_sel:[0,0,1]
	v_med3_f32 v66, v66, s13, v98
	v_med3_f32 v67, v67, s13, v98
	v_cvt_pk_fp8_f32 v132, v113, v114 op_sel:[0,0,1]
	v_cvt_pk_fp8_f32 v99, v66, v67 op_sel:[0,0,1]
	global_store_dword v[80:81], v129, off
	global_store_dword v[80:81], v130, off offset:256
	global_store_dword v[80:81], v131, off offset:512
	global_store_dword v[80:81], v132, off offset:768
	global_store_dword v[80:81], v133, off offset:1024
	global_store_dword v[80:81], v134, off offset:1280
	global_store_dword v[80:81], v102, off offset:1536
	global_store_dword v[80:81], v99, off offset:1792
	v_lshl_add_u64 v[80:81], v[80:81], 0, s[6:7]
	s_cbranch_scc0 .Ln1_next
	s_cmp_lt_i32 s2, s12
	s_cbranch_scc0 .Ln1_b_nopf
	s_ashr_i32 s14, s2, 12
	s_cmp_eq_u32 s14, s8
	s_cbranch_scc0 .Ln1_b_nopf
	global_load_dwordx4 v[100:103], v[82:83], off offset:-4096 nt
	global_load_dwordx4 v[104:107], v[82:83], off offset:-3072 nt
	global_load_dwordx4 v[108:111], v[82:83], off offset:-2048 nt
	global_load_dwordx4 v[112:115], v[82:83], off offset:-1024 nt
	global_load_dwordx4 v[116:119], v[82:83], off nt
	global_load_dwordx4 v[120:123], v[82:83], off offset:1024 nt
	global_load_dwordx4 v[124:127], v[82:83], off offset:2048 nt
	global_load_dwordx4 v[66:69], v[82:83], off offset:3072 nt
	s_add_i32 s2, s2, 1
	v_lshl_add_u64 v[82:83], v[82:83], 0, s[4:5]
	s_waitcnt vmcnt(16)
	s_cmp_eq_u32 s8, s8
	s_branch .Ln1_procB

; __device__ __forceinline__ void phase_norm_x(const Frame& F, const float* x, const float* g, const float* modl, int ish, int isc, unsigned char* XN8) {
;     ...
;         for (int i = 0; i < 8; ++i) v[i] = __builtin_nontemporal_load((const f32x4*)(x + (size_t)t * D + 256 * i + 4 * F.lane));
; #pragma unroll
;         for (int i = 0; i < 8; ++i) ss += v[i][0] * v[i][0] + v[i][1] * v[i][1] + v[i][2] * v[i][2] + v[i][3] * v[i][3];
;         const float r = rsqrtf(wave_sum(ss) * (1.f / D) + EPS);
; #pragma unroll
;         for (int i = 0; i < 8; ++i) { const f32x4 y = v[i] * r * gs[i] + shv[i];
;             *(unsigned*)(XN8 + (size_t)t * D + 256 * i + 4 * F.lane) = pk4_fp8(y[0], y[1], y[2], y[3]); }
.Ln1_procB:
	v_mul_f32_e32 v99, v161, v161
	v_mul_f32_e32 v144, v165, v165
	v_mul_f32_e32 v145, v169, v169
	v_fmac_f32_e32 v99, v160, v160
	v_fmac_f32_e32 v144, v164, v164
	v_mul_f32_e32 v146, v173, v173
	v_mov_b32_e32 v130, v177
	v_mov_b32_e32 v131, v181
	v_fmac_f32_e32 v145, v168, v168
	v_fmac_f32_e32 v99, v162, v162
	v_fmac_f32_e32 v144, v166, v166
	v_mov_b32_e32 v128, v176
	v_mov_b32_e32 v129, v180
	v_fmac_f32_e32 v146, v172, v172
	v_pk_mul_f32 v[130:131], v[130:131], v[130:131]
	v_fmac_f32_e32 v145, v170, v170
	v_fmac_f32_e32 v99, v163, v163
	v_fmac_f32_e32 v144, v167, v167
	v_mov_b32_e32 v132, v178
	v_mov_b32_e32 v133, v182
	v_mov_b32_e32 v138, v185
	v_mov_b32_e32 v139, v189
	v_fmac_f32_e32 v146, v174, v174
	v_pk_fma_f32 v[128:129], v[128:129], v[128:129], v[130:131]
	v_fmac_f32_e32 v145, v171, v171
	v_add_f32_e32 v99, v99, v144
	v_mov_b32_e32 v134, v179
	v_mov_b32_e32 v135, v183
	v_mov_b32_e32 v136, v184
	v_mov_b32_e32 v137, v188
	v_pk_mul_f32 v[138:139], v[138:139], v[138:139]
	v_fmac_f32_e32 v146, v175, v175
	v_pk_fma_f32 v[128:129], v[132:133], v[132:133], v[128:129]
	v_add_f32_e32 v99, v99, v145
	v_mov_b32_e32 v140, v186
	v_mov_b32_e32 v141, v190
	v_pk_fma_f32 v[130:131], v[136:137], v[136:137], v[138:139]
	v_pk_fma_f32 v[128:129], v[134:135], v[134:135], v[128:129]
	v_add_f32_e32 v99, v99, v146
	v_mov_b32_e32 v142, v187
	v_mov_b32_e32 v143, v191
	v_pk_fma_f32 v[130:131], v[140:141], v[140:141], v[130:131]
	v_add_f32_e32 v99, v99, v128
	v_pk_fma_f32 v[130:131], v[142:143], v[142:143], v[130:131]
	v_add_f32_e32 v99, v99, v129
	v_add_f32_e32 v99, v99, v130
	v_add_f32_e32 v99, v99, v131
	ds_bpermute_b32 v128, v1, v99
	v_mov_b32_e32 v129, 0
	v_mov_b32_e32 v133, 0
	v_mov_b32_e32 v130, 0
	v_mov_b32_e32 v134, 0
	s_waitcnt lgkmcnt(0)
	v_add_f32_e32 v99, v99, v128
	ds_bpermute_b32 v128, v84, v99
	v_mov_b32_e32 v131, 0
	v_mov_b32_e32 v132, 0
	s_waitcnt lgkmcnt(0)
	v_add_f32_e32 v99, v99, v128
	ds_bpermute_b32 v128, v85, v99
	s_waitcnt lgkmcnt(0)
	v_add_f32_e32 v99, v99, v128
	ds_bpermute_b32 v128, v86, v99
	s_waitcnt lgkmcnt(0)
	v_add_f32_e32 v99, v99, v128
	ds_bpermute_b32 v128, v87, v99
	s_waitcnt lgkmcnt(0)
	v_add_f32_e32 v99, v99, v128
	ds_bpermute_b32 v128, v88, v99
	s_waitcnt lgkmcnt(0)
	v_add_f32_e32 v99, v99, v128
	v_fmamk_f32 v99, v99, 0x3a000000, v97
	v_mul_f32_e32 v128, 0x4b800000, v99
	v_cmp_gt_f32_e32 vcc, s3, v99
	s_nop 1
	v_cndmask_b32_e32 v99, v99, v128, vcc
	v_rsq_f32_e32 v99, v99
	s_nop 0
	v_mul_f32_e32 v128, 0x45800000, v99
	v_cndmask_b32_e32 v128, v99, v128, vcc
	v_pk_mul_f32 v[160:161], v[160:161], v[128:129] op_sel_hi:[1,0]
	v_pk_mul_f32 v[162:163], v[162:163], v[128:129] op_sel_hi:[1,0]
	v_pk_fma_f32 v[160:161], v[34:35], v[160:161], v[26:27]
	v_pk_mul_f32 v[164:165], v[164:165], v[128:129] op_sel_hi:[1,0]
	v_med3_f32 v99, v160, s13, v98
	v_med3_f32 v160, v161, s13, v98
	v_pk_mul_f32 v[166:167], v[166:167], v[128:129] op_sel_hi:[1,0]
	v_pk_mul_f32 v[168:169], v[168:169], v[128:129] op_sel_hi:[1,0]
	v_pk_mul_f32 v[170:171], v[170:171], v[128:129] op_sel_hi:[1,0]
	v_pk_mul_f32 v[172:173], v[172:173], v[128:129] op_sel_hi:[1,0]
	v_pk_mul_f32 v[174:175], v[174:175], v[128:129] op_sel_hi:[1,0]
	v_pk_mul_f32 v[176:177], v[176:177], v[128:129] op_sel_hi:[1,0]
	v_pk_mul_f32 v[178:179], v[178:179], v[128:129] op_sel_hi:[1,0]
	v_pk_mul_f32 v[180:181], v[180:181], v[128:129] op_sel_hi:[1,0]
	v_pk_mul_f32 v[182:183], v[182:183], v[128:129] op_sel_hi:[1,0]
	v_pk_mul_f32 v[184:185], v[184:185], v[128:129] op_sel_hi:[1,0]
	v_pk_mul_f32 v[186:187], v[186:187], v[128:129] op_sel_hi:[1,0]
	v_cvt_pk_fp8_f32 v129, v99, v160
	v_pk_fma_f32 v[162:163], v[36:37], v[162:163], v[28:29]
	v_pk_fma_f32 v[166:167], v[40:41], v[166:167], v[24:25]
	v_med3_f32 v161, v162, s13, v98
	v_med3_f32 v162, v163, s13, v98
	v_pk_fma_f32 v[164:165], v[38:39], v[164:165], v[22:23]
	v_pk_fma_f32 v[170:171], v[44:45], v[170:171], v[20:21]
	v_pk_fma_f32 v[168:169], v[42:43], v[168:169], v[18:19]
	v_pk_fma_f32 v[174:175], v[48:49], v[174:175], v[16:17]
	v_pk_fma_f32 v[172:173], v[46:47], v[172:173], v[14:15]
	v_pk_fma_f32 v[178:179], v[52:53], v[178:179], v[12:13]
	v_pk_fma_f32 v[176:177], v[50:51], v[176:177], v[10:11]
	v_pk_fma_f32 v[182:183], v[56:57], v[182:183], v[8:9]
	v_pk_fma_f32 v[180:181], v[54:55], v[180:181], v[6:7]
	v_pk_fma_f32 v[184:185], v[58:59], v[184:185], v[2:3]
	v_cvt_pk_fp8_f32 v129, v161, v162 op_sel:[0,0,1]
	v_med3_f32 v163, v164, s13, v98
	v_med3_f32 v164, v165, s13, v98
	v_med3_f32 v165, v166, s13, v98
	v_med3_f32 v166, v167, s13, v98
	v_med3_f32 v167, v168, s13, v98
	v_med3_f32 v168, v169, s13, v98
	v_med3_f32 v169, v170, s13, v98
	v_med3_f32 v170, v171, s13, v98
	v_med3_f32 v171, v172, s13, v98
	v_med3_f32 v172, v173, s13, v98
	v_med3_f32 v173, v174, s13, v98
	v_med3_f32 v174, v175, s13, v98
	v_med3_f32 v175, v176, s13, v98
	v_med3_f32 v176, v177, s13, v98
	v_med3_f32 v177, v178, s13, v98
	v_med3_f32 v178, v179, s13, v98
	v_med3_f32 v179, v180, s13, v98
	v_med3_f32 v180, v181, s13, v98
	v_med3_f32 v181, v182, s13, v98
	v_med3_f32 v182, v183, s13, v98
	v_med3_f32 v183, v184, s13, v98
	v_med3_f32 v99, v185, s13, v98
	v_mov_b32_e32 v162, 0
	v_cvt_pk_fp8_f32 v162, v183, v99
	v_cvt_pk_fp8_f32 v133, v175, v176
	v_pk_fma_f32 v[160:161], v[60:61], v[186:187], v[4:5]
	v_pk_mul_f32 v[188:189], v[188:189], v[128:129] op_sel_hi:[1,0]
	v_cvt_pk_fp8_f32 v130, v163, v164
	v_cvt_pk_fp8_f32 v134, v179, v180
	v_med3_f32 v99, v160, s13, v98
	v_med3_f32 v160, v161, s13, v98
	v_pk_fma_f32 v[188:189], v[62:63], v[188:189], v[30:31]
	v_cvt_pk_fp8_f32 v131, v167, v168
	v_cvt_pk_fp8_f32 v162, v99, v160 op_sel:[0,0,1]
	v_med3_f32 v188, v188, s13, v98
	v_med3_f32 v189, v189, s13, v98
	v_mov_b32_e32 v99, 0
	v_cvt_pk_fp8_f32 v132, v171, v172
	v_cvt_pk_fp8_f32 v99, v188, v189
	v_cvt_pk_fp8_f32 v133, v177, v178 op_sel:[0,0,1]
	v_pk_mul_f32 v[190:191], v[190:191], v[128:129] op_sel_hi:[1,0]
	v_cvt_pk_fp8_f32 v130, v165, v166 op_sel:[0,0,1]
	v_cvt_pk_fp8_f32 v134, v181, v182 op_sel:[0,0,1]
	v_pk_fma_f32 v[188:189], v[64:65], v[190:191], v[32:33]
	v_cvt_pk_fp8_f32 v131, v169, v170 op_sel:[0,0,1]
	v_med3_f32 v188, v188, s13, v98
	v_med3_f32 v189, v189, s13, v98
	v_cvt_pk_fp8_f32 v132, v173, v174 op_sel:[0,0,1]
	v_cvt_pk_fp8_f32 v99, v188, v189 op_sel:[0,0,1]
	global_store_dword v[80:81], v129, off
	global_store_dword v[80:81], v130, off offset:256
	global_store_dword v[80:81], v131, off offset:512
	global_store_dword v[80:81], v132, off offset:768
	global_store_dword v[80:81], v133, off offset:1024
	global_store_dword v[80:81], v134, off offset:1280
	global_store_dword v[80:81], v162, off offset:1536
	global_store_dword v[80:81], v99, off offset:1792
	v_lshl_add_u64 v[80:81], v[80:81], 0, s[6:7]
	s_cbranch_scc1 .Ln1_PA
.Ln1_next:
	s_cmp_lt_i32 s2, s12
	s_cbranch_scc0 .LBB0_221

; __device__ __forceinline__ void xcd_barrier(const XcdBarrier& b) {
;     asm volatile("s_waitcnt vmcnt(0)" ::: "memory");
;     __syncthreads();
;     if (threadIdx.x == 0) {
;         unsigned* bar = b.bar;
;         __builtin_amdgcn_s_waitcnt(0);
;         unsigned nloc = b.st[0], nx = b.st[1];
;         if (nloc == 0u) { xcd_barrier_complete(bar, b.x, nloc, nx); b.st[0] = nloc; b.st[1] = nx; }
.LBB0_221:
	s_and_saveexec_b64 s[2:3], s[96:97]
	s_cbranch_execz .LBB0_224
	s_mov_b64 s[4:5], exec
	v_mbcnt_lo_u32_b32 v1, s4, 0
	v_mbcnt_hi_u32_b32 v1, s5, v1
	v_cmp_eq_u32_e32 vcc, 0, v1
	s_and_b64 s[6:7], exec, vcc
	s_mov_b64 exec, s[6:7]
	s_cbranch_execz .LBB0_224
	s_bcnt1_i32_b64 s4, s[4:5]
	v_mov_b32_e32 v1, 0x1000
	v_mov_b32_e32 v2, s4
.LBB0_224:
	s_or_b64 exec, exec, s[2:3]
	v_readlane_b32 s8, v255, 4
	v_readlane_b32 s9, v255, 5
	s_cmp_lt_i32 s9, 3
	v_readlane_b32 s10, v255, 6
	v_readlane_b32 s11, v255, 7
	s_cbranch_scc1 .LBB0_274
	s_waitcnt vmcnt(0)
	s_barrier
	s_and_saveexec_b64 s[2:3], s[96:97]
	s_cbranch_execz .LBB0_273
	v_readlane_b32 s4, v255, 10
	s_waitcnt vmcnt(0) expcnt(0) lgkmcnt(0)
	s_nop 0
	v_mov_b32_e32 v1, s4
	ds_read_b32 v3, v1
	ds_read_b32 v1, v1 offset:4
	s_waitcnt lgkmcnt(1)
	v_cmp_ne_u32_e32 vcc, 0, v3
	s_cbranch_vccnz .LBB0_241
	v_readlane_b32 s4, v255, 0
	v_readlane_b32 s5, v255, 1
	s_load_dwordx2 s[8:9], s[4:5], 0x4
	v_readlane_b32 s10, v255, 8
	v_readlane_b32 s11, v255, 9
	s_add_u32 s4, s10, 0x1000
	s_addc_u32 s5, s11, 0
	s_add_u32 s6, s10, 0x1100
	s_addc_u32 s7, s11, 0
	s_waitcnt lgkmcnt(0)
	s_mul_i32 s20, s8, s93
	s_add_u32 s8, s10, 0x1200
	s_mul_i32 s20, s20, s9
	s_addc_u32 s9, s11, 0
	s_add_u32 s10, s10, 0x1300
	s_addc_u32 s11, s11, 0
	s_mov_b32 s21, 1
	v_mov_b32_e32 v17, 0
	s_branch .LBB0_229

; __device__ __forceinline__ void xcd_barrier(const XcdBarrier& b) {
;     asm volatile("s_waitcnt vmcnt(0)" ::: "memory");
;     __syncthreads();
;     if (threadIdx.x == 0) {
;         unsigned* bar = b.bar;
;         __builtin_amdgcn_s_waitcnt(0);
;         unsigned nloc = b.st[0], nx = b.st[1];
;         if (nloc == 0u) { xcd_barrier_complete(bar, b.x, nloc, nx); b.st[0] = nloc; b.st[1] = nx; }
.LBB0_303:
	s_and_saveexec_b64 s[2:3], s[96:97]
	s_cbranch_execz .LBB0_306
	s_mov_b64 s[4:5], exec
	v_mbcnt_lo_u32_b32 v1, s4, 0
	v_mbcnt_hi_u32_b32 v1, s5, v1
	v_cmp_eq_u32_e32 vcc, 0, v1
	s_and_b64 s[6:7], exec, vcc
	s_mov_b64 exec, s[6:7]
	s_cbranch_execz .LBB0_306
	s_bcnt1_i32_b64 s4, s[4:5]
	v_mov_b32_e32 v1, 0x1000
	v_mov_b32_e32 v2, s4
.LBB0_306:
	s_or_b64 exec, exec, s[2:3]
	v_readlane_b32 s8, v255, 4
	v_readlane_b32 s9, v255, 5
	s_cmp_lt_i32 s9, 4
	v_readlane_b32 s10, v255, 6
	v_readlane_b32 s11, v255, 7
	s_cbranch_scc1 .LBB0_356
	s_waitcnt vmcnt(0)
	s_waitcnt vmcnt(0)
	s_barrier
	s_and_saveexec_b64 s[2:3], s[96:97]
	s_cbranch_execz .LBB0_355
	v_readlane_b32 s4, v255, 10
	s_waitcnt vmcnt(0) expcnt(0) lgkmcnt(0)
	s_nop 0
	v_mov_b32_e32 v1, s4
	ds_read_b32 v3, v1
	ds_read_b32 v1, v1 offset:4
	s_waitcnt lgkmcnt(1)
	v_cmp_ne_u32_e32 vcc, 0, v3
	s_cbranch_vccnz .LBB0_323
	v_readlane_b32 s4, v255, 0
	v_readlane_b32 s5, v255, 1
	s_load_dwordx2 s[8:9], s[4:5], 0x4
	v_readlane_b32 s10, v255, 8
	v_readlane_b32 s11, v255, 9
	s_add_u32 s4, s10, 0x1000
	s_addc_u32 s5, s11, 0
	s_add_u32 s6, s10, 0x1100
	s_addc_u32 s7, s11, 0
	s_waitcnt lgkmcnt(0)
	s_mul_i32 s20, s8, s93
	s_add_u32 s8, s10, 0x1200
	s_mul_i32 s20, s20, s9
	s_addc_u32 s9, s11, 0
	s_add_u32 s10, s10, 0x1300
	s_addc_u32 s11, s11, 0
	s_mov_b32 s21, 1
	v_mov_b32_e32 v17, 0
	s_branch .LBB0_311

; #define LAS __attribute__((address_space(3)))
; __device__ __forceinline__ int crow(int r, int hi) { return (r & 3) + 8 * (r >> 2) + 4 * hi; }
; __device__ __forceinline__ void qkt(f32x16& p0, f32x16& p1, const LAS char* Ks, const bf16x8* qr, int r32, int hi) {
;     p0 = f32x16{}; p1 = f32x16{};
; #pragma unroll
;     for (int d0 = 0; d0 < 8; ++d0) { const int cb = (d0 * 16 + hi * 8) * 2;
;         const bf16x8 b0 = *(const LAS bf16x8*)(Ks + KSWZ(r32, cb));
;         const bf16x8 b1 = *(const LAS bf16x8*)(Ks + KSWZ(32 + r32, cb));
;         p0 = __builtin_amdgcn_mfma_f32_32x32x16_bf16(b0, qr[d0], p0, 0, 0, 0);
;         p1 = __builtin_amdgcn_mfma_f32_32x32x16_bf16(b1, qr[d0], p1, 0, 0, 0); }
; }
; template <int MODE>
; __device__ __forceinline__ void attn_unit(const AttnArgs& A, int b, int qb, int qc, int kc, int vc, int oc, float slope2, int dmax, LAS char* lds) {
;     ...
;         const bool active = (k0 <= r0) && !wdone && (MODE == 0 || k0 + 63 + dmax >= r0);
;         if (active) {
;             f32x16 p0, p1;
;             qkt(p0, p1, lds + L_K + bf * SHM_T, qr, r32, hi);
;             const int vb = vb0 + bf * SHM_T;
;             bf16x8 pa0, pa1, pa2, pa3;
;             if (MODE == 0) {
;                 const bool need_mask = (k0 + 63 >= r0);
;                 float lsum = 0.f;
;                 float lk0[16], lk1[16];
; #pragma unroll
;                 for (int r = 0; r < 16; ++r) {
;                     { const float zl = p0[r] * QK_C, u = __builtin_amdgcn_exp2f(-fabsf(zl)), L = __builtin_amdgcn_logf(1.f + u), sp = fmaxf(zl, 0.f) + L;
;                       const bool ok = !need_mask || (k0 + crow(r, hi) < tq); lk0[r] = ok ? -sp : 0.f; p0[r] = ok ? (zl - sp) : -INFINITY; lsum += lk0[r]; }
;                     { const float zl = p1[r] * QK_C, u = __builtin_amdgcn_exp2f(-fabsf(zl)), L = __builtin_amdgcn_logf(1.f + u), sp = fmaxf(zl, 0.f) + L;
;                       const bool ok = !need_mask || (k0 + 32 + crow(r, hi) < tq); lk1[r] = ok ? -sp : 0.f; p1[r] = ok ? (zl - sp) : -INFINITY; lsum += lk1[r]; }
.LBB0_372:
	s_cmp_gt_i32 s38, s35
	s_cselect_b64 s[16:17], -1, 0
	s_or_b64 s[16:17], s[16:17], s[14:15]
	s_and_b64 vcc, exec, s[16:17]
	s_cbranch_vccnz .LBB0_374
	s_lshl_b32 s16, s41, 14
	v_add_u32_e32 v67, s16, v199
	v_add_u32_e32 v72, v67, v184
	ds_read_b128 v[68:71], v72 offset:32768
	ds_read_b128 v[72:75], v72 offset:40960
	v_add_u32_e32 v104, v67, v185
	ds_read_b128 v[100:103], v104 offset:32768
	ds_read_b128 v[104:107], v104 offset:40960
	s_add_i32 s14, s38, 63
	s_waitcnt lgkmcnt(0)
	v_mfma_f32_32x32x16_bf16 v[84:99], v[68:71], v[122:125], 0
	s_cmp_lt_i32 s14, s35
	s_cselect_b64 s[14:15], -1, 0
	v_mov_b32_e32 v254, 0x7fffffff
	v_cndmask_b32_e64 v253, v210, v254, s[14:15]
	s_mov_b32 s22, s20
	s_mov_b32 s23, s20
	s_mov_b32 s21, s20
	v_mfma_f32_32x32x16_bf16 v[68:83], v[72:75], v[122:125], 0
	v_mfma_f32_32x32x16_bf16 v[84:99], v[100:103], v[126:129], v[84:99]
	v_mfma_f32_32x32x16_bf16 v[68:83], v[104:107], v[126:129], v[68:83]
	v_add_u32_e32 v104, v67, v186
	ds_read_b128 v[100:103], v104 offset:32768
	ds_read_b128 v[104:107], v104 offset:40960
	s_waitcnt lgkmcnt(0)
	v_mfma_f32_32x32x16_bf16 v[84:99], v[100:103], v[130:133], v[84:99]
	v_mfma_f32_32x32x16_bf16 v[68:83], v[104:107], v[130:133], v[68:83]
	v_add_u32_e32 v104, v67, v187
	ds_read_b128 v[100:103], v104 offset:32768
	ds_read_b128 v[104:107], v104 offset:40960
	s_waitcnt lgkmcnt(0)
	v_mfma_f32_32x32x16_bf16 v[84:99], v[100:103], v[134:137], v[84:99]
	v_mfma_f32_32x32x16_bf16 v[68:83], v[104:107], v[134:137], v[68:83]
	v_add_u32_e32 v104, v67, v188
	ds_read_b128 v[100:103], v104 offset:32768
	ds_read_b128 v[104:107], v104 offset:40960
	s_waitcnt lgkmcnt(0)
	v_mfma_f32_32x32x16_bf16 v[84:99], v[100:103], v[138:141], v[84:99]
	v_mfma_f32_32x32x16_bf16 v[68:83], v[104:107], v[138:141], v[68:83]
	v_add_u32_e32 v104, v67, v189
	ds_read_b128 v[100:103], v104 offset:32768
	ds_read_b128 v[104:107], v104 offset:40960
	s_waitcnt lgkmcnt(0)
	v_mfma_f32_32x32x16_bf16 v[84:99], v[100:103], v[142:145], v[84:99]
	v_mfma_f32_32x32x16_bf16 v[68:83], v[104:107], v[142:145], v[68:83]
	v_add_u32_e32 v104, v67, v190
	ds_read_b128 v[100:103], v104 offset:32768
	ds_read_b128 v[104:107], v104 offset:40960
	v_add_u32_e32 v67, v67, v191
	s_waitcnt lgkmcnt(0)
	v_mfma_f32_32x32x16_bf16 v[84:99], v[100:103], v[146:149], v[84:99]
	v_mfma_f32_32x32x16_bf16 v[68:83], v[104:107], v[146:149], v[68:83]
	ds_read_b128 v[100:103], v67 offset:32768
	ds_read_b128 v[104:107], v67 offset:40960
	v_add_u32_e32 v67, s38, v192
	v_sub_u32_e32 v254, v253, v67
	v_cmp_lt_i32_e32 vcc, 0, v254
	s_waitcnt lgkmcnt(0)
	v_mfma_f32_32x32x16_bf16 v[84:99], v[100:103], v[150:153], v[84:99]
	v_mfma_f32_32x32x16_bf16 v[68:83], v[104:107], v[150:153], v[68:83]
	s_nop 9
	s_cmp_lg_u64 s[14:15], 0
	s_cbranch_scc1 .Lsb_unmasked
	v_mul_f32_e32 v100, 0x3e0293ee, v84
	v_exp_f32_e64 v102, -|v100|
	v_max_f32_e32 v100, 0, v100
	v_add_f32_e32 v102, 1.0, v102
	v_log_f32_e32 v102, v102
	s_nop 0
	v_add_f32_e32 v102, v100, v102
	v_fma_f32 v84, v84, s26, -v102
	v_cndmask_b32_e32 v211, v208, v84, vcc
	v_mul_f32_e32 v84, 0x3e0293ee, v68
	v_exp_f32_e64 v103, -|v84|
	v_max_f32_e32 v84, 0, v84
	v_cndmask_b32_e64 v100, 0, -v102, vcc
	v_cmp_lt_i32_e32 vcc, 32, v254
	v_add_f32_e32 v103, 1.0, v103
	v_log_f32_e32 v103, v103
	v_add_f32_e32 v102, 0, v100
	v_add_f32_e32 v103, v84, v103
	v_fma_f32 v68, v68, s26, -v103
	v_cndmask_b32_e64 v84, 0, -v103, vcc
	v_cndmask_b32_e32 v212, v208, v68, vcc
	v_mul_f32_e32 v68, 0x3e0293ee, v85
	v_add_f32_e32 v101, v102, v84
	v_exp_f32_e64 v102, -|v68|
	v_max_f32_e32 v68, 0, v68
	v_add_f32_e32 v102, 1.0, v102
	v_log_f32_e32 v102, v102
	s_nop 0
	v_add_f32_e32 v102, v68, v102
	v_cmp_lt_i32_e32 vcc, 1, v254
	v_fma_f32 v85, v85, s26, -v102
	v_cndmask_b32_e32 v213, v208, v85, vcc
	v_mul_f32_e32 v85, 0x3e0293ee, v69
	v_cndmask_b32_e64 v68, 0, -v102, vcc
	v_exp_f32_e64 v102, -|v85|
	v_max_f32_e32 v85, 0, v85
	v_add_f32_e32 v101, v68, v101
	v_add_f32_e32 v102, 1.0, v102
	v_log_f32_e32 v102, v102
	s_nop 0
	v_add_f32_e32 v102, v85, v102
	v_cmp_lt_i32_e32 vcc, 33, v254
	v_fma_f32 v69, v69, s26, -v102
	v_cndmask_b32_e32 v214, v208, v69, vcc
	v_mul_f32_e32 v69, 0x3e0293ee, v86
	v_cndmask_b32_e64 v85, 0, -v102, vcc
	v_exp_f32_e64 v102, -|v69|
	v_max_f32_e32 v69, 0, v69
	v_add_f32_e32 v101, v85, v101
	v_cvt_pkrtz_f16_f32 v238, v84, v85
	v_add_f32_e32 v102, 1.0, v102
	v_log_f32_e32 v102, v102
	s_nop 0
	v_add_f32_e32 v102, v69, v102
	v_cmp_lt_i32_e32 vcc, 2, v254
	v_fma_f32 v86, v86, s26, -v102
	v_cndmask_b32_e32 v215, v208, v86, vcc
	v_mul_f32_e32 v86, 0x3e0293ee, v70
	v_cndmask_b32_e64 v69, 0, -v102, vcc
	v_exp_f32_e64 v102, -|v86|
	v_max_f32_e32 v86, 0, v86
	v_add_f32_e32 v101, v69, v101
	v_add_f32_e32 v102, 1.0, v102
	v_log_f32_e32 v102, v102
	s_nop 0
	v_add_f32_e32 v102, v86, v102
	v_cmp_lt_i32_e32 vcc, 34, v254
	v_fma_f32 v70, v70, s26, -v102
	v_cndmask_b32_e32 v216, v208, v70, vcc
	v_mul_f32_e32 v70, 0x3e0293ee, v87
	v_cndmask_b32_e64 v86, 0, -v102, vcc
	v_exp_f32_e64 v102, -|v70|
	v_max_f32_e32 v70, 0, v70
	v_add_f32_e32 v101, v86, v101
	v_add_f32_e32 v102, 1.0, v102
	v_log_f32_e32 v102, v102
	s_nop 0
	v_add_f32_e32 v102, v70, v102
	v_cmp_lt_i32_e32 vcc, 3, v254
	v_fma_f32 v87, v87, s26, -v102
	v_cndmask_b32_e32 v217, v208, v87, vcc
	v_mul_f32_e32 v87, 0x3e0293ee, v71
	v_cndmask_b32_e64 v70, 0, -v102, vcc
	v_exp_f32_e64 v102, -|v87|
	v_max_f32_e32 v87, 0, v87
	v_add_f32_e32 v101, v70, v101
	v_add_f32_e32 v102, 1.0, v102
	v_log_f32_e32 v102, v102
	s_nop 0
	v_add_f32_e32 v102, v87, v102
	v_cmp_lt_i32_e32 vcc, 35, v254
	v_fma_f32 v71, v71, s26, -v102
	v_cndmask_b32_e32 v218, v208, v71, vcc
	v_mul_f32_e32 v71, 0x3e0293ee, v88
; __device__ __forceinline__ int crow(int r, int hi) { return (r & 3) + 8 * (r >> 2) + 4 * hi; }
; template <int MODE>
; __device__ __forceinline__ void attn_unit(const AttnArgs& A, int b, int qb, int qc, int kc, int vc, int oc, float slope2, int dmax, LAS char* lds) {
;     ...
;                 for (int r = 0; r < 16; ++r) {
;                     { const float zl = p0[r] * QK_C, u = __builtin_amdgcn_exp2f(-fabsf(zl)), L = __builtin_amdgcn_logf(1.f + u), sp = fmaxf(zl, 0.f) + L;
;                       const bool ok = !need_mask || (k0 + crow(r, hi) < tq); lk0[r] = ok ? -sp : 0.f; p0[r] = ok ? (zl - sp) : -INFINITY; lsum += lk0[r]; }
;                     { const float zl = p1[r] * QK_C, u = __builtin_amdgcn_exp2f(-fabsf(zl)), L = __builtin_amdgcn_logf(1.f + u), sp = fmaxf(zl, 0.f) + L;
;                       const bool ok = !need_mask || (k0 + 32 + crow(r, hi) < tq); lk1[r] = ok ? -sp : 0.f; p1[r] = ok ? (zl - sp) : -INFINITY; lsum += lk1[r]; }
;                 }
;                 f16x8 f0, f1, f2, f3; PK4H(lk0, 0, f0); PK4H(lk0, 8, f1); PK4H(lk1, 0, f2); PK4H(lk1, 8, f3);
	v_cndmask_b32_e64 v87, 0, -v102, vcc
	v_exp_f32_e64 v102, -|v71|
	v_max_f32_e32 v71, 0, v71
	v_add_f32_e32 v101, v87, v101
	v_cvt_pkrtz_f16_f32 v239, v86, v87
	v_add_f32_e32 v102, 1.0, v102
	v_log_f32_e32 v102, v102
	s_nop 0
	v_add_f32_e32 v102, v71, v102
	v_cmp_lt_i32_e32 vcc, 8, v254
	v_fma_f32 v88, v88, s26, -v102
	v_cndmask_b32_e32 v219, v208, v88, vcc
	v_mul_f32_e32 v88, 0x3e0293ee, v72
	v_cndmask_b32_e64 v71, 0, -v102, vcc
	v_exp_f32_e64 v102, -|v88|
	v_max_f32_e32 v88, 0, v88
	v_add_f32_e32 v101, v71, v101
	v_add_f32_e32 v102, 1.0, v102
	v_log_f32_e32 v102, v102
	s_nop 0
	v_add_f32_e32 v102, v88, v102
	v_cmp_lt_i32_e32 vcc, 40, v254
	v_fma_f32 v72, v72, s26, -v102
	v_cndmask_b32_e32 v220, v208, v72, vcc
	v_mul_f32_e32 v72, 0x3e0293ee, v89
	v_cndmask_b32_e64 v88, 0, -v102, vcc
	v_exp_f32_e64 v102, -|v72|
	v_max_f32_e32 v72, 0, v72
	v_add_f32_e32 v101, v88, v101
	v_add_f32_e32 v102, 1.0, v102
	v_log_f32_e32 v102, v102
	s_nop 0
	v_add_f32_e32 v102, v72, v102
	v_cmp_lt_i32_e32 vcc, 9, v254
	v_fma_f32 v89, v89, s26, -v102
	v_cndmask_b32_e32 v221, v208, v89, vcc
	v_mul_f32_e32 v89, 0x3e0293ee, v73
	v_cndmask_b32_e64 v72, 0, -v102, vcc
	v_exp_f32_e64 v102, -|v89|
	v_max_f32_e32 v89, 0, v89
	v_add_f32_e32 v101, v72, v101
	v_add_f32_e32 v102, 1.0, v102
	v_log_f32_e32 v102, v102
	s_nop 0
	v_add_f32_e32 v102, v89, v102
	v_cmp_lt_i32_e32 vcc, 41, v254
	v_fma_f32 v73, v73, s26, -v102
	v_cndmask_b32_e32 v222, v208, v73, vcc
	v_mul_f32_e32 v73, 0x3e0293ee, v90
	v_cndmask_b32_e64 v89, 0, -v102, vcc
	v_exp_f32_e64 v102, -|v73|
	v_max_f32_e32 v73, 0, v73
	v_add_f32_e32 v101, v89, v101
	v_cvt_pkrtz_f16_f32 v240, v88, v89
	v_add_f32_e32 v102, 1.0, v102
	v_log_f32_e32 v102, v102
	v_permlane32_swap_b32_e32 v238, v240
	v_add_f32_e32 v102, v73, v102
	v_cmp_lt_i32_e32 vcc, 10, v254
	v_fma_f32 v90, v90, s26, -v102
	v_cndmask_b32_e32 v223, v208, v90, vcc
	v_mul_f32_e32 v90, 0x3e0293ee, v74
	v_cndmask_b32_e64 v73, 0, -v102, vcc
	v_exp_f32_e64 v102, -|v90|
	v_max_f32_e32 v90, 0, v90
	v_add_f32_e32 v101, v73, v101
	v_add_f32_e32 v102, 1.0, v102
	v_log_f32_e32 v102, v102
	s_nop 0
	v_add_f32_e32 v102, v90, v102
	v_cmp_lt_i32_e32 vcc, 42, v254
	v_fma_f32 v74, v74, s26, -v102
	v_cndmask_b32_e32 v224, v208, v74, vcc
	v_mul_f32_e32 v74, 0x3e0293ee, v91
	v_cndmask_b32_e64 v90, 0, -v102, vcc
	v_exp_f32_e64 v102, -|v74|
	v_max_f32_e32 v74, 0, v74
	v_add_f32_e32 v101, v90, v101
	v_add_f32_e32 v102, 1.0, v102
	v_log_f32_e32 v102, v102
	s_nop 0
	v_add_f32_e32 v102, v74, v102
	v_cmp_lt_i32_e32 vcc, 11, v254
	v_fma_f32 v91, v91, s26, -v102
	v_cndmask_b32_e32 v225, v208, v91, vcc
	v_mul_f32_e32 v91, 0x3e0293ee, v75
	v_cndmask_b32_e64 v74, 0, -v102, vcc
	v_exp_f32_e64 v102, -|v91|
	v_max_f32_e32 v91, 0, v91
	v_add_f32_e32 v101, v74, v101
	v_add_f32_e32 v102, 1.0, v102
	v_log_f32_e32 v102, v102
	s_nop 0
	v_add_f32_e32 v102, v91, v102
	v_cmp_lt_i32_e32 vcc, 43, v254
	v_fma_f32 v75, v75, s26, -v102
	v_cndmask_b32_e32 v226, v208, v75, vcc
	v_mul_f32_e32 v75, 0x3e0293ee, v92
	v_cndmask_b32_e64 v91, 0, -v102, vcc
	v_exp_f32_e64 v102, -|v75|
	v_max_f32_e32 v75, 0, v75
	v_add_f32_e32 v101, v91, v101
	v_cvt_pkrtz_f16_f32 v241, v90, v91
	v_add_f32_e32 v102, 1.0, v102
	v_log_f32_e32 v102, v102
	v_permlane32_swap_b32_e32 v239, v241
	v_add_f32_e32 v102, v75, v102
	v_cmp_lt_i32_e32 vcc, 16, v254
	v_fma_f32 v92, v92, s26, -v102
	v_cndmask_b32_e32 v227, v208, v92, vcc
	v_mul_f32_e32 v92, 0x3e0293ee, v76
	v_cndmask_b32_e64 v75, 0, -v102, vcc
	v_exp_f32_e64 v102, -|v92|
	v_max_f32_e32 v92, 0, v92
	v_add_f32_e32 v101, v75, v101
	v_add_f32_e32 v102, 1.0, v102
	v_log_f32_e32 v102, v102
	s_nop 0
	v_add_f32_e32 v102, v92, v102
	v_cmp_lt_i32_e32 vcc, 48, v254
	v_fma_f32 v76, v76, s26, -v102
	v_cndmask_b32_e32 v228, v208, v76, vcc
	v_mul_f32_e32 v76, 0x3e0293ee, v93
	v_cndmask_b32_e64 v92, 0, -v102, vcc
	v_exp_f32_e64 v102, -|v76|
	v_max_f32_e32 v76, 0, v76
	v_add_f32_e32 v101, v92, v101
	v_add_f32_e32 v102, 1.0, v102
	v_log_f32_e32 v102, v102
	s_nop 0
	v_add_f32_e32 v102, v76, v102
	v_cmp_lt_i32_e32 vcc, 17, v254
	v_fma_f32 v93, v93, s26, -v102
	v_cndmask_b32_e32 v229, v208, v93, vcc
	v_mul_f32_e32 v93, 0x3e0293ee, v77
	v_cndmask_b32_e64 v76, 0, -v102, vcc
	v_exp_f32_e64 v102, -|v93|
	v_max_f32_e32 v93, 0, v93
	v_add_f32_e32 v101, v76, v101
	v_add_f32_e32 v102, 1.0, v102
	v_log_f32_e32 v102, v102
	s_nop 0
	v_add_f32_e32 v102, v93, v102
	v_cmp_lt_i32_e32 vcc, 49, v254
	v_fma_f32 v77, v77, s26, -v102
	v_cndmask_b32_e32 v231, v208, v77, vcc
	v_mul_f32_e32 v77, 0x3e0293ee, v94
	v_cndmask_b32_e64 v93, 0, -v102, vcc
	v_exp_f32_e64 v102, -|v77|
	v_max_f32_e32 v77, 0, v77
	v_add_f32_e32 v101, v93, v101
	v_cvt_pkrtz_f16_f32 v242, v92, v93
	v_add_f32_e32 v102, 1.0, v102
	v_log_f32_e32 v102, v102
	s_nop 0
	v_add_f32_e32 v102, v77, v102
	v_cmp_lt_i32_e32 vcc, 18, v254
	v_fma_f32 v94, v94, s26, -v102
	v_cndmask_b32_e64 v77, 0, -v102, vcc
	v_cndmask_b32_e32 v232, v208, v94, vcc
	v_add_f32_e32 v94, v77, v101
	v_mul_f32_e32 v101, 0x3e0293ee, v78
	v_exp_f32_e64 v102, -|v101|
	v_max_f32_e32 v101, 0, v101
	v_add_f32_e32 v102, 1.0, v102
	v_log_f32_e32 v102, v102
	s_nop 0
	v_add_f32_e32 v101, v101, v102
	v_cmp_lt_i32_e32 vcc, 50, v254
	v_fma_f32 v78, v78, s26, -v101
	v_cndmask_b32_e64 v106, 0, -v101, vcc
	v_cndmask_b32_e32 v233, v208, v78, vcc
	v_add_f32_e32 v78, v106, v94
	v_mul_f32_e32 v94, 0x3e0293ee, v95
	v_exp_f32_e64 v101, -|v94|
	v_max_f32_e32 v94, 0, v94
	v_cvt_pkrtz_f16_f32 v102, v75, v76
	v_mov_b32_e32 v75, v66
	v_add_f32_e32 v101, 1.0, v101
	v_log_f32_e32 v101, v101
	v_mov_b32_e32 v76, v66
	v_add_f32_e32 v94, v94, v101
	v_cmp_lt_i32_e32 vcc, 19, v254
	v_cvt_pkrtz_f16_f32 v101, v73, v74
; __device__ __forceinline__ int crow(int r, int hi) { return (r & 3) + 8 * (r >> 2) + 4 * hi; }
; template <int MODE>
; __device__ __forceinline__ void attn_unit(const AttnArgs& A, int b, int qb, int qc, int kc, int vc, int oc, float slope2, int dmax, LAS char* lds) {
;     ...
;                 for (int r = 0; r < 16; ++r) {
;                     { const float zl = p0[r] * QK_C, u = __builtin_amdgcn_exp2f(-fabsf(zl)), L = __builtin_amdgcn_logf(1.f + u), sp = fmaxf(zl, 0.f) + L;
;                       const bool ok = !need_mask || (k0 + crow(r, hi) < tq); lk0[r] = ok ? -sp : 0.f; p0[r] = ok ? (zl - sp) : -INFINITY; lsum += lk0[r]; }
;                     { const float zl = p1[r] * QK_C, u = __builtin_amdgcn_exp2f(-fabsf(zl)), L = __builtin_amdgcn_logf(1.f + u), sp = fmaxf(zl, 0.f) + L;
;                       const bool ok = !need_mask || (k0 + 32 + crow(r, hi) < tq); lk1[r] = ok ? -sp : 0.f; p1[r] = ok ? (zl - sp) : -INFINITY; lsum += lk1[r]; }
;                 }
;                 f16x8 f0, f1, f2, f3; PK4H(lk0, 0, f0); PK4H(lk0, 8, f1); PK4H(lk1, 0, f2); PK4H(lk1, 8, f3);
;                 f32x16 w0, w1;
; #pragma unroll
;                 for (int r = 0; r < 16; ++r) { w0[r] = carry; w1[r] = carry; }
	v_cndmask_b32_e64 v103, 0, -v94, vcc
	v_fma_f32 v94, v95, s26, -v94
	v_cndmask_b32_e32 v234, v208, v94, vcc
	v_mul_f32_e32 v94, 0x3e0293ee, v79
	v_exp_f32_e64 v95, -|v94|
	v_max_f32_e32 v94, 0, v94
	v_add_f32_e32 v78, v103, v78
	v_cvt_pkrtz_f16_f32 v103, v77, v103
	v_add_f32_e32 v95, 1.0, v95
	v_log_f32_e32 v95, v95
	v_mov_b32_e32 v73, v66
	v_mov_b32_e32 v74, v66
	v_mov_b32_e32 v77, v66
	v_add_f32_e32 v94, v94, v95
	v_cmp_lt_i32_e32 vcc, 51, v254
	v_fma_f32 v79, v79, s26, -v94
	v_cndmask_b32_e32 v235, v208, v79, vcc
	v_mul_f32_e32 v79, 0x3e0293ee, v96
	v_cndmask_b32_e64 v95, 0, -v94, vcc
	v_exp_f32_e64 v94, -|v79|
	v_max_f32_e32 v79, 0, v79
	v_add_f32_e32 v78, v95, v78
	v_cvt_pkrtz_f16_f32 v243, v106, v95
	v_add_f32_e32 v94, 1.0, v94
	v_log_f32_e32 v94, v94
	s_nop 0
	v_add_f32_e32 v79, v79, v94
	v_cmp_lt_i32_e32 vcc, 24, v254
	s_nop 0
	v_cndmask_b32_e64 v94, 0, -v79, vcc
	v_fma_f32 v79, v96, s26, -v79
	v_cndmask_b32_e32 v236, v208, v79, vcc
	v_mul_f32_e32 v79, 0x3e0293ee, v80
	v_exp_f32_e64 v96, -|v79|
	v_max_f32_e32 v79, 0, v79
	v_add_f32_e32 v78, v94, v78
	v_add_f32_e32 v96, 1.0, v96
	v_log_f32_e32 v96, v96
	s_nop 0
	v_add_f32_e32 v79, v79, v96
	v_cmp_lt_i32_e32 vcc, 56, v254
	s_nop 0
	v_cndmask_b32_e64 v96, 0, -v79, vcc
	v_fma_f32 v79, v80, s26, -v79
	v_cndmask_b32_e32 v237, v208, v79, vcc
	v_mul_f32_e32 v79, 0x3e0293ee, v97
	v_exp_f32_e64 v80, -|v79|
	v_max_f32_e32 v79, 0, v79
	v_add_f32_e32 v78, v96, v78
	v_add_f32_e32 v80, 1.0, v80
	v_log_f32_e32 v80, v80
	s_nop 0
	v_add_f32_e32 v79, v79, v80
	v_cmp_lt_i32_e32 vcc, 25, v254
	s_nop 0
	v_cndmask_b32_e64 v80, 0, -v79, vcc
	v_fma_f32 v79, v97, s26, -v79
	v_cndmask_b32_e32 v246, v208, v79, vcc
	v_mul_f32_e32 v79, 0x3e0293ee, v81
	v_exp_f32_e64 v97, -|v79|
	v_max_f32_e32 v79, 0, v79
	v_add_f32_e32 v78, v80, v78
	v_cvt_pkrtz_f16_f32 v104, v94, v80
	v_add_f32_e32 v97, 1.0, v97
	v_log_f32_e32 v97, v97
	v_mov_b32_e32 v80, v66
	v_permlane32_swap_b32_e32 v102, v104
	v_add_f32_e32 v79, v79, v97
	v_cmp_lt_i32_e32 vcc, 57, v254
	s_nop 0
	v_cndmask_b32_e64 v97, 0, -v79, vcc
	v_fma_f32 v79, v81, s26, -v79
	v_cndmask_b32_e32 v247, v208, v79, vcc
	v_mul_f32_e32 v79, 0x3e0293ee, v98
	v_exp_f32_e64 v81, -|v79|
	v_max_f32_e32 v79, 0, v79
	v_add_f32_e32 v78, v97, v78
	v_cvt_pkrtz_f16_f32 v244, v96, v97
	v_add_f32_e32 v81, 1.0, v81
	v_log_f32_e32 v81, v81
	v_permlane32_swap_b32_e32 v242, v244
	v_add_f32_e32 v79, v79, v81
	v_cmp_lt_i32_e32 vcc, 26, v254
	s_nop 0
	v_cndmask_b32_e64 v81, 0, -v79, vcc
	v_fma_f32 v79, v98, s26, -v79
	v_cndmask_b32_e32 v248, v208, v79, vcc
	v_mul_f32_e32 v79, 0x3e0293ee, v82
	v_exp_f32_e64 v98, -|v79|
	v_max_f32_e32 v79, 0, v79
	v_add_f32_e32 v78, v81, v78
	v_add_f32_e32 v98, 1.0, v98
	v_log_f32_e32 v98, v98
	s_nop 0
	v_add_f32_e32 v79, v79, v98
	v_cmp_lt_i32_e32 vcc, 58, v254
	s_nop 0
	v_cndmask_b32_e64 v107, 0, -v79, vcc
	v_fma_f32 v79, v82, s26, -v79
	v_cndmask_b32_e32 v249, v208, v79, vcc
	v_mul_f32_e32 v79, 0x3e0293ee, v99
	v_exp_f32_e64 v82, -|v79|
	v_max_f32_e32 v79, 0, v79
	v_add_f32_e32 v78, v107, v78
	v_add_f32_e32 v82, 1.0, v82
	v_log_f32_e32 v82, v82
	s_nop 0
	v_add_f32_e32 v79, v79, v82
	v_cmp_lt_i32_e32 vcc, 27, v254
	v_cndmask_b32_e64 v82, 0, -v79, vcc
	v_fma_f32 v79, v99, s26, -v79
	v_cndmask_b32_e32 v250, v208, v79, vcc
	v_mul_f32_e32 v79, 0x3e0293ee, v83
	v_exp_f32_e64 v98, -|v79|
	v_max_f32_e32 v79, 0, v79
	v_cmp_lt_i32_e32 vcc, 59, v254
	v_add_f32_e32 v98, 1.0, v98
	v_log_f32_e32 v98, v98
	v_add_f32_e32 v78, v82, v78
	v_cvt_pkrtz_f16_f32 v99, v69, v70
	s_nop 1
	v_permlane32_swap_b32_e32 v99, v101
	v_add_f32_e32 v79, v79, v98
	v_cndmask_b32_e64 v67, 0, -v79, vcc
	v_fma_f32 v79, v83, s26, -v79
	v_cvt_pkrtz_f16_f32 v98, v100, v68
	v_cvt_pkrtz_f16_f32 v100, v71, v72
	v_cndmask_b32_e32 v251, v208, v79, vcc
	v_add_f32_e32 v252, v67, v78
	v_permlane32_swap_b32_e32 v98, v100
	v_cvt_pkrtz_f16_f32 v105, v81, v82
	v_cvt_pkrtz_f16_f32 v245, v107, v67
	v_mov_b32_e32 v67, v66
	v_mov_b32_e32 v68, v66
	v_mov_b32_e32 v69, v66
	v_mov_b32_e32 v70, v66
	v_mov_b32_e32 v71, v66
	v_mov_b32_e32 v72, v66
	v_mov_b32_e32 v78, v66
	v_mov_b32_e32 v79, v66
	v_mov_b32_e32 v81, v66
	v_permlane32_swap_b32_e32 v103, v105
	s_nop 0
; template <int MODE>
; __device__ __forceinline__ void attn_unit(const AttnArgs& A, int b, int qb, int qc, int kc, int vc, int oc, float slope2, int dmax, LAS char* lds) {
;     ...
;                 w0 = __builtin_amdgcn_mfma_f32_32x32x16_f16(tri0, f0, w0, 0, 0, 0); w0 = __builtin_amdgcn_mfma_f32_32x32x16_f16(tri1, f1, w0, 0, 0, 0);
;                 w0 = __builtin_amdgcn_mfma_f32_32x32x16_f16(ones, f2, w0, 0, 0, 0); w0 = __builtin_amdgcn_mfma_f32_32x32x16_f16(ones, f3, w0, 0, 0, 0);
;                 w1 = __builtin_amdgcn_mfma_f32_32x32x16_f16(tri0, f2, w1, 0, 0, 0); w1 = __builtin_amdgcn_mfma_f32_32x32x16_f16(tri1, f3, w1, 0, 0, 0);
; #pragma unroll
;                 for (int r = 0; r < 16; ++r) { p0[r] = __builtin_amdgcn_exp2f(p0[r] + w0[r]); p1[r] = __builtin_amdgcn_exp2f(p1[r] + w1[r]); }
;                 carry += xhalf_sum(lsum);
;                 wdone = __all(carry < -150.f);
;             } else {
;                 const bool need_mask = (k0 + 63 > r0);
;                 const float fb = (float)(k0 - tq + 4 * hi);
;                 float mx = -1e30f;
; #pragma unroll
;                 for (int r = 0; r < 16; ++r) { const float t0 = fb + (float)((r & 3) + 8 * (r >> 2)), t1 = t0 + 32.f;
;                     float z0 = fmaf(slope2, t0, p0[r] * QK_C), z1 = fmaf(slope2, t1, p1[r] * QK_C);
;                     if (need_mask) { if (t0 > 0.f) z0 = -INFINITY; if (t1 > 0.f) z1 = -INFINITY; }
;                     p0[r] = z0; p1[r] = z1; mx = fmaxf(mx, fmaxf(z0, z1)); }
;                 mx = xhalf_max(mx);
;                 const float mn = fmaxf(m_run, mx), alpha = __builtin_amdgcn_exp2f(m_run - mn); m_run = mn;
;                 float ps = 0.f;
; #pragma unroll
;                 for (int r = 0; r < 16; ++r) { p0[r] = __builtin_amdgcn_exp2f(p0[r] - mn); p1[r] = __builtin_amdgcn_exp2f(p1[r] - mn); ps += p0[r] + p1[r]; }
;                 l_run = l_run * alpha + xhalf_sum(ps);
;                 if (__any(alpha < 1.f)) { if (hi == 0) ws[r32] = alpha; asm volatile("s_waitcnt lgkmcnt(0)" ::: "memory");
; #pragma unroll
;                     for (int r = 0; r < 16; ++r) { const float a_ = ws[crow(r, hi)];
; #pragma unroll
;                         for (int d = 0; d < 4; ++d) o[d][r] *= a_; } }
;             }
;             PK4BF(p0, 0, pa0); PK4BF(p0, 8, pa1); PK4BF(p1, 0, pa2); PK4BF(p1, 8, pa3);
;             SBAR();
;             {
.Lsb_join:
	v_mfma_f32_32x32x16_f16 v[82:97], v[114:117], v[98:101], v[66:81]
	v_mov_b64_e32 v[100:101], s[22:23]
	v_mov_b64_e32 v[98:99], s[20:21]
	v_permlane32_swap_b32_e32 v243, v245
	v_mfma_f32_32x32x16_f16 v[82:97], v[118:121], v[102:105], v[82:97]
	v_mfma_f32_32x32x16_f16 v[82:97], v[98:101], v[238:241], v[82:97]
	v_mfma_f32_32x32x16_f16 v[82:97], v[98:101], v[242:245], v[82:97]
	v_mov_b64_e32 v[112:113], v[80:81]
	v_mov_b64_e32 v[110:111], v[78:79]
	v_mov_b64_e32 v[108:109], v[76:77]
	v_mov_b64_e32 v[106:107], v[74:75]
	v_mov_b64_e32 v[104:105], v[72:73]
	v_mov_b64_e32 v[102:103], v[70:71]
	v_mov_b64_e32 v[100:101], v[68:69]
	v_mov_b64_e32 v[98:99], v[66:67]
	s_nop 3
	v_add_f32_e32 v67, v211, v82
	v_add_f32_e32 v97, v250, v97
	v_mfma_f32_32x32x16_f16 v[98:113], v[114:117], v[238:241], v[98:113]
	v_exp_f32_e32 v67, v67
	v_exp_f32_e32 v97, v97
	v_mfma_f32_32x32x16_f16 v[98:113], v[118:121], v[242:245], v[98:113]
	s_nop 11
	v_add_f32_e32 v69, v214, v99
	v_mov_b32_e32 v99, v252
	s_nop 1
	v_permlane32_swap_b32_e32 v252, v99
	v_add_f32_e32 v99, v252, v99
	v_add_f32_e32 v68, v212, v98
	v_add_f32_e32 v70, v216, v100
	v_add_f32_e32 v71, v218, v101
	v_add_f32_e32 v72, v220, v102
	v_add_f32_e32 v73, v222, v103
	v_add_f32_e32 v74, v224, v104
	v_add_f32_e32 v75, v226, v105
	v_add_f32_e32 v66, v66, v99
	v_exp_f32_e32 v76, v68
	v_add_f32_e32 v68, v213, v83
	v_exp_f32_e32 v77, v69
	v_add_f32_e32 v69, v215, v84
	v_exp_f32_e32 v78, v70
	v_add_f32_e32 v70, v217, v85
	v_exp_f32_e32 v79, v71
	v_add_f32_e32 v71, v219, v86
	v_exp_f32_e32 v80, v72
	v_add_f32_e32 v72, v221, v87
	v_exp_f32_e32 v81, v73
	v_add_f32_e32 v73, v223, v88
	v_exp_f32_e32 v82, v74
	v_add_f32_e32 v74, v225, v89
	v_exp_f32_e32 v83, v75
	v_add_f32_e32 v75, v227, v90
	v_cmp_gt_f32_e32 vcc, s27, v66
	v_exp_f32_e32 v68, v68
	v_exp_f32_e32 v69, v69
	v_exp_f32_e32 v70, v70
	v_exp_f32_e32 v71, v71
	v_exp_f32_e32 v72, v72
	v_exp_f32_e32 v73, v73
	v_exp_f32_e32 v74, v74
	v_exp_f32_e32 v75, v75
	v_add_f32_e32 v84, v228, v106
	v_add_f32_e32 v85, v229, v91
	v_add_f32_e32 v86, v231, v107
	v_add_f32_e32 v87, v232, v92
	v_add_f32_e32 v88, v233, v108
	v_add_f32_e32 v89, v234, v93
	v_add_f32_e32 v90, v235, v109
	v_add_f32_e32 v91, v236, v94
	v_add_f32_e32 v92, v237, v110
	v_add_f32_e32 v93, v246, v95
	v_add_f32_e32 v94, v247, v111
	v_add_f32_e32 v95, v248, v96
	v_add_f32_e32 v96, v249, v112
	v_add_f32_e32 v98, v251, v113
	s_cmp_eq_u64 vcc, exec
	v_exp_f32_e32 v84, v84
	v_exp_f32_e32 v85, v85
	v_exp_f32_e32 v86, v86
	v_exp_f32_e32 v87, v87
	v_exp_f32_e32 v88, v88
	v_exp_f32_e32 v89, v89
	v_exp_f32_e32 v90, v90
	v_exp_f32_e32 v91, v91
	v_exp_f32_e32 v92, v92
	v_exp_f32_e32 v93, v93
	v_exp_f32_e32 v94, v94
	v_exp_f32_e32 v95, v95
	v_exp_f32_e32 v96, v96
	v_exp_f32_e32 v98, v98
	s_cselect_b64 s[14:15], -1, 0
	v_cvt_pk_bf16_f32 v68, v67, v68
	v_cvt_pk_bf16_f32 v69, v69, v70
	v_cvt_pk_bf16_f32 v70, v71, v72
	v_cvt_pk_bf16_f32 v71, v73, v74
	v_cvt_pk_bf16_f32 v72, v75, v85
	v_cvt_pk_bf16_f32 v73, v87, v89
	v_cvt_pk_bf16_f32 v74, v91, v93
	v_cvt_pk_bf16_f32 v75, v95, v97
	v_cvt_pk_bf16_f32 v76, v76, v77
	v_cvt_pk_bf16_f32 v77, v78, v79
	v_cvt_pk_bf16_f32 v78, v80, v81
	v_cvt_pk_bf16_f32 v79, v82, v83
	v_cvt_pk_bf16_f32 v80, v84, v86
	v_cvt_pk_bf16_f32 v81, v88, v90
	v_cvt_pk_bf16_f32 v82, v92, v94
	v_cvt_pk_bf16_f32 v83, v96, v98
	v_add_u32_e32 v100, s16, v200
	v_permlane32_swap_b32_e32 v68, v70
	v_permlane32_swap_b32_e32 v69, v71
	v_permlane32_swap_b32_e32 v72, v74
	v_permlane32_swap_b32_e32 v73, v75
	v_permlane32_swap_b32_e32 v76, v78
	v_permlane32_swap_b32_e32 v77, v79
	v_permlane32_swap_b32_e32 v80, v82
	v_permlane32_swap_b32_e32 v81, v83
	ds_read_b64_tr_b16 v[84:85], v100 offset:0
	ds_read_b64_tr_b16 v[86:87], v100 offset:0x800
	ds_read_b64_tr_b16 v[88:89], v100 offset:0x1000
	ds_read_b64_tr_b16 v[90:91], v100 offset:0x1800
	ds_read_b64_tr_b16 v[92:93], v100 offset:0x200
	ds_read_b64_tr_b16 v[94:95], v100 offset:0xa00
	ds_read_b64_tr_b16 v[96:97], v100 offset:0x1200
	ds_read_b64_tr_b16 v[98:99], v100 offset:0x1a00
	s_waitcnt lgkmcnt(4)
	s_nop 0
	v_mfma_f32_32x32x16_bf16 v[2:17], v[68:71], v[84:87], v[2:17]
	v_mfma_f32_32x32x16_bf16 v[2:17], v[72:75], v[88:91], v[2:17]
	ds_read_b64_tr_b16 v[84:85], v100 offset:0x400
	ds_read_b64_tr_b16 v[86:87], v100 offset:0xc00
	ds_read_b64_tr_b16 v[88:89], v100 offset:0x1400
	ds_read_b64_tr_b16 v[90:91], v100 offset:0x1c00
	s_waitcnt lgkmcnt(4)
	v_mfma_f32_32x32x16_bf16 v[18:33], v[68:71], v[92:95], v[18:33]
	v_mfma_f32_32x32x16_bf16 v[18:33], v[72:75], v[96:99], v[18:33]
	ds_read_b64_tr_b16 v[92:93], v100 offset:0x600
	ds_read_b64_tr_b16 v[94:95], v100 offset:0xe00
	ds_read_b64_tr_b16 v[96:97], v100 offset:0x1600
	ds_read_b64_tr_b16 v[98:99], v100 offset:0x1e00
	s_waitcnt lgkmcnt(4)
	v_mfma_f32_32x32x16_bf16 v[34:49], v[68:71], v[84:87], v[34:49]
	v_mfma_f32_32x32x16_bf16 v[34:49], v[72:75], v[88:91], v[34:49]
	ds_read_b64_tr_b16 v[84:85], v100 offset:0x2000
	ds_read_b64_tr_b16 v[86:87], v100 offset:0x2800
	ds_read_b64_tr_b16 v[88:89], v100 offset:0x3000
	ds_read_b64_tr_b16 v[90:91], v100 offset:0x3800
	s_waitcnt lgkmcnt(4)
	v_mfma_f32_32x32x16_bf16 v[50:65], v[68:71], v[92:95], v[50:65]
	v_mfma_f32_32x32x16_bf16 v[50:65], v[72:75], v[96:99], v[50:65]
	ds_read_b64_tr_b16 v[68:69], v100 offset:0x2200
	ds_read_b64_tr_b16 v[70:71], v100 offset:0x2a00
	ds_read_b64_tr_b16 v[72:73], v100 offset:0x3200
	ds_read_b64_tr_b16 v[74:75], v100 offset:0x3a00
	s_waitcnt lgkmcnt(4)
	v_mfma_f32_32x32x16_bf16 v[2:17], v[76:79], v[84:87], v[2:17]
	v_mfma_f32_32x32x16_bf16 v[2:17], v[80:83], v[88:91], v[2:17]
	ds_read_b64_tr_b16 v[84:85], v100 offset:0x2400
	ds_read_b64_tr_b16 v[86:87], v100 offset:0x2c00
	ds_read_b64_tr_b16 v[88:89], v100 offset:0x3400
	ds_read_b64_tr_b16 v[90:91], v100 offset:0x3c00
	s_waitcnt lgkmcnt(4)
	v_mfma_f32_32x32x16_bf16 v[18:33], v[76:79], v[68:71], v[18:33]
	v_mfma_f32_32x32x16_bf16 v[18:33], v[80:83], v[72:75], v[18:33]
	ds_read_b64_tr_b16 v[68:69], v100 offset:0x2600
	ds_read_b64_tr_b16 v[70:71], v100 offset:0x2e00
	ds_read_b64_tr_b16 v[72:73], v100 offset:0x3600
	ds_read_b64_tr_b16 v[74:75], v100 offset:0x3e00
	s_waitcnt lgkmcnt(4)
	v_mfma_f32_32x32x16_bf16 v[34:49], v[76:79], v[84:87], v[34:49]
	v_mfma_f32_32x32x16_bf16 v[34:49], v[80:83], v[88:91], v[34:49]
	s_waitcnt lgkmcnt(0)
	v_mfma_f32_32x32x16_bf16 v[50:65], v[76:79], v[68:71], v[50:65]
	v_mfma_f32_32x32x16_bf16 v[50:65], v[80:83], v[72:75], v[50:65]

; __device__ __forceinline__ int crow(int r, int hi) { return (r & 3) + 8 * (r >> 2) + 4 * hi; }
; template <int MODE>
; __device__ __forceinline__ void attn_unit(const AttnArgs& A, int b, int qb, int qc, int kc, int vc, int oc, float slope2, int dmax, LAS char* lds) {
;     ...
;                 for (int r = 0; r < 16; ++r) {
;                     { const float zl = p0[r] * QK_C, u = __builtin_amdgcn_exp2f(-fabsf(zl)), L = __builtin_amdgcn_logf(1.f + u), sp = fmaxf(zl, 0.f) + L;
;                       const bool ok = !need_mask || (k0 + crow(r, hi) < tq); lk0[r] = ok ? -sp : 0.f; p0[r] = ok ? (zl - sp) : -INFINITY; lsum += lk0[r]; }
;                     { const float zl = p1[r] * QK_C, u = __builtin_amdgcn_exp2f(-fabsf(zl)), L = __builtin_amdgcn_logf(1.f + u), sp = fmaxf(zl, 0.f) + L;
;                       const bool ok = !need_mask || (k0 + 32 + crow(r, hi) < tq); lk1[r] = ok ? -sp : 0.f; p1[r] = ok ? (zl - sp) : -INFINITY; lsum += lk1[r]; }
;                 }
;                 f16x8 f0, f1, f2, f3; PK4H(lk0, 0, f0); PK4H(lk0, 8, f1); PK4H(lk1, 0, f2); PK4H(lk1, 8, f3);
.Lsb_unmasked:
	v_mul_f32_e32 v100, 0x3e0293ee, v84
	v_exp_f32_e64 v102, -|v100|
	v_max_f32_e32 v100, 0, v100
	v_add_f32_e32 v102, 1.0, v102
	v_log_f32_e32 v102, v102
	s_nop 0
	v_add_f32_e64 v100, -v100, -v102
	v_fma_f32 v211, v84, s26, v100
	v_mul_f32_e32 v84, 0x3e0293ee, v68
	v_exp_f32_e64 v103, -|v84|
	v_max_f32_e32 v84, 0, v84
	v_add_f32_e32 v103, 1.0, v103
	v_log_f32_e32 v103, v103
	v_add_f32_e32 v102, 0, v100
	v_add_f32_e64 v84, -v84, -v103
	v_fma_f32 v212, v68, s26, v84
	v_mul_f32_e32 v68, 0x3e0293ee, v85
	v_add_f32_e32 v101, v102, v84
	v_exp_f32_e64 v102, -|v68|
	v_max_f32_e32 v68, 0, v68
	v_add_f32_e32 v102, 1.0, v102
	v_log_f32_e32 v102, v102
	s_nop 0
	v_add_f32_e64 v68, -v68, -v102
	v_fma_f32 v213, v85, s26, v68
	v_mul_f32_e32 v85, 0x3e0293ee, v69
	v_exp_f32_e64 v102, -|v85|
	v_max_f32_e32 v85, 0, v85
	v_add_f32_e32 v101, v68, v101
	v_add_f32_e32 v102, 1.0, v102
	v_log_f32_e32 v102, v102
	s_nop 0
	v_add_f32_e64 v85, -v85, -v102
	v_fma_f32 v214, v69, s26, v85
	v_mul_f32_e32 v69, 0x3e0293ee, v86
	v_exp_f32_e64 v102, -|v69|
	v_max_f32_e32 v69, 0, v69
	v_add_f32_e32 v101, v85, v101
	v_cvt_pkrtz_f16_f32 v238, v84, v85
	v_add_f32_e32 v102, 1.0, v102
	v_log_f32_e32 v102, v102
	s_nop 0
	v_add_f32_e64 v69, -v69, -v102
	v_fma_f32 v215, v86, s26, v69
	v_mul_f32_e32 v86, 0x3e0293ee, v70
	v_exp_f32_e64 v102, -|v86|
	v_max_f32_e32 v86, 0, v86
	v_add_f32_e32 v101, v69, v101
	v_add_f32_e32 v102, 1.0, v102
	v_log_f32_e32 v102, v102
	s_nop 0
	v_add_f32_e64 v86, -v86, -v102
	v_fma_f32 v216, v70, s26, v86
	v_mul_f32_e32 v70, 0x3e0293ee, v87
	v_exp_f32_e64 v102, -|v70|
	v_max_f32_e32 v70, 0, v70
	v_add_f32_e32 v101, v86, v101
	v_add_f32_e32 v102, 1.0, v102
	v_log_f32_e32 v102, v102
	s_nop 0
	v_add_f32_e64 v70, -v70, -v102
	v_fma_f32 v217, v87, s26, v70
	v_mul_f32_e32 v87, 0x3e0293ee, v71
	v_exp_f32_e64 v102, -|v87|
	v_max_f32_e32 v87, 0, v87
	v_add_f32_e32 v101, v70, v101
	v_add_f32_e32 v102, 1.0, v102
	v_log_f32_e32 v102, v102
	s_nop 0
	v_add_f32_e64 v87, -v87, -v102
	v_fma_f32 v218, v71, s26, v87
	v_mul_f32_e32 v71, 0x3e0293ee, v88
	v_exp_f32_e64 v102, -|v71|
	v_max_f32_e32 v71, 0, v71
	v_add_f32_e32 v101, v87, v101
	v_cvt_pkrtz_f16_f32 v239, v86, v87
	v_add_f32_e32 v102, 1.0, v102
	v_log_f32_e32 v102, v102
	s_nop 0
	v_add_f32_e64 v71, -v71, -v102
	v_fma_f32 v219, v88, s26, v71
	v_mul_f32_e32 v88, 0x3e0293ee, v72
	v_exp_f32_e64 v102, -|v88|
	v_max_f32_e32 v88, 0, v88
	v_add_f32_e32 v101, v71, v101
	v_add_f32_e32 v102, 1.0, v102
	v_log_f32_e32 v102, v102
	s_nop 0
	v_add_f32_e64 v88, -v88, -v102
	v_fma_f32 v220, v72, s26, v88
	v_mul_f32_e32 v72, 0x3e0293ee, v89
	v_exp_f32_e64 v102, -|v72|
	v_max_f32_e32 v72, 0, v72
	v_add_f32_e32 v101, v88, v101
	v_add_f32_e32 v102, 1.0, v102
	v_log_f32_e32 v102, v102
	s_nop 0
	v_add_f32_e64 v72, -v72, -v102
	v_fma_f32 v221, v89, s26, v72
	v_mul_f32_e32 v89, 0x3e0293ee, v73
	v_exp_f32_e64 v102, -|v89|
	v_max_f32_e32 v89, 0, v89
	v_add_f32_e32 v101, v72, v101
	v_add_f32_e32 v102, 1.0, v102
	v_log_f32_e32 v102, v102
	s_nop 0
	v_add_f32_e64 v89, -v89, -v102
	v_fma_f32 v222, v73, s26, v89
	v_mul_f32_e32 v73, 0x3e0293ee, v90
	v_exp_f32_e64 v102, -|v73|
	v_max_f32_e32 v73, 0, v73
	v_add_f32_e32 v101, v89, v101
	v_cvt_pkrtz_f16_f32 v240, v88, v89
	v_add_f32_e32 v102, 1.0, v102
	v_log_f32_e32 v102, v102
	v_permlane32_swap_b32_e32 v238, v240
	v_add_f32_e64 v73, -v73, -v102
	v_fma_f32 v223, v90, s26, v73
	v_mul_f32_e32 v90, 0x3e0293ee, v74
	v_exp_f32_e64 v102, -|v90|
	v_max_f32_e32 v90, 0, v90
	v_add_f32_e32 v101, v73, v101
	v_add_f32_e32 v102, 1.0, v102
	v_log_f32_e32 v102, v102
	s_nop 0
	v_add_f32_e64 v90, -v90, -v102
	v_fma_f32 v224, v74, s26, v90
	v_mul_f32_e32 v74, 0x3e0293ee, v91
	v_exp_f32_e64 v102, -|v74|
	v_max_f32_e32 v74, 0, v74
	v_add_f32_e32 v101, v90, v101
	v_add_f32_e32 v102, 1.0, v102
	v_log_f32_e32 v102, v102
	s_nop 0
	v_add_f32_e64 v74, -v74, -v102
	v_fma_f32 v225, v91, s26, v74
	v_mul_f32_e32 v91, 0x3e0293ee, v75
	v_exp_f32_e64 v102, -|v91|
	v_max_f32_e32 v91, 0, v91
	v_add_f32_e32 v101, v74, v101
	v_add_f32_e32 v102, 1.0, v102
	v_log_f32_e32 v102, v102
	s_nop 0
	v_add_f32_e64 v91, -v91, -v102
	v_fma_f32 v226, v75, s26, v91
	v_mul_f32_e32 v75, 0x3e0293ee, v92
	v_exp_f32_e64 v102, -|v75|
	v_max_f32_e32 v75, 0, v75
	v_add_f32_e32 v101, v91, v101
	v_cvt_pkrtz_f16_f32 v241, v90, v91
	v_add_f32_e32 v102, 1.0, v102
	v_log_f32_e32 v102, v102
	v_permlane32_swap_b32_e32 v239, v241
	v_add_f32_e64 v75, -v75, -v102
	v_fma_f32 v227, v92, s26, v75
	v_mul_f32_e32 v92, 0x3e0293ee, v76
	v_exp_f32_e64 v102, -|v92|
	v_max_f32_e32 v92, 0, v92
	v_add_f32_e32 v101, v75, v101
	v_add_f32_e32 v102, 1.0, v102
	v_log_f32_e32 v102, v102
	s_nop 0
	v_add_f32_e64 v92, -v92, -v102
	v_fma_f32 v228, v76, s26, v92
	v_mul_f32_e32 v76, 0x3e0293ee, v93
	v_exp_f32_e64 v102, -|v76|
	v_max_f32_e32 v76, 0, v76
	v_add_f32_e32 v101, v92, v101
	v_add_f32_e32 v102, 1.0, v102
	v_log_f32_e32 v102, v102
	s_nop 0
	v_add_f32_e64 v76, -v76, -v102
	v_fma_f32 v229, v93, s26, v76
	v_mul_f32_e32 v93, 0x3e0293ee, v77
	v_exp_f32_e64 v102, -|v93|
	v_max_f32_e32 v93, 0, v93
	v_add_f32_e32 v101, v76, v101
	v_add_f32_e32 v102, 1.0, v102
	v_log_f32_e32 v102, v102
	s_nop 0
	v_add_f32_e64 v93, -v93, -v102
	v_fma_f32 v231, v77, s26, v93
	v_mul_f32_e32 v77, 0x3e0293ee, v94
	v_exp_f32_e64 v102, -|v77|
	v_max_f32_e32 v77, 0, v77
; __device__ __forceinline__ int crow(int r, int hi) { return (r & 3) + 8 * (r >> 2) + 4 * hi; }
; template <int MODE>
; __device__ __forceinline__ void attn_unit(const AttnArgs& A, int b, int qb, int qc, int kc, int vc, int oc, float slope2, int dmax, LAS char* lds) {
;     ...
;                 for (int r = 0; r < 16; ++r) {
;                     { const float zl = p0[r] * QK_C, u = __builtin_amdgcn_exp2f(-fabsf(zl)), L = __builtin_amdgcn_logf(1.f + u), sp = fmaxf(zl, 0.f) + L;
;                       const bool ok = !need_mask || (k0 + crow(r, hi) < tq); lk0[r] = ok ? -sp : 0.f; p0[r] = ok ? (zl - sp) : -INFINITY; lsum += lk0[r]; }
;                     { const float zl = p1[r] * QK_C, u = __builtin_amdgcn_exp2f(-fabsf(zl)), L = __builtin_amdgcn_logf(1.f + u), sp = fmaxf(zl, 0.f) + L;
;                       const bool ok = !need_mask || (k0 + 32 + crow(r, hi) < tq); lk1[r] = ok ? -sp : 0.f; p1[r] = ok ? (zl - sp) : -INFINITY; lsum += lk1[r]; }
;                 }
;                 f16x8 f0, f1, f2, f3; PK4H(lk0, 0, f0); PK4H(lk0, 8, f1); PK4H(lk1, 0, f2); PK4H(lk1, 8, f3);
;                 f32x16 w0, w1;
; #pragma unroll
;                 for (int r = 0; r < 16; ++r) { w0[r] = carry; w1[r] = carry; }
	v_add_f32_e32 v101, v93, v101
	v_cvt_pkrtz_f16_f32 v242, v92, v93
	v_add_f32_e32 v102, 1.0, v102
	v_log_f32_e32 v102, v102
	s_nop 0
	v_add_f32_e64 v77, -v77, -v102
	v_fma_f32 v232, v94, s26, v77
	v_add_f32_e32 v94, v77, v101
	v_mul_f32_e32 v101, 0x3e0293ee, v78
	v_exp_f32_e64 v102, -|v101|
	v_max_f32_e32 v101, 0, v101
	v_add_f32_e32 v102, 1.0, v102
	v_log_f32_e32 v102, v102
	s_nop 0
	v_add_f32_e64 v106, -v101, -v102
	v_fma_f32 v233, v78, s26, v106
	v_add_f32_e32 v78, v106, v94
	v_mul_f32_e32 v94, 0x3e0293ee, v95
	v_exp_f32_e64 v101, -|v94|
	v_max_f32_e32 v94, 0, v94
	v_cvt_pkrtz_f16_f32 v102, v75, v76
	v_mov_b32_e32 v75, v66
	v_add_f32_e32 v101, 1.0, v101
	v_log_f32_e32 v101, v101
	v_mov_b32_e32 v76, v66
	v_add_f32_e64 v103, -v94, -v101
	v_cvt_pkrtz_f16_f32 v101, v73, v74
	v_fma_f32 v234, v95, s26, v103
	v_mul_f32_e32 v94, 0x3e0293ee, v79
	v_exp_f32_e64 v95, -|v94|
	v_max_f32_e32 v94, 0, v94
	v_add_f32_e32 v78, v103, v78
	v_cvt_pkrtz_f16_f32 v103, v77, v103
	v_add_f32_e32 v95, 1.0, v95
	v_log_f32_e32 v95, v95
	v_mov_b32_e32 v73, v66
	v_mov_b32_e32 v74, v66
	v_mov_b32_e32 v77, v66
	v_add_f32_e64 v95, -v94, -v95
	v_fma_f32 v235, v79, s26, v95
	v_mul_f32_e32 v79, 0x3e0293ee, v96
	v_exp_f32_e64 v94, -|v79|
	v_max_f32_e32 v79, 0, v79
	v_add_f32_e32 v78, v95, v78
	v_cvt_pkrtz_f16_f32 v243, v106, v95
	v_add_f32_e32 v94, 1.0, v94
	v_log_f32_e32 v94, v94
	s_nop 0
	v_add_f32_e64 v94, -v79, -v94
	s_nop 0
	v_fma_f32 v236, v96, s26, v94
	v_mul_f32_e32 v79, 0x3e0293ee, v80
	v_exp_f32_e64 v96, -|v79|
	v_max_f32_e32 v79, 0, v79
	v_add_f32_e32 v78, v94, v78
	v_add_f32_e32 v96, 1.0, v96
	v_log_f32_e32 v96, v96
	s_nop 0
	v_add_f32_e64 v96, -v79, -v96
	s_nop 0
	v_fma_f32 v237, v80, s26, v96
	v_mul_f32_e32 v79, 0x3e0293ee, v97
	v_exp_f32_e64 v80, -|v79|
	v_max_f32_e32 v79, 0, v79
	v_add_f32_e32 v78, v96, v78
	v_add_f32_e32 v80, 1.0, v80
	v_log_f32_e32 v80, v80
	s_nop 0
	v_add_f32_e64 v80, -v79, -v80
	s_nop 0
	v_fma_f32 v246, v97, s26, v80
	v_mul_f32_e32 v79, 0x3e0293ee, v81
	v_exp_f32_e64 v97, -|v79|
	v_max_f32_e32 v79, 0, v79
	v_add_f32_e32 v78, v80, v78
	v_cvt_pkrtz_f16_f32 v104, v94, v80
	v_add_f32_e32 v97, 1.0, v97
	v_log_f32_e32 v97, v97
	v_mov_b32_e32 v80, v66
	v_permlane32_swap_b32_e32 v102, v104
	v_add_f32_e64 v97, -v79, -v97
	s_nop 0
	v_fma_f32 v247, v81, s26, v97
	v_mul_f32_e32 v79, 0x3e0293ee, v98
	v_exp_f32_e64 v81, -|v79|
	v_max_f32_e32 v79, 0, v79
	v_add_f32_e32 v78, v97, v78
	v_cvt_pkrtz_f16_f32 v244, v96, v97
	v_add_f32_e32 v81, 1.0, v81
	v_log_f32_e32 v81, v81
	v_permlane32_swap_b32_e32 v242, v244
	v_add_f32_e64 v81, -v79, -v81
	s_nop 0
	v_fma_f32 v248, v98, s26, v81
	v_mul_f32_e32 v79, 0x3e0293ee, v82
	v_exp_f32_e64 v98, -|v79|
	v_max_f32_e32 v79, 0, v79
	v_add_f32_e32 v78, v81, v78
	v_add_f32_e32 v98, 1.0, v98
	v_log_f32_e32 v98, v98
	s_nop 0
	v_add_f32_e64 v107, -v79, -v98
	s_nop 0
	v_fma_f32 v249, v82, s26, v107
	v_mul_f32_e32 v79, 0x3e0293ee, v99
	v_exp_f32_e64 v82, -|v79|
	v_max_f32_e32 v79, 0, v79
	v_add_f32_e32 v78, v107, v78
	v_add_f32_e32 v82, 1.0, v82
	v_log_f32_e32 v82, v82
	s_nop 0
	v_add_f32_e64 v82, -v79, -v82
	v_fma_f32 v250, v99, s26, v82
	v_mul_f32_e32 v79, 0x3e0293ee, v83
	v_exp_f32_e64 v98, -|v79|
	v_max_f32_e32 v79, 0, v79
	v_add_f32_e32 v98, 1.0, v98
	v_log_f32_e32 v98, v98
	v_add_f32_e32 v78, v82, v78
	v_cvt_pkrtz_f16_f32 v99, v69, v70
	s_nop 1
	v_permlane32_swap_b32_e32 v99, v101
	v_add_f32_e64 v67, -v79, -v98
	v_fma_f32 v251, v83, s26, v67
	v_cvt_pkrtz_f16_f32 v98, v100, v68
	v_cvt_pkrtz_f16_f32 v100, v71, v72
	v_add_f32_e32 v252, v67, v78
	s_nop 0
	v_permlane32_swap_b32_e32 v98, v100
	v_cvt_pkrtz_f16_f32 v105, v81, v82
	v_cvt_pkrtz_f16_f32 v245, v107, v67
	v_mov_b32_e32 v67, v66
	v_mov_b32_e32 v68, v66
	v_mov_b32_e32 v69, v66
	v_mov_b32_e32 v70, v66
	v_mov_b32_e32 v71, v66
	v_mov_b32_e32 v72, v66
	v_mov_b32_e32 v78, v66
	v_mov_b32_e32 v79, v66
	v_mov_b32_e32 v81, v66
	v_permlane32_swap_b32_e32 v103, v105
	s_nop 0
	s_branch .Lsb_join
.LBB0_378:
	s_and_saveexec_b64 s[2:3], s[96:97]
	s_cbranch_execz .LBB0_381
	s_mov_b64 s[4:5], exec
	v_mbcnt_lo_u32_b32 v1, s4, 0
	v_mbcnt_hi_u32_b32 v1, s5, v1
	v_cmp_eq_u32_e32 vcc, 0, v1
	s_and_b64 s[6:7], exec, vcc
	s_mov_b64 exec, s[6:7]
	s_cbranch_execz .LBB0_381
	s_bcnt1_i32_b64 s4, s[4:5]
	v_mov_b32_e32 v1, 0x1000
	v_mov_b32_e32 v2, s4
.LBB0_381:
	s_or_b64 exec, exec, s[2:3]
	v_readlane_b32 s8, v255, 4
	v_readlane_b32 s9, v255, 5
	s_cmp_lt_i32 s9, 6
	v_readlane_b32 s10, v255, 6
	v_readlane_b32 s11, v255, 7
	s_cbranch_scc1 .LBB0_431
	s_waitcnt vmcnt(0)
	s_waitcnt vmcnt(0)
	s_barrier
	s_and_saveexec_b64 s[2:3], s[96:97]
	s_cbranch_execz .LBB0_430
	v_readlane_b32 s4, v255, 10
	s_waitcnt vmcnt(0) expcnt(0) lgkmcnt(0)
	s_nop 0
	v_mov_b32_e32 v1, s4
	ds_read_b32 v3, v1
	ds_read_b32 v1, v1 offset:4
	s_waitcnt lgkmcnt(1)
	v_cmp_ne_u32_e32 vcc, 0, v3
	s_cbranch_vccnz .LBB0_398
	v_readlane_b32 s4, v255, 0
	v_readlane_b32 s5, v255, 1
	s_load_dwordx2 s[8:9], s[4:5], 0x4
	v_readlane_b32 s10, v255, 8
	v_readlane_b32 s11, v255, 9
	s_add_u32 s4, s10, 0x1000
	s_addc_u32 s5, s11, 0
	s_add_u32 s6, s10, 0x1100
	s_addc_u32 s7, s11, 0
	s_waitcnt lgkmcnt(0)
	s_mul_i32 s20, s8, s93
	s_add_u32 s8, s10, 0x1200
	s_mul_i32 s20, s20, s9
	s_addc_u32 s9, s11, 0
	s_add_u32 s10, s10, 0x1300
	s_addc_u32 s11, s11, 0
	s_mov_b32 s21, 1
	v_mov_b32_e32 v17, 0
	s_branch .LBB0_386

; __device__ __forceinline__ void xcd_barrier(const XcdBarrier& b) {
;     asm volatile("s_waitcnt vmcnt(0)" ::: "memory");
;     __syncthreads();
;     if (threadIdx.x == 0) {
;         unsigned* bar = b.bar;
;         __builtin_amdgcn_s_waitcnt(0);
;         unsigned nloc = b.st[0], nx = b.st[1];
;         if (nloc == 0u) { xcd_barrier_complete(bar, b.x, nloc, nx); b.st[0] = nloc; b.st[1] = nx; }
.LBB0_471:
	s_mov_b64 s[4:5], exec
	v_mbcnt_lo_u32_b32 v1, s4, 0
	v_mbcnt_hi_u32_b32 v1, s5, v1
	v_cmp_eq_u32_e32 vcc, 0, v1
	s_and_b64 s[6:7], exec, vcc
	s_mov_b64 exec, s[6:7]
	s_cbranch_execz .LBB0_473
	s_bcnt1_i32_b64 s4, s[4:5]
	v_mov_b32_e32 v1, 0x1000
	v_mov_b32_e32 v2, s4
.LBB0_473:
	s_or_b64 exec, exec, s[2:3]
	v_readlane_b32 s8, v255, 4
	v_readlane_b32 s9, v255, 5
	s_cmp_lt_i32 s9, 8
	v_readlane_b32 s10, v255, 6
	v_readlane_b32 s11, v255, 7
	s_cbranch_scc1 .LBB0_523
	s_waitcnt vmcnt(0)
	s_waitcnt vmcnt(0)
	s_barrier
	s_and_saveexec_b64 s[2:3], s[96:97]
	s_cbranch_execz .LBB0_522
	v_readlane_b32 s4, v255, 10
	s_waitcnt vmcnt(0) expcnt(0) lgkmcnt(0)
	s_nop 0
	v_mov_b32_e32 v1, s4
	ds_read_b32 v3, v1
	ds_read_b32 v1, v1 offset:4
	s_waitcnt lgkmcnt(1)
	v_cmp_ne_u32_e32 vcc, 0, v3
	s_cbranch_vccnz .LBB0_490
	v_readlane_b32 s4, v255, 0
	v_readlane_b32 s5, v255, 1
	s_load_dwordx2 s[8:9], s[4:5], 0x4
	v_readlane_b32 s10, v255, 8
	v_readlane_b32 s11, v255, 9
	s_add_u32 s4, s10, 0x1000
	s_addc_u32 s5, s11, 0
	s_add_u32 s6, s10, 0x1100
	s_addc_u32 s7, s11, 0
	s_waitcnt lgkmcnt(0)
	s_mul_i32 s18, s8, s93
	s_add_u32 s8, s10, 0x1200
	s_mul_i32 s18, s18, s9
	s_addc_u32 s9, s11, 0
	s_add_u32 s10, s10, 0x1300
	s_addc_u32 s11, s11, 0
	s_mov_b32 s19, 1
	v_mov_b32_e32 v17, 0
	s_branch .LBB0_478

; #define LAS __attribute__((address_space(3)))
; __device__ __forceinline__ void phase_nrr(const Frame& F, const Args& a, int l, const bf16_t* XA, const float* g, const float* modl, unsigned char* XN8) {
;     ...
;         __syncthreads();
; #pragma unroll
;         for (int rb = 0; rb < 4; ++rb) *(LAS f32x4*)(Pl + (size_t)((kq * 64 + 16 * rb + fr) * NE + 16 * eb + 4 * fq)) = acc[rb];
;         __syncthreads();
;         const float bias = rbias[lane];
; #pragma unroll
;         for (int i = 0; i < 8; ++i) { const int t = tb + i;
;             const float lg = Pl[(w * 8 + i) * NE + lane] + Pl[(64 + w * 8 + i) * NE + lane]; const float sc = 1.f / (1.f + __expf(-lg)); const float bb = sc + bias;
;             float m1 = bb; m1 = fmaxf(m1, __shfl_xor(m1, 1)); m1 = fmaxf(m1, __shfl_xor(m1, 2)); m1 = fmaxf(m1, __shfl_xor(m1, 4));
;             const unsigned long long eq = __ballot(bb == m1); const int gbase = lane & ~7; const unsigned grpmask = (unsigned)((eq >> gbase) & 0xffull);
;             const int first = gbase + __builtin_ctz(grpmask);
;             float m2 = (lane == first) ? -INFINITY : bb; m2 = fmaxf(m2, __shfl_xor(m2, 1)); m2 = fmaxf(m2, __shfl_xor(m2, 2)); m2 = fmaxf(m2, __shfl_xor(m2, 4));
;             const float gsum = m1 + m2; const int gq = lane >> 3;
;             int grank = 0;
; #pragma unroll
;             for (int g2 = 0; g2 < 8; ++g2) { const float v = __int_as_float(__builtin_amdgcn_readlane(__float_as_int(gsum), g2 * 8)); grank += (v > gsum || (v == gsum && g2 < gq)) ? 1 : 0; }
;             const bool keep = grank < 4; const float val = keep ? bb : -INFINITY;
;             int rank = 0;
; #pragma unroll 8
;             for (int e2 = 0; e2 < 64; ++e2) { const float v = __int_as_float(__builtin_amdgcn_readlane(__float_as_int(val), e2)); rank += (v > val || (v == val && e2 < lane)) ? 1 : 0; }
.LBB0_535:
	s_barrier
	ds_write_b128 v242, v[110:113]
	ds_write_b128 v242, v[118:121] offset:4096
	s_nop 0
	ds_write_b128 v242, v[126:129] offset:8192
	s_nop 1
	ds_write_b128 v242, v[130:133] offset:12288
	s_waitcnt lgkmcnt(0)
	s_barrier
	global_load_dword v3, v[198:199], off
	s_waitcnt vmcnt(15)
	v_add_u32_e32 v4, s76, v226
	ds_read2st64_b32 v[6:7], v4 offset1:64
	s_mov_b32 s3, 0
	s_waitcnt lgkmcnt(0)
	v_add_f32_e32 v2, v6, v7
	v_mul_f32_e32 v2, 0xbfb8aa3b, v2
	v_exp_f32_e32 v2, v2
	s_nop 0
	v_add_f32_e32 v2, 1.0, v2
	v_div_scale_f32 v5, s[22:23], v2, v2, 1.0
	v_rcp_f32_e32 v6, v5
	s_nop 0
	v_fma_f32 v7, -v5, v6, 1.0
	v_fmac_f32_e32 v6, v7, v6
	v_div_scale_f32 v7, vcc, 1.0, v2, 1.0
	v_mul_f32_e32 v8, v7, v6
	v_fma_f32 v9, -v5, v8, v7
	v_fmac_f32_e32 v8, v9, v6
	v_fma_f32 v5, -v5, v8, v7
	v_div_fmas_f32 v5, v5, v6, v8
	v_div_fixup_f32 v2, v5, v2, 1.0
	s_waitcnt vmcnt(0)
	v_add_f32_e32 v5, v3, v2
	s_nop 1
	s_waitcnt lgkmcnt(0)
	v_max_f32_dpp v6, v5, v5 quad_perm:[1,0,3,2] row_mask:0xf bank_mask:0xf
	s_nop 1
	s_waitcnt lgkmcnt(0)
	v_max_f32_dpp v6, v6, v6 quad_perm:[2,3,0,1] row_mask:0xf bank_mask:0xf
	s_nop 1
	s_waitcnt lgkmcnt(0)
	v_max_f32_dpp v8, v6, v6 row_half_mirror row_mask:0xf bank_mask:0xf
	v_cmp_eq_f32_e32 vcc, v5, v8
	s_nop 1
	v_lshrrev_b64 v[6:7], v200, vcc
	v_ffbl_b32_sdwa v6, v6 dst_sel:DWORD dst_unused:UNUSED_PAD src0_sel:BYTE_0
	v_add_u32_e32 v6, v6, v200
	v_cmp_ne_u32_e32 vcc, v230, v6
	s_nop 1
	v_cndmask_b32_e32 v6, v245, v5, vcc
	s_nop 1
	s_waitcnt lgkmcnt(0)
	v_max_f32_dpp v6, v6, v6 quad_perm:[1,0,3,2] row_mask:0xf bank_mask:0xf
	s_nop 1
	s_waitcnt lgkmcnt(0)
	v_max_f32_dpp v6, v6, v6 quad_perm:[2,3,0,1] row_mask:0xf bank_mask:0xf
	s_nop 1
	s_waitcnt lgkmcnt(0)
	v_max_f32_dpp v6, v6, v6 row_half_mirror row_mask:0xf bank_mask:0xf
	v_add_f32_e32 v6, v8, v6
	s_nop 0
	v_readlane_b32 s5, v6, 0
	s_nop 1
	v_cmp_eq_f32_e64 s[22:23], s5, v6
	v_cmp_gt_f32_e32 vcc, s5, v6
	s_and_b64 s[22:23], s[6:7], s[22:23]
	s_or_b64 s[22:23], vcc, s[22:23]
	v_readlane_b32 s5, v6, 8
	v_cndmask_b32_e64 v7, 0, 1, s[22:23]
	s_nop 0
	v_cmp_eq_f32_e64 s[22:23], s5, v6
	v_cmp_gt_f32_e32 vcc, s5, v6
	s_and_b64 s[22:23], s[8:9], s[22:23]
	s_or_b64 s[22:23], vcc, s[22:23]
	v_readlane_b32 s5, v6, 16
	v_cndmask_b32_e64 v8, 0, 1, s[22:23]
	s_nop 0
	v_cmp_eq_f32_e64 s[22:23], s5, v6
	v_cmp_gt_f32_e32 vcc, s5, v6
	s_and_b64 s[22:23], s[10:11], s[22:23]
	s_or_b64 s[22:23], vcc, s[22:23]
	v_readlane_b32 s5, v6, 24
	v_cndmask_b32_e64 v9, 0, 1, s[22:23]
	s_nop 0
	v_cmp_eq_f32_e64 s[22:23], s5, v6
	v_cmp_gt_f32_e32 vcc, s5, v6
	s_and_b64 s[22:23], s[12:13], s[22:23]
	s_or_b64 s[22:23], vcc, s[22:23]
	v_readlane_b32 s5, v6, 32
	v_cndmask_b32_e64 v10, 0, 1, s[22:23]
	s_nop 0
	v_cmp_eq_f32_e64 s[22:23], s5, v6
	v_cmp_gt_f32_e32 vcc, s5, v6
	s_and_b64 s[22:23], s[14:15], s[22:23]
	s_or_b64 s[22:23], vcc, s[22:23]
	v_readlane_b32 s5, v6, 40
	v_cndmask_b32_e64 v11, 0, 1, s[22:23]
	s_nop 0
	v_cmp_eq_f32_e64 s[22:23], s5, v6
	v_cmp_gt_f32_e32 vcc, s5, v6
	s_and_b64 s[22:23], s[16:17], s[22:23]
	s_or_b64 s[22:23], vcc, s[22:23]
	v_readlane_b32 s5, v6, 48
	v_cndmask_b32_e64 v12, 0, 1, s[22:23]
	s_nop 0
	v_cmp_eq_f32_e64 s[22:23], s5, v6
	v_cmp_gt_f32_e32 vcc, s5, v6
	s_and_b64 s[22:23], s[18:19], s[22:23]
	v_readlane_b32 s5, v6, 56
	s_or_b64 s[22:23], vcc, s[22:23]
	v_cndmask_b32_e64 v13, 0, 1, s[22:23]
	v_cmp_gt_f32_e32 vcc, s5, v6
	s_nop 1
	v_cndmask_b32_e64 v6, 0, 1, vcc
	v_add_u32_e32 v6, v8, v6
	v_add3_u32 v6, v6, v7, v9
	v_add3_u32 v6, v6, v10, v11
	v_add3_u32 v6, v6, v12, v13
	v_cmp_gt_u32_e32 vcc, 4, v6
	v_mov_b32_e32 v6, 0
	s_nop 0
	v_cndmask_b32_e32 v5, v245, v5, vcc
	v_ashrrev_i32_e32 v9, 31, v5
	v_sub_u32_e32 v8, 63, v230
	v_and_b32_e32 v9, 0x7fffffff, v9
	v_xor_b32_e32 v9, v5, v9
	s_nop 0
	v_readlane_b32 s25, v9, 0
	s_movk_i32 s24, 63
	v_readlane_b32 s23, v9, 1
	s_movk_i32 s22, 62
	v_cmp_gt_i64_e32 vcc, s[24:25], v[8:9]
	v_readlane_b32 s25, v9, 2
	s_movk_i32 s24, 61
	v_addc_co_u32_e32 v6, vcc, 0, v6, vcc
	v_cmp_gt_i64_e32 vcc, s[22:23], v[8:9]
	v_readlane_b32 s23, v9, 3
	s_movk_i32 s22, 60
	v_addc_co_u32_e32 v6, vcc, 0, v6, vcc
	v_cmp_gt_i64_e32 vcc, s[24:25], v[8:9]
	v_readlane_b32 s25, v9, 4
	s_movk_i32 s24, 59
	v_addc_co_u32_e32 v6, vcc, 0, v6, vcc
	v_cmp_gt_i64_e32 vcc, s[22:23], v[8:9]
	v_readlane_b32 s23, v9, 5
	s_movk_i32 s22, 58
	v_addc_co_u32_e32 v6, vcc, 0, v6, vcc
	v_cmp_gt_i64_e32 vcc, s[24:25], v[8:9]
	v_readlane_b32 s25, v9, 6
	s_movk_i32 s24, 57
	v_addc_co_u32_e32 v6, vcc, 0, v6, vcc
	v_cmp_gt_i64_e32 vcc, s[22:23], v[8:9]
	v_readlane_b32 s23, v9, 7
	s_movk_i32 s22, 56
	v_addc_co_u32_e32 v6, vcc, 0, v6, vcc
	v_cmp_gt_i64_e32 vcc, s[24:25], v[8:9]
	v_readlane_b32 s25, v9, 8
	s_movk_i32 s24, 55
	v_addc_co_u32_e32 v6, vcc, 0, v6, vcc
	v_cmp_gt_i64_e32 vcc, s[22:23], v[8:9]
	v_readlane_b32 s23, v9, 9
	s_movk_i32 s22, 54
	v_addc_co_u32_e32 v6, vcc, 0, v6, vcc
	v_cmp_gt_i64_e32 vcc, s[24:25], v[8:9]
	v_readlane_b32 s25, v9, 10
	s_movk_i32 s24, 53
	v_addc_co_u32_e32 v6, vcc, 0, v6, vcc
	v_cmp_gt_i64_e32 vcc, s[22:23], v[8:9]
	v_readlane_b32 s23, v9, 11
	s_movk_i32 s22, 52
	v_addc_co_u32_e32 v6, vcc, 0, v6, vcc
	v_cmp_gt_i64_e32 vcc, s[24:25], v[8:9]
	v_readlane_b32 s25, v9, 12
	s_movk_i32 s24, 51
	v_addc_co_u32_e32 v6, vcc, 0, v6, vcc
	v_cmp_gt_i64_e32 vcc, s[22:23], v[8:9]
	v_readlane_b32 s23, v9, 13
	s_movk_i32 s22, 50
	v_addc_co_u32_e32 v6, vcc, 0, v6, vcc
	v_cmp_gt_i64_e32 vcc, s[24:25], v[8:9]
	v_readlane_b32 s25, v9, 14
	s_movk_i32 s24, 49
	v_addc_co_u32_e32 v6, vcc, 0, v6, vcc
	v_cmp_gt_i64_e32 vcc, s[22:23], v[8:9]
	v_readlane_b32 s23, v9, 15
	s_movk_i32 s22, 48
	v_addc_co_u32_e32 v6, vcc, 0, v6, vcc
	v_cmp_gt_i64_e32 vcc, s[24:25], v[8:9]
; __device__ __forceinline__ float wave_sum(float v) {
; #pragma unroll
;     for (int o = 1; o < 64; o <<= 1) v += __shfl_xor(v, o);
;     return v;
; __device__ __forceinline__ void phase_nrr(const Frame& F, const Args& a, int l, const bf16_t* XA, const float* g, const float* modl, unsigned char* XN8) {
;     ...
;             int rank = 0;
; #pragma unroll 8
;             for (int e2 = 0; e2 < 64; ++e2) { const float v = __int_as_float(__builtin_amdgcn_readlane(__float_as_int(val), e2)); rank += (v > val || (v == val && e2 < lane)) ? 1 : 0; }
;             const bool sel = rank < TOPK;
;             const float ssum = wave_sum(sel ? sc : 0.f);
;             if (sel) { const int p = atomicAdd((int*)(hist + lane), 1); top_e[t * TOPK + rank] = lane; gate[t * TOPK + rank] = sc / ssum * 2.5f; lpos[t * TOPK + rank] = p; }
	v_readlane_b32 s25, v9, 16
	s_movk_i32 s24, 47
	v_addc_co_u32_e32 v6, vcc, 0, v6, vcc
	v_cmp_gt_i64_e32 vcc, s[22:23], v[8:9]
	v_readlane_b32 s23, v9, 17
	s_movk_i32 s22, 46
	v_addc_co_u32_e32 v6, vcc, 0, v6, vcc
	v_cmp_gt_i64_e32 vcc, s[24:25], v[8:9]
	v_readlane_b32 s25, v9, 18
	s_movk_i32 s24, 45
	v_addc_co_u32_e32 v6, vcc, 0, v6, vcc
	v_cmp_gt_i64_e32 vcc, s[22:23], v[8:9]
	v_readlane_b32 s23, v9, 19
	s_movk_i32 s22, 44
	v_addc_co_u32_e32 v6, vcc, 0, v6, vcc
	v_cmp_gt_i64_e32 vcc, s[24:25], v[8:9]
	v_readlane_b32 s25, v9, 20
	s_movk_i32 s24, 43
	v_addc_co_u32_e32 v6, vcc, 0, v6, vcc
	v_cmp_gt_i64_e32 vcc, s[22:23], v[8:9]
	v_readlane_b32 s23, v9, 21
	s_movk_i32 s22, 42
	v_addc_co_u32_e32 v6, vcc, 0, v6, vcc
	v_cmp_gt_i64_e32 vcc, s[24:25], v[8:9]
	v_readlane_b32 s25, v9, 22
	s_movk_i32 s24, 41
	v_addc_co_u32_e32 v6, vcc, 0, v6, vcc
	v_cmp_gt_i64_e32 vcc, s[22:23], v[8:9]
	v_readlane_b32 s23, v9, 23
	s_movk_i32 s22, 40
	v_addc_co_u32_e32 v6, vcc, 0, v6, vcc
	v_cmp_gt_i64_e32 vcc, s[24:25], v[8:9]
	v_readlane_b32 s25, v9, 24
	s_movk_i32 s24, 39
	v_addc_co_u32_e32 v6, vcc, 0, v6, vcc
	v_cmp_gt_i64_e32 vcc, s[22:23], v[8:9]
	v_readlane_b32 s23, v9, 25
	s_movk_i32 s22, 38
	v_addc_co_u32_e32 v6, vcc, 0, v6, vcc
	v_cmp_gt_i64_e32 vcc, s[24:25], v[8:9]
	v_readlane_b32 s25, v9, 26
	s_movk_i32 s24, 37
	v_addc_co_u32_e32 v6, vcc, 0, v6, vcc
	v_cmp_gt_i64_e32 vcc, s[22:23], v[8:9]
	v_readlane_b32 s23, v9, 27
	s_movk_i32 s22, 36
	v_addc_co_u32_e32 v6, vcc, 0, v6, vcc
	v_cmp_gt_i64_e32 vcc, s[24:25], v[8:9]
	v_readlane_b32 s25, v9, 28
	s_movk_i32 s24, 35
	v_addc_co_u32_e32 v6, vcc, 0, v6, vcc
	v_cmp_gt_i64_e32 vcc, s[22:23], v[8:9]
	v_readlane_b32 s23, v9, 29
	s_movk_i32 s22, 34
	v_addc_co_u32_e32 v6, vcc, 0, v6, vcc
	v_cmp_gt_i64_e32 vcc, s[24:25], v[8:9]
	v_readlane_b32 s25, v9, 30
	s_movk_i32 s24, 33
	v_addc_co_u32_e32 v6, vcc, 0, v6, vcc
	v_cmp_gt_i64_e32 vcc, s[22:23], v[8:9]
	v_readlane_b32 s23, v9, 31
	s_movk_i32 s22, 32
	v_addc_co_u32_e32 v6, vcc, 0, v6, vcc
	v_cmp_gt_i64_e32 vcc, s[24:25], v[8:9]
	v_readlane_b32 s25, v9, 32
	s_movk_i32 s24, 31
	v_addc_co_u32_e32 v6, vcc, 0, v6, vcc
	v_cmp_gt_i64_e32 vcc, s[22:23], v[8:9]
	v_readlane_b32 s23, v9, 33
	s_movk_i32 s22, 30
	v_addc_co_u32_e32 v6, vcc, 0, v6, vcc
	v_cmp_gt_i64_e32 vcc, s[24:25], v[8:9]
	v_readlane_b32 s25, v9, 34
	s_movk_i32 s24, 29
	v_addc_co_u32_e32 v6, vcc, 0, v6, vcc
	v_cmp_gt_i64_e32 vcc, s[22:23], v[8:9]
	v_readlane_b32 s23, v9, 35
	s_movk_i32 s22, 28
	v_addc_co_u32_e32 v6, vcc, 0, v6, vcc
	v_cmp_gt_i64_e32 vcc, s[24:25], v[8:9]
	v_readlane_b32 s25, v9, 36
	s_movk_i32 s24, 27
	v_addc_co_u32_e32 v6, vcc, 0, v6, vcc
	v_cmp_gt_i64_e32 vcc, s[22:23], v[8:9]
	v_readlane_b32 s23, v9, 37
	s_movk_i32 s22, 26
	v_addc_co_u32_e32 v6, vcc, 0, v6, vcc
	v_cmp_gt_i64_e32 vcc, s[24:25], v[8:9]
	v_readlane_b32 s25, v9, 38
	s_movk_i32 s24, 25
	v_addc_co_u32_e32 v6, vcc, 0, v6, vcc
	v_cmp_gt_i64_e32 vcc, s[22:23], v[8:9]
	v_readlane_b32 s23, v9, 39
	s_movk_i32 s22, 24
	v_addc_co_u32_e32 v6, vcc, 0, v6, vcc
	v_cmp_gt_i64_e32 vcc, s[24:25], v[8:9]
	v_readlane_b32 s25, v9, 40
	s_movk_i32 s24, 23
	v_addc_co_u32_e32 v6, vcc, 0, v6, vcc
	v_cmp_gt_i64_e32 vcc, s[22:23], v[8:9]
	v_readlane_b32 s23, v9, 41
	s_movk_i32 s22, 22
	v_addc_co_u32_e32 v6, vcc, 0, v6, vcc
	v_cmp_gt_i64_e32 vcc, s[24:25], v[8:9]
	v_readlane_b32 s25, v9, 42
	s_movk_i32 s24, 21
	v_addc_co_u32_e32 v6, vcc, 0, v6, vcc
	v_cmp_gt_i64_e32 vcc, s[22:23], v[8:9]
	v_readlane_b32 s23, v9, 43
	s_movk_i32 s22, 20
	v_addc_co_u32_e32 v6, vcc, 0, v6, vcc
	v_cmp_gt_i64_e32 vcc, s[24:25], v[8:9]
	v_readlane_b32 s25, v9, 44
	s_movk_i32 s24, 19
	v_addc_co_u32_e32 v6, vcc, 0, v6, vcc
	v_cmp_gt_i64_e32 vcc, s[22:23], v[8:9]
	v_readlane_b32 s23, v9, 45
	s_movk_i32 s22, 18
	v_addc_co_u32_e32 v6, vcc, 0, v6, vcc
	v_cmp_gt_i64_e32 vcc, s[24:25], v[8:9]
	v_readlane_b32 s25, v9, 46
	s_movk_i32 s24, 17
	v_addc_co_u32_e32 v6, vcc, 0, v6, vcc
	v_cmp_gt_i64_e32 vcc, s[22:23], v[8:9]
	v_readlane_b32 s23, v9, 47
	s_movk_i32 s22, 16
	v_addc_co_u32_e32 v6, vcc, 0, v6, vcc
	v_cmp_gt_i64_e32 vcc, s[24:25], v[8:9]
	v_readlane_b32 s25, v9, 48
	s_movk_i32 s24, 15
	v_addc_co_u32_e32 v6, vcc, 0, v6, vcc
	v_cmp_gt_i64_e32 vcc, s[22:23], v[8:9]
	v_readlane_b32 s23, v9, 49
	s_movk_i32 s22, 14
	v_addc_co_u32_e32 v6, vcc, 0, v6, vcc
	v_cmp_gt_i64_e32 vcc, s[24:25], v[8:9]
	v_readlane_b32 s25, v9, 50
	s_movk_i32 s24, 13
	v_addc_co_u32_e32 v6, vcc, 0, v6, vcc
	v_cmp_gt_i64_e32 vcc, s[22:23], v[8:9]
	v_readlane_b32 s23, v9, 51
	s_movk_i32 s22, 12
	v_addc_co_u32_e32 v6, vcc, 0, v6, vcc
	v_cmp_gt_i64_e32 vcc, s[24:25], v[8:9]
	v_readlane_b32 s25, v9, 52
	s_movk_i32 s24, 11
	v_addc_co_u32_e32 v6, vcc, 0, v6, vcc
	v_cmp_gt_i64_e32 vcc, s[22:23], v[8:9]
	v_readlane_b32 s23, v9, 53
	s_movk_i32 s22, 10
	v_addc_co_u32_e32 v6, vcc, 0, v6, vcc
	v_cmp_gt_i64_e32 vcc, s[24:25], v[8:9]
	v_readlane_b32 s25, v9, 54
	s_movk_i32 s24, 9
	v_addc_co_u32_e32 v6, vcc, 0, v6, vcc
	v_cmp_gt_i64_e32 vcc, s[22:23], v[8:9]
	v_readlane_b32 s23, v9, 55
	s_movk_i32 s22, 8
	v_addc_co_u32_e32 v6, vcc, 0, v6, vcc
	v_cmp_gt_i64_e32 vcc, s[24:25], v[8:9]
	v_readlane_b32 s25, v9, 56
	s_movk_i32 s24, 7
	v_addc_co_u32_e32 v6, vcc, 0, v6, vcc
	v_cmp_gt_i64_e32 vcc, s[22:23], v[8:9]
	v_readlane_b32 s23, v9, 57
	s_movk_i32 s22, 6
	v_addc_co_u32_e32 v6, vcc, 0, v6, vcc
	v_cmp_gt_i64_e32 vcc, s[24:25], v[8:9]
	v_readlane_b32 s25, v9, 58
	s_movk_i32 s24, 5
	v_addc_co_u32_e32 v6, vcc, 0, v6, vcc
	v_cmp_gt_i64_e32 vcc, s[22:23], v[8:9]
	v_readlane_b32 s23, v9, 59
	s_movk_i32 s22, 4
	v_addc_co_u32_e32 v6, vcc, 0, v6, vcc
	v_cmp_gt_i64_e32 vcc, s[24:25], v[8:9]
	v_readlane_b32 s25, v9, 60
	s_movk_i32 s24, 3
	v_addc_co_u32_e32 v6, vcc, 0, v6, vcc
	v_cmp_gt_i64_e32 vcc, s[22:23], v[8:9]
	v_readlane_b32 s23, v9, 61
	s_movk_i32 s22, 2
	v_addc_co_u32_e32 v6, vcc, 0, v6, vcc
	v_cmp_gt_i64_e32 vcc, s[24:25], v[8:9]
	v_readlane_b32 s25, v9, 62
	s_movk_i32 s24, 1
	v_addc_co_u32_e32 v6, vcc, 0, v6, vcc
	v_cmp_gt_i64_e32 vcc, s[22:23], v[8:9]
	v_readlane_b32 s23, v9, 63
	s_movk_i32 s22, 0
	v_addc_co_u32_e32 v6, vcc, 0, v6, vcc
	v_cmp_gt_i64_e32 vcc, s[24:25], v[8:9]
	s_nop 1
	v_addc_co_u32_e32 v6, vcc, 0, v6, vcc
	v_cmp_gt_i64_e32 vcc, s[22:23], v[8:9]
	s_nop 1
	v_addc_co_u32_e32 v6, vcc, 0, v6, vcc
	v_cmp_gt_u32_e32 vcc, 6, v6
	s_mul_i32 s36, s44, 6
	s_nop 0
	v_cndmask_b32_e32 v5, 0, v2, vcc
	s_nop 1
	v_add_f32_dpp v5, v5, v5 quad_perm:[1,0,3,2] row_mask:0xf bank_mask:0xf
	s_nop 1
	v_add_f32_dpp v5, v5, v5 quad_perm:[2,3,0,1] row_mask:0xf bank_mask:0xf
	s_nop 1
	v_add_f32_dpp v5, v5, v5 row_half_mirror row_mask:0xf bank_mask:0xf
	s_nop 1
	v_add_f32_dpp v5, v5, v5 row_mirror row_mask:0xf bank_mask:0xf
	s_nop 0
	ds_bpermute_b32 v7, v222, v5
	s_waitcnt lgkmcnt(0)
	v_add_f32_e32 v5, v5, v7
	v_mov_b32_e32 v7, v5
	s_nop 1
	v_permlane32_swap_b32_e32 v7, v5
	s_and_saveexec_b64 s[22:23], vcc
	s_cbranch_execz .LBB0_539
; __device__ __forceinline__ void phase_nrr(const Frame& F, const Args& a, int l, const bf16_t* XA, const float* g, const float* modl, unsigned char* XN8) {
;     ...
;         for (int i = 0; i < 8; ++i) { const int t = tb + i;
;             const float lg = Pl[(w * 8 + i) * NE + lane] + Pl[(64 + w * 8 + i) * NE + lane]; const float sc = 1.f / (1.f + __expf(-lg)); const float bb = sc + bias;
;             float m1 = bb; m1 = fmaxf(m1, __shfl_xor(m1, 1)); m1 = fmaxf(m1, __shfl_xor(m1, 2)); m1 = fmaxf(m1, __shfl_xor(m1, 4));
;             const unsigned long long eq = __ballot(bb == m1); const int gbase = lane & ~7; const unsigned grpmask = (unsigned)((eq >> gbase) & 0xffull);
;             const int first = gbase + __builtin_ctz(grpmask);
;             float m2 = (lane == first) ? -INFINITY : bb; m2 = fmaxf(m2, __shfl_xor(m2, 1)); m2 = fmaxf(m2, __shfl_xor(m2, 2)); m2 = fmaxf(m2, __shfl_xor(m2, 4));
;             const float gsum = m1 + m2; const int gq = lane >> 3;
;             int grank = 0;
; #pragma unroll
;             for (int g2 = 0; g2 < 8; ++g2) { const float v = __int_as_float(__builtin_amdgcn_readlane(__float_as_int(gsum), g2 * 8)); grank += (v > gsum || (v == gsum && g2 < gq)) ? 1 : 0; }
;             const bool keep = grank < 4; const float val = keep ? bb : -INFINITY;
;             int rank = 0;
; #pragma unroll 8
;             for (int e2 = 0; e2 < 64; ++e2) { const float v = __int_as_float(__builtin_amdgcn_readlane(__float_as_int(val), e2)); rank += (v > val || (v == val && e2 < lane)) ? 1 : 0; }
;             const bool sel = rank < TOPK;
;             const float ssum = wave_sum(sel ? sc : 0.f);
;             if (sel) { const int p = atomicAdd((int*)(hist + lane), 1); top_e[t * TOPK + rank] = lane; gate[t * TOPK + rank] = sc / ssum * 2.5f; lpos[t * TOPK + rank] = p; }
	s_waitcnt lgkmcnt(0)
	v_add_f32_e32 v5, v5, v7
	v_div_scale_f32 v11, s[24:25], v5, v5, v2
	v_or_b32_e32 v6, s36, v6
	v_rcp_f32_e32 v12, v11
	v_ashrrev_i32_e32 v7, 31, v6
	v_lshlrev_b64 v[6:7], 2, v[6:7]
	v_lshl_add_u64 v[8:9], s[26:27], 0, v[6:7]
	ds_add_rtn_u32 v10, v227, v243
	global_store_dword v[8:9], v230, off
	v_fma_f32 v8, -v11, v12, 1.0
	v_fmac_f32_e32 v12, v8, v12
	v_div_scale_f32 v8, vcc, v2, v5, v2
	v_mul_f32_e32 v9, v8, v12
	v_fma_f32 v13, -v11, v9, v8
	v_fmac_f32_e32 v9, v13, v12
	v_fma_f32 v8, -v11, v9, v8
	v_div_fmas_f32 v8, v8, v12, v9
	v_div_fixup_f32 v2, v8, v5, v2
	v_mul_f32_e32 v2, 0x40200000, v2
	v_lshl_add_u64 v[8:9], s[28:29], 0, v[6:7]
	v_lshl_add_u64 v[6:7], s[30:31], 0, v[6:7]
	global_store_dword v[8:9], v2, off
	s_waitcnt lgkmcnt(0)
	global_store_dword v[6:7], v10, off
.LBB0_539:
	s_or_b64 exec, exec, s[22:23]
	v_add_u32_e32 v2, s77, v226
	ds_read_b32 v2, v2
	ds_read_b32 v5, v4 offset:16640
	s_mov_b32 s3, 0
	s_waitcnt lgkmcnt(0)
	v_add_f32_e32 v2, v2, v5
	v_mul_f32_e32 v2, 0xbfb8aa3b, v2
	v_exp_f32_e32 v2, v2
	s_nop 0
	v_add_f32_e32 v2, 1.0, v2
	v_div_scale_f32 v5, s[22:23], v2, v2, 1.0
	v_rcp_f32_e32 v6, v5
	s_nop 0
	v_fma_f32 v7, -v5, v6, 1.0
	v_fmac_f32_e32 v6, v7, v6
	v_div_scale_f32 v7, vcc, 1.0, v2, 1.0
	v_mul_f32_e32 v8, v7, v6
	v_fma_f32 v9, -v5, v8, v7
	v_fmac_f32_e32 v8, v9, v6
	v_fma_f32 v5, -v5, v8, v7
	v_div_fmas_f32 v5, v5, v6, v8
	v_div_fixup_f32 v5, v5, v2, 1.0
	v_add_f32_e32 v2, v3, v5
	s_nop 1
	s_waitcnt lgkmcnt(0)
	v_max_f32_dpp v6, v2, v2 quad_perm:[1,0,3,2] row_mask:0xf bank_mask:0xf
	s_nop 1
	s_waitcnt lgkmcnt(0)
	v_max_f32_dpp v6, v6, v6 quad_perm:[2,3,0,1] row_mask:0xf bank_mask:0xf
	s_nop 1
	s_waitcnt lgkmcnt(0)
	v_max_f32_dpp v8, v6, v6 row_half_mirror row_mask:0xf bank_mask:0xf
	v_cmp_eq_f32_e32 vcc, v2, v8
	s_nop 1
	v_lshrrev_b64 v[6:7], v200, vcc
	v_ffbl_b32_sdwa v6, v6 dst_sel:DWORD dst_unused:UNUSED_PAD src0_sel:BYTE_0
	v_add_u32_e32 v6, v6, v200
	v_cmp_ne_u32_e32 vcc, v230, v6
	s_nop 1
	v_cndmask_b32_e32 v6, v245, v2, vcc
	s_nop 1
	s_waitcnt lgkmcnt(0)
	v_max_f32_dpp v6, v6, v6 quad_perm:[1,0,3,2] row_mask:0xf bank_mask:0xf
	s_nop 1
	s_waitcnt lgkmcnt(0)
	v_max_f32_dpp v6, v6, v6 quad_perm:[2,3,0,1] row_mask:0xf bank_mask:0xf
	s_nop 1
	s_waitcnt lgkmcnt(0)
	v_max_f32_dpp v6, v6, v6 row_half_mirror row_mask:0xf bank_mask:0xf
	v_add_f32_e32 v6, v8, v6
	s_nop 0
	v_readlane_b32 s5, v6, 0
	s_nop 1
	v_cmp_eq_f32_e64 s[22:23], s5, v6
	v_cmp_gt_f32_e32 vcc, s5, v6
	s_and_b64 s[22:23], s[6:7], s[22:23]
	s_or_b64 s[22:23], vcc, s[22:23]
	v_readlane_b32 s5, v6, 8
	v_cndmask_b32_e64 v7, 0, 1, s[22:23]
	s_nop 0
	v_cmp_eq_f32_e64 s[22:23], s5, v6
	v_cmp_gt_f32_e32 vcc, s5, v6
	s_and_b64 s[22:23], s[8:9], s[22:23]
	s_or_b64 s[22:23], vcc, s[22:23]
	v_readlane_b32 s5, v6, 16
	v_cndmask_b32_e64 v8, 0, 1, s[22:23]
	s_nop 0
	v_cmp_eq_f32_e64 s[22:23], s5, v6
	v_cmp_gt_f32_e32 vcc, s5, v6
	s_and_b64 s[22:23], s[10:11], s[22:23]
	s_or_b64 s[22:23], vcc, s[22:23]
	v_readlane_b32 s5, v6, 24
	v_cndmask_b32_e64 v9, 0, 1, s[22:23]
	s_nop 0
	v_cmp_eq_f32_e64 s[22:23], s5, v6
	v_cmp_gt_f32_e32 vcc, s5, v6
	s_and_b64 s[22:23], s[12:13], s[22:23]
	s_or_b64 s[22:23], vcc, s[22:23]
	v_readlane_b32 s5, v6, 32
	v_cndmask_b32_e64 v10, 0, 1, s[22:23]
	s_nop 0
	v_cmp_eq_f32_e64 s[22:23], s5, v6
	v_cmp_gt_f32_e32 vcc, s5, v6
	s_and_b64 s[22:23], s[14:15], s[22:23]
	s_or_b64 s[22:23], vcc, s[22:23]
	v_readlane_b32 s5, v6, 40
	v_cndmask_b32_e64 v11, 0, 1, s[22:23]
	s_nop 0
	v_cmp_eq_f32_e64 s[22:23], s5, v6
	v_cmp_gt_f32_e32 vcc, s5, v6
	s_and_b64 s[22:23], s[16:17], s[22:23]
	s_or_b64 s[22:23], vcc, s[22:23]
	v_readlane_b32 s5, v6, 48
	v_cndmask_b32_e64 v12, 0, 1, s[22:23]
	s_nop 0
	v_cmp_eq_f32_e64 s[22:23], s5, v6
	v_cmp_gt_f32_e32 vcc, s5, v6
	s_and_b64 s[22:23], s[18:19], s[22:23]
	v_readlane_b32 s5, v6, 56
	s_or_b64 s[22:23], vcc, s[22:23]
	v_cndmask_b32_e64 v13, 0, 1, s[22:23]
	v_cmp_gt_f32_e32 vcc, s5, v6
	s_nop 1
	v_cndmask_b32_e64 v6, 0, 1, vcc
	v_add_u32_e32 v6, v8, v6
	v_add3_u32 v6, v6, v7, v9
	v_add3_u32 v6, v6, v10, v11
	v_add3_u32 v6, v6, v12, v13
	v_cmp_gt_u32_e32 vcc, 4, v6
	s_nop 1
	v_cndmask_b32_e32 v6, v245, v2, vcc
	v_mov_b32_e32 v2, 0
	v_ashrrev_i32_e32 v9, 31, v6
	v_sub_u32_e32 v8, 63, v230
	v_and_b32_e32 v9, 0x7fffffff, v9
	v_xor_b32_e32 v9, v6, v9
	s_nop 0
	v_readlane_b32 s25, v9, 0
	s_movk_i32 s24, 63
	v_readlane_b32 s23, v9, 1
	s_movk_i32 s22, 62
	v_cmp_gt_i64_e32 vcc, s[24:25], v[8:9]
	v_readlane_b32 s25, v9, 2
	s_movk_i32 s24, 61
	v_addc_co_u32_e32 v2, vcc, 0, v2, vcc
	v_cmp_gt_i64_e32 vcc, s[22:23], v[8:9]
	v_readlane_b32 s23, v9, 3
	s_movk_i32 s22, 60
	v_addc_co_u32_e32 v2, vcc, 0, v2, vcc
	v_cmp_gt_i64_e32 vcc, s[24:25], v[8:9]
	v_readlane_b32 s25, v9, 4
	s_movk_i32 s24, 59
	v_addc_co_u32_e32 v2, vcc, 0, v2, vcc
	v_cmp_gt_i64_e32 vcc, s[22:23], v[8:9]
	v_readlane_b32 s23, v9, 5
	s_movk_i32 s22, 58
	v_addc_co_u32_e32 v2, vcc, 0, v2, vcc
	v_cmp_gt_i64_e32 vcc, s[24:25], v[8:9]
	v_readlane_b32 s25, v9, 6
	s_movk_i32 s24, 57
	v_addc_co_u32_e32 v2, vcc, 0, v2, vcc
	v_cmp_gt_i64_e32 vcc, s[22:23], v[8:9]
	v_readlane_b32 s23, v9, 7
	s_movk_i32 s22, 56
	v_addc_co_u32_e32 v2, vcc, 0, v2, vcc
	v_cmp_gt_i64_e32 vcc, s[24:25], v[8:9]
	v_readlane_b32 s25, v9, 8
	s_movk_i32 s24, 55
	v_addc_co_u32_e32 v2, vcc, 0, v2, vcc
	v_cmp_gt_i64_e32 vcc, s[22:23], v[8:9]
	v_readlane_b32 s23, v9, 9
	s_movk_i32 s22, 54
	v_addc_co_u32_e32 v2, vcc, 0, v2, vcc
	v_cmp_gt_i64_e32 vcc, s[24:25], v[8:9]
	v_readlane_b32 s25, v9, 10
	s_movk_i32 s24, 53
	v_addc_co_u32_e32 v2, vcc, 0, v2, vcc
	v_cmp_gt_i64_e32 vcc, s[22:23], v[8:9]
	v_readlane_b32 s23, v9, 11
	s_movk_i32 s22, 52
	v_addc_co_u32_e32 v2, vcc, 0, v2, vcc
; __device__ __forceinline__ void phase_nrr(const Frame& F, const Args& a, int l, const bf16_t* XA, const float* g, const float* modl, unsigned char* XN8) {
;     ...
;             int rank = 0;
; #pragma unroll 8
;             for (int e2 = 0; e2 < 64; ++e2) { const float v = __int_as_float(__builtin_amdgcn_readlane(__float_as_int(val), e2)); rank += (v > val || (v == val && e2 < lane)) ? 1 : 0; }
	v_cmp_gt_i64_e32 vcc, s[24:25], v[8:9]
	v_readlane_b32 s25, v9, 12
	s_movk_i32 s24, 51
	v_addc_co_u32_e32 v2, vcc, 0, v2, vcc
	v_cmp_gt_i64_e32 vcc, s[22:23], v[8:9]
	v_readlane_b32 s23, v9, 13
	s_movk_i32 s22, 50
	v_addc_co_u32_e32 v2, vcc, 0, v2, vcc
	v_cmp_gt_i64_e32 vcc, s[24:25], v[8:9]
	v_readlane_b32 s25, v9, 14
	s_movk_i32 s24, 49
	v_addc_co_u32_e32 v2, vcc, 0, v2, vcc
	v_cmp_gt_i64_e32 vcc, s[22:23], v[8:9]
	v_readlane_b32 s23, v9, 15
	s_movk_i32 s22, 48
	v_addc_co_u32_e32 v2, vcc, 0, v2, vcc
	v_cmp_gt_i64_e32 vcc, s[24:25], v[8:9]
	v_readlane_b32 s25, v9, 16
	s_movk_i32 s24, 47
	v_addc_co_u32_e32 v2, vcc, 0, v2, vcc
	v_cmp_gt_i64_e32 vcc, s[22:23], v[8:9]
	v_readlane_b32 s23, v9, 17
	s_movk_i32 s22, 46
	v_addc_co_u32_e32 v2, vcc, 0, v2, vcc
	v_cmp_gt_i64_e32 vcc, s[24:25], v[8:9]
	v_readlane_b32 s25, v9, 18
	s_movk_i32 s24, 45
	v_addc_co_u32_e32 v2, vcc, 0, v2, vcc
	v_cmp_gt_i64_e32 vcc, s[22:23], v[8:9]
	v_readlane_b32 s23, v9, 19
	s_movk_i32 s22, 44
	v_addc_co_u32_e32 v2, vcc, 0, v2, vcc
	v_cmp_gt_i64_e32 vcc, s[24:25], v[8:9]
	v_readlane_b32 s25, v9, 20
	s_movk_i32 s24, 43
	v_addc_co_u32_e32 v2, vcc, 0, v2, vcc
	v_cmp_gt_i64_e32 vcc, s[22:23], v[8:9]
	v_readlane_b32 s23, v9, 21
	s_movk_i32 s22, 42
	v_addc_co_u32_e32 v2, vcc, 0, v2, vcc
	v_cmp_gt_i64_e32 vcc, s[24:25], v[8:9]
	v_readlane_b32 s25, v9, 22
	s_movk_i32 s24, 41
	v_addc_co_u32_e32 v2, vcc, 0, v2, vcc
	v_cmp_gt_i64_e32 vcc, s[22:23], v[8:9]
	v_readlane_b32 s23, v9, 23
	s_movk_i32 s22, 40
	v_addc_co_u32_e32 v2, vcc, 0, v2, vcc
	v_cmp_gt_i64_e32 vcc, s[24:25], v[8:9]
	v_readlane_b32 s25, v9, 24
	s_movk_i32 s24, 39
	v_addc_co_u32_e32 v2, vcc, 0, v2, vcc
	v_cmp_gt_i64_e32 vcc, s[22:23], v[8:9]
	v_readlane_b32 s23, v9, 25
	s_movk_i32 s22, 38
	v_addc_co_u32_e32 v2, vcc, 0, v2, vcc
	v_cmp_gt_i64_e32 vcc, s[24:25], v[8:9]
	v_readlane_b32 s25, v9, 26
	s_movk_i32 s24, 37
	v_addc_co_u32_e32 v2, vcc, 0, v2, vcc
	v_cmp_gt_i64_e32 vcc, s[22:23], v[8:9]
	v_readlane_b32 s23, v9, 27
	s_movk_i32 s22, 36
	v_addc_co_u32_e32 v2, vcc, 0, v2, vcc
	v_cmp_gt_i64_e32 vcc, s[24:25], v[8:9]
	v_readlane_b32 s25, v9, 28
	s_movk_i32 s24, 35
	v_addc_co_u32_e32 v2, vcc, 0, v2, vcc
	v_cmp_gt_i64_e32 vcc, s[22:23], v[8:9]
	v_readlane_b32 s23, v9, 29
	s_movk_i32 s22, 34
	v_addc_co_u32_e32 v2, vcc, 0, v2, vcc
	v_cmp_gt_i64_e32 vcc, s[24:25], v[8:9]
	v_readlane_b32 s25, v9, 30
	s_movk_i32 s24, 33
	v_addc_co_u32_e32 v2, vcc, 0, v2, vcc
	v_cmp_gt_i64_e32 vcc, s[22:23], v[8:9]
	v_readlane_b32 s23, v9, 31
	s_movk_i32 s22, 32
	v_addc_co_u32_e32 v2, vcc, 0, v2, vcc
	v_cmp_gt_i64_e32 vcc, s[24:25], v[8:9]
	v_readlane_b32 s25, v9, 32
	s_movk_i32 s24, 31
	v_addc_co_u32_e32 v2, vcc, 0, v2, vcc
	v_cmp_gt_i64_e32 vcc, s[22:23], v[8:9]
	v_readlane_b32 s23, v9, 33
	s_movk_i32 s22, 30
	v_addc_co_u32_e32 v2, vcc, 0, v2, vcc
	v_cmp_gt_i64_e32 vcc, s[24:25], v[8:9]
	v_readlane_b32 s25, v9, 34
	s_movk_i32 s24, 29
	v_addc_co_u32_e32 v2, vcc, 0, v2, vcc
	v_cmp_gt_i64_e32 vcc, s[22:23], v[8:9]
	v_readlane_b32 s23, v9, 35
	s_movk_i32 s22, 28
	v_addc_co_u32_e32 v2, vcc, 0, v2, vcc
	v_cmp_gt_i64_e32 vcc, s[24:25], v[8:9]
	v_readlane_b32 s25, v9, 36
	s_movk_i32 s24, 27
	v_addc_co_u32_e32 v2, vcc, 0, v2, vcc
	v_cmp_gt_i64_e32 vcc, s[22:23], v[8:9]
	v_readlane_b32 s23, v9, 37
	s_movk_i32 s22, 26
	v_addc_co_u32_e32 v2, vcc, 0, v2, vcc
	v_cmp_gt_i64_e32 vcc, s[24:25], v[8:9]
	v_readlane_b32 s25, v9, 38
	s_movk_i32 s24, 25
	v_addc_co_u32_e32 v2, vcc, 0, v2, vcc
	v_cmp_gt_i64_e32 vcc, s[22:23], v[8:9]
	v_readlane_b32 s23, v9, 39
	s_movk_i32 s22, 24
	v_addc_co_u32_e32 v2, vcc, 0, v2, vcc
	v_cmp_gt_i64_e32 vcc, s[24:25], v[8:9]
	v_readlane_b32 s25, v9, 40
	s_movk_i32 s24, 23
	v_addc_co_u32_e32 v2, vcc, 0, v2, vcc
	v_cmp_gt_i64_e32 vcc, s[22:23], v[8:9]
	v_readlane_b32 s23, v9, 41
	s_movk_i32 s22, 22
	v_addc_co_u32_e32 v2, vcc, 0, v2, vcc
	v_cmp_gt_i64_e32 vcc, s[24:25], v[8:9]
	v_readlane_b32 s25, v9, 42
	s_movk_i32 s24, 21
	v_addc_co_u32_e32 v2, vcc, 0, v2, vcc
	v_cmp_gt_i64_e32 vcc, s[22:23], v[8:9]
	v_readlane_b32 s23, v9, 43
	s_movk_i32 s22, 20
	v_addc_co_u32_e32 v2, vcc, 0, v2, vcc
	v_cmp_gt_i64_e32 vcc, s[24:25], v[8:9]
	v_readlane_b32 s25, v9, 44
	s_movk_i32 s24, 19
	v_addc_co_u32_e32 v2, vcc, 0, v2, vcc
	v_cmp_gt_i64_e32 vcc, s[22:23], v[8:9]
	v_readlane_b32 s23, v9, 45
	s_movk_i32 s22, 18
	v_addc_co_u32_e32 v2, vcc, 0, v2, vcc
	v_cmp_gt_i64_e32 vcc, s[24:25], v[8:9]
	v_readlane_b32 s25, v9, 46
	s_movk_i32 s24, 17
	v_addc_co_u32_e32 v2, vcc, 0, v2, vcc
	v_cmp_gt_i64_e32 vcc, s[22:23], v[8:9]
	v_readlane_b32 s23, v9, 47
	s_movk_i32 s22, 16
	v_addc_co_u32_e32 v2, vcc, 0, v2, vcc
	v_cmp_gt_i64_e32 vcc, s[24:25], v[8:9]
	v_readlane_b32 s25, v9, 48
	s_movk_i32 s24, 15
	v_addc_co_u32_e32 v2, vcc, 0, v2, vcc
	v_cmp_gt_i64_e32 vcc, s[22:23], v[8:9]
	v_readlane_b32 s23, v9, 49
	s_movk_i32 s22, 14
	v_addc_co_u32_e32 v2, vcc, 0, v2, vcc
	v_cmp_gt_i64_e32 vcc, s[24:25], v[8:9]
	v_readlane_b32 s25, v9, 50
	s_movk_i32 s24, 13
	v_addc_co_u32_e32 v2, vcc, 0, v2, vcc
	v_cmp_gt_i64_e32 vcc, s[22:23], v[8:9]
	v_readlane_b32 s23, v9, 51
	s_movk_i32 s22, 12
	v_addc_co_u32_e32 v2, vcc, 0, v2, vcc
	v_cmp_gt_i64_e32 vcc, s[24:25], v[8:9]
	v_readlane_b32 s25, v9, 52
	s_movk_i32 s24, 11
	v_addc_co_u32_e32 v2, vcc, 0, v2, vcc
	v_cmp_gt_i64_e32 vcc, s[22:23], v[8:9]
	v_readlane_b32 s23, v9, 53
	s_movk_i32 s22, 10
	v_addc_co_u32_e32 v2, vcc, 0, v2, vcc
	v_cmp_gt_i64_e32 vcc, s[24:25], v[8:9]
	v_readlane_b32 s25, v9, 54
	s_movk_i32 s24, 9
	v_addc_co_u32_e32 v2, vcc, 0, v2, vcc
	v_cmp_gt_i64_e32 vcc, s[22:23], v[8:9]
	v_readlane_b32 s23, v9, 55
	s_movk_i32 s22, 8
	v_addc_co_u32_e32 v2, vcc, 0, v2, vcc
	v_cmp_gt_i64_e32 vcc, s[24:25], v[8:9]
; __device__ __forceinline__ float wave_sum(float v) {
; #pragma unroll
;     for (int o = 1; o < 64; o <<= 1) v += __shfl_xor(v, o);
;     return v;
; __device__ __forceinline__ void phase_nrr(const Frame& F, const Args& a, int l, const bf16_t* XA, const float* g, const float* modl, unsigned char* XN8) {
;     ...
;         for (int i = 0; i < 8; ++i) { const int t = tb + i;
;             const float lg = Pl[(w * 8 + i) * NE + lane] + Pl[(64 + w * 8 + i) * NE + lane]; const float sc = 1.f / (1.f + __expf(-lg)); const float bb = sc + bias;
;             float m1 = bb; m1 = fmaxf(m1, __shfl_xor(m1, 1)); m1 = fmaxf(m1, __shfl_xor(m1, 2)); m1 = fmaxf(m1, __shfl_xor(m1, 4));
;             const unsigned long long eq = __ballot(bb == m1); const int gbase = lane & ~7; const unsigned grpmask = (unsigned)((eq >> gbase) & 0xffull);
;             const int first = gbase + __builtin_ctz(grpmask);
;             float m2 = (lane == first) ? -INFINITY : bb; m2 = fmaxf(m2, __shfl_xor(m2, 1)); m2 = fmaxf(m2, __shfl_xor(m2, 2)); m2 = fmaxf(m2, __shfl_xor(m2, 4));
;             const float gsum = m1 + m2; const int gq = lane >> 3;
;             int grank = 0;
; #pragma unroll
;             for (int g2 = 0; g2 < 8; ++g2) { const float v = __int_as_float(__builtin_amdgcn_readlane(__float_as_int(gsum), g2 * 8)); grank += (v > gsum || (v == gsum && g2 < gq)) ? 1 : 0; }
;             const bool keep = grank < 4; const float val = keep ? bb : -INFINITY;
;             int rank = 0;
; #pragma unroll 8
;             for (int e2 = 0; e2 < 64; ++e2) { const float v = __int_as_float(__builtin_amdgcn_readlane(__float_as_int(val), e2)); rank += (v > val || (v == val && e2 < lane)) ? 1 : 0; }
;             const bool sel = rank < TOPK;
;             const float ssum = wave_sum(sel ? sc : 0.f);
;             if (sel) { const int p = atomicAdd((int*)(hist + lane), 1); top_e[t * TOPK + rank] = lane; gate[t * TOPK + rank] = sc / ssum * 2.5f; lpos[t * TOPK + rank] = p; }
	v_readlane_b32 s25, v9, 56
	s_movk_i32 s24, 7
	v_addc_co_u32_e32 v2, vcc, 0, v2, vcc
	v_cmp_gt_i64_e32 vcc, s[22:23], v[8:9]
	v_readlane_b32 s23, v9, 57
	s_movk_i32 s22, 6
	v_addc_co_u32_e32 v2, vcc, 0, v2, vcc
	v_cmp_gt_i64_e32 vcc, s[24:25], v[8:9]
	v_readlane_b32 s25, v9, 58
	s_movk_i32 s24, 5
	v_addc_co_u32_e32 v2, vcc, 0, v2, vcc
	v_cmp_gt_i64_e32 vcc, s[22:23], v[8:9]
	v_readlane_b32 s23, v9, 59
	s_movk_i32 s22, 4
	v_addc_co_u32_e32 v2, vcc, 0, v2, vcc
	v_cmp_gt_i64_e32 vcc, s[24:25], v[8:9]
	v_readlane_b32 s25, v9, 60
	s_movk_i32 s24, 3
	v_addc_co_u32_e32 v2, vcc, 0, v2, vcc
	v_cmp_gt_i64_e32 vcc, s[22:23], v[8:9]
	v_readlane_b32 s23, v9, 61
	s_movk_i32 s22, 2
	v_addc_co_u32_e32 v2, vcc, 0, v2, vcc
	v_cmp_gt_i64_e32 vcc, s[24:25], v[8:9]
	v_readlane_b32 s25, v9, 62
	s_movk_i32 s24, 1
	v_addc_co_u32_e32 v2, vcc, 0, v2, vcc
	v_cmp_gt_i64_e32 vcc, s[22:23], v[8:9]
	v_readlane_b32 s23, v9, 63
	s_movk_i32 s22, 0
	v_addc_co_u32_e32 v2, vcc, 0, v2, vcc
	v_cmp_gt_i64_e32 vcc, s[24:25], v[8:9]
	s_nop 1
	v_addc_co_u32_e32 v2, vcc, 0, v2, vcc
	v_cmp_gt_i64_e32 vcc, s[22:23], v[8:9]
	s_nop 1
	v_addc_co_u32_e32 v2, vcc, 0, v2, vcc
	v_cmp_gt_u32_e32 vcc, 6, v2
	s_nop 1
	v_cndmask_b32_e32 v6, 0, v5, vcc
	s_nop 1
	v_add_f32_dpp v6, v6, v6 quad_perm:[1,0,3,2] row_mask:0xf bank_mask:0xf
	s_nop 1
	v_add_f32_dpp v6, v6, v6 quad_perm:[2,3,0,1] row_mask:0xf bank_mask:0xf
	s_nop 1
	v_add_f32_dpp v6, v6, v6 row_half_mirror row_mask:0xf bank_mask:0xf
	s_nop 1
	v_add_f32_dpp v6, v6, v6 row_mirror row_mask:0xf bank_mask:0xf
	s_nop 0
	ds_bpermute_b32 v7, v222, v6
	s_waitcnt lgkmcnt(0)
	v_add_f32_e32 v6, v6, v7
	v_mov_b32_e32 v7, v6
	s_nop 1
	v_permlane32_swap_b32_e32 v7, v6
	s_and_saveexec_b64 s[22:23], vcc
	s_cbranch_execz .LBB0_543
	s_waitcnt lgkmcnt(0)
	v_add_f32_e32 v10, v6, v7
	v_mad_u64_u32 v[6:7], s[24:25], s42, 6, v[2:3]
	v_div_scale_f32 v2, s[24:25], v10, v10, v5
	v_rcp_f32_e32 v12, v2
	v_ashrrev_i32_e32 v7, 31, v6
	v_lshlrev_b64 v[6:7], 2, v[6:7]
	v_lshl_add_u64 v[8:9], s[26:27], 0, v[6:7]
	ds_add_rtn_u32 v11, v227, v243
	global_store_dword v[8:9], v230, off
	v_fma_f32 v8, -v2, v12, 1.0
	v_fmac_f32_e32 v12, v8, v12
	v_div_scale_f32 v8, vcc, v5, v10, v5
	v_mul_f32_e32 v9, v8, v12
	v_fma_f32 v13, -v2, v9, v8
	v_fmac_f32_e32 v9, v13, v12
	v_fma_f32 v2, -v2, v9, v8
	v_div_fmas_f32 v2, v2, v12, v9
	v_div_fixup_f32 v2, v2, v10, v5
	v_mul_f32_e32 v2, 0x40200000, v2
	v_lshl_add_u64 v[8:9], s[28:29], 0, v[6:7]
	v_lshl_add_u64 v[6:7], s[30:31], 0, v[6:7]
	global_store_dword v[8:9], v2, off
	s_waitcnt lgkmcnt(0)
	global_store_dword v[6:7], v11, off
.LBB0_543:
	s_or_b64 exec, exec, s[22:23]
	v_add_u32_e32 v2, s78, v226
	ds_read_b32 v2, v2
	ds_read_b32 v5, v4 offset:16896
	s_mov_b32 s3, 0
	s_waitcnt lgkmcnt(0)
	v_add_f32_e32 v2, v2, v5
	v_mul_f32_e32 v2, 0xbfb8aa3b, v2
	v_exp_f32_e32 v2, v2
	s_nop 0
	v_add_f32_e32 v2, 1.0, v2
	v_div_scale_f32 v5, s[22:23], v2, v2, 1.0
	v_rcp_f32_e32 v6, v5
	s_nop 0
	v_fma_f32 v7, -v5, v6, 1.0
	v_fmac_f32_e32 v6, v7, v6
	v_div_scale_f32 v7, vcc, 1.0, v2, 1.0
	v_mul_f32_e32 v8, v7, v6
	v_fma_f32 v9, -v5, v8, v7
	v_fmac_f32_e32 v8, v9, v6
	v_fma_f32 v5, -v5, v8, v7
	v_div_fmas_f32 v5, v5, v6, v8
	v_div_fixup_f32 v5, v5, v2, 1.0
	v_add_f32_e32 v2, v3, v5
	s_nop 1
	s_waitcnt lgkmcnt(0)
	v_max_f32_dpp v6, v2, v2 quad_perm:[1,0,3,2] row_mask:0xf bank_mask:0xf
	s_nop 1
	s_waitcnt lgkmcnt(0)
	v_max_f32_dpp v6, v6, v6 quad_perm:[2,3,0,1] row_mask:0xf bank_mask:0xf
	s_nop 1
	s_waitcnt lgkmcnt(0)
	v_max_f32_dpp v8, v6, v6 row_half_mirror row_mask:0xf bank_mask:0xf
	v_cmp_eq_f32_e32 vcc, v2, v8
	s_nop 1
	v_lshrrev_b64 v[6:7], v200, vcc
	v_ffbl_b32_sdwa v6, v6 dst_sel:DWORD dst_unused:UNUSED_PAD src0_sel:BYTE_0
	v_add_u32_e32 v6, v6, v200
	v_cmp_ne_u32_e32 vcc, v230, v6
	s_nop 1
	v_cndmask_b32_e32 v6, v245, v2, vcc
	s_nop 1
	s_waitcnt lgkmcnt(0)
	v_max_f32_dpp v6, v6, v6 quad_perm:[1,0,3,2] row_mask:0xf bank_mask:0xf
	s_nop 1
	s_waitcnt lgkmcnt(0)
	v_max_f32_dpp v6, v6, v6 quad_perm:[2,3,0,1] row_mask:0xf bank_mask:0xf
	s_nop 1
	s_waitcnt lgkmcnt(0)
	v_max_f32_dpp v6, v6, v6 row_half_mirror row_mask:0xf bank_mask:0xf
	v_add_f32_e32 v6, v8, v6
	s_nop 0
	v_readlane_b32 s5, v6, 0
	s_nop 1
	v_cmp_eq_f32_e64 s[22:23], s5, v6
	v_cmp_gt_f32_e32 vcc, s5, v6
	s_and_b64 s[22:23], s[6:7], s[22:23]
	s_or_b64 s[22:23], vcc, s[22:23]
	v_readlane_b32 s5, v6, 8
	v_cndmask_b32_e64 v7, 0, 1, s[22:23]
	s_nop 0
	v_cmp_eq_f32_e64 s[22:23], s5, v6
	v_cmp_gt_f32_e32 vcc, s5, v6
	s_and_b64 s[22:23], s[8:9], s[22:23]
	s_or_b64 s[22:23], vcc, s[22:23]
	v_readlane_b32 s5, v6, 16
	v_cndmask_b32_e64 v8, 0, 1, s[22:23]
	s_nop 0
	v_cmp_eq_f32_e64 s[22:23], s5, v6
	v_cmp_gt_f32_e32 vcc, s5, v6
	s_and_b64 s[22:23], s[10:11], s[22:23]
	s_or_b64 s[22:23], vcc, s[22:23]
	v_readlane_b32 s5, v6, 24
	v_cndmask_b32_e64 v9, 0, 1, s[22:23]
	s_nop 0
	v_cmp_eq_f32_e64 s[22:23], s5, v6
	v_cmp_gt_f32_e32 vcc, s5, v6
	s_and_b64 s[22:23], s[12:13], s[22:23]
	s_or_b64 s[22:23], vcc, s[22:23]
	v_readlane_b32 s5, v6, 32
	v_cndmask_b32_e64 v10, 0, 1, s[22:23]
	s_nop 0
	v_cmp_eq_f32_e64 s[22:23], s5, v6
	v_cmp_gt_f32_e32 vcc, s5, v6
	s_and_b64 s[22:23], s[14:15], s[22:23]
	s_or_b64 s[22:23], vcc, s[22:23]
	v_readlane_b32 s5, v6, 40
	v_cndmask_b32_e64 v11, 0, 1, s[22:23]
	s_nop 0
	v_cmp_eq_f32_e64 s[22:23], s5, v6
	v_cmp_gt_f32_e32 vcc, s5, v6
	s_and_b64 s[22:23], s[16:17], s[22:23]
	s_or_b64 s[22:23], vcc, s[22:23]
	v_readlane_b32 s5, v6, 48
	v_cndmask_b32_e64 v12, 0, 1, s[22:23]
	s_nop 0
	v_cmp_eq_f32_e64 s[22:23], s5, v6
	v_cmp_gt_f32_e32 vcc, s5, v6
	s_and_b64 s[22:23], s[18:19], s[22:23]
	v_readlane_b32 s5, v6, 56
	s_or_b64 s[22:23], vcc, s[22:23]
	v_cndmask_b32_e64 v13, 0, 1, s[22:23]
; __device__ __forceinline__ void phase_nrr(const Frame& F, const Args& a, int l, const bf16_t* XA, const float* g, const float* modl, unsigned char* XN8) {
;     ...
;             const float gsum = m1 + m2; const int gq = lane >> 3;
;             int grank = 0;
; #pragma unroll
;             for (int g2 = 0; g2 < 8; ++g2) { const float v = __int_as_float(__builtin_amdgcn_readlane(__float_as_int(gsum), g2 * 8)); grank += (v > gsum || (v == gsum && g2 < gq)) ? 1 : 0; }
;             const bool keep = grank < 4; const float val = keep ? bb : -INFINITY;
;             int rank = 0;
; #pragma unroll 8
;             for (int e2 = 0; e2 < 64; ++e2) { const float v = __int_as_float(__builtin_amdgcn_readlane(__float_as_int(val), e2)); rank += (v > val || (v == val && e2 < lane)) ? 1 : 0; }
	v_cmp_gt_f32_e32 vcc, s5, v6
	s_nop 1
	v_cndmask_b32_e64 v6, 0, 1, vcc
	v_add_u32_e32 v6, v8, v6
	v_add3_u32 v6, v6, v7, v9
	v_add3_u32 v6, v6, v10, v11
	v_add3_u32 v6, v6, v12, v13
	v_cmp_gt_u32_e32 vcc, 4, v6
	s_nop 1
	v_cndmask_b32_e32 v6, v245, v2, vcc
	v_mov_b32_e32 v2, 0
	v_ashrrev_i32_e32 v9, 31, v6
	v_sub_u32_e32 v8, 63, v230
	v_and_b32_e32 v9, 0x7fffffff, v9
	v_xor_b32_e32 v9, v6, v9
	s_nop 0
	v_readlane_b32 s25, v9, 0
	s_movk_i32 s24, 63
	v_readlane_b32 s23, v9, 1
	s_movk_i32 s22, 62
	v_cmp_gt_i64_e32 vcc, s[24:25], v[8:9]
	v_readlane_b32 s25, v9, 2
	s_movk_i32 s24, 61
	v_addc_co_u32_e32 v2, vcc, 0, v2, vcc
	v_cmp_gt_i64_e32 vcc, s[22:23], v[8:9]
	v_readlane_b32 s23, v9, 3
	s_movk_i32 s22, 60
	v_addc_co_u32_e32 v2, vcc, 0, v2, vcc
	v_cmp_gt_i64_e32 vcc, s[24:25], v[8:9]
	v_readlane_b32 s25, v9, 4
	s_movk_i32 s24, 59
	v_addc_co_u32_e32 v2, vcc, 0, v2, vcc
	v_cmp_gt_i64_e32 vcc, s[22:23], v[8:9]
	v_readlane_b32 s23, v9, 5
	s_movk_i32 s22, 58
	v_addc_co_u32_e32 v2, vcc, 0, v2, vcc
	v_cmp_gt_i64_e32 vcc, s[24:25], v[8:9]
	v_readlane_b32 s25, v9, 6
	s_movk_i32 s24, 57
	v_addc_co_u32_e32 v2, vcc, 0, v2, vcc
	v_cmp_gt_i64_e32 vcc, s[22:23], v[8:9]
	v_readlane_b32 s23, v9, 7
	s_movk_i32 s22, 56
	v_addc_co_u32_e32 v2, vcc, 0, v2, vcc
	v_cmp_gt_i64_e32 vcc, s[24:25], v[8:9]
	v_readlane_b32 s25, v9, 8
	s_movk_i32 s24, 55
	v_addc_co_u32_e32 v2, vcc, 0, v2, vcc
	v_cmp_gt_i64_e32 vcc, s[22:23], v[8:9]
	v_readlane_b32 s23, v9, 9
	s_movk_i32 s22, 54
	v_addc_co_u32_e32 v2, vcc, 0, v2, vcc
	v_cmp_gt_i64_e32 vcc, s[24:25], v[8:9]
	v_readlane_b32 s25, v9, 10
	s_movk_i32 s24, 53
	v_addc_co_u32_e32 v2, vcc, 0, v2, vcc
	v_cmp_gt_i64_e32 vcc, s[22:23], v[8:9]
	v_readlane_b32 s23, v9, 11
	s_movk_i32 s22, 52
	v_addc_co_u32_e32 v2, vcc, 0, v2, vcc
	v_cmp_gt_i64_e32 vcc, s[24:25], v[8:9]
	v_readlane_b32 s25, v9, 12
	s_movk_i32 s24, 51
	v_addc_co_u32_e32 v2, vcc, 0, v2, vcc
	v_cmp_gt_i64_e32 vcc, s[22:23], v[8:9]
	v_readlane_b32 s23, v9, 13
	s_movk_i32 s22, 50
	v_addc_co_u32_e32 v2, vcc, 0, v2, vcc
	v_cmp_gt_i64_e32 vcc, s[24:25], v[8:9]
	v_readlane_b32 s25, v9, 14
	s_movk_i32 s24, 49
	v_addc_co_u32_e32 v2, vcc, 0, v2, vcc
	v_cmp_gt_i64_e32 vcc, s[22:23], v[8:9]
	v_readlane_b32 s23, v9, 15
	s_movk_i32 s22, 48
	v_addc_co_u32_e32 v2, vcc, 0, v2, vcc
	v_cmp_gt_i64_e32 vcc, s[24:25], v[8:9]
	v_readlane_b32 s25, v9, 16
	s_movk_i32 s24, 47
	v_addc_co_u32_e32 v2, vcc, 0, v2, vcc
	v_cmp_gt_i64_e32 vcc, s[22:23], v[8:9]
	v_readlane_b32 s23, v9, 17
	s_movk_i32 s22, 46
	v_addc_co_u32_e32 v2, vcc, 0, v2, vcc
	v_cmp_gt_i64_e32 vcc, s[24:25], v[8:9]
	v_readlane_b32 s25, v9, 18
	s_movk_i32 s24, 45
	v_addc_co_u32_e32 v2, vcc, 0, v2, vcc
	v_cmp_gt_i64_e32 vcc, s[22:23], v[8:9]
	v_readlane_b32 s23, v9, 19
	s_movk_i32 s22, 44
	v_addc_co_u32_e32 v2, vcc, 0, v2, vcc
	v_cmp_gt_i64_e32 vcc, s[24:25], v[8:9]
	v_readlane_b32 s25, v9, 20
	s_movk_i32 s24, 43
	v_addc_co_u32_e32 v2, vcc, 0, v2, vcc
	v_cmp_gt_i64_e32 vcc, s[22:23], v[8:9]
	v_readlane_b32 s23, v9, 21
	s_movk_i32 s22, 42
	v_addc_co_u32_e32 v2, vcc, 0, v2, vcc
	v_cmp_gt_i64_e32 vcc, s[24:25], v[8:9]
	v_readlane_b32 s25, v9, 22
	s_movk_i32 s24, 41
	v_addc_co_u32_e32 v2, vcc, 0, v2, vcc
	v_cmp_gt_i64_e32 vcc, s[22:23], v[8:9]
	v_readlane_b32 s23, v9, 23
	s_movk_i32 s22, 40
	v_addc_co_u32_e32 v2, vcc, 0, v2, vcc
	v_cmp_gt_i64_e32 vcc, s[24:25], v[8:9]
	v_readlane_b32 s25, v9, 24
	s_movk_i32 s24, 39
	v_addc_co_u32_e32 v2, vcc, 0, v2, vcc
	v_cmp_gt_i64_e32 vcc, s[22:23], v[8:9]
	v_readlane_b32 s23, v9, 25
	s_movk_i32 s22, 38
	v_addc_co_u32_e32 v2, vcc, 0, v2, vcc
	v_cmp_gt_i64_e32 vcc, s[24:25], v[8:9]
	v_readlane_b32 s25, v9, 26
	s_movk_i32 s24, 37
	v_addc_co_u32_e32 v2, vcc, 0, v2, vcc
	v_cmp_gt_i64_e32 vcc, s[22:23], v[8:9]
	v_readlane_b32 s23, v9, 27
	s_movk_i32 s22, 36
	v_addc_co_u32_e32 v2, vcc, 0, v2, vcc
	v_cmp_gt_i64_e32 vcc, s[24:25], v[8:9]
	v_readlane_b32 s25, v9, 28
	s_movk_i32 s24, 35
	v_addc_co_u32_e32 v2, vcc, 0, v2, vcc
	v_cmp_gt_i64_e32 vcc, s[22:23], v[8:9]
	v_readlane_b32 s23, v9, 29
	s_movk_i32 s22, 34
	v_addc_co_u32_e32 v2, vcc, 0, v2, vcc
	v_cmp_gt_i64_e32 vcc, s[24:25], v[8:9]
	v_readlane_b32 s25, v9, 30
	s_movk_i32 s24, 33
	v_addc_co_u32_e32 v2, vcc, 0, v2, vcc
	v_cmp_gt_i64_e32 vcc, s[22:23], v[8:9]
	v_readlane_b32 s23, v9, 31
	s_movk_i32 s22, 32
	v_addc_co_u32_e32 v2, vcc, 0, v2, vcc
	v_cmp_gt_i64_e32 vcc, s[24:25], v[8:9]
	v_readlane_b32 s25, v9, 32
	s_movk_i32 s24, 31
	v_addc_co_u32_e32 v2, vcc, 0, v2, vcc
	v_cmp_gt_i64_e32 vcc, s[22:23], v[8:9]
	v_readlane_b32 s23, v9, 33
	s_movk_i32 s22, 30
	v_addc_co_u32_e32 v2, vcc, 0, v2, vcc
	v_cmp_gt_i64_e32 vcc, s[24:25], v[8:9]
	v_readlane_b32 s25, v9, 34
	s_movk_i32 s24, 29
	v_addc_co_u32_e32 v2, vcc, 0, v2, vcc
	v_cmp_gt_i64_e32 vcc, s[22:23], v[8:9]
	v_readlane_b32 s23, v9, 35
	s_movk_i32 s22, 28
	v_addc_co_u32_e32 v2, vcc, 0, v2, vcc
	v_cmp_gt_i64_e32 vcc, s[24:25], v[8:9]
	v_readlane_b32 s25, v9, 36
	s_movk_i32 s24, 27
	v_addc_co_u32_e32 v2, vcc, 0, v2, vcc
	v_cmp_gt_i64_e32 vcc, s[22:23], v[8:9]
	v_readlane_b32 s23, v9, 37
	s_movk_i32 s22, 26
	v_addc_co_u32_e32 v2, vcc, 0, v2, vcc
	v_cmp_gt_i64_e32 vcc, s[24:25], v[8:9]
	v_readlane_b32 s25, v9, 38
	s_movk_i32 s24, 25
	v_addc_co_u32_e32 v2, vcc, 0, v2, vcc
	v_cmp_gt_i64_e32 vcc, s[22:23], v[8:9]
	v_readlane_b32 s23, v9, 39
	s_movk_i32 s22, 24
	v_addc_co_u32_e32 v2, vcc, 0, v2, vcc
	v_cmp_gt_i64_e32 vcc, s[24:25], v[8:9]
	v_readlane_b32 s25, v9, 40
	s_movk_i32 s24, 23
	v_addc_co_u32_e32 v2, vcc, 0, v2, vcc
	v_cmp_gt_i64_e32 vcc, s[22:23], v[8:9]
	v_readlane_b32 s23, v9, 41
	s_movk_i32 s22, 22
	v_addc_co_u32_e32 v2, vcc, 0, v2, vcc
	v_cmp_gt_i64_e32 vcc, s[24:25], v[8:9]
	v_readlane_b32 s25, v9, 42
; __device__ __forceinline__ float wave_sum(float v) {
; #pragma unroll
;     for (int o = 1; o < 64; o <<= 1) v += __shfl_xor(v, o);
;     return v;
; __device__ __forceinline__ void phase_nrr(const Frame& F, const Args& a, int l, const bf16_t* XA, const float* g, const float* modl, unsigned char* XN8) {
;     ...
;             int rank = 0;
; #pragma unroll 8
;             for (int e2 = 0; e2 < 64; ++e2) { const float v = __int_as_float(__builtin_amdgcn_readlane(__float_as_int(val), e2)); rank += (v > val || (v == val && e2 < lane)) ? 1 : 0; }
;             const bool sel = rank < TOPK;
;             const float ssum = wave_sum(sel ? sc : 0.f);
;             if (sel) { const int p = atomicAdd((int*)(hist + lane), 1); top_e[t * TOPK + rank] = lane; gate[t * TOPK + rank] = sc / ssum * 2.5f; lpos[t * TOPK + rank] = p; }
	s_movk_i32 s24, 21
	v_addc_co_u32_e32 v2, vcc, 0, v2, vcc
	v_cmp_gt_i64_e32 vcc, s[22:23], v[8:9]
	v_readlane_b32 s23, v9, 43
	s_movk_i32 s22, 20
	v_addc_co_u32_e32 v2, vcc, 0, v2, vcc
	v_cmp_gt_i64_e32 vcc, s[24:25], v[8:9]
	v_readlane_b32 s25, v9, 44
	s_movk_i32 s24, 19
	v_addc_co_u32_e32 v2, vcc, 0, v2, vcc
	v_cmp_gt_i64_e32 vcc, s[22:23], v[8:9]
	v_readlane_b32 s23, v9, 45
	s_movk_i32 s22, 18
	v_addc_co_u32_e32 v2, vcc, 0, v2, vcc
	v_cmp_gt_i64_e32 vcc, s[24:25], v[8:9]
	v_readlane_b32 s25, v9, 46
	s_movk_i32 s24, 17
	v_addc_co_u32_e32 v2, vcc, 0, v2, vcc
	v_cmp_gt_i64_e32 vcc, s[22:23], v[8:9]
	v_readlane_b32 s23, v9, 47
	s_movk_i32 s22, 16
	v_addc_co_u32_e32 v2, vcc, 0, v2, vcc
	v_cmp_gt_i64_e32 vcc, s[24:25], v[8:9]
	v_readlane_b32 s25, v9, 48
	s_movk_i32 s24, 15
	v_addc_co_u32_e32 v2, vcc, 0, v2, vcc
	v_cmp_gt_i64_e32 vcc, s[22:23], v[8:9]
	v_readlane_b32 s23, v9, 49
	s_movk_i32 s22, 14
	v_addc_co_u32_e32 v2, vcc, 0, v2, vcc
	v_cmp_gt_i64_e32 vcc, s[24:25], v[8:9]
	v_readlane_b32 s25, v9, 50
	s_movk_i32 s24, 13
	v_addc_co_u32_e32 v2, vcc, 0, v2, vcc
	v_cmp_gt_i64_e32 vcc, s[22:23], v[8:9]
	v_readlane_b32 s23, v9, 51
	s_movk_i32 s22, 12
	v_addc_co_u32_e32 v2, vcc, 0, v2, vcc
	v_cmp_gt_i64_e32 vcc, s[24:25], v[8:9]
	v_readlane_b32 s25, v9, 52
	s_movk_i32 s24, 11
	v_addc_co_u32_e32 v2, vcc, 0, v2, vcc
	v_cmp_gt_i64_e32 vcc, s[22:23], v[8:9]
	v_readlane_b32 s23, v9, 53
	s_movk_i32 s22, 10
	v_addc_co_u32_e32 v2, vcc, 0, v2, vcc
	v_cmp_gt_i64_e32 vcc, s[24:25], v[8:9]
	v_readlane_b32 s25, v9, 54
	s_movk_i32 s24, 9
	v_addc_co_u32_e32 v2, vcc, 0, v2, vcc
	v_cmp_gt_i64_e32 vcc, s[22:23], v[8:9]
	v_readlane_b32 s23, v9, 55
	s_movk_i32 s22, 8
	v_addc_co_u32_e32 v2, vcc, 0, v2, vcc
	v_cmp_gt_i64_e32 vcc, s[24:25], v[8:9]
	v_readlane_b32 s25, v9, 56
	s_movk_i32 s24, 7
	v_addc_co_u32_e32 v2, vcc, 0, v2, vcc
	v_cmp_gt_i64_e32 vcc, s[22:23], v[8:9]
	v_readlane_b32 s23, v9, 57
	s_movk_i32 s22, 6
	v_addc_co_u32_e32 v2, vcc, 0, v2, vcc
	v_cmp_gt_i64_e32 vcc, s[24:25], v[8:9]
	v_readlane_b32 s25, v9, 58
	s_movk_i32 s24, 5
	v_addc_co_u32_e32 v2, vcc, 0, v2, vcc
	v_cmp_gt_i64_e32 vcc, s[22:23], v[8:9]
	v_readlane_b32 s23, v9, 59
	s_movk_i32 s22, 4
	v_addc_co_u32_e32 v2, vcc, 0, v2, vcc
	v_cmp_gt_i64_e32 vcc, s[24:25], v[8:9]
	v_readlane_b32 s25, v9, 60
	s_movk_i32 s24, 3
	v_addc_co_u32_e32 v2, vcc, 0, v2, vcc
	v_cmp_gt_i64_e32 vcc, s[22:23], v[8:9]
	v_readlane_b32 s23, v9, 61
	s_movk_i32 s22, 2
	v_addc_co_u32_e32 v2, vcc, 0, v2, vcc
	v_cmp_gt_i64_e32 vcc, s[24:25], v[8:9]
	v_readlane_b32 s25, v9, 62
	s_movk_i32 s24, 1
	v_addc_co_u32_e32 v2, vcc, 0, v2, vcc
	v_cmp_gt_i64_e32 vcc, s[22:23], v[8:9]
	v_readlane_b32 s23, v9, 63
	s_movk_i32 s22, 0
	v_addc_co_u32_e32 v2, vcc, 0, v2, vcc
	v_cmp_gt_i64_e32 vcc, s[24:25], v[8:9]
	s_nop 1
	v_addc_co_u32_e32 v2, vcc, 0, v2, vcc
	v_cmp_gt_i64_e32 vcc, s[22:23], v[8:9]
	s_nop 1
	v_addc_co_u32_e32 v2, vcc, 0, v2, vcc
	v_cmp_gt_u32_e32 vcc, 6, v2
	s_nop 1
	v_cndmask_b32_e32 v6, 0, v5, vcc
	s_nop 1
	v_add_f32_dpp v6, v6, v6 quad_perm:[1,0,3,2] row_mask:0xf bank_mask:0xf
	s_nop 1
	v_add_f32_dpp v6, v6, v6 quad_perm:[2,3,0,1] row_mask:0xf bank_mask:0xf
	s_nop 1
	v_add_f32_dpp v6, v6, v6 row_half_mirror row_mask:0xf bank_mask:0xf
	s_nop 1
	v_add_f32_dpp v6, v6, v6 row_mirror row_mask:0xf bank_mask:0xf
	s_nop 0
	ds_bpermute_b32 v7, v222, v6
	s_waitcnt lgkmcnt(0)
	v_add_f32_e32 v6, v6, v7
	v_mov_b32_e32 v7, v6
	s_nop 1
	v_permlane32_swap_b32_e32 v7, v6
	s_and_saveexec_b64 s[22:23], vcc
	s_cbranch_execz .LBB0_547
	s_waitcnt lgkmcnt(0)
	v_add_f32_e32 v10, v6, v7
	v_mad_u64_u32 v[6:7], s[24:25], s40, 6, v[2:3]
	v_div_scale_f32 v2, s[24:25], v10, v10, v5
	v_rcp_f32_e32 v12, v2
	v_ashrrev_i32_e32 v7, 31, v6
	v_lshlrev_b64 v[6:7], 2, v[6:7]
	v_lshl_add_u64 v[8:9], s[26:27], 0, v[6:7]
	ds_add_rtn_u32 v11, v227, v243
	global_store_dword v[8:9], v230, off
	v_fma_f32 v8, -v2, v12, 1.0
	v_fmac_f32_e32 v12, v8, v12
	v_div_scale_f32 v8, vcc, v5, v10, v5
	v_mul_f32_e32 v9, v8, v12
	v_fma_f32 v13, -v2, v9, v8
	v_fmac_f32_e32 v9, v13, v12
	v_fma_f32 v2, -v2, v9, v8
	v_div_fmas_f32 v2, v2, v12, v9
	v_div_fixup_f32 v2, v2, v10, v5
	v_mul_f32_e32 v2, 0x40200000, v2
	v_lshl_add_u64 v[8:9], s[28:29], 0, v[6:7]
	v_lshl_add_u64 v[6:7], s[30:31], 0, v[6:7]
	global_store_dword v[8:9], v2, off
	s_waitcnt lgkmcnt(0)
	global_store_dword v[6:7], v11, off
; __device__ __forceinline__ void phase_nrr(const Frame& F, const Args& a, int l, const bf16_t* XA, const float* g, const float* modl, unsigned char* XN8) {
;     ...
;         for (int i = 0; i < 8; ++i) { const int t = tb + i;
;             const float lg = Pl[(w * 8 + i) * NE + lane] + Pl[(64 + w * 8 + i) * NE + lane]; const float sc = 1.f / (1.f + __expf(-lg)); const float bb = sc + bias;
;             float m1 = bb; m1 = fmaxf(m1, __shfl_xor(m1, 1)); m1 = fmaxf(m1, __shfl_xor(m1, 2)); m1 = fmaxf(m1, __shfl_xor(m1, 4));
;             const unsigned long long eq = __ballot(bb == m1); const int gbase = lane & ~7; const unsigned grpmask = (unsigned)((eq >> gbase) & 0xffull);
;             const int first = gbase + __builtin_ctz(grpmask);
;             float m2 = (lane == first) ? -INFINITY : bb; m2 = fmaxf(m2, __shfl_xor(m2, 1)); m2 = fmaxf(m2, __shfl_xor(m2, 2)); m2 = fmaxf(m2, __shfl_xor(m2, 4));
;             const float gsum = m1 + m2; const int gq = lane >> 3;
;             int grank = 0;
; #pragma unroll
;             for (int g2 = 0; g2 < 8; ++g2) { const float v = __int_as_float(__builtin_amdgcn_readlane(__float_as_int(gsum), g2 * 8)); grank += (v > gsum || (v == gsum && g2 < gq)) ? 1 : 0; }
;             const bool keep = grank < 4; const float val = keep ? bb : -INFINITY;
;             int rank = 0;
; #pragma unroll 8
;             for (int e2 = 0; e2 < 64; ++e2) { const float v = __int_as_float(__builtin_amdgcn_readlane(__float_as_int(val), e2)); rank += (v > val || (v == val && e2 < lane)) ? 1 : 0; }
.LBB0_547:
	s_or_b64 exec, exec, s[22:23]
	v_add_u32_e32 v2, s79, v226
	ds_read_b32 v2, v2
	ds_read_b32 v5, v4 offset:17152
	s_mov_b32 s3, 0
	s_waitcnt lgkmcnt(0)
	v_add_f32_e32 v2, v2, v5
	v_mul_f32_e32 v2, 0xbfb8aa3b, v2
	v_exp_f32_e32 v2, v2
	s_nop 0
	v_add_f32_e32 v2, 1.0, v2
	v_div_scale_f32 v5, s[22:23], v2, v2, 1.0
	v_rcp_f32_e32 v6, v5
	s_nop 0
	v_fma_f32 v7, -v5, v6, 1.0
	v_fmac_f32_e32 v6, v7, v6
	v_div_scale_f32 v7, vcc, 1.0, v2, 1.0
	v_mul_f32_e32 v8, v7, v6
	v_fma_f32 v9, -v5, v8, v7
	v_fmac_f32_e32 v8, v9, v6
	v_fma_f32 v5, -v5, v8, v7
	v_div_fmas_f32 v5, v5, v6, v8
	v_div_fixup_f32 v5, v5, v2, 1.0
	v_add_f32_e32 v2, v3, v5
	s_nop 1
	s_waitcnt lgkmcnt(0)
	v_max_f32_dpp v6, v2, v2 quad_perm:[1,0,3,2] row_mask:0xf bank_mask:0xf
	s_nop 1
	s_waitcnt lgkmcnt(0)
	v_max_f32_dpp v6, v6, v6 quad_perm:[2,3,0,1] row_mask:0xf bank_mask:0xf
	s_nop 1
	s_waitcnt lgkmcnt(0)
	v_max_f32_dpp v8, v6, v6 row_half_mirror row_mask:0xf bank_mask:0xf
	v_cmp_eq_f32_e32 vcc, v2, v8
	s_nop 1
	v_lshrrev_b64 v[6:7], v200, vcc
	v_ffbl_b32_sdwa v6, v6 dst_sel:DWORD dst_unused:UNUSED_PAD src0_sel:BYTE_0
	v_add_u32_e32 v6, v6, v200
	v_cmp_ne_u32_e32 vcc, v230, v6
	s_nop 1
	v_cndmask_b32_e32 v6, v245, v2, vcc
	s_nop 1
	s_waitcnt lgkmcnt(0)
	v_max_f32_dpp v6, v6, v6 quad_perm:[1,0,3,2] row_mask:0xf bank_mask:0xf
	s_nop 1
	s_waitcnt lgkmcnt(0)
	v_max_f32_dpp v6, v6, v6 quad_perm:[2,3,0,1] row_mask:0xf bank_mask:0xf
	s_nop 1
	s_waitcnt lgkmcnt(0)
	v_max_f32_dpp v6, v6, v6 row_half_mirror row_mask:0xf bank_mask:0xf
	v_add_f32_e32 v6, v8, v6
	s_nop 0
	v_readlane_b32 s5, v6, 0
	s_nop 1
	v_cmp_eq_f32_e64 s[22:23], s5, v6
	v_cmp_gt_f32_e32 vcc, s5, v6
	s_and_b64 s[22:23], s[6:7], s[22:23]
	s_or_b64 s[22:23], vcc, s[22:23]
	v_readlane_b32 s5, v6, 8
	v_cndmask_b32_e64 v7, 0, 1, s[22:23]
	s_nop 0
	v_cmp_eq_f32_e64 s[22:23], s5, v6
	v_cmp_gt_f32_e32 vcc, s5, v6
	s_and_b64 s[22:23], s[8:9], s[22:23]
	s_or_b64 s[22:23], vcc, s[22:23]
	v_readlane_b32 s5, v6, 16
	v_cndmask_b32_e64 v8, 0, 1, s[22:23]
	s_nop 0
	v_cmp_eq_f32_e64 s[22:23], s5, v6
	v_cmp_gt_f32_e32 vcc, s5, v6
	s_and_b64 s[22:23], s[10:11], s[22:23]
	s_or_b64 s[22:23], vcc, s[22:23]
	v_readlane_b32 s5, v6, 24
	v_cndmask_b32_e64 v9, 0, 1, s[22:23]
	s_nop 0
	v_cmp_eq_f32_e64 s[22:23], s5, v6
	v_cmp_gt_f32_e32 vcc, s5, v6
	s_and_b64 s[22:23], s[12:13], s[22:23]
	s_or_b64 s[22:23], vcc, s[22:23]
	v_readlane_b32 s5, v6, 32
	v_cndmask_b32_e64 v10, 0, 1, s[22:23]
	s_nop 0
	v_cmp_eq_f32_e64 s[22:23], s5, v6
	v_cmp_gt_f32_e32 vcc, s5, v6
	s_and_b64 s[22:23], s[14:15], s[22:23]
	s_or_b64 s[22:23], vcc, s[22:23]
	v_readlane_b32 s5, v6, 40
	v_cndmask_b32_e64 v11, 0, 1, s[22:23]
	s_nop 0
	v_cmp_eq_f32_e64 s[22:23], s5, v6
	v_cmp_gt_f32_e32 vcc, s5, v6
	s_and_b64 s[22:23], s[16:17], s[22:23]
	s_or_b64 s[22:23], vcc, s[22:23]
	v_readlane_b32 s5, v6, 48
	v_cndmask_b32_e64 v12, 0, 1, s[22:23]
	s_nop 0
	v_cmp_eq_f32_e64 s[22:23], s5, v6
	v_cmp_gt_f32_e32 vcc, s5, v6
	s_and_b64 s[22:23], s[18:19], s[22:23]
	v_readlane_b32 s5, v6, 56
	s_or_b64 s[22:23], vcc, s[22:23]
	v_cndmask_b32_e64 v13, 0, 1, s[22:23]
	v_cmp_gt_f32_e32 vcc, s5, v6
	s_nop 1
	v_cndmask_b32_e64 v6, 0, 1, vcc
	v_add_u32_e32 v6, v8, v6
	v_add3_u32 v6, v6, v7, v9
	v_add3_u32 v6, v6, v10, v11
	v_add3_u32 v6, v6, v12, v13
	v_cmp_gt_u32_e32 vcc, 4, v6
	s_nop 1
	v_cndmask_b32_e32 v6, v245, v2, vcc
	v_mov_b32_e32 v2, 0
	v_ashrrev_i32_e32 v9, 31, v6
	v_sub_u32_e32 v8, 63, v230
	v_and_b32_e32 v9, 0x7fffffff, v9
	v_xor_b32_e32 v9, v6, v9
	s_nop 0
	v_readlane_b32 s25, v9, 0
	s_movk_i32 s24, 63
	v_readlane_b32 s23, v9, 1
	s_movk_i32 s22, 62
	v_cmp_gt_i64_e32 vcc, s[24:25], v[8:9]
	v_readlane_b32 s25, v9, 2
	s_movk_i32 s24, 61
	v_addc_co_u32_e32 v2, vcc, 0, v2, vcc
	v_cmp_gt_i64_e32 vcc, s[22:23], v[8:9]
	v_readlane_b32 s23, v9, 3
	s_movk_i32 s22, 60
	v_addc_co_u32_e32 v2, vcc, 0, v2, vcc
	v_cmp_gt_i64_e32 vcc, s[24:25], v[8:9]
	v_readlane_b32 s25, v9, 4
	s_movk_i32 s24, 59
	v_addc_co_u32_e32 v2, vcc, 0, v2, vcc
	v_cmp_gt_i64_e32 vcc, s[22:23], v[8:9]
	v_readlane_b32 s23, v9, 5
	s_movk_i32 s22, 58
	v_addc_co_u32_e32 v2, vcc, 0, v2, vcc
	v_cmp_gt_i64_e32 vcc, s[24:25], v[8:9]
	v_readlane_b32 s25, v9, 6
	s_movk_i32 s24, 57
	v_addc_co_u32_e32 v2, vcc, 0, v2, vcc
	v_cmp_gt_i64_e32 vcc, s[22:23], v[8:9]
	v_readlane_b32 s23, v9, 7
	s_movk_i32 s22, 56
	v_addc_co_u32_e32 v2, vcc, 0, v2, vcc
	v_cmp_gt_i64_e32 vcc, s[24:25], v[8:9]
	v_readlane_b32 s25, v9, 8
	s_movk_i32 s24, 55
	v_addc_co_u32_e32 v2, vcc, 0, v2, vcc
	v_cmp_gt_i64_e32 vcc, s[22:23], v[8:9]
	v_readlane_b32 s23, v9, 9
	s_movk_i32 s22, 54
	v_addc_co_u32_e32 v2, vcc, 0, v2, vcc
	v_cmp_gt_i64_e32 vcc, s[24:25], v[8:9]
	v_readlane_b32 s25, v9, 10
	s_movk_i32 s24, 53
	v_addc_co_u32_e32 v2, vcc, 0, v2, vcc
	v_cmp_gt_i64_e32 vcc, s[22:23], v[8:9]
	v_readlane_b32 s23, v9, 11
	s_movk_i32 s22, 52
	v_addc_co_u32_e32 v2, vcc, 0, v2, vcc
	v_cmp_gt_i64_e32 vcc, s[24:25], v[8:9]
	v_readlane_b32 s25, v9, 12
	s_movk_i32 s24, 51
	v_addc_co_u32_e32 v2, vcc, 0, v2, vcc
	v_cmp_gt_i64_e32 vcc, s[22:23], v[8:9]
	v_readlane_b32 s23, v9, 13
	s_movk_i32 s22, 50
	v_addc_co_u32_e32 v2, vcc, 0, v2, vcc
	v_cmp_gt_i64_e32 vcc, s[24:25], v[8:9]
	v_readlane_b32 s25, v9, 14
	s_movk_i32 s24, 49
	v_addc_co_u32_e32 v2, vcc, 0, v2, vcc
	v_cmp_gt_i64_e32 vcc, s[22:23], v[8:9]
	v_readlane_b32 s23, v9, 15
	s_movk_i32 s22, 48
	v_addc_co_u32_e32 v2, vcc, 0, v2, vcc
	v_cmp_gt_i64_e32 vcc, s[24:25], v[8:9]
	v_readlane_b32 s25, v9, 16
	s_movk_i32 s24, 47
	v_addc_co_u32_e32 v2, vcc, 0, v2, vcc
	v_cmp_gt_i64_e32 vcc, s[22:23], v[8:9]
	v_readlane_b32 s23, v9, 17
	s_movk_i32 s22, 46
	v_addc_co_u32_e32 v2, vcc, 0, v2, vcc
	v_cmp_gt_i64_e32 vcc, s[24:25], v[8:9]
; __device__ __forceinline__ float wave_sum(float v) {
; #pragma unroll
;     for (int o = 1; o < 64; o <<= 1) v += __shfl_xor(v, o);
;     return v;
; __device__ __forceinline__ void phase_nrr(const Frame& F, const Args& a, int l, const bf16_t* XA, const float* g, const float* modl, unsigned char* XN8) {
;     ...
;             int rank = 0;
; #pragma unroll 8
;             for (int e2 = 0; e2 < 64; ++e2) { const float v = __int_as_float(__builtin_amdgcn_readlane(__float_as_int(val), e2)); rank += (v > val || (v == val && e2 < lane)) ? 1 : 0; }
;             const bool sel = rank < TOPK;
;             const float ssum = wave_sum(sel ? sc : 0.f);
;             if (sel) { const int p = atomicAdd((int*)(hist + lane), 1); top_e[t * TOPK + rank] = lane; gate[t * TOPK + rank] = sc / ssum * 2.5f; lpos[t * TOPK + rank] = p; }
	v_readlane_b32 s25, v9, 18
	s_movk_i32 s24, 45
	v_addc_co_u32_e32 v2, vcc, 0, v2, vcc
	v_cmp_gt_i64_e32 vcc, s[22:23], v[8:9]
	v_readlane_b32 s23, v9, 19
	s_movk_i32 s22, 44
	v_addc_co_u32_e32 v2, vcc, 0, v2, vcc
	v_cmp_gt_i64_e32 vcc, s[24:25], v[8:9]
	v_readlane_b32 s25, v9, 20
	s_movk_i32 s24, 43
	v_addc_co_u32_e32 v2, vcc, 0, v2, vcc
	v_cmp_gt_i64_e32 vcc, s[22:23], v[8:9]
	v_readlane_b32 s23, v9, 21
	s_movk_i32 s22, 42
	v_addc_co_u32_e32 v2, vcc, 0, v2, vcc
	v_cmp_gt_i64_e32 vcc, s[24:25], v[8:9]
	v_readlane_b32 s25, v9, 22
	s_movk_i32 s24, 41
	v_addc_co_u32_e32 v2, vcc, 0, v2, vcc
	v_cmp_gt_i64_e32 vcc, s[22:23], v[8:9]
	v_readlane_b32 s23, v9, 23
	s_movk_i32 s22, 40
	v_addc_co_u32_e32 v2, vcc, 0, v2, vcc
	v_cmp_gt_i64_e32 vcc, s[24:25], v[8:9]
	v_readlane_b32 s25, v9, 24
	s_movk_i32 s24, 39
	v_addc_co_u32_e32 v2, vcc, 0, v2, vcc
	v_cmp_gt_i64_e32 vcc, s[22:23], v[8:9]
	v_readlane_b32 s23, v9, 25
	s_movk_i32 s22, 38
	v_addc_co_u32_e32 v2, vcc, 0, v2, vcc
	v_cmp_gt_i64_e32 vcc, s[24:25], v[8:9]
	v_readlane_b32 s25, v9, 26
	s_movk_i32 s24, 37
	v_addc_co_u32_e32 v2, vcc, 0, v2, vcc
	v_cmp_gt_i64_e32 vcc, s[22:23], v[8:9]
	v_readlane_b32 s23, v9, 27
	s_movk_i32 s22, 36
	v_addc_co_u32_e32 v2, vcc, 0, v2, vcc
	v_cmp_gt_i64_e32 vcc, s[24:25], v[8:9]
	v_readlane_b32 s25, v9, 28
	s_movk_i32 s24, 35
	v_addc_co_u32_e32 v2, vcc, 0, v2, vcc
	v_cmp_gt_i64_e32 vcc, s[22:23], v[8:9]
	v_readlane_b32 s23, v9, 29
	s_movk_i32 s22, 34
	v_addc_co_u32_e32 v2, vcc, 0, v2, vcc
	v_cmp_gt_i64_e32 vcc, s[24:25], v[8:9]
	v_readlane_b32 s25, v9, 30
	s_movk_i32 s24, 33
	v_addc_co_u32_e32 v2, vcc, 0, v2, vcc
	v_cmp_gt_i64_e32 vcc, s[22:23], v[8:9]
	v_readlane_b32 s23, v9, 31
	s_movk_i32 s22, 32
	v_addc_co_u32_e32 v2, vcc, 0, v2, vcc
	v_cmp_gt_i64_e32 vcc, s[24:25], v[8:9]
	v_readlane_b32 s25, v9, 32
	s_movk_i32 s24, 31
	v_addc_co_u32_e32 v2, vcc, 0, v2, vcc
	v_cmp_gt_i64_e32 vcc, s[22:23], v[8:9]
	v_readlane_b32 s23, v9, 33
	s_movk_i32 s22, 30
	v_addc_co_u32_e32 v2, vcc, 0, v2, vcc
	v_cmp_gt_i64_e32 vcc, s[24:25], v[8:9]
	v_readlane_b32 s25, v9, 34
	s_movk_i32 s24, 29
	v_addc_co_u32_e32 v2, vcc, 0, v2, vcc
	v_cmp_gt_i64_e32 vcc, s[22:23], v[8:9]
	v_readlane_b32 s23, v9, 35
	s_movk_i32 s22, 28
	v_addc_co_u32_e32 v2, vcc, 0, v2, vcc
	v_cmp_gt_i64_e32 vcc, s[24:25], v[8:9]
	v_readlane_b32 s25, v9, 36
	s_movk_i32 s24, 27
	v_addc_co_u32_e32 v2, vcc, 0, v2, vcc
	v_cmp_gt_i64_e32 vcc, s[22:23], v[8:9]
	v_readlane_b32 s23, v9, 37
	s_movk_i32 s22, 26
	v_addc_co_u32_e32 v2, vcc, 0, v2, vcc
	v_cmp_gt_i64_e32 vcc, s[24:25], v[8:9]
	v_readlane_b32 s25, v9, 38
	s_movk_i32 s24, 25
	v_addc_co_u32_e32 v2, vcc, 0, v2, vcc
	v_cmp_gt_i64_e32 vcc, s[22:23], v[8:9]
	v_readlane_b32 s23, v9, 39
	s_movk_i32 s22, 24
	v_addc_co_u32_e32 v2, vcc, 0, v2, vcc
	v_cmp_gt_i64_e32 vcc, s[24:25], v[8:9]
	v_readlane_b32 s25, v9, 40
	s_movk_i32 s24, 23
	v_addc_co_u32_e32 v2, vcc, 0, v2, vcc
	v_cmp_gt_i64_e32 vcc, s[22:23], v[8:9]
	v_readlane_b32 s23, v9, 41
	s_movk_i32 s22, 22
	v_addc_co_u32_e32 v2, vcc, 0, v2, vcc
	v_cmp_gt_i64_e32 vcc, s[24:25], v[8:9]
	v_readlane_b32 s25, v9, 42
	s_movk_i32 s24, 21
	v_addc_co_u32_e32 v2, vcc, 0, v2, vcc
	v_cmp_gt_i64_e32 vcc, s[22:23], v[8:9]
	v_readlane_b32 s23, v9, 43
	s_movk_i32 s22, 20
	v_addc_co_u32_e32 v2, vcc, 0, v2, vcc
	v_cmp_gt_i64_e32 vcc, s[24:25], v[8:9]
	v_readlane_b32 s25, v9, 44
	s_movk_i32 s24, 19
	v_addc_co_u32_e32 v2, vcc, 0, v2, vcc
	v_cmp_gt_i64_e32 vcc, s[22:23], v[8:9]
	v_readlane_b32 s23, v9, 45
	s_movk_i32 s22, 18
	v_addc_co_u32_e32 v2, vcc, 0, v2, vcc
	v_cmp_gt_i64_e32 vcc, s[24:25], v[8:9]
	v_readlane_b32 s25, v9, 46
	s_movk_i32 s24, 17
	v_addc_co_u32_e32 v2, vcc, 0, v2, vcc
	v_cmp_gt_i64_e32 vcc, s[22:23], v[8:9]
	v_readlane_b32 s23, v9, 47
	s_movk_i32 s22, 16
	v_addc_co_u32_e32 v2, vcc, 0, v2, vcc
	v_cmp_gt_i64_e32 vcc, s[24:25], v[8:9]
	v_readlane_b32 s25, v9, 48
	s_movk_i32 s24, 15
	v_addc_co_u32_e32 v2, vcc, 0, v2, vcc
	v_cmp_gt_i64_e32 vcc, s[22:23], v[8:9]
	v_readlane_b32 s23, v9, 49
	s_movk_i32 s22, 14
	v_addc_co_u32_e32 v2, vcc, 0, v2, vcc
	v_cmp_gt_i64_e32 vcc, s[24:25], v[8:9]
	v_readlane_b32 s25, v9, 50
	s_movk_i32 s24, 13
	v_addc_co_u32_e32 v2, vcc, 0, v2, vcc
	v_cmp_gt_i64_e32 vcc, s[22:23], v[8:9]
	v_readlane_b32 s23, v9, 51
	s_movk_i32 s22, 12
	v_addc_co_u32_e32 v2, vcc, 0, v2, vcc
	v_cmp_gt_i64_e32 vcc, s[24:25], v[8:9]
	v_readlane_b32 s25, v9, 52
	s_movk_i32 s24, 11
	v_addc_co_u32_e32 v2, vcc, 0, v2, vcc
	v_cmp_gt_i64_e32 vcc, s[22:23], v[8:9]
	v_readlane_b32 s23, v9, 53
	s_movk_i32 s22, 10
	v_addc_co_u32_e32 v2, vcc, 0, v2, vcc
	v_cmp_gt_i64_e32 vcc, s[24:25], v[8:9]
	v_readlane_b32 s25, v9, 54
	s_movk_i32 s24, 9
	v_addc_co_u32_e32 v2, vcc, 0, v2, vcc
	v_cmp_gt_i64_e32 vcc, s[22:23], v[8:9]
	v_readlane_b32 s23, v9, 55
	s_movk_i32 s22, 8
	v_addc_co_u32_e32 v2, vcc, 0, v2, vcc
	v_cmp_gt_i64_e32 vcc, s[24:25], v[8:9]
	v_readlane_b32 s25, v9, 56
	s_movk_i32 s24, 7
	v_addc_co_u32_e32 v2, vcc, 0, v2, vcc
	v_cmp_gt_i64_e32 vcc, s[22:23], v[8:9]
	v_readlane_b32 s23, v9, 57
	s_movk_i32 s22, 6
	v_addc_co_u32_e32 v2, vcc, 0, v2, vcc
	v_cmp_gt_i64_e32 vcc, s[24:25], v[8:9]
	v_readlane_b32 s25, v9, 58
	s_movk_i32 s24, 5
	v_addc_co_u32_e32 v2, vcc, 0, v2, vcc
	v_cmp_gt_i64_e32 vcc, s[22:23], v[8:9]
	v_readlane_b32 s23, v9, 59
	s_movk_i32 s22, 4
	v_addc_co_u32_e32 v2, vcc, 0, v2, vcc
	v_cmp_gt_i64_e32 vcc, s[24:25], v[8:9]
	v_readlane_b32 s25, v9, 60
	s_movk_i32 s24, 3
	v_addc_co_u32_e32 v2, vcc, 0, v2, vcc
	v_cmp_gt_i64_e32 vcc, s[22:23], v[8:9]
	v_readlane_b32 s23, v9, 61
	s_movk_i32 s22, 2
	v_addc_co_u32_e32 v2, vcc, 0, v2, vcc
	v_cmp_gt_i64_e32 vcc, s[24:25], v[8:9]
	v_readlane_b32 s25, v9, 62
	s_movk_i32 s24, 1
	v_addc_co_u32_e32 v2, vcc, 0, v2, vcc
	v_cmp_gt_i64_e32 vcc, s[22:23], v[8:9]
	v_readlane_b32 s23, v9, 63
	s_movk_i32 s22, 0
	v_addc_co_u32_e32 v2, vcc, 0, v2, vcc
	v_cmp_gt_i64_e32 vcc, s[24:25], v[8:9]
	s_nop 1
	v_addc_co_u32_e32 v2, vcc, 0, v2, vcc
	v_cmp_gt_i64_e32 vcc, s[22:23], v[8:9]
	s_nop 1
	v_addc_co_u32_e32 v2, vcc, 0, v2, vcc
	v_cmp_gt_u32_e32 vcc, 6, v2
	s_nop 1
	v_cndmask_b32_e32 v6, 0, v5, vcc
	s_nop 1
	v_add_f32_dpp v6, v6, v6 quad_perm:[1,0,3,2] row_mask:0xf bank_mask:0xf
	s_nop 1
	v_add_f32_dpp v6, v6, v6 quad_perm:[2,3,0,1] row_mask:0xf bank_mask:0xf
	s_nop 1
	v_add_f32_dpp v6, v6, v6 row_half_mirror row_mask:0xf bank_mask:0xf
	s_nop 1
	v_add_f32_dpp v6, v6, v6 row_mirror row_mask:0xf bank_mask:0xf
	s_nop 0
	ds_bpermute_b32 v7, v222, v6
	s_waitcnt lgkmcnt(0)
	v_add_f32_e32 v6, v6, v7
	v_mov_b32_e32 v7, v6
	s_nop 1
	v_permlane32_swap_b32_e32 v7, v6
	s_and_saveexec_b64 s[22:23], vcc
	s_cbranch_execz .LBB0_551
; __device__ __forceinline__ void phase_nrr(const Frame& F, const Args& a, int l, const bf16_t* XA, const float* g, const float* modl, unsigned char* XN8) {
;     ...
;         for (int i = 0; i < 8; ++i) { const int t = tb + i;
;             const float lg = Pl[(w * 8 + i) * NE + lane] + Pl[(64 + w * 8 + i) * NE + lane]; const float sc = 1.f / (1.f + __expf(-lg)); const float bb = sc + bias;
;             float m1 = bb; m1 = fmaxf(m1, __shfl_xor(m1, 1)); m1 = fmaxf(m1, __shfl_xor(m1, 2)); m1 = fmaxf(m1, __shfl_xor(m1, 4));
;             const unsigned long long eq = __ballot(bb == m1); const int gbase = lane & ~7; const unsigned grpmask = (unsigned)((eq >> gbase) & 0xffull);
;             const int first = gbase + __builtin_ctz(grpmask);
;             float m2 = (lane == first) ? -INFINITY : bb; m2 = fmaxf(m2, __shfl_xor(m2, 1)); m2 = fmaxf(m2, __shfl_xor(m2, 2)); m2 = fmaxf(m2, __shfl_xor(m2, 4));
;             const float gsum = m1 + m2; const int gq = lane >> 3;
;             int grank = 0;
; #pragma unroll
;             for (int g2 = 0; g2 < 8; ++g2) { const float v = __int_as_float(__builtin_amdgcn_readlane(__float_as_int(gsum), g2 * 8)); grank += (v > gsum || (v == gsum && g2 < gq)) ? 1 : 0; }
;             const bool keep = grank < 4; const float val = keep ? bb : -INFINITY;
;             int rank = 0;
; #pragma unroll 8
;             for (int e2 = 0; e2 < 64; ++e2) { const float v = __int_as_float(__builtin_amdgcn_readlane(__float_as_int(val), e2)); rank += (v > val || (v == val && e2 < lane)) ? 1 : 0; }
;     ...
;             if (sel) { const int p = atomicAdd((int*)(hist + lane), 1); top_e[t * TOPK + rank] = lane; gate[t * TOPK + rank] = sc / ssum * 2.5f; lpos[t * TOPK + rank] = p; }
	s_waitcnt lgkmcnt(0)
	v_add_f32_e32 v10, v6, v7
	v_mad_u64_u32 v[6:7], s[4:5], s4, 6, v[2:3]
	v_div_scale_f32 v2, s[4:5], v10, v10, v5
	v_rcp_f32_e32 v12, v2
	v_ashrrev_i32_e32 v7, 31, v6
	v_lshlrev_b64 v[6:7], 2, v[6:7]
	v_lshl_add_u64 v[8:9], s[26:27], 0, v[6:7]
	ds_add_rtn_u32 v11, v227, v243
	global_store_dword v[8:9], v230, off
	v_fma_f32 v8, -v2, v12, 1.0
	v_fmac_f32_e32 v12, v8, v12
	v_div_scale_f32 v8, vcc, v5, v10, v5
	v_mul_f32_e32 v9, v8, v12
	v_fma_f32 v13, -v2, v9, v8
	v_fmac_f32_e32 v9, v13, v12
	v_fma_f32 v2, -v2, v9, v8
	v_div_fmas_f32 v2, v2, v12, v9
	v_div_fixup_f32 v2, v2, v10, v5
	v_mul_f32_e32 v2, 0x40200000, v2
	v_lshl_add_u64 v[8:9], s[28:29], 0, v[6:7]
	v_lshl_add_u64 v[6:7], s[30:31], 0, v[6:7]
	global_store_dword v[8:9], v2, off
	s_waitcnt lgkmcnt(0)
	global_store_dword v[6:7], v11, off
.LBB0_551:
	s_or_b64 exec, exec, s[22:23]
	v_add_u32_e32 v2, s84, v226
	ds_read_b32 v2, v2
	ds_read_b32 v5, v4 offset:17408
	s_mov_b32 s3, 0
	s_waitcnt lgkmcnt(0)
	v_add_f32_e32 v2, v2, v5
	v_mul_f32_e32 v2, 0xbfb8aa3b, v2
	v_exp_f32_e32 v2, v2
	s_nop 0
	v_add_f32_e32 v2, 1.0, v2
	v_div_scale_f32 v5, s[4:5], v2, v2, 1.0
	v_rcp_f32_e32 v6, v5
	s_nop 0
	v_fma_f32 v7, -v5, v6, 1.0
	v_fmac_f32_e32 v6, v7, v6
	v_div_scale_f32 v7, vcc, 1.0, v2, 1.0
	v_mul_f32_e32 v8, v7, v6
	v_fma_f32 v9, -v5, v8, v7
	v_fmac_f32_e32 v8, v9, v6
	v_fma_f32 v5, -v5, v8, v7
	v_div_fmas_f32 v5, v5, v6, v8
	v_div_fixup_f32 v2, v5, v2, 1.0
	v_add_f32_e32 v5, v3, v2
	s_nop 1
	s_waitcnt lgkmcnt(0)
	v_max_f32_dpp v6, v5, v5 quad_perm:[1,0,3,2] row_mask:0xf bank_mask:0xf
	s_nop 1
	s_waitcnt lgkmcnt(0)
	v_max_f32_dpp v6, v6, v6 quad_perm:[2,3,0,1] row_mask:0xf bank_mask:0xf
	s_nop 1
	s_waitcnt lgkmcnt(0)
	v_max_f32_dpp v8, v6, v6 row_half_mirror row_mask:0xf bank_mask:0xf
	v_cmp_eq_f32_e32 vcc, v5, v8
	s_nop 1
	v_lshrrev_b64 v[6:7], v200, vcc
	v_ffbl_b32_sdwa v6, v6 dst_sel:DWORD dst_unused:UNUSED_PAD src0_sel:BYTE_0
	v_add_u32_e32 v6, v6, v200
	v_cmp_ne_u32_e32 vcc, v230, v6
	s_nop 1
	v_cndmask_b32_e32 v6, v245, v5, vcc
	s_nop 1
	s_waitcnt lgkmcnt(0)
	v_max_f32_dpp v6, v6, v6 quad_perm:[1,0,3,2] row_mask:0xf bank_mask:0xf
	s_nop 1
	s_waitcnt lgkmcnt(0)
	v_max_f32_dpp v6, v6, v6 quad_perm:[2,3,0,1] row_mask:0xf bank_mask:0xf
	s_nop 1
	s_waitcnt lgkmcnt(0)
	v_max_f32_dpp v6, v6, v6 row_half_mirror row_mask:0xf bank_mask:0xf
	v_add_f32_e32 v6, v8, v6
	s_nop 0
	v_readlane_b32 s4, v6, 0
	s_nop 1
	v_cmp_eq_f32_e64 s[22:23], s4, v6
	v_cmp_gt_f32_e32 vcc, s4, v6
	s_and_b64 s[4:5], s[6:7], s[22:23]
	s_or_b64 s[4:5], vcc, s[4:5]
	v_cndmask_b32_e64 v7, 0, 1, s[4:5]
	v_readlane_b32 s4, v6, 8
	s_nop 1
	v_cmp_eq_f32_e64 s[22:23], s4, v6
	v_cmp_gt_f32_e32 vcc, s4, v6
	s_and_b64 s[4:5], s[8:9], s[22:23]
	s_or_b64 s[4:5], vcc, s[4:5]
	v_cndmask_b32_e64 v8, 0, 1, s[4:5]
	v_readlane_b32 s4, v6, 16
	s_nop 1
	v_cmp_eq_f32_e64 s[22:23], s4, v6
	v_cmp_gt_f32_e32 vcc, s4, v6
	s_and_b64 s[4:5], s[10:11], s[22:23]
	s_or_b64 s[4:5], vcc, s[4:5]
	v_cndmask_b32_e64 v9, 0, 1, s[4:5]
	v_readlane_b32 s4, v6, 24
	s_nop 1
	v_cmp_eq_f32_e64 s[22:23], s4, v6
	v_cmp_gt_f32_e32 vcc, s4, v6
	s_and_b64 s[4:5], s[12:13], s[22:23]
	s_or_b64 s[4:5], vcc, s[4:5]
	v_cndmask_b32_e64 v10, 0, 1, s[4:5]
	v_readlane_b32 s4, v6, 32
	s_nop 1
	v_cmp_eq_f32_e64 s[22:23], s4, v6
	v_cmp_gt_f32_e32 vcc, s4, v6
	s_and_b64 s[4:5], s[14:15], s[22:23]
	s_or_b64 s[4:5], vcc, s[4:5]
	v_cndmask_b32_e64 v11, 0, 1, s[4:5]
	v_readlane_b32 s4, v6, 40
	s_nop 1
	v_cmp_eq_f32_e64 s[22:23], s4, v6
	v_cmp_gt_f32_e32 vcc, s4, v6
	s_and_b64 s[4:5], s[16:17], s[22:23]
	s_or_b64 s[4:5], vcc, s[4:5]
	v_cndmask_b32_e64 v12, 0, 1, s[4:5]
	v_readlane_b32 s4, v6, 48
	s_nop 1
	v_cmp_eq_f32_e64 s[22:23], s4, v6
	v_cmp_gt_f32_e32 vcc, s4, v6
	s_and_b64 s[4:5], s[18:19], s[22:23]
	s_or_b64 s[4:5], vcc, s[4:5]
	v_cndmask_b32_e64 v13, 0, 1, s[4:5]
	v_readlane_b32 s4, v6, 56
	s_nop 1
	v_cmp_gt_f32_e32 vcc, s4, v6
	s_nop 1
	v_cndmask_b32_e64 v6, 0, 1, vcc
	v_add_u32_e32 v6, v8, v6
	v_add3_u32 v6, v6, v7, v9
	v_add3_u32 v6, v6, v10, v11
	v_add3_u32 v6, v6, v12, v13
	v_cmp_gt_u32_e32 vcc, 4, v6
	v_mov_b32_e32 v6, 0
	s_nop 0
	v_cndmask_b32_e32 v5, v245, v5, vcc
	v_ashrrev_i32_e32 v9, 31, v5
	v_sub_u32_e32 v8, 63, v230
	v_and_b32_e32 v9, 0x7fffffff, v9
	v_xor_b32_e32 v9, v5, v9
	s_nop 0
	v_readlane_b32 s25, v9, 0
	s_movk_i32 s24, 63
	v_readlane_b32 s23, v9, 1
	s_movk_i32 s22, 62
	v_cmp_gt_i64_e32 vcc, s[24:25], v[8:9]
	v_readlane_b32 s25, v9, 2
	s_movk_i32 s24, 61
	v_addc_co_u32_e32 v6, vcc, 0, v6, vcc
	v_cmp_gt_i64_e32 vcc, s[22:23], v[8:9]
	v_readlane_b32 s23, v9, 3
	s_movk_i32 s22, 60
	v_addc_co_u32_e32 v6, vcc, 0, v6, vcc
	v_cmp_gt_i64_e32 vcc, s[24:25], v[8:9]
	v_readlane_b32 s25, v9, 4
	s_movk_i32 s24, 59
	v_addc_co_u32_e32 v6, vcc, 0, v6, vcc
	v_cmp_gt_i64_e32 vcc, s[22:23], v[8:9]
	v_readlane_b32 s23, v9, 5
	s_movk_i32 s22, 58
	v_addc_co_u32_e32 v6, vcc, 0, v6, vcc
	v_cmp_gt_i64_e32 vcc, s[24:25], v[8:9]
	v_readlane_b32 s25, v9, 6
	s_movk_i32 s24, 57
	v_addc_co_u32_e32 v6, vcc, 0, v6, vcc
	v_cmp_gt_i64_e32 vcc, s[22:23], v[8:9]
	v_readlane_b32 s23, v9, 7
	s_movk_i32 s22, 56
	v_addc_co_u32_e32 v6, vcc, 0, v6, vcc
	v_cmp_gt_i64_e32 vcc, s[24:25], v[8:9]
	v_readlane_b32 s25, v9, 8
	s_movk_i32 s24, 55
	v_addc_co_u32_e32 v6, vcc, 0, v6, vcc
	v_cmp_gt_i64_e32 vcc, s[22:23], v[8:9]
	v_readlane_b32 s23, v9, 9
	s_movk_i32 s22, 54
	v_addc_co_u32_e32 v6, vcc, 0, v6, vcc
	v_cmp_gt_i64_e32 vcc, s[24:25], v[8:9]
	v_readlane_b32 s25, v9, 10
	s_movk_i32 s24, 53
	v_addc_co_u32_e32 v6, vcc, 0, v6, vcc
	v_cmp_gt_i64_e32 vcc, s[22:23], v[8:9]
	v_readlane_b32 s23, v9, 11
	s_movk_i32 s22, 52
	v_addc_co_u32_e32 v6, vcc, 0, v6, vcc
	v_cmp_gt_i64_e32 vcc, s[24:25], v[8:9]
; __device__ __forceinline__ void phase_nrr(const Frame& F, const Args& a, int l, const bf16_t* XA, const float* g, const float* modl, unsigned char* XN8) {
;     ...
;             int rank = 0;
; #pragma unroll 8
;             for (int e2 = 0; e2 < 64; ++e2) { const float v = __int_as_float(__builtin_amdgcn_readlane(__float_as_int(val), e2)); rank += (v > val || (v == val && e2 < lane)) ? 1 : 0; }
	v_readlane_b32 s25, v9, 12
	s_movk_i32 s24, 51
	v_addc_co_u32_e32 v6, vcc, 0, v6, vcc
	v_cmp_gt_i64_e32 vcc, s[22:23], v[8:9]
	v_readlane_b32 s23, v9, 13
	s_movk_i32 s22, 50
	v_addc_co_u32_e32 v6, vcc, 0, v6, vcc
	v_cmp_gt_i64_e32 vcc, s[24:25], v[8:9]
	v_readlane_b32 s25, v9, 14
	s_movk_i32 s24, 49
	v_addc_co_u32_e32 v6, vcc, 0, v6, vcc
	v_cmp_gt_i64_e32 vcc, s[22:23], v[8:9]
	v_readlane_b32 s23, v9, 15
	s_movk_i32 s22, 48
	v_addc_co_u32_e32 v6, vcc, 0, v6, vcc
	v_cmp_gt_i64_e32 vcc, s[24:25], v[8:9]
	v_readlane_b32 s25, v9, 16
	s_movk_i32 s24, 47
	v_addc_co_u32_e32 v6, vcc, 0, v6, vcc
	v_cmp_gt_i64_e32 vcc, s[22:23], v[8:9]
	v_readlane_b32 s23, v9, 17
	s_movk_i32 s22, 46
	v_addc_co_u32_e32 v6, vcc, 0, v6, vcc
	v_cmp_gt_i64_e32 vcc, s[24:25], v[8:9]
	v_readlane_b32 s25, v9, 18
	s_movk_i32 s24, 45
	v_addc_co_u32_e32 v6, vcc, 0, v6, vcc
	v_cmp_gt_i64_e32 vcc, s[22:23], v[8:9]
	v_readlane_b32 s23, v9, 19
	s_movk_i32 s22, 44
	v_addc_co_u32_e32 v6, vcc, 0, v6, vcc
	v_cmp_gt_i64_e32 vcc, s[24:25], v[8:9]
	v_readlane_b32 s25, v9, 20
	s_movk_i32 s24, 43
	v_addc_co_u32_e32 v6, vcc, 0, v6, vcc
	v_cmp_gt_i64_e32 vcc, s[22:23], v[8:9]
	v_readlane_b32 s23, v9, 21
	s_movk_i32 s22, 42
	v_addc_co_u32_e32 v6, vcc, 0, v6, vcc
	v_cmp_gt_i64_e32 vcc, s[24:25], v[8:9]
	v_readlane_b32 s25, v9, 22
	s_movk_i32 s24, 41
	v_addc_co_u32_e32 v6, vcc, 0, v6, vcc
	v_cmp_gt_i64_e32 vcc, s[22:23], v[8:9]
	v_readlane_b32 s23, v9, 23
	s_movk_i32 s22, 40
	v_addc_co_u32_e32 v6, vcc, 0, v6, vcc
	v_cmp_gt_i64_e32 vcc, s[24:25], v[8:9]
	v_readlane_b32 s25, v9, 24
	s_movk_i32 s24, 39
	v_addc_co_u32_e32 v6, vcc, 0, v6, vcc
	v_cmp_gt_i64_e32 vcc, s[22:23], v[8:9]
	v_readlane_b32 s23, v9, 25
	s_movk_i32 s22, 38
	v_addc_co_u32_e32 v6, vcc, 0, v6, vcc
	v_cmp_gt_i64_e32 vcc, s[24:25], v[8:9]
	v_readlane_b32 s25, v9, 26
	s_movk_i32 s24, 37
	v_addc_co_u32_e32 v6, vcc, 0, v6, vcc
	v_cmp_gt_i64_e32 vcc, s[22:23], v[8:9]
	v_readlane_b32 s23, v9, 27
	s_movk_i32 s22, 36
	v_addc_co_u32_e32 v6, vcc, 0, v6, vcc
	v_cmp_gt_i64_e32 vcc, s[24:25], v[8:9]
	v_readlane_b32 s25, v9, 28
	s_movk_i32 s24, 35
	v_addc_co_u32_e32 v6, vcc, 0, v6, vcc
	v_cmp_gt_i64_e32 vcc, s[22:23], v[8:9]
	v_readlane_b32 s23, v9, 29
	s_movk_i32 s22, 34
	v_addc_co_u32_e32 v6, vcc, 0, v6, vcc
	v_cmp_gt_i64_e32 vcc, s[24:25], v[8:9]
	v_readlane_b32 s25, v9, 30
	s_movk_i32 s24, 33
	v_addc_co_u32_e32 v6, vcc, 0, v6, vcc
	v_cmp_gt_i64_e32 vcc, s[22:23], v[8:9]
	v_readlane_b32 s23, v9, 31
	s_movk_i32 s22, 32
	v_addc_co_u32_e32 v6, vcc, 0, v6, vcc
	v_cmp_gt_i64_e32 vcc, s[24:25], v[8:9]
	v_readlane_b32 s25, v9, 32
	s_movk_i32 s24, 31
	v_addc_co_u32_e32 v6, vcc, 0, v6, vcc
	v_cmp_gt_i64_e32 vcc, s[22:23], v[8:9]
	v_readlane_b32 s23, v9, 33
	s_movk_i32 s22, 30
	v_addc_co_u32_e32 v6, vcc, 0, v6, vcc
	v_cmp_gt_i64_e32 vcc, s[24:25], v[8:9]
	v_readlane_b32 s25, v9, 34
	s_movk_i32 s24, 29
	v_addc_co_u32_e32 v6, vcc, 0, v6, vcc
	v_cmp_gt_i64_e32 vcc, s[22:23], v[8:9]
	v_readlane_b32 s23, v9, 35
	s_movk_i32 s22, 28
	v_addc_co_u32_e32 v6, vcc, 0, v6, vcc
	v_cmp_gt_i64_e32 vcc, s[24:25], v[8:9]
	v_readlane_b32 s25, v9, 36
	s_movk_i32 s24, 27
	v_addc_co_u32_e32 v6, vcc, 0, v6, vcc
	v_cmp_gt_i64_e32 vcc, s[22:23], v[8:9]
	v_readlane_b32 s23, v9, 37
	s_movk_i32 s22, 26
	v_addc_co_u32_e32 v6, vcc, 0, v6, vcc
	v_cmp_gt_i64_e32 vcc, s[24:25], v[8:9]
	v_readlane_b32 s25, v9, 38
	s_movk_i32 s24, 25
	v_addc_co_u32_e32 v6, vcc, 0, v6, vcc
	v_cmp_gt_i64_e32 vcc, s[22:23], v[8:9]
	v_readlane_b32 s23, v9, 39
	s_movk_i32 s22, 24
	v_addc_co_u32_e32 v6, vcc, 0, v6, vcc
	v_cmp_gt_i64_e32 vcc, s[24:25], v[8:9]
	v_readlane_b32 s25, v9, 40
	s_movk_i32 s24, 23
	v_addc_co_u32_e32 v6, vcc, 0, v6, vcc
	v_cmp_gt_i64_e32 vcc, s[22:23], v[8:9]
	v_readlane_b32 s23, v9, 41
	s_movk_i32 s22, 22
	v_addc_co_u32_e32 v6, vcc, 0, v6, vcc
	v_cmp_gt_i64_e32 vcc, s[24:25], v[8:9]
	v_readlane_b32 s25, v9, 42
	s_movk_i32 s24, 21
	v_addc_co_u32_e32 v6, vcc, 0, v6, vcc
	v_cmp_gt_i64_e32 vcc, s[22:23], v[8:9]
	v_readlane_b32 s23, v9, 43
	s_movk_i32 s22, 20
	v_addc_co_u32_e32 v6, vcc, 0, v6, vcc
	v_cmp_gt_i64_e32 vcc, s[24:25], v[8:9]
	v_readlane_b32 s25, v9, 44
	s_movk_i32 s24, 19
	v_addc_co_u32_e32 v6, vcc, 0, v6, vcc
	v_cmp_gt_i64_e32 vcc, s[22:23], v[8:9]
	v_readlane_b32 s23, v9, 45
	s_movk_i32 s22, 18
	v_addc_co_u32_e32 v6, vcc, 0, v6, vcc
	v_cmp_gt_i64_e32 vcc, s[24:25], v[8:9]
	v_readlane_b32 s25, v9, 46
	s_movk_i32 s24, 17
	v_addc_co_u32_e32 v6, vcc, 0, v6, vcc
	v_cmp_gt_i64_e32 vcc, s[22:23], v[8:9]
	v_readlane_b32 s23, v9, 47
	s_movk_i32 s22, 16
	v_addc_co_u32_e32 v6, vcc, 0, v6, vcc
	v_cmp_gt_i64_e32 vcc, s[24:25], v[8:9]
	v_readlane_b32 s25, v9, 48
	s_movk_i32 s24, 15
	v_addc_co_u32_e32 v6, vcc, 0, v6, vcc
	v_cmp_gt_i64_e32 vcc, s[22:23], v[8:9]
	v_readlane_b32 s23, v9, 49
	s_movk_i32 s22, 14
	v_addc_co_u32_e32 v6, vcc, 0, v6, vcc
	v_cmp_gt_i64_e32 vcc, s[24:25], v[8:9]
	v_readlane_b32 s25, v9, 50
	s_movk_i32 s24, 13
	v_addc_co_u32_e32 v6, vcc, 0, v6, vcc
	v_cmp_gt_i64_e32 vcc, s[22:23], v[8:9]
	v_readlane_b32 s23, v9, 51
	s_movk_i32 s22, 12
	v_addc_co_u32_e32 v6, vcc, 0, v6, vcc
	v_cmp_gt_i64_e32 vcc, s[24:25], v[8:9]
	v_readlane_b32 s25, v9, 52
	s_movk_i32 s24, 11
	v_addc_co_u32_e32 v6, vcc, 0, v6, vcc
	v_cmp_gt_i64_e32 vcc, s[22:23], v[8:9]
	v_readlane_b32 s23, v9, 53
	s_movk_i32 s22, 10
	v_addc_co_u32_e32 v6, vcc, 0, v6, vcc
	v_cmp_gt_i64_e32 vcc, s[24:25], v[8:9]
	v_readlane_b32 s25, v9, 54
	s_movk_i32 s24, 9
	v_addc_co_u32_e32 v6, vcc, 0, v6, vcc
	v_cmp_gt_i64_e32 vcc, s[22:23], v[8:9]
	v_readlane_b32 s23, v9, 55
	s_movk_i32 s22, 8
	v_addc_co_u32_e32 v6, vcc, 0, v6, vcc
	v_cmp_gt_i64_e32 vcc, s[24:25], v[8:9]
	v_readlane_b32 s25, v9, 56
	s_movk_i32 s24, 7
; __device__ __forceinline__ float wave_sum(float v) {
; #pragma unroll
;     for (int o = 1; o < 64; o <<= 1) v += __shfl_xor(v, o);
;     return v;
; __device__ __forceinline__ void phase_nrr(const Frame& F, const Args& a, int l, const bf16_t* XA, const float* g, const float* modl, unsigned char* XN8) {
;     ...
;         for (int i = 0; i < 8; ++i) { const int t = tb + i;
;             const float lg = Pl[(w * 8 + i) * NE + lane] + Pl[(64 + w * 8 + i) * NE + lane]; const float sc = 1.f / (1.f + __expf(-lg)); const float bb = sc + bias;
;             float m1 = bb; m1 = fmaxf(m1, __shfl_xor(m1, 1)); m1 = fmaxf(m1, __shfl_xor(m1, 2)); m1 = fmaxf(m1, __shfl_xor(m1, 4));
;             const unsigned long long eq = __ballot(bb == m1); const int gbase = lane & ~7; const unsigned grpmask = (unsigned)((eq >> gbase) & 0xffull);
;             const int first = gbase + __builtin_ctz(grpmask);
;             float m2 = (lane == first) ? -INFINITY : bb; m2 = fmaxf(m2, __shfl_xor(m2, 1)); m2 = fmaxf(m2, __shfl_xor(m2, 2)); m2 = fmaxf(m2, __shfl_xor(m2, 4));
;             const float gsum = m1 + m2; const int gq = lane >> 3;
;             int grank = 0;
; #pragma unroll
;             for (int g2 = 0; g2 < 8; ++g2) { const float v = __int_as_float(__builtin_amdgcn_readlane(__float_as_int(gsum), g2 * 8)); grank += (v > gsum || (v == gsum && g2 < gq)) ? 1 : 0; }
;             const bool keep = grank < 4; const float val = keep ? bb : -INFINITY;
;             int rank = 0;
; #pragma unroll 8
;             for (int e2 = 0; e2 < 64; ++e2) { const float v = __int_as_float(__builtin_amdgcn_readlane(__float_as_int(val), e2)); rank += (v > val || (v == val && e2 < lane)) ? 1 : 0; }
;             const bool sel = rank < TOPK;
;             const float ssum = wave_sum(sel ? sc : 0.f);
;             if (sel) { const int p = atomicAdd((int*)(hist + lane), 1); top_e[t * TOPK + rank] = lane; gate[t * TOPK + rank] = sc / ssum * 2.5f; lpos[t * TOPK + rank] = p; }
	v_addc_co_u32_e32 v6, vcc, 0, v6, vcc
	v_cmp_gt_i64_e32 vcc, s[22:23], v[8:9]
	v_readlane_b32 s23, v9, 57
	s_movk_i32 s22, 6
	v_addc_co_u32_e32 v6, vcc, 0, v6, vcc
	v_cmp_gt_i64_e32 vcc, s[24:25], v[8:9]
	v_readlane_b32 s25, v9, 58
	s_movk_i32 s24, 5
	v_addc_co_u32_e32 v6, vcc, 0, v6, vcc
	v_cmp_gt_i64_e32 vcc, s[22:23], v[8:9]
	v_readlane_b32 s23, v9, 59
	s_movk_i32 s22, 4
	v_addc_co_u32_e32 v6, vcc, 0, v6, vcc
	v_cmp_gt_i64_e32 vcc, s[24:25], v[8:9]
	v_readlane_b32 s25, v9, 60
	s_movk_i32 s24, 3
	v_addc_co_u32_e32 v6, vcc, 0, v6, vcc
	v_cmp_gt_i64_e32 vcc, s[22:23], v[8:9]
	v_readlane_b32 s23, v9, 61
	s_movk_i32 s22, 2
	v_addc_co_u32_e32 v6, vcc, 0, v6, vcc
	v_cmp_gt_i64_e32 vcc, s[24:25], v[8:9]
	v_readlane_b32 s25, v9, 62
	s_movk_i32 s24, 1
	v_addc_co_u32_e32 v6, vcc, 0, v6, vcc
	v_cmp_gt_i64_e32 vcc, s[22:23], v[8:9]
	v_readlane_b32 s23, v9, 63
	s_movk_i32 s22, 0
	v_addc_co_u32_e32 v6, vcc, 0, v6, vcc
	v_cmp_gt_i64_e32 vcc, s[24:25], v[8:9]
	s_nop 1
	v_addc_co_u32_e32 v6, vcc, 0, v6, vcc
	v_cmp_gt_i64_e32 vcc, s[22:23], v[8:9]
	s_nop 1
	v_addc_co_u32_e32 v6, vcc, 0, v6, vcc
	v_cmp_gt_u32_e32 vcc, 6, v6
	s_nop 1
	v_cndmask_b32_e32 v5, 0, v2, vcc
	s_nop 1
	v_add_f32_dpp v5, v5, v5 quad_perm:[1,0,3,2] row_mask:0xf bank_mask:0xf
	s_nop 1
	v_add_f32_dpp v5, v5, v5 quad_perm:[2,3,0,1] row_mask:0xf bank_mask:0xf
	s_nop 1
	v_add_f32_dpp v5, v5, v5 row_half_mirror row_mask:0xf bank_mask:0xf
	s_nop 1
	v_add_f32_dpp v5, v5, v5 row_mirror row_mask:0xf bank_mask:0xf
	s_nop 0
	ds_bpermute_b32 v7, v222, v5
	s_waitcnt lgkmcnt(0)
	v_add_f32_e32 v5, v5, v7
	v_mov_b32_e32 v7, v5
	s_nop 1
	v_permlane32_swap_b32_e32 v7, v5
	s_and_saveexec_b64 s[4:5], vcc
	s_cbranch_execz .LBB0_555
	s_waitcnt lgkmcnt(0)
	v_add_f32_e32 v5, v5, v7
	s_mul_i32 s2, s2, 6
	v_or_b32_e32 v6, s2, v6
	v_div_scale_f32 v11, s[2:3], v5, v5, v2
	v_rcp_f32_e32 v12, v11
	v_ashrrev_i32_e32 v7, 31, v6
	v_lshlrev_b64 v[6:7], 2, v[6:7]
	v_lshl_add_u64 v[8:9], s[26:27], 0, v[6:7]
	ds_add_rtn_u32 v10, v227, v243
	global_store_dword v[8:9], v230, off
	v_fma_f32 v8, -v11, v12, 1.0
	v_fmac_f32_e32 v12, v8, v12
	v_div_scale_f32 v8, vcc, v2, v5, v2
	v_mul_f32_e32 v9, v8, v12
	v_fma_f32 v13, -v11, v9, v8
	v_fmac_f32_e32 v9, v13, v12
	v_fma_f32 v8, -v11, v9, v8
	v_div_fmas_f32 v8, v8, v12, v9
	v_div_fixup_f32 v2, v8, v5, v2
	v_mul_f32_e32 v2, 0x40200000, v2
	v_lshl_add_u64 v[8:9], s[28:29], 0, v[6:7]
	v_lshl_add_u64 v[6:7], s[30:31], 0, v[6:7]
	global_store_dword v[8:9], v2, off
	s_waitcnt lgkmcnt(0)
	global_store_dword v[6:7], v10, off
.LBB0_555:
	s_or_b64 exec, exec, s[4:5]
	v_add_u32_e32 v2, s85, v226
	ds_read_b32 v2, v2
	ds_read_b32 v5, v4 offset:17664
	s_waitcnt lgkmcnt(0)
	v_add_f32_e32 v2, v2, v5
	v_mul_f32_e32 v2, 0xbfb8aa3b, v2
	v_exp_f32_e32 v2, v2
	s_nop 0
	v_add_f32_e32 v2, 1.0, v2
	v_div_scale_f32 v5, s[2:3], v2, v2, 1.0
	v_rcp_f32_e32 v6, v5
	s_mov_b32 s2, 0
	v_fma_f32 v7, -v5, v6, 1.0
	v_fmac_f32_e32 v6, v7, v6
	v_div_scale_f32 v7, vcc, 1.0, v2, 1.0
	v_mul_f32_e32 v8, v7, v6
	v_fma_f32 v9, -v5, v8, v7
	v_fmac_f32_e32 v8, v9, v6
	v_fma_f32 v5, -v5, v8, v7
	v_div_fmas_f32 v5, v5, v6, v8
	v_div_fixup_f32 v2, v5, v2, 1.0
	v_add_f32_e32 v5, v3, v2
	s_nop 1
	s_waitcnt lgkmcnt(0)
	v_max_f32_dpp v6, v5, v5 quad_perm:[1,0,3,2] row_mask:0xf bank_mask:0xf
	s_nop 1
	s_waitcnt lgkmcnt(0)
	v_max_f32_dpp v6, v6, v6 quad_perm:[2,3,0,1] row_mask:0xf bank_mask:0xf
	s_nop 1
	s_waitcnt lgkmcnt(0)
	v_max_f32_dpp v8, v6, v6 row_half_mirror row_mask:0xf bank_mask:0xf
	v_cmp_eq_f32_e32 vcc, v5, v8
	s_nop 1
	v_lshrrev_b64 v[6:7], v200, vcc
	v_ffbl_b32_sdwa v6, v6 dst_sel:DWORD dst_unused:UNUSED_PAD src0_sel:BYTE_0
	v_add_u32_e32 v6, v6, v200
	v_cmp_ne_u32_e32 vcc, v230, v6
	s_nop 1
	v_cndmask_b32_e32 v6, v245, v5, vcc
	s_nop 1
	s_waitcnt lgkmcnt(0)
	v_max_f32_dpp v6, v6, v6 quad_perm:[1,0,3,2] row_mask:0xf bank_mask:0xf
	s_nop 1
	s_waitcnt lgkmcnt(0)
	v_max_f32_dpp v6, v6, v6 quad_perm:[2,3,0,1] row_mask:0xf bank_mask:0xf
	s_nop 1
	s_waitcnt lgkmcnt(0)
	v_max_f32_dpp v6, v6, v6 row_half_mirror row_mask:0xf bank_mask:0xf
	v_add_f32_e32 v6, v8, v6
	s_nop 0
	v_readlane_b32 s3, v6, 0
	s_nop 1
	v_cmp_eq_f32_e64 s[22:23], s3, v6
	v_cmp_gt_f32_e32 vcc, s3, v6
	s_and_b64 s[4:5], s[6:7], s[22:23]
	v_readlane_b32 s3, v6, 8
	s_or_b64 s[4:5], vcc, s[4:5]
	v_cndmask_b32_e64 v7, 0, 1, s[4:5]
	v_cmp_eq_f32_e64 s[22:23], s3, v6
	v_cmp_gt_f32_e32 vcc, s3, v6
	s_and_b64 s[4:5], s[8:9], s[22:23]
	v_readlane_b32 s3, v6, 16
	s_or_b64 s[4:5], vcc, s[4:5]
	v_cndmask_b32_e64 v8, 0, 1, s[4:5]
	v_cmp_eq_f32_e64 s[22:23], s3, v6
	v_cmp_gt_f32_e32 vcc, s3, v6
	s_and_b64 s[4:5], s[10:11], s[22:23]
	v_readlane_b32 s3, v6, 24
	s_or_b64 s[4:5], vcc, s[4:5]
	v_cndmask_b32_e64 v9, 0, 1, s[4:5]
	v_cmp_eq_f32_e64 s[22:23], s3, v6
	v_cmp_gt_f32_e32 vcc, s3, v6
	s_and_b64 s[4:5], s[12:13], s[22:23]
	v_readlane_b32 s3, v6, 32
	s_or_b64 s[4:5], vcc, s[4:5]
	v_cndmask_b32_e64 v10, 0, 1, s[4:5]
	v_cmp_eq_f32_e64 s[22:23], s3, v6
	v_cmp_gt_f32_e32 vcc, s3, v6
	s_and_b64 s[4:5], s[14:15], s[22:23]
	v_readlane_b32 s3, v6, 40
	s_or_b64 s[4:5], vcc, s[4:5]
	v_cndmask_b32_e64 v11, 0, 1, s[4:5]
	v_cmp_eq_f32_e64 s[22:23], s3, v6
	v_cmp_gt_f32_e32 vcc, s3, v6
	s_and_b64 s[4:5], s[16:17], s[22:23]
	v_readlane_b32 s3, v6, 48
	s_or_b64 s[4:5], vcc, s[4:5]
	v_cndmask_b32_e64 v12, 0, 1, s[4:5]
	v_cmp_eq_f32_e64 s[22:23], s3, v6
	v_cmp_gt_f32_e32 vcc, s3, v6
	s_and_b64 s[4:5], s[18:19], s[22:23]
	v_readlane_b32 s3, v6, 56
	s_or_b64 s[4:5], vcc, s[4:5]
	v_cndmask_b32_e64 v13, 0, 1, s[4:5]
	v_cmp_gt_f32_e32 vcc, s3, v6
	s_nop 1
	v_cndmask_b32_e64 v6, 0, 1, vcc
	v_add_u32_e32 v6, v8, v6
	v_add3_u32 v6, v6, v7, v9
	v_add3_u32 v6, v6, v10, v11
	v_add3_u32 v6, v6, v12, v13
; __device__ __forceinline__ void phase_nrr(const Frame& F, const Args& a, int l, const bf16_t* XA, const float* g, const float* modl, unsigned char* XN8) {
;     ...
;             const bool keep = grank < 4; const float val = keep ? bb : -INFINITY;
;             int rank = 0;
; #pragma unroll 8
;             for (int e2 = 0; e2 < 64; ++e2) { const float v = __int_as_float(__builtin_amdgcn_readlane(__float_as_int(val), e2)); rank += (v > val || (v == val && e2 < lane)) ? 1 : 0; }
	v_cmp_gt_u32_e32 vcc, 4, v6
	v_mov_b32_e32 v6, 0
	s_nop 0
	v_cndmask_b32_e32 v5, v245, v5, vcc
	v_ashrrev_i32_e32 v9, 31, v5
	v_sub_u32_e32 v8, 63, v230
	v_and_b32_e32 v9, 0x7fffffff, v9
	v_xor_b32_e32 v9, v5, v9
	s_nop 0
	v_readlane_b32 s25, v9, 0
	s_movk_i32 s24, 63
	v_readlane_b32 s23, v9, 1
	s_movk_i32 s22, 62
	v_cmp_gt_i64_e32 vcc, s[24:25], v[8:9]
	v_readlane_b32 s25, v9, 2
	s_movk_i32 s24, 61
	v_addc_co_u32_e32 v6, vcc, 0, v6, vcc
	v_cmp_gt_i64_e32 vcc, s[22:23], v[8:9]
	v_readlane_b32 s23, v9, 3
	s_movk_i32 s22, 60
	v_addc_co_u32_e32 v6, vcc, 0, v6, vcc
	v_cmp_gt_i64_e32 vcc, s[24:25], v[8:9]
	v_readlane_b32 s25, v9, 4
	s_movk_i32 s24, 59
	v_addc_co_u32_e32 v6, vcc, 0, v6, vcc
	v_cmp_gt_i64_e32 vcc, s[22:23], v[8:9]
	v_readlane_b32 s23, v9, 5
	s_movk_i32 s22, 58
	v_addc_co_u32_e32 v6, vcc, 0, v6, vcc
	v_cmp_gt_i64_e32 vcc, s[24:25], v[8:9]
	v_readlane_b32 s25, v9, 6
	s_movk_i32 s24, 57
	v_addc_co_u32_e32 v6, vcc, 0, v6, vcc
	v_cmp_gt_i64_e32 vcc, s[22:23], v[8:9]
	v_readlane_b32 s23, v9, 7
	s_movk_i32 s22, 56
	v_addc_co_u32_e32 v6, vcc, 0, v6, vcc
	v_cmp_gt_i64_e32 vcc, s[24:25], v[8:9]
	v_readlane_b32 s25, v9, 8
	s_movk_i32 s24, 55
	v_addc_co_u32_e32 v6, vcc, 0, v6, vcc
	v_cmp_gt_i64_e32 vcc, s[22:23], v[8:9]
	v_readlane_b32 s23, v9, 9
	s_movk_i32 s22, 54
	v_addc_co_u32_e32 v6, vcc, 0, v6, vcc
	v_cmp_gt_i64_e32 vcc, s[24:25], v[8:9]
	v_readlane_b32 s25, v9, 10
	s_movk_i32 s24, 53
	v_addc_co_u32_e32 v6, vcc, 0, v6, vcc
	v_cmp_gt_i64_e32 vcc, s[22:23], v[8:9]
	v_readlane_b32 s23, v9, 11
	s_movk_i32 s22, 52
	v_addc_co_u32_e32 v6, vcc, 0, v6, vcc
	v_cmp_gt_i64_e32 vcc, s[24:25], v[8:9]
	v_readlane_b32 s25, v9, 12
	s_movk_i32 s24, 51
	v_addc_co_u32_e32 v6, vcc, 0, v6, vcc
	v_cmp_gt_i64_e32 vcc, s[22:23], v[8:9]
	v_readlane_b32 s23, v9, 13
	s_movk_i32 s22, 50
	v_addc_co_u32_e32 v6, vcc, 0, v6, vcc
	v_cmp_gt_i64_e32 vcc, s[24:25], v[8:9]
	v_readlane_b32 s25, v9, 14
	s_movk_i32 s24, 49
	v_addc_co_u32_e32 v6, vcc, 0, v6, vcc
	v_cmp_gt_i64_e32 vcc, s[22:23], v[8:9]
	v_readlane_b32 s23, v9, 15
	s_movk_i32 s22, 48
	v_addc_co_u32_e32 v6, vcc, 0, v6, vcc
	v_cmp_gt_i64_e32 vcc, s[24:25], v[8:9]
	v_readlane_b32 s25, v9, 16
	s_movk_i32 s24, 47
	v_addc_co_u32_e32 v6, vcc, 0, v6, vcc
	v_cmp_gt_i64_e32 vcc, s[22:23], v[8:9]
	v_readlane_b32 s23, v9, 17
	s_movk_i32 s22, 46
	v_addc_co_u32_e32 v6, vcc, 0, v6, vcc
	v_cmp_gt_i64_e32 vcc, s[24:25], v[8:9]
	v_readlane_b32 s25, v9, 18
	s_movk_i32 s24, 45
	v_addc_co_u32_e32 v6, vcc, 0, v6, vcc
	v_cmp_gt_i64_e32 vcc, s[22:23], v[8:9]
	v_readlane_b32 s23, v9, 19
	s_movk_i32 s22, 44
	v_addc_co_u32_e32 v6, vcc, 0, v6, vcc
	v_cmp_gt_i64_e32 vcc, s[24:25], v[8:9]
	v_readlane_b32 s25, v9, 20
	s_movk_i32 s24, 43
	v_addc_co_u32_e32 v6, vcc, 0, v6, vcc
	v_cmp_gt_i64_e32 vcc, s[22:23], v[8:9]
	v_readlane_b32 s23, v9, 21
	s_movk_i32 s22, 42
	v_addc_co_u32_e32 v6, vcc, 0, v6, vcc
	v_cmp_gt_i64_e32 vcc, s[24:25], v[8:9]
	v_readlane_b32 s25, v9, 22
	s_movk_i32 s24, 41
	v_addc_co_u32_e32 v6, vcc, 0, v6, vcc
	v_cmp_gt_i64_e32 vcc, s[22:23], v[8:9]
	v_readlane_b32 s23, v9, 23
	s_movk_i32 s22, 40
	v_addc_co_u32_e32 v6, vcc, 0, v6, vcc
	v_cmp_gt_i64_e32 vcc, s[24:25], v[8:9]
	v_readlane_b32 s25, v9, 24
	s_movk_i32 s24, 39
	v_addc_co_u32_e32 v6, vcc, 0, v6, vcc
	v_cmp_gt_i64_e32 vcc, s[22:23], v[8:9]
	v_readlane_b32 s23, v9, 25
	s_movk_i32 s22, 38
	v_addc_co_u32_e32 v6, vcc, 0, v6, vcc
	v_cmp_gt_i64_e32 vcc, s[24:25], v[8:9]
	v_readlane_b32 s25, v9, 26
	s_movk_i32 s24, 37
	v_addc_co_u32_e32 v6, vcc, 0, v6, vcc
	v_cmp_gt_i64_e32 vcc, s[22:23], v[8:9]
	v_readlane_b32 s23, v9, 27
	s_movk_i32 s22, 36
	v_addc_co_u32_e32 v6, vcc, 0, v6, vcc
	v_cmp_gt_i64_e32 vcc, s[24:25], v[8:9]
	v_readlane_b32 s25, v9, 28
	s_movk_i32 s24, 35
	v_addc_co_u32_e32 v6, vcc, 0, v6, vcc
	v_cmp_gt_i64_e32 vcc, s[22:23], v[8:9]
	v_readlane_b32 s23, v9, 29
	s_movk_i32 s22, 34
	v_addc_co_u32_e32 v6, vcc, 0, v6, vcc
	v_cmp_gt_i64_e32 vcc, s[24:25], v[8:9]
	v_readlane_b32 s25, v9, 30
	s_movk_i32 s24, 33
	v_addc_co_u32_e32 v6, vcc, 0, v6, vcc
	v_cmp_gt_i64_e32 vcc, s[22:23], v[8:9]
	v_readlane_b32 s23, v9, 31
	s_movk_i32 s22, 32
	v_addc_co_u32_e32 v6, vcc, 0, v6, vcc
	v_cmp_gt_i64_e32 vcc, s[24:25], v[8:9]
	v_readlane_b32 s25, v9, 32
	s_movk_i32 s24, 31
	v_addc_co_u32_e32 v6, vcc, 0, v6, vcc
	v_cmp_gt_i64_e32 vcc, s[22:23], v[8:9]
	v_readlane_b32 s23, v9, 33
	s_movk_i32 s22, 30
	v_addc_co_u32_e32 v6, vcc, 0, v6, vcc
	v_cmp_gt_i64_e32 vcc, s[24:25], v[8:9]
	v_readlane_b32 s25, v9, 34
	s_movk_i32 s24, 29
	v_addc_co_u32_e32 v6, vcc, 0, v6, vcc
	v_cmp_gt_i64_e32 vcc, s[22:23], v[8:9]
	v_readlane_b32 s23, v9, 35
	s_movk_i32 s22, 28
	v_addc_co_u32_e32 v6, vcc, 0, v6, vcc
	v_cmp_gt_i64_e32 vcc, s[24:25], v[8:9]
	v_readlane_b32 s25, v9, 36
	s_movk_i32 s24, 27
	v_addc_co_u32_e32 v6, vcc, 0, v6, vcc
	v_cmp_gt_i64_e32 vcc, s[22:23], v[8:9]
	v_readlane_b32 s23, v9, 37
	s_movk_i32 s22, 26
	v_addc_co_u32_e32 v6, vcc, 0, v6, vcc
	v_cmp_gt_i64_e32 vcc, s[24:25], v[8:9]
	v_readlane_b32 s25, v9, 38
	s_movk_i32 s24, 25
	v_addc_co_u32_e32 v6, vcc, 0, v6, vcc
	v_cmp_gt_i64_e32 vcc, s[22:23], v[8:9]
	v_readlane_b32 s23, v9, 39
	s_movk_i32 s22, 24
	v_addc_co_u32_e32 v6, vcc, 0, v6, vcc
	v_cmp_gt_i64_e32 vcc, s[24:25], v[8:9]
	v_readlane_b32 s25, v9, 40
	s_movk_i32 s24, 23
	v_addc_co_u32_e32 v6, vcc, 0, v6, vcc
	v_cmp_gt_i64_e32 vcc, s[22:23], v[8:9]
	v_readlane_b32 s23, v9, 41
	s_movk_i32 s22, 22
	v_addc_co_u32_e32 v6, vcc, 0, v6, vcc
	v_cmp_gt_i64_e32 vcc, s[24:25], v[8:9]
	v_readlane_b32 s25, v9, 42
	s_movk_i32 s24, 21
	v_addc_co_u32_e32 v6, vcc, 0, v6, vcc
	v_cmp_gt_i64_e32 vcc, s[22:23], v[8:9]
	v_readlane_b32 s23, v9, 43
	s_movk_i32 s22, 20
	v_addc_co_u32_e32 v6, vcc, 0, v6, vcc
; __device__ __forceinline__ float wave_sum(float v) {
; #pragma unroll
;     for (int o = 1; o < 64; o <<= 1) v += __shfl_xor(v, o);
;     return v;
; __device__ __forceinline__ void phase_nrr(const Frame& F, const Args& a, int l, const bf16_t* XA, const float* g, const float* modl, unsigned char* XN8) {
;     ...
;             int rank = 0;
; #pragma unroll 8
;             for (int e2 = 0; e2 < 64; ++e2) { const float v = __int_as_float(__builtin_amdgcn_readlane(__float_as_int(val), e2)); rank += (v > val || (v == val && e2 < lane)) ? 1 : 0; }
;             const bool sel = rank < TOPK;
;             const float ssum = wave_sum(sel ? sc : 0.f);
;             if (sel) { const int p = atomicAdd((int*)(hist + lane), 1); top_e[t * TOPK + rank] = lane; gate[t * TOPK + rank] = sc / ssum * 2.5f; lpos[t * TOPK + rank] = p; }
	v_cmp_gt_i64_e32 vcc, s[24:25], v[8:9]
	v_readlane_b32 s25, v9, 44
	s_movk_i32 s24, 19
	v_addc_co_u32_e32 v6, vcc, 0, v6, vcc
	v_cmp_gt_i64_e32 vcc, s[22:23], v[8:9]
	v_readlane_b32 s23, v9, 45
	s_movk_i32 s22, 18
	v_addc_co_u32_e32 v6, vcc, 0, v6, vcc
	v_cmp_gt_i64_e32 vcc, s[24:25], v[8:9]
	v_readlane_b32 s25, v9, 46
	s_movk_i32 s24, 17
	v_addc_co_u32_e32 v6, vcc, 0, v6, vcc
	v_cmp_gt_i64_e32 vcc, s[22:23], v[8:9]
	v_readlane_b32 s23, v9, 47
	s_movk_i32 s22, 16
	v_addc_co_u32_e32 v6, vcc, 0, v6, vcc
	v_cmp_gt_i64_e32 vcc, s[24:25], v[8:9]
	v_readlane_b32 s25, v9, 48
	s_movk_i32 s24, 15
	v_addc_co_u32_e32 v6, vcc, 0, v6, vcc
	v_cmp_gt_i64_e32 vcc, s[22:23], v[8:9]
	v_readlane_b32 s23, v9, 49
	s_movk_i32 s22, 14
	v_addc_co_u32_e32 v6, vcc, 0, v6, vcc
	v_cmp_gt_i64_e32 vcc, s[24:25], v[8:9]
	v_readlane_b32 s25, v9, 50
	s_movk_i32 s24, 13
	v_addc_co_u32_e32 v6, vcc, 0, v6, vcc
	v_cmp_gt_i64_e32 vcc, s[22:23], v[8:9]
	v_readlane_b32 s23, v9, 51
	s_movk_i32 s22, 12
	v_addc_co_u32_e32 v6, vcc, 0, v6, vcc
	v_cmp_gt_i64_e32 vcc, s[24:25], v[8:9]
	v_readlane_b32 s25, v9, 52
	s_movk_i32 s24, 11
	v_addc_co_u32_e32 v6, vcc, 0, v6, vcc
	v_cmp_gt_i64_e32 vcc, s[22:23], v[8:9]
	v_readlane_b32 s23, v9, 53
	s_movk_i32 s22, 10
	v_addc_co_u32_e32 v6, vcc, 0, v6, vcc
	v_cmp_gt_i64_e32 vcc, s[24:25], v[8:9]
	v_readlane_b32 s25, v9, 54
	s_movk_i32 s24, 9
	v_addc_co_u32_e32 v6, vcc, 0, v6, vcc
	v_cmp_gt_i64_e32 vcc, s[22:23], v[8:9]
	v_readlane_b32 s23, v9, 55
	s_movk_i32 s22, 8
	v_addc_co_u32_e32 v6, vcc, 0, v6, vcc
	v_cmp_gt_i64_e32 vcc, s[24:25], v[8:9]
	v_readlane_b32 s25, v9, 56
	s_movk_i32 s24, 7
	v_addc_co_u32_e32 v6, vcc, 0, v6, vcc
	v_cmp_gt_i64_e32 vcc, s[22:23], v[8:9]
	v_readlane_b32 s23, v9, 57
	s_movk_i32 s22, 6
	v_addc_co_u32_e32 v6, vcc, 0, v6, vcc
	v_cmp_gt_i64_e32 vcc, s[24:25], v[8:9]
	v_readlane_b32 s25, v9, 58
	s_movk_i32 s24, 5
	v_addc_co_u32_e32 v6, vcc, 0, v6, vcc
	v_cmp_gt_i64_e32 vcc, s[22:23], v[8:9]
	v_readlane_b32 s23, v9, 59
	s_movk_i32 s22, 4
	v_addc_co_u32_e32 v6, vcc, 0, v6, vcc
	v_cmp_gt_i64_e32 vcc, s[24:25], v[8:9]
	v_readlane_b32 s25, v9, 60
	s_movk_i32 s24, 3
	v_addc_co_u32_e32 v6, vcc, 0, v6, vcc
	v_cmp_gt_i64_e32 vcc, s[22:23], v[8:9]
	v_readlane_b32 s23, v9, 61
	s_movk_i32 s22, 2
	v_addc_co_u32_e32 v6, vcc, 0, v6, vcc
	v_cmp_gt_i64_e32 vcc, s[24:25], v[8:9]
	v_readlane_b32 s25, v9, 62
	s_movk_i32 s24, 1
	v_addc_co_u32_e32 v6, vcc, 0, v6, vcc
	v_cmp_gt_i64_e32 vcc, s[22:23], v[8:9]
	v_readlane_b32 s23, v9, 63
	s_movk_i32 s22, 0
	v_addc_co_u32_e32 v6, vcc, 0, v6, vcc
	v_cmp_gt_i64_e32 vcc, s[24:25], v[8:9]
	s_nop 1
	v_addc_co_u32_e32 v6, vcc, 0, v6, vcc
	v_cmp_gt_i64_e32 vcc, s[22:23], v[8:9]
	s_nop 1
	v_addc_co_u32_e32 v6, vcc, 0, v6, vcc
	v_cmp_gt_u32_e32 vcc, 6, v6
	s_nop 1
	v_cndmask_b32_e32 v5, 0, v2, vcc
	s_nop 1
	v_add_f32_dpp v5, v5, v5 quad_perm:[1,0,3,2] row_mask:0xf bank_mask:0xf
	s_nop 1
	v_add_f32_dpp v5, v5, v5 quad_perm:[2,3,0,1] row_mask:0xf bank_mask:0xf
	s_nop 1
	v_add_f32_dpp v5, v5, v5 row_half_mirror row_mask:0xf bank_mask:0xf
	s_nop 1
	v_add_f32_dpp v5, v5, v5 row_mirror row_mask:0xf bank_mask:0xf
	s_nop 0
	ds_bpermute_b32 v7, v222, v5
	s_waitcnt lgkmcnt(0)
	v_add_f32_e32 v5, v5, v7
	v_mov_b32_e32 v7, v5
	s_nop 1
	v_permlane32_swap_b32_e32 v7, v5
	s_and_saveexec_b64 s[2:3], vcc
	s_cbranch_execz .LBB0_559
	s_waitcnt lgkmcnt(0)
	v_add_f32_e32 v5, v5, v7
	v_div_scale_f32 v11, s[4:5], v5, v5, v2
	v_add3_u32 v6, s36, 30, v6
	v_rcp_f32_e32 v12, v11
	v_ashrrev_i32_e32 v7, 31, v6
	v_lshlrev_b64 v[6:7], 2, v[6:7]
	v_lshl_add_u64 v[8:9], s[26:27], 0, v[6:7]
	ds_add_rtn_u32 v10, v227, v243
	global_store_dword v[8:9], v230, off
	v_fma_f32 v8, -v11, v12, 1.0
	v_fmac_f32_e32 v12, v8, v12
	v_div_scale_f32 v8, vcc, v2, v5, v2
	v_mul_f32_e32 v9, v8, v12
	v_fma_f32 v13, -v11, v9, v8
	v_fmac_f32_e32 v9, v13, v12
	v_fma_f32 v8, -v11, v9, v8
	v_div_fmas_f32 v8, v8, v12, v9
	v_div_fixup_f32 v2, v8, v5, v2
	v_mul_f32_e32 v2, 0x40200000, v2
	v_lshl_add_u64 v[8:9], s[28:29], 0, v[6:7]
	v_lshl_add_u64 v[6:7], s[30:31], 0, v[6:7]
	global_store_dword v[8:9], v2, off
	s_waitcnt lgkmcnt(0)
	global_store_dword v[6:7], v10, off
.LBB0_559:
	s_or_b64 exec, exec, s[2:3]
	v_add_u32_e32 v2, s86, v226
	ds_read_b32 v2, v2
	ds_read_b32 v5, v4 offset:17920
	s_waitcnt lgkmcnt(0)
	v_add_f32_e32 v2, v2, v5
	v_mul_f32_e32 v2, 0xbfb8aa3b, v2
	v_exp_f32_e32 v2, v2
	s_nop 0
	v_add_f32_e32 v2, 1.0, v2
	v_div_scale_f32 v5, s[2:3], v2, v2, 1.0
	v_rcp_f32_e32 v6, v5
	s_mov_b32 s2, 0
	v_fma_f32 v7, -v5, v6, 1.0
	v_fmac_f32_e32 v6, v7, v6
	v_div_scale_f32 v7, vcc, 1.0, v2, 1.0
	v_mul_f32_e32 v8, v7, v6
	v_fma_f32 v9, -v5, v8, v7
	v_fmac_f32_e32 v8, v9, v6
	v_fma_f32 v5, -v5, v8, v7
	v_div_fmas_f32 v5, v5, v6, v8
	v_div_fixup_f32 v2, v5, v2, 1.0
	v_add_f32_e32 v5, v3, v2
	s_nop 1
	s_waitcnt lgkmcnt(0)
	v_max_f32_dpp v6, v5, v5 quad_perm:[1,0,3,2] row_mask:0xf bank_mask:0xf
	s_nop 1
	s_waitcnt lgkmcnt(0)
	v_max_f32_dpp v6, v6, v6 quad_perm:[2,3,0,1] row_mask:0xf bank_mask:0xf
	s_nop 1
	s_waitcnt lgkmcnt(0)
	v_max_f32_dpp v8, v6, v6 row_half_mirror row_mask:0xf bank_mask:0xf
	v_cmp_eq_f32_e32 vcc, v5, v8
	s_nop 1
	v_lshrrev_b64 v[6:7], v200, vcc
	v_ffbl_b32_sdwa v6, v6 dst_sel:DWORD dst_unused:UNUSED_PAD src0_sel:BYTE_0
	v_add_u32_e32 v6, v6, v200
	v_cmp_ne_u32_e32 vcc, v230, v6
	s_nop 1
	v_cndmask_b32_e32 v6, v245, v5, vcc
	s_nop 1
	s_waitcnt lgkmcnt(0)
	v_max_f32_dpp v6, v6, v6 quad_perm:[1,0,3,2] row_mask:0xf bank_mask:0xf
	s_nop 1
	s_waitcnt lgkmcnt(0)
	v_max_f32_dpp v6, v6, v6 quad_perm:[2,3,0,1] row_mask:0xf bank_mask:0xf
	s_nop 1
	s_waitcnt lgkmcnt(0)
; __device__ __forceinline__ void phase_nrr(const Frame& F, const Args& a, int l, const bf16_t* XA, const float* g, const float* modl, unsigned char* XN8) {
;     ...
;             const float gsum = m1 + m2; const int gq = lane >> 3;
;             int grank = 0;
; #pragma unroll
;             for (int g2 = 0; g2 < 8; ++g2) { const float v = __int_as_float(__builtin_amdgcn_readlane(__float_as_int(gsum), g2 * 8)); grank += (v > gsum || (v == gsum && g2 < gq)) ? 1 : 0; }
;             const bool keep = grank < 4; const float val = keep ? bb : -INFINITY;
;             int rank = 0;
; #pragma unroll 8
;             for (int e2 = 0; e2 < 64; ++e2) { const float v = __int_as_float(__builtin_amdgcn_readlane(__float_as_int(val), e2)); rank += (v > val || (v == val && e2 < lane)) ? 1 : 0; }
	v_max_f32_dpp v6, v6, v6 row_half_mirror row_mask:0xf bank_mask:0xf
	v_add_f32_e32 v6, v8, v6
	s_nop 0
	v_readlane_b32 s3, v6, 0
	s_nop 1
	v_cmp_eq_f32_e64 s[22:23], s3, v6
	v_cmp_gt_f32_e32 vcc, s3, v6
	s_and_b64 s[4:5], s[6:7], s[22:23]
	v_readlane_b32 s3, v6, 8
	s_or_b64 s[4:5], vcc, s[4:5]
	v_cndmask_b32_e64 v7, 0, 1, s[4:5]
	v_cmp_eq_f32_e64 s[22:23], s3, v6
	v_cmp_gt_f32_e32 vcc, s3, v6
	s_and_b64 s[4:5], s[8:9], s[22:23]
	v_readlane_b32 s3, v6, 16
	s_or_b64 s[4:5], vcc, s[4:5]
	v_cndmask_b32_e64 v8, 0, 1, s[4:5]
	v_cmp_eq_f32_e64 s[22:23], s3, v6
	v_cmp_gt_f32_e32 vcc, s3, v6
	s_and_b64 s[4:5], s[10:11], s[22:23]
	v_readlane_b32 s3, v6, 24
	s_or_b64 s[4:5], vcc, s[4:5]
	v_cndmask_b32_e64 v9, 0, 1, s[4:5]
	v_cmp_eq_f32_e64 s[22:23], s3, v6
	v_cmp_gt_f32_e32 vcc, s3, v6
	s_and_b64 s[4:5], s[12:13], s[22:23]
	v_readlane_b32 s3, v6, 32
	s_or_b64 s[4:5], vcc, s[4:5]
	v_cndmask_b32_e64 v10, 0, 1, s[4:5]
	v_cmp_eq_f32_e64 s[22:23], s3, v6
	v_cmp_gt_f32_e32 vcc, s3, v6
	s_and_b64 s[4:5], s[14:15], s[22:23]
	v_readlane_b32 s3, v6, 40
	s_or_b64 s[4:5], vcc, s[4:5]
	v_cndmask_b32_e64 v11, 0, 1, s[4:5]
	v_cmp_eq_f32_e64 s[22:23], s3, v6
	v_cmp_gt_f32_e32 vcc, s3, v6
	s_and_b64 s[4:5], s[16:17], s[22:23]
	v_readlane_b32 s3, v6, 48
	s_or_b64 s[4:5], vcc, s[4:5]
	v_cndmask_b32_e64 v12, 0, 1, s[4:5]
	v_cmp_eq_f32_e64 s[22:23], s3, v6
	v_cmp_gt_f32_e32 vcc, s3, v6
	s_and_b64 s[4:5], s[18:19], s[22:23]
	v_readlane_b32 s3, v6, 56
	s_or_b64 s[4:5], vcc, s[4:5]
	v_cndmask_b32_e64 v13, 0, 1, s[4:5]
	v_cmp_gt_f32_e32 vcc, s3, v6
	s_nop 1
	v_cndmask_b32_e64 v6, 0, 1, vcc
	v_add_u32_e32 v6, v8, v6
	v_add3_u32 v6, v6, v7, v9
	v_add3_u32 v6, v6, v10, v11
	v_add3_u32 v6, v6, v12, v13
	v_cmp_gt_u32_e32 vcc, 4, v6
	v_mov_b32_e32 v6, 0
	s_nop 0
	v_cndmask_b32_e32 v5, v245, v5, vcc
	v_ashrrev_i32_e32 v9, 31, v5
	v_sub_u32_e32 v8, 63, v230
	v_and_b32_e32 v9, 0x7fffffff, v9
	v_xor_b32_e32 v9, v5, v9
	s_nop 0
	v_readlane_b32 s25, v9, 0
	s_movk_i32 s24, 63
	v_readlane_b32 s23, v9, 1
	s_movk_i32 s22, 62
	v_cmp_gt_i64_e32 vcc, s[24:25], v[8:9]
	v_readlane_b32 s25, v9, 2
	s_movk_i32 s24, 61
	v_addc_co_u32_e32 v6, vcc, 0, v6, vcc
	v_cmp_gt_i64_e32 vcc, s[22:23], v[8:9]
	v_readlane_b32 s23, v9, 3
	s_movk_i32 s22, 60
	v_addc_co_u32_e32 v6, vcc, 0, v6, vcc
	v_cmp_gt_i64_e32 vcc, s[24:25], v[8:9]
	v_readlane_b32 s25, v9, 4
	s_movk_i32 s24, 59
	v_addc_co_u32_e32 v6, vcc, 0, v6, vcc
	v_cmp_gt_i64_e32 vcc, s[22:23], v[8:9]
	v_readlane_b32 s23, v9, 5
	s_movk_i32 s22, 58
	v_addc_co_u32_e32 v6, vcc, 0, v6, vcc
	v_cmp_gt_i64_e32 vcc, s[24:25], v[8:9]
	v_readlane_b32 s25, v9, 6
	s_movk_i32 s24, 57
	v_addc_co_u32_e32 v6, vcc, 0, v6, vcc
	v_cmp_gt_i64_e32 vcc, s[22:23], v[8:9]
	v_readlane_b32 s23, v9, 7
	s_movk_i32 s22, 56
	v_addc_co_u32_e32 v6, vcc, 0, v6, vcc
	v_cmp_gt_i64_e32 vcc, s[24:25], v[8:9]
	v_readlane_b32 s25, v9, 8
	s_movk_i32 s24, 55
	v_addc_co_u32_e32 v6, vcc, 0, v6, vcc
	v_cmp_gt_i64_e32 vcc, s[22:23], v[8:9]
	v_readlane_b32 s23, v9, 9
	s_movk_i32 s22, 54
	v_addc_co_u32_e32 v6, vcc, 0, v6, vcc
	v_cmp_gt_i64_e32 vcc, s[24:25], v[8:9]
	v_readlane_b32 s25, v9, 10
	s_movk_i32 s24, 53
	v_addc_co_u32_e32 v6, vcc, 0, v6, vcc
	v_cmp_gt_i64_e32 vcc, s[22:23], v[8:9]
	v_readlane_b32 s23, v9, 11
	s_movk_i32 s22, 52
	v_addc_co_u32_e32 v6, vcc, 0, v6, vcc
	v_cmp_gt_i64_e32 vcc, s[24:25], v[8:9]
	v_readlane_b32 s25, v9, 12
	s_movk_i32 s24, 51
	v_addc_co_u32_e32 v6, vcc, 0, v6, vcc
	v_cmp_gt_i64_e32 vcc, s[22:23], v[8:9]
	v_readlane_b32 s23, v9, 13
	s_movk_i32 s22, 50
	v_addc_co_u32_e32 v6, vcc, 0, v6, vcc
	v_cmp_gt_i64_e32 vcc, s[24:25], v[8:9]
	v_readlane_b32 s25, v9, 14
	s_movk_i32 s24, 49
	v_addc_co_u32_e32 v6, vcc, 0, v6, vcc
	v_cmp_gt_i64_e32 vcc, s[22:23], v[8:9]
	v_readlane_b32 s23, v9, 15
	s_movk_i32 s22, 48
	v_addc_co_u32_e32 v6, vcc, 0, v6, vcc
	v_cmp_gt_i64_e32 vcc, s[24:25], v[8:9]
	v_readlane_b32 s25, v9, 16
	s_movk_i32 s24, 47
	v_addc_co_u32_e32 v6, vcc, 0, v6, vcc
	v_cmp_gt_i64_e32 vcc, s[22:23], v[8:9]
	v_readlane_b32 s23, v9, 17
	s_movk_i32 s22, 46
	v_addc_co_u32_e32 v6, vcc, 0, v6, vcc
	v_cmp_gt_i64_e32 vcc, s[24:25], v[8:9]
	v_readlane_b32 s25, v9, 18
	s_movk_i32 s24, 45
	v_addc_co_u32_e32 v6, vcc, 0, v6, vcc
	v_cmp_gt_i64_e32 vcc, s[22:23], v[8:9]
	v_readlane_b32 s23, v9, 19
	s_movk_i32 s22, 44
	v_addc_co_u32_e32 v6, vcc, 0, v6, vcc
	v_cmp_gt_i64_e32 vcc, s[24:25], v[8:9]
	v_readlane_b32 s25, v9, 20
	s_movk_i32 s24, 43
	v_addc_co_u32_e32 v6, vcc, 0, v6, vcc
	v_cmp_gt_i64_e32 vcc, s[22:23], v[8:9]
	v_readlane_b32 s23, v9, 21
	s_movk_i32 s22, 42
	v_addc_co_u32_e32 v6, vcc, 0, v6, vcc
	v_cmp_gt_i64_e32 vcc, s[24:25], v[8:9]
	v_readlane_b32 s25, v9, 22
	s_movk_i32 s24, 41
	v_addc_co_u32_e32 v6, vcc, 0, v6, vcc
	v_cmp_gt_i64_e32 vcc, s[22:23], v[8:9]
	v_readlane_b32 s23, v9, 23
	s_movk_i32 s22, 40
	v_addc_co_u32_e32 v6, vcc, 0, v6, vcc
	v_cmp_gt_i64_e32 vcc, s[24:25], v[8:9]
	v_readlane_b32 s25, v9, 24
	s_movk_i32 s24, 39
	v_addc_co_u32_e32 v6, vcc, 0, v6, vcc
	v_cmp_gt_i64_e32 vcc, s[22:23], v[8:9]
	v_readlane_b32 s23, v9, 25
	s_movk_i32 s22, 38
	v_addc_co_u32_e32 v6, vcc, 0, v6, vcc
	v_cmp_gt_i64_e32 vcc, s[24:25], v[8:9]
	v_readlane_b32 s25, v9, 26
	s_movk_i32 s24, 37
	v_addc_co_u32_e32 v6, vcc, 0, v6, vcc
	v_cmp_gt_i64_e32 vcc, s[22:23], v[8:9]
	v_readlane_b32 s23, v9, 27
	s_movk_i32 s22, 36
	v_addc_co_u32_e32 v6, vcc, 0, v6, vcc
	v_cmp_gt_i64_e32 vcc, s[24:25], v[8:9]
	v_readlane_b32 s25, v9, 28
	s_movk_i32 s24, 35
	v_addc_co_u32_e32 v6, vcc, 0, v6, vcc
	v_cmp_gt_i64_e32 vcc, s[22:23], v[8:9]
	v_readlane_b32 s23, v9, 29
	s_movk_i32 s22, 34
	v_addc_co_u32_e32 v6, vcc, 0, v6, vcc
	v_cmp_gt_i64_e32 vcc, s[24:25], v[8:9]
	v_readlane_b32 s25, v9, 30
	s_movk_i32 s24, 33
; __device__ __forceinline__ float wave_sum(float v) {
; #pragma unroll
;     for (int o = 1; o < 64; o <<= 1) v += __shfl_xor(v, o);
;     return v;
; __device__ __forceinline__ void phase_nrr(const Frame& F, const Args& a, int l, const bf16_t* XA, const float* g, const float* modl, unsigned char* XN8) {
;     ...
;             int rank = 0;
; #pragma unroll 8
;             for (int e2 = 0; e2 < 64; ++e2) { const float v = __int_as_float(__builtin_amdgcn_readlane(__float_as_int(val), e2)); rank += (v > val || (v == val && e2 < lane)) ? 1 : 0; }
;             const bool sel = rank < TOPK;
;             const float ssum = wave_sum(sel ? sc : 0.f);
;             if (sel) { const int p = atomicAdd((int*)(hist + lane), 1); top_e[t * TOPK + rank] = lane; gate[t * TOPK + rank] = sc / ssum * 2.5f; lpos[t * TOPK + rank] = p; }
	v_addc_co_u32_e32 v6, vcc, 0, v6, vcc
	v_cmp_gt_i64_e32 vcc, s[22:23], v[8:9]
	v_readlane_b32 s23, v9, 31
	s_movk_i32 s22, 32
	v_addc_co_u32_e32 v6, vcc, 0, v6, vcc
	v_cmp_gt_i64_e32 vcc, s[24:25], v[8:9]
	v_readlane_b32 s25, v9, 32
	s_movk_i32 s24, 31
	v_addc_co_u32_e32 v6, vcc, 0, v6, vcc
	v_cmp_gt_i64_e32 vcc, s[22:23], v[8:9]
	v_readlane_b32 s23, v9, 33
	s_movk_i32 s22, 30
	v_addc_co_u32_e32 v6, vcc, 0, v6, vcc
	v_cmp_gt_i64_e32 vcc, s[24:25], v[8:9]
	v_readlane_b32 s25, v9, 34
	s_movk_i32 s24, 29
	v_addc_co_u32_e32 v6, vcc, 0, v6, vcc
	v_cmp_gt_i64_e32 vcc, s[22:23], v[8:9]
	v_readlane_b32 s23, v9, 35
	s_movk_i32 s22, 28
	v_addc_co_u32_e32 v6, vcc, 0, v6, vcc
	v_cmp_gt_i64_e32 vcc, s[24:25], v[8:9]
	v_readlane_b32 s25, v9, 36
	s_movk_i32 s24, 27
	v_addc_co_u32_e32 v6, vcc, 0, v6, vcc
	v_cmp_gt_i64_e32 vcc, s[22:23], v[8:9]
	v_readlane_b32 s23, v9, 37
	s_movk_i32 s22, 26
	v_addc_co_u32_e32 v6, vcc, 0, v6, vcc
	v_cmp_gt_i64_e32 vcc, s[24:25], v[8:9]
	v_readlane_b32 s25, v9, 38
	s_movk_i32 s24, 25
	v_addc_co_u32_e32 v6, vcc, 0, v6, vcc
	v_cmp_gt_i64_e32 vcc, s[22:23], v[8:9]
	v_readlane_b32 s23, v9, 39
	s_movk_i32 s22, 24
	v_addc_co_u32_e32 v6, vcc, 0, v6, vcc
	v_cmp_gt_i64_e32 vcc, s[24:25], v[8:9]
	v_readlane_b32 s25, v9, 40
	s_movk_i32 s24, 23
	v_addc_co_u32_e32 v6, vcc, 0, v6, vcc
	v_cmp_gt_i64_e32 vcc, s[22:23], v[8:9]
	v_readlane_b32 s23, v9, 41
	s_movk_i32 s22, 22
	v_addc_co_u32_e32 v6, vcc, 0, v6, vcc
	v_cmp_gt_i64_e32 vcc, s[24:25], v[8:9]
	v_readlane_b32 s25, v9, 42
	s_movk_i32 s24, 21
	v_addc_co_u32_e32 v6, vcc, 0, v6, vcc
	v_cmp_gt_i64_e32 vcc, s[22:23], v[8:9]
	v_readlane_b32 s23, v9, 43
	s_movk_i32 s22, 20
	v_addc_co_u32_e32 v6, vcc, 0, v6, vcc
	v_cmp_gt_i64_e32 vcc, s[24:25], v[8:9]
	v_readlane_b32 s25, v9, 44
	s_movk_i32 s24, 19
	v_addc_co_u32_e32 v6, vcc, 0, v6, vcc
	v_cmp_gt_i64_e32 vcc, s[22:23], v[8:9]
	v_readlane_b32 s23, v9, 45
	s_movk_i32 s22, 18
	v_addc_co_u32_e32 v6, vcc, 0, v6, vcc
	v_cmp_gt_i64_e32 vcc, s[24:25], v[8:9]
	v_readlane_b32 s25, v9, 46
	s_movk_i32 s24, 17
	v_addc_co_u32_e32 v6, vcc, 0, v6, vcc
	v_cmp_gt_i64_e32 vcc, s[22:23], v[8:9]
	v_readlane_b32 s23, v9, 47
	s_movk_i32 s22, 16
	v_addc_co_u32_e32 v6, vcc, 0, v6, vcc
	v_cmp_gt_i64_e32 vcc, s[24:25], v[8:9]
	v_readlane_b32 s25, v9, 48
	s_movk_i32 s24, 15
	v_addc_co_u32_e32 v6, vcc, 0, v6, vcc
	v_cmp_gt_i64_e32 vcc, s[22:23], v[8:9]
	v_readlane_b32 s23, v9, 49
	s_movk_i32 s22, 14
	v_addc_co_u32_e32 v6, vcc, 0, v6, vcc
	v_cmp_gt_i64_e32 vcc, s[24:25], v[8:9]
	v_readlane_b32 s25, v9, 50
	s_movk_i32 s24, 13
	v_addc_co_u32_e32 v6, vcc, 0, v6, vcc
	v_cmp_gt_i64_e32 vcc, s[22:23], v[8:9]
	v_readlane_b32 s23, v9, 51
	s_movk_i32 s22, 12
	v_addc_co_u32_e32 v6, vcc, 0, v6, vcc
	v_cmp_gt_i64_e32 vcc, s[24:25], v[8:9]
	v_readlane_b32 s25, v9, 52
	s_movk_i32 s24, 11
	v_addc_co_u32_e32 v6, vcc, 0, v6, vcc
	v_cmp_gt_i64_e32 vcc, s[22:23], v[8:9]
	v_readlane_b32 s23, v9, 53
	s_movk_i32 s22, 10
	v_addc_co_u32_e32 v6, vcc, 0, v6, vcc
	v_cmp_gt_i64_e32 vcc, s[24:25], v[8:9]
	v_readlane_b32 s25, v9, 54
	s_movk_i32 s24, 9
	v_addc_co_u32_e32 v6, vcc, 0, v6, vcc
	v_cmp_gt_i64_e32 vcc, s[22:23], v[8:9]
	v_readlane_b32 s23, v9, 55
	s_movk_i32 s22, 8
	v_addc_co_u32_e32 v6, vcc, 0, v6, vcc
	v_cmp_gt_i64_e32 vcc, s[24:25], v[8:9]
	v_readlane_b32 s25, v9, 56
	s_movk_i32 s24, 7
	v_addc_co_u32_e32 v6, vcc, 0, v6, vcc
	v_cmp_gt_i64_e32 vcc, s[22:23], v[8:9]
	v_readlane_b32 s23, v9, 57
	s_movk_i32 s22, 6
	v_addc_co_u32_e32 v6, vcc, 0, v6, vcc
	v_cmp_gt_i64_e32 vcc, s[24:25], v[8:9]
	v_readlane_b32 s25, v9, 58
	s_movk_i32 s24, 5
	v_addc_co_u32_e32 v6, vcc, 0, v6, vcc
	v_cmp_gt_i64_e32 vcc, s[22:23], v[8:9]
	v_readlane_b32 s23, v9, 59
	s_movk_i32 s22, 4
	v_addc_co_u32_e32 v6, vcc, 0, v6, vcc
	v_cmp_gt_i64_e32 vcc, s[24:25], v[8:9]
	v_readlane_b32 s25, v9, 60
	s_movk_i32 s24, 3
	v_addc_co_u32_e32 v6, vcc, 0, v6, vcc
	v_cmp_gt_i64_e32 vcc, s[22:23], v[8:9]
	v_readlane_b32 s23, v9, 61
	s_movk_i32 s22, 2
	v_addc_co_u32_e32 v6, vcc, 0, v6, vcc
	v_cmp_gt_i64_e32 vcc, s[24:25], v[8:9]
	v_readlane_b32 s25, v9, 62
	s_movk_i32 s24, 1
	v_addc_co_u32_e32 v6, vcc, 0, v6, vcc
	v_cmp_gt_i64_e32 vcc, s[22:23], v[8:9]
	v_readlane_b32 s23, v9, 63
	s_movk_i32 s22, 0
	v_addc_co_u32_e32 v6, vcc, 0, v6, vcc
	v_cmp_gt_i64_e32 vcc, s[24:25], v[8:9]
	s_nop 1
	v_addc_co_u32_e32 v6, vcc, 0, v6, vcc
	v_cmp_gt_i64_e32 vcc, s[22:23], v[8:9]
	s_nop 1
	v_addc_co_u32_e32 v6, vcc, 0, v6, vcc
	v_cmp_gt_u32_e32 vcc, 6, v6
	s_nop 1
	v_cndmask_b32_e32 v5, 0, v2, vcc
	s_nop 1
	v_add_f32_dpp v5, v5, v5 quad_perm:[1,0,3,2] row_mask:0xf bank_mask:0xf
	s_nop 1
	v_add_f32_dpp v5, v5, v5 quad_perm:[2,3,0,1] row_mask:0xf bank_mask:0xf
	s_nop 1
	v_add_f32_dpp v5, v5, v5 row_half_mirror row_mask:0xf bank_mask:0xf
	s_nop 1
	v_add_f32_dpp v5, v5, v5 row_mirror row_mask:0xf bank_mask:0xf
	s_nop 0
	ds_bpermute_b32 v7, v222, v5
	s_waitcnt lgkmcnt(0)
	v_add_f32_e32 v5, v5, v7
	v_mov_b32_e32 v7, v5
	s_nop 1
	v_permlane32_swap_b32_e32 v7, v5
	s_and_saveexec_b64 s[2:3], vcc
	s_cbranch_execz .LBB0_563
	s_waitcnt lgkmcnt(0)
	v_add_f32_e32 v5, v5, v7
	v_div_scale_f32 v11, s[4:5], v5, v5, v2
	v_add3_u32 v6, s36, 36, v6
	v_rcp_f32_e32 v12, v11
	v_ashrrev_i32_e32 v7, 31, v6
	v_lshlrev_b64 v[6:7], 2, v[6:7]
	v_lshl_add_u64 v[8:9], s[26:27], 0, v[6:7]
	ds_add_rtn_u32 v10, v227, v243
	global_store_dword v[8:9], v230, off
	v_fma_f32 v8, -v11, v12, 1.0
	v_fmac_f32_e32 v12, v8, v12
	v_div_scale_f32 v8, vcc, v2, v5, v2
	v_mul_f32_e32 v9, v8, v12
	v_fma_f32 v13, -v11, v9, v8
	v_fmac_f32_e32 v9, v13, v12
	v_fma_f32 v8, -v11, v9, v8
	v_div_fmas_f32 v8, v8, v12, v9
	v_div_fixup_f32 v2, v8, v5, v2
	v_mul_f32_e32 v2, 0x40200000, v2
	v_lshl_add_u64 v[8:9], s[28:29], 0, v[6:7]
	v_lshl_add_u64 v[6:7], s[30:31], 0, v[6:7]
	global_store_dword v[8:9], v2, off
	s_waitcnt lgkmcnt(0)
	global_store_dword v[6:7], v10, off
; __device__ __forceinline__ void phase_nrr(const Frame& F, const Args& a, int l, const bf16_t* XA, const float* g, const float* modl, unsigned char* XN8) {
;     ...
;         for (int i = 0; i < 8; ++i) { const int t = tb + i;
;             const float lg = Pl[(w * 8 + i) * NE + lane] + Pl[(64 + w * 8 + i) * NE + lane]; const float sc = 1.f / (1.f + __expf(-lg)); const float bb = sc + bias;
;             float m1 = bb; m1 = fmaxf(m1, __shfl_xor(m1, 1)); m1 = fmaxf(m1, __shfl_xor(m1, 2)); m1 = fmaxf(m1, __shfl_xor(m1, 4));
;             const unsigned long long eq = __ballot(bb == m1); const int gbase = lane & ~7; const unsigned grpmask = (unsigned)((eq >> gbase) & 0xffull);
;             const int first = gbase + __builtin_ctz(grpmask);
;             float m2 = (lane == first) ? -INFINITY : bb; m2 = fmaxf(m2, __shfl_xor(m2, 1)); m2 = fmaxf(m2, __shfl_xor(m2, 2)); m2 = fmaxf(m2, __shfl_xor(m2, 4));
;             const float gsum = m1 + m2; const int gq = lane >> 3;
;             int grank = 0;
; #pragma unroll
;             for (int g2 = 0; g2 < 8; ++g2) { const float v = __int_as_float(__builtin_amdgcn_readlane(__float_as_int(gsum), g2 * 8)); grank += (v > gsum || (v == gsum && g2 < gq)) ? 1 : 0; }
;             const bool keep = grank < 4; const float val = keep ? bb : -INFINITY;
;             int rank = 0;
; #pragma unroll 8
;             for (int e2 = 0; e2 < 64; ++e2) { const float v = __int_as_float(__builtin_amdgcn_readlane(__float_as_int(val), e2)); rank += (v > val || (v == val && e2 < lane)) ? 1 : 0; }
.LBB0_563:
	s_or_b64 exec, exec, s[2:3]
	v_add_u32_e32 v2, s87, v226
	ds_read_b32 v2, v2
	ds_read_b32 v4, v4 offset:18176
	s_waitcnt lgkmcnt(0)
	v_add_f32_e32 v2, v2, v4
	v_mul_f32_e32 v2, 0xbfb8aa3b, v2
	v_exp_f32_e32 v2, v2
	s_nop 0
	v_add_f32_e32 v2, 1.0, v2
	v_div_scale_f32 v4, s[2:3], v2, v2, 1.0
	v_rcp_f32_e32 v5, v4
	s_mov_b32 s2, 0
	v_fma_f32 v6, -v4, v5, 1.0
	v_fmac_f32_e32 v5, v6, v5
	v_div_scale_f32 v6, vcc, 1.0, v2, 1.0
	v_mul_f32_e32 v7, v6, v5
	v_fma_f32 v8, -v4, v7, v6
	v_fmac_f32_e32 v7, v8, v5
	v_fma_f32 v4, -v4, v7, v6
	v_div_fmas_f32 v4, v4, v5, v7
	v_div_fixup_f32 v2, v4, v2, 1.0
	v_add_f32_e32 v3, v3, v2
	s_nop 1
	s_waitcnt lgkmcnt(0)
	v_max_f32_dpp v4, v3, v3 quad_perm:[1,0,3,2] row_mask:0xf bank_mask:0xf
	s_nop 1
	s_waitcnt lgkmcnt(0)
	v_max_f32_dpp v4, v4, v4 quad_perm:[2,3,0,1] row_mask:0xf bank_mask:0xf
	s_nop 1
	s_waitcnt lgkmcnt(0)
	v_max_f32_dpp v6, v4, v4 row_half_mirror row_mask:0xf bank_mask:0xf
	v_cmp_eq_f32_e32 vcc, v3, v6
	s_nop 1
	v_lshrrev_b64 v[4:5], v200, vcc
	v_ffbl_b32_sdwa v4, v4 dst_sel:DWORD dst_unused:UNUSED_PAD src0_sel:BYTE_0
	v_add_u32_e32 v4, v4, v200
	v_cmp_ne_u32_e32 vcc, v230, v4
	s_nop 1
	v_cndmask_b32_e32 v4, v245, v3, vcc
	s_nop 1
	s_waitcnt lgkmcnt(0)
	v_max_f32_dpp v4, v4, v4 quad_perm:[1,0,3,2] row_mask:0xf bank_mask:0xf
	s_nop 1
	s_waitcnt lgkmcnt(0)
	v_max_f32_dpp v4, v4, v4 quad_perm:[2,3,0,1] row_mask:0xf bank_mask:0xf
	s_nop 1
	s_waitcnt lgkmcnt(0)
	v_max_f32_dpp v4, v4, v4 row_half_mirror row_mask:0xf bank_mask:0xf
	v_add_f32_e32 v4, v6, v4
	s_nop 0
	v_readlane_b32 s3, v4, 0
	s_nop 1
	v_cmp_eq_f32_e64 s[22:23], s3, v4
	v_cmp_gt_f32_e32 vcc, s3, v4
	s_and_b64 s[4:5], s[6:7], s[22:23]
	v_readlane_b32 s3, v4, 8
	s_or_b64 s[4:5], vcc, s[4:5]
	v_cndmask_b32_e64 v5, 0, 1, s[4:5]
	v_cmp_eq_f32_e64 s[22:23], s3, v4
	v_cmp_gt_f32_e32 vcc, s3, v4
	s_and_b64 s[4:5], s[8:9], s[22:23]
	v_readlane_b32 s3, v4, 16
	s_or_b64 s[4:5], vcc, s[4:5]
	v_cndmask_b32_e64 v6, 0, 1, s[4:5]
	v_cmp_eq_f32_e64 s[22:23], s3, v4
	v_cmp_gt_f32_e32 vcc, s3, v4
	s_and_b64 s[4:5], s[10:11], s[22:23]
	v_readlane_b32 s3, v4, 24
	s_or_b64 s[4:5], vcc, s[4:5]
	v_cndmask_b32_e64 v7, 0, 1, s[4:5]
	v_cmp_eq_f32_e64 s[22:23], s3, v4
	v_cmp_gt_f32_e32 vcc, s3, v4
	s_and_b64 s[4:5], s[12:13], s[22:23]
	v_readlane_b32 s3, v4, 32
	s_or_b64 s[4:5], vcc, s[4:5]
	v_cndmask_b32_e64 v8, 0, 1, s[4:5]
	v_cmp_eq_f32_e64 s[22:23], s3, v4
	v_cmp_gt_f32_e32 vcc, s3, v4
	s_and_b64 s[4:5], s[14:15], s[22:23]
	v_readlane_b32 s3, v4, 40
	s_or_b64 s[4:5], vcc, s[4:5]
	v_cndmask_b32_e64 v9, 0, 1, s[4:5]
	v_cmp_eq_f32_e64 s[22:23], s3, v4
	v_cmp_gt_f32_e32 vcc, s3, v4
	s_and_b64 s[4:5], s[16:17], s[22:23]
	v_readlane_b32 s3, v4, 48
	s_or_b64 s[4:5], vcc, s[4:5]
	v_cndmask_b32_e64 v10, 0, 1, s[4:5]
	v_cmp_eq_f32_e64 s[22:23], s3, v4
	v_cmp_gt_f32_e32 vcc, s3, v4
	s_and_b64 s[4:5], s[18:19], s[22:23]
	v_readlane_b32 s3, v4, 56
	s_or_b64 s[4:5], vcc, s[4:5]
	v_cndmask_b32_e64 v11, 0, 1, s[4:5]
	v_cmp_gt_f32_e32 vcc, s3, v4
	s_nop 1
	v_cndmask_b32_e64 v4, 0, 1, vcc
	v_add_u32_e32 v4, v6, v4
	v_add3_u32 v4, v4, v5, v7
	v_add3_u32 v4, v4, v8, v9
	v_add3_u32 v4, v4, v10, v11
	v_cmp_gt_u32_e32 vcc, 4, v4
	v_mov_b32_e32 v4, 0
	s_nop 0
	v_cndmask_b32_e32 v3, v245, v3, vcc
	v_ashrrev_i32_e32 v9, 31, v3
	v_sub_u32_e32 v8, 63, v230
	v_and_b32_e32 v9, 0x7fffffff, v9
	v_xor_b32_e32 v9, v3, v9
	s_nop 0
	v_readlane_b32 s25, v9, 0
	s_movk_i32 s24, 63
	v_readlane_b32 s23, v9, 1
	s_movk_i32 s22, 62
	v_cmp_gt_i64_e32 vcc, s[24:25], v[8:9]
	v_readlane_b32 s25, v9, 2
	s_movk_i32 s24, 61
	v_addc_co_u32_e32 v4, vcc, 0, v4, vcc
	v_cmp_gt_i64_e32 vcc, s[22:23], v[8:9]
	v_readlane_b32 s23, v9, 3
	s_movk_i32 s22, 60
	v_addc_co_u32_e32 v4, vcc, 0, v4, vcc
	v_cmp_gt_i64_e32 vcc, s[24:25], v[8:9]
	v_readlane_b32 s25, v9, 4
	s_movk_i32 s24, 59
	v_addc_co_u32_e32 v4, vcc, 0, v4, vcc
	v_cmp_gt_i64_e32 vcc, s[22:23], v[8:9]
	v_readlane_b32 s23, v9, 5
	s_movk_i32 s22, 58
	v_addc_co_u32_e32 v4, vcc, 0, v4, vcc
	v_cmp_gt_i64_e32 vcc, s[24:25], v[8:9]
	v_readlane_b32 s25, v9, 6
	s_movk_i32 s24, 57
	v_addc_co_u32_e32 v4, vcc, 0, v4, vcc
	v_cmp_gt_i64_e32 vcc, s[22:23], v[8:9]
	v_readlane_b32 s23, v9, 7
	s_movk_i32 s22, 56
	v_addc_co_u32_e32 v4, vcc, 0, v4, vcc
	v_cmp_gt_i64_e32 vcc, s[24:25], v[8:9]
	v_readlane_b32 s25, v9, 8
	s_movk_i32 s24, 55
	v_addc_co_u32_e32 v4, vcc, 0, v4, vcc
	v_cmp_gt_i64_e32 vcc, s[22:23], v[8:9]
	v_readlane_b32 s23, v9, 9
	s_movk_i32 s22, 54
	v_addc_co_u32_e32 v4, vcc, 0, v4, vcc
	v_cmp_gt_i64_e32 vcc, s[24:25], v[8:9]
	v_readlane_b32 s25, v9, 10
	s_movk_i32 s24, 53
	v_addc_co_u32_e32 v4, vcc, 0, v4, vcc
	v_cmp_gt_i64_e32 vcc, s[22:23], v[8:9]
	v_readlane_b32 s23, v9, 11
	s_movk_i32 s22, 52
	v_addc_co_u32_e32 v4, vcc, 0, v4, vcc
	v_cmp_gt_i64_e32 vcc, s[24:25], v[8:9]
	v_readlane_b32 s25, v9, 12
	s_movk_i32 s24, 51
	v_addc_co_u32_e32 v4, vcc, 0, v4, vcc
	v_cmp_gt_i64_e32 vcc, s[22:23], v[8:9]
	v_readlane_b32 s23, v9, 13
	s_movk_i32 s22, 50
	v_addc_co_u32_e32 v4, vcc, 0, v4, vcc
	v_cmp_gt_i64_e32 vcc, s[24:25], v[8:9]
	v_readlane_b32 s25, v9, 14
	s_movk_i32 s24, 49
	v_addc_co_u32_e32 v4, vcc, 0, v4, vcc
	v_cmp_gt_i64_e32 vcc, s[22:23], v[8:9]
	v_readlane_b32 s23, v9, 15
	s_movk_i32 s22, 48
	v_addc_co_u32_e32 v4, vcc, 0, v4, vcc
	v_cmp_gt_i64_e32 vcc, s[24:25], v[8:9]
	v_readlane_b32 s25, v9, 16
	s_movk_i32 s24, 47
	v_addc_co_u32_e32 v4, vcc, 0, v4, vcc
	v_cmp_gt_i64_e32 vcc, s[22:23], v[8:9]
	v_readlane_b32 s23, v9, 17
	s_movk_i32 s22, 46
	v_addc_co_u32_e32 v4, vcc, 0, v4, vcc
	v_cmp_gt_i64_e32 vcc, s[24:25], v[8:9]
	v_readlane_b32 s25, v9, 18
	s_movk_i32 s24, 45
	v_addc_co_u32_e32 v4, vcc, 0, v4, vcc
	v_cmp_gt_i64_e32 vcc, s[22:23], v[8:9]
; __device__ __forceinline__ float wave_sum(float v) {
; #pragma unroll
;     for (int o = 1; o < 64; o <<= 1) v += __shfl_xor(v, o);
;     return v;
; __device__ __forceinline__ void phase_nrr(const Frame& F, const Args& a, int l, const bf16_t* XA, const float* g, const float* modl, unsigned char* XN8) {
;     ...
;             int rank = 0;
; #pragma unroll 8
;             for (int e2 = 0; e2 < 64; ++e2) { const float v = __int_as_float(__builtin_amdgcn_readlane(__float_as_int(val), e2)); rank += (v > val || (v == val && e2 < lane)) ? 1 : 0; }
;             const bool sel = rank < TOPK;
;             const float ssum = wave_sum(sel ? sc : 0.f);
;             if (sel) { const int p = atomicAdd((int*)(hist + lane), 1); top_e[t * TOPK + rank] = lane; gate[t * TOPK + rank] = sc / ssum * 2.5f; lpos[t * TOPK + rank] = p; }
	v_readlane_b32 s23, v9, 19
	s_movk_i32 s22, 44
	v_addc_co_u32_e32 v4, vcc, 0, v4, vcc
	v_cmp_gt_i64_e32 vcc, s[24:25], v[8:9]
	v_readlane_b32 s25, v9, 20
	s_movk_i32 s24, 43
	v_addc_co_u32_e32 v4, vcc, 0, v4, vcc
	v_cmp_gt_i64_e32 vcc, s[22:23], v[8:9]
	v_readlane_b32 s23, v9, 21
	s_movk_i32 s22, 42
	v_addc_co_u32_e32 v4, vcc, 0, v4, vcc
	v_cmp_gt_i64_e32 vcc, s[24:25], v[8:9]
	v_readlane_b32 s25, v9, 22
	s_movk_i32 s24, 41
	v_addc_co_u32_e32 v4, vcc, 0, v4, vcc
	v_cmp_gt_i64_e32 vcc, s[22:23], v[8:9]
	v_readlane_b32 s23, v9, 23
	s_movk_i32 s22, 40
	v_addc_co_u32_e32 v4, vcc, 0, v4, vcc
	v_cmp_gt_i64_e32 vcc, s[24:25], v[8:9]
	v_readlane_b32 s25, v9, 24
	s_movk_i32 s24, 39
	v_addc_co_u32_e32 v4, vcc, 0, v4, vcc
	v_cmp_gt_i64_e32 vcc, s[22:23], v[8:9]
	v_readlane_b32 s23, v9, 25
	s_movk_i32 s22, 38
	v_addc_co_u32_e32 v4, vcc, 0, v4, vcc
	v_cmp_gt_i64_e32 vcc, s[24:25], v[8:9]
	v_readlane_b32 s25, v9, 26
	s_movk_i32 s24, 37
	v_addc_co_u32_e32 v4, vcc, 0, v4, vcc
	v_cmp_gt_i64_e32 vcc, s[22:23], v[8:9]
	v_readlane_b32 s23, v9, 27
	s_movk_i32 s22, 36
	v_addc_co_u32_e32 v4, vcc, 0, v4, vcc
	v_cmp_gt_i64_e32 vcc, s[24:25], v[8:9]
	v_readlane_b32 s25, v9, 28
	s_movk_i32 s24, 35
	v_addc_co_u32_e32 v4, vcc, 0, v4, vcc
	v_cmp_gt_i64_e32 vcc, s[22:23], v[8:9]
	v_readlane_b32 s23, v9, 29
	s_movk_i32 s22, 34
	v_addc_co_u32_e32 v4, vcc, 0, v4, vcc
	v_cmp_gt_i64_e32 vcc, s[24:25], v[8:9]
	v_readlane_b32 s25, v9, 30
	s_movk_i32 s24, 33
	v_addc_co_u32_e32 v4, vcc, 0, v4, vcc
	v_cmp_gt_i64_e32 vcc, s[22:23], v[8:9]
	v_readlane_b32 s23, v9, 31
	s_movk_i32 s22, 32
	v_addc_co_u32_e32 v4, vcc, 0, v4, vcc
	v_cmp_gt_i64_e32 vcc, s[24:25], v[8:9]
	v_readlane_b32 s25, v9, 32
	s_movk_i32 s24, 31
	v_addc_co_u32_e32 v4, vcc, 0, v4, vcc
	v_cmp_gt_i64_e32 vcc, s[22:23], v[8:9]
	v_readlane_b32 s23, v9, 33
	s_movk_i32 s22, 30
	v_addc_co_u32_e32 v4, vcc, 0, v4, vcc
	v_cmp_gt_i64_e32 vcc, s[24:25], v[8:9]
	v_readlane_b32 s25, v9, 34
	s_movk_i32 s24, 29
	v_addc_co_u32_e32 v4, vcc, 0, v4, vcc
	v_cmp_gt_i64_e32 vcc, s[22:23], v[8:9]
	v_readlane_b32 s23, v9, 35
	s_movk_i32 s22, 28
	v_addc_co_u32_e32 v4, vcc, 0, v4, vcc
	v_cmp_gt_i64_e32 vcc, s[24:25], v[8:9]
	v_readlane_b32 s25, v9, 36
	s_movk_i32 s24, 27
	v_addc_co_u32_e32 v4, vcc, 0, v4, vcc
	v_cmp_gt_i64_e32 vcc, s[22:23], v[8:9]
	v_readlane_b32 s23, v9, 37
	s_movk_i32 s22, 26
	v_addc_co_u32_e32 v4, vcc, 0, v4, vcc
	v_cmp_gt_i64_e32 vcc, s[24:25], v[8:9]
	v_readlane_b32 s25, v9, 38
	s_movk_i32 s24, 25
	v_addc_co_u32_e32 v4, vcc, 0, v4, vcc
	v_cmp_gt_i64_e32 vcc, s[22:23], v[8:9]
	v_readlane_b32 s23, v9, 39
	s_movk_i32 s22, 24
	v_addc_co_u32_e32 v4, vcc, 0, v4, vcc
	v_cmp_gt_i64_e32 vcc, s[24:25], v[8:9]
	v_readlane_b32 s25, v9, 40
	s_movk_i32 s24, 23
	v_addc_co_u32_e32 v4, vcc, 0, v4, vcc
	v_cmp_gt_i64_e32 vcc, s[22:23], v[8:9]
	v_readlane_b32 s23, v9, 41
	s_movk_i32 s22, 22
	v_addc_co_u32_e32 v4, vcc, 0, v4, vcc
	v_cmp_gt_i64_e32 vcc, s[24:25], v[8:9]
	v_readlane_b32 s25, v9, 42
	s_movk_i32 s24, 21
	v_addc_co_u32_e32 v4, vcc, 0, v4, vcc
	v_cmp_gt_i64_e32 vcc, s[22:23], v[8:9]
	v_readlane_b32 s23, v9, 43
	s_movk_i32 s22, 20
	v_addc_co_u32_e32 v4, vcc, 0, v4, vcc
	v_cmp_gt_i64_e32 vcc, s[24:25], v[8:9]
	v_readlane_b32 s25, v9, 44
	s_movk_i32 s24, 19
	v_addc_co_u32_e32 v4, vcc, 0, v4, vcc
	v_cmp_gt_i64_e32 vcc, s[22:23], v[8:9]
	v_readlane_b32 s23, v9, 45
	s_movk_i32 s22, 18
	v_addc_co_u32_e32 v4, vcc, 0, v4, vcc
	v_cmp_gt_i64_e32 vcc, s[24:25], v[8:9]
	v_readlane_b32 s25, v9, 46
	s_movk_i32 s24, 17
	v_addc_co_u32_e32 v4, vcc, 0, v4, vcc
	v_cmp_gt_i64_e32 vcc, s[22:23], v[8:9]
	v_readlane_b32 s23, v9, 47
	s_movk_i32 s22, 16
	v_addc_co_u32_e32 v4, vcc, 0, v4, vcc
	v_cmp_gt_i64_e32 vcc, s[24:25], v[8:9]
	v_readlane_b32 s25, v9, 48
	s_movk_i32 s24, 15
	v_addc_co_u32_e32 v4, vcc, 0, v4, vcc
	v_cmp_gt_i64_e32 vcc, s[22:23], v[8:9]
	v_readlane_b32 s23, v9, 49
	s_movk_i32 s22, 14
	v_addc_co_u32_e32 v4, vcc, 0, v4, vcc
	v_cmp_gt_i64_e32 vcc, s[24:25], v[8:9]
	v_readlane_b32 s25, v9, 50
	s_movk_i32 s24, 13
	v_addc_co_u32_e32 v4, vcc, 0, v4, vcc
	v_cmp_gt_i64_e32 vcc, s[22:23], v[8:9]
	v_readlane_b32 s23, v9, 51
	s_movk_i32 s22, 12
	v_addc_co_u32_e32 v4, vcc, 0, v4, vcc
	v_cmp_gt_i64_e32 vcc, s[24:25], v[8:9]
	v_readlane_b32 s25, v9, 52
	s_movk_i32 s24, 11
	v_addc_co_u32_e32 v4, vcc, 0, v4, vcc
	v_cmp_gt_i64_e32 vcc, s[22:23], v[8:9]
	v_readlane_b32 s23, v9, 53
	s_movk_i32 s22, 10
	v_addc_co_u32_e32 v4, vcc, 0, v4, vcc
	v_cmp_gt_i64_e32 vcc, s[24:25], v[8:9]
	v_readlane_b32 s25, v9, 54
	s_movk_i32 s24, 9
	v_addc_co_u32_e32 v4, vcc, 0, v4, vcc
	v_cmp_gt_i64_e32 vcc, s[22:23], v[8:9]
	v_readlane_b32 s23, v9, 55
	s_movk_i32 s22, 8
	v_addc_co_u32_e32 v4, vcc, 0, v4, vcc
	v_cmp_gt_i64_e32 vcc, s[24:25], v[8:9]
	v_readlane_b32 s25, v9, 56
	s_movk_i32 s24, 7
	v_addc_co_u32_e32 v4, vcc, 0, v4, vcc
	v_cmp_gt_i64_e32 vcc, s[22:23], v[8:9]
	v_readlane_b32 s23, v9, 57
	s_movk_i32 s22, 6
	v_addc_co_u32_e32 v4, vcc, 0, v4, vcc
	v_cmp_gt_i64_e32 vcc, s[24:25], v[8:9]
	v_readlane_b32 s25, v9, 58
	s_movk_i32 s24, 5
	v_addc_co_u32_e32 v4, vcc, 0, v4, vcc
	v_cmp_gt_i64_e32 vcc, s[22:23], v[8:9]
	v_readlane_b32 s23, v9, 59
	s_movk_i32 s22, 4
	v_addc_co_u32_e32 v4, vcc, 0, v4, vcc
	v_cmp_gt_i64_e32 vcc, s[24:25], v[8:9]
	v_readlane_b32 s25, v9, 60
	s_movk_i32 s24, 3
	v_addc_co_u32_e32 v4, vcc, 0, v4, vcc
	v_cmp_gt_i64_e32 vcc, s[22:23], v[8:9]
	v_readlane_b32 s23, v9, 61
	s_movk_i32 s22, 2
	v_addc_co_u32_e32 v4, vcc, 0, v4, vcc
	v_cmp_gt_i64_e32 vcc, s[24:25], v[8:9]
	v_readlane_b32 s25, v9, 62
	s_movk_i32 s24, 1
	v_addc_co_u32_e32 v4, vcc, 0, v4, vcc
	v_cmp_gt_i64_e32 vcc, s[22:23], v[8:9]
	v_readlane_b32 s23, v9, 63
	s_movk_i32 s22, 0
	v_addc_co_u32_e32 v4, vcc, 0, v4, vcc
	v_cmp_gt_i64_e32 vcc, s[24:25], v[8:9]
	s_nop 1
	v_addc_co_u32_e32 v4, vcc, 0, v4, vcc
	v_cmp_gt_i64_e32 vcc, s[22:23], v[8:9]
	s_nop 1
	v_addc_co_u32_e32 v4, vcc, 0, v4, vcc
	v_cmp_gt_u32_e32 vcc, 6, v4
	s_nop 1
	v_cndmask_b32_e32 v3, 0, v2, vcc
	s_nop 1
	v_add_f32_dpp v3, v3, v3 quad_perm:[1,0,3,2] row_mask:0xf bank_mask:0xf
	s_nop 1
	v_add_f32_dpp v3, v3, v3 quad_perm:[2,3,0,1] row_mask:0xf bank_mask:0xf
	s_nop 1
	v_add_f32_dpp v3, v3, v3 row_half_mirror row_mask:0xf bank_mask:0xf
	s_nop 1
	v_add_f32_dpp v3, v3, v3 row_mirror row_mask:0xf bank_mask:0xf
	s_nop 0
	ds_bpermute_b32 v5, v222, v3
	s_waitcnt lgkmcnt(0)
	v_add_f32_e32 v3, v3, v5
	v_mov_b32_e32 v5, v3
	s_nop 1
	v_permlane32_swap_b32_e32 v5, v3
	s_and_saveexec_b64 s[2:3], vcc
	s_cbranch_execz .LBB0_567
; __device__ __forceinline__ void phase_nrr(const Frame& F, const Args& a, int l, const bf16_t* XA, const float* g, const float* modl, unsigned char* XN8) {
;     ...
;             if (sel) { const int p = atomicAdd((int*)(hist + lane), 1); top_e[t * TOPK + rank] = lane; gate[t * TOPK + rank] = sc / ssum * 2.5f; lpos[t * TOPK + rank] = p; }
	s_waitcnt lgkmcnt(0)
	v_add_f32_e32 v3, v3, v5
	v_div_scale_f32 v9, s[4:5], v3, v3, v2
	v_add3_u32 v4, s36, 42, v4
	v_rcp_f32_e32 v10, v9
	v_ashrrev_i32_e32 v5, 31, v4
	v_lshlrev_b64 v[4:5], 2, v[4:5]
	v_lshl_add_u64 v[6:7], s[26:27], 0, v[4:5]
	ds_add_rtn_u32 v8, v227, v243
	global_store_dword v[6:7], v230, off
	v_fma_f32 v6, -v9, v10, 1.0
	v_fmac_f32_e32 v10, v6, v10
	v_div_scale_f32 v6, vcc, v2, v3, v2
	v_mul_f32_e32 v7, v6, v10
	v_fma_f32 v11, -v9, v7, v6
	v_fmac_f32_e32 v7, v11, v10
	v_fma_f32 v6, -v9, v7, v6
	v_div_fmas_f32 v6, v6, v10, v7
	v_div_fixup_f32 v2, v6, v3, v2
	v_mul_f32_e32 v6, 0x40200000, v2
	v_lshl_add_u64 v[2:3], s[28:29], 0, v[4:5]
	global_store_dword v[2:3], v6, off
	v_lshl_add_u64 v[2:3], s[30:31], 0, v[4:5]
	s_waitcnt lgkmcnt(0)
	global_store_dword v[2:3], v8, off

; __device__ __forceinline__ unsigned xb_add(unsigned* p, unsigned v) { return __hip_atomic_fetch_add(p, v, __ATOMIC_RELAXED, __HIP_MEMORY_SCOPE_AGENT); }
; __device__ __forceinline__ void xcd_barrier(const XcdBarrier& b) {
;     asm volatile("s_waitcnt vmcnt(0)" ::: "memory");
;     __syncthreads();
;     if (threadIdx.x == 0) {
;         unsigned* bar = b.bar;
;         __builtin_amdgcn_s_waitcnt(0);
;         unsigned nloc = b.st[0], nx = b.st[1];
;         if (nloc == 0u) { xcd_barrier_complete(bar, b.x, nloc, nx); b.st[0] = nloc; b.st[1] = nx; }
;         const unsigned old = xb_add(&bar[XB_XSUB(b.x)], 1u);
.LBB0_569:
	s_and_saveexec_b64 s[2:3], s[96:97]
	v_readlane_b32 s88, v255, 24
	v_readlane_b32 s89, v255, 25
	v_readlane_b32 s90, v255, 26
	v_readlane_b32 s91, v255, 27
	s_cbranch_execz .LBB0_572
	s_mov_b64 s[4:5], exec
	v_mbcnt_lo_u32_b32 v1, s4, 0
	v_mbcnt_hi_u32_b32 v1, s5, v1
	v_cmp_eq_u32_e32 vcc, 0, v1
	s_and_b64 s[6:7], exec, vcc
	s_mov_b64 exec, s[6:7]
	s_cbranch_execz .LBB0_572
	s_bcnt1_i32_b64 s4, s[4:5]
	v_mov_b32_e32 v1, 0x1000
	v_mov_b32_e32 v2, s4
.LBB0_572:
	s_or_b64 exec, exec, s[2:3]
	v_readlane_b32 s8, v255, 4
	v_readlane_b32 s9, v255, 5
	v_readlane_b32 s72, v255, 29
	s_cmp_lt_i32 s9, 9
	v_readlane_b32 s87, v255, 28
	v_readlane_b32 s73, v255, 30
	v_readlane_b32 s10, v255, 6
	v_readlane_b32 s11, v255, 7
	s_cbranch_scc1 .LBB0_622
	s_waitcnt vmcnt(0)
	s_waitcnt vmcnt(0)
	s_barrier
	s_and_saveexec_b64 s[2:3], s[96:97]
	s_cbranch_execz .LBB0_621
	v_readlane_b32 s4, v255, 10
	s_waitcnt vmcnt(0) expcnt(0) lgkmcnt(0)
	s_nop 0
	v_mov_b32_e32 v1, s4
	ds_read_b32 v3, v1
	ds_read_b32 v1, v1 offset:4
	s_waitcnt lgkmcnt(1)
	v_cmp_ne_u32_e32 vcc, 0, v3
	s_cbranch_vccnz .LBB0_589
	v_readlane_b32 s4, v255, 0
	v_readlane_b32 s5, v255, 1
	s_load_dwordx2 s[8:9], s[4:5], 0x4
	v_readlane_b32 s10, v255, 8
	v_readlane_b32 s11, v255, 9
	s_add_u32 s4, s10, 0x1000
	s_addc_u32 s5, s11, 0
	s_add_u32 s6, s10, 0x1100
	s_addc_u32 s7, s11, 0
	s_waitcnt lgkmcnt(0)
	s_mul_i32 s18, s8, s93
	s_add_u32 s8, s10, 0x1200
	s_mul_i32 s18, s18, s9
	s_addc_u32 s9, s11, 0
	s_add_u32 s10, s10, 0x1300
	s_addc_u32 s11, s11, 0
	s_mov_b32 s19, 1
	v_mov_b32_e32 v17, 0
	s_branch .LBB0_577

; __device__ __forceinline__ unsigned xb_add(unsigned* p, unsigned v) { return __hip_atomic_fetch_add(p, v, __ATOMIC_RELAXED, __HIP_MEMORY_SCOPE_AGENT); }
; __device__ __forceinline__ void xcd_barrier(const XcdBarrier& b) {
;     asm volatile("s_waitcnt vmcnt(0)" ::: "memory");
;     __syncthreads();
;     if (threadIdx.x == 0) {
;         unsigned* bar = b.bar;
;         __builtin_amdgcn_s_waitcnt(0);
;         unsigned nloc = b.st[0], nx = b.st[1];
;         if (nloc == 0u) { xcd_barrier_complete(bar, b.x, nloc, nx); b.st[0] = nloc; b.st[1] = nx; }
;         const unsigned old = xb_add(&bar[XB_XSUB(b.x)], 1u);
.LBB0_678:
	s_and_saveexec_b64 s[2:3], s[96:97]
	s_cbranch_execz .LBB0_681
	s_mov_b64 s[4:5], exec
	v_mbcnt_lo_u32_b32 v1, s4, 0
	v_mbcnt_hi_u32_b32 v1, s5, v1
	v_cmp_eq_u32_e32 vcc, 0, v1
	s_and_b64 s[6:7], exec, vcc
	s_mov_b64 exec, s[6:7]
	s_cbranch_execz .LBB0_681
	s_bcnt1_i32_b64 s4, s[4:5]
	v_mov_b32_e32 v1, 0x1000
	v_mov_b32_e32 v2, s4
.LBB0_681:
	s_or_b64 exec, exec, s[2:3]
	v_readlane_b32 s8, v255, 4
	v_readlane_b32 s9, v255, 5
	s_cmp_lt_i32 s9, 12
	v_readlane_b32 s10, v255, 6
	v_readlane_b32 s11, v255, 7
	s_cbranch_scc1 .LBB0_731
	s_waitcnt vmcnt(0)
	s_barrier
	s_and_saveexec_b64 s[2:3], s[96:97]
	s_cbranch_execz .LBB0_730
	v_readlane_b32 s4, v255, 10
	s_waitcnt vmcnt(0) expcnt(0) lgkmcnt(0)
	s_nop 0
	v_mov_b32_e32 v1, s4
	ds_read_b32 v3, v1
	ds_read_b32 v1, v1 offset:4
	s_waitcnt lgkmcnt(1)
	v_cmp_ne_u32_e32 vcc, 0, v3
	s_cbranch_vccnz .LBB0_698
	v_readlane_b32 s4, v255, 0
	v_readlane_b32 s5, v255, 1
	s_load_dwordx2 s[8:9], s[4:5], 0x4
	v_readlane_b32 s10, v255, 8
	v_readlane_b32 s11, v255, 9
	s_add_u32 s4, s10, 0x1000
	s_addc_u32 s5, s11, 0
	s_add_u32 s6, s10, 0x1100
	s_addc_u32 s7, s11, 0
	s_waitcnt lgkmcnt(0)
	s_mul_i32 s18, s8, s93
	s_add_u32 s8, s10, 0x1200
	s_mul_i32 s18, s18, s9
	s_addc_u32 s9, s11, 0
	s_add_u32 s10, s10, 0x1300
	s_addc_u32 s11, s11, 0
	s_mov_b32 s19, 1
	v_mov_b32_e32 v17, 0
	s_branch .LBB0_686

; __device__ __forceinline__ unsigned xb_add(unsigned* p, unsigned v) { return __hip_atomic_fetch_add(p, v, __ATOMIC_RELAXED, __HIP_MEMORY_SCOPE_AGENT); }
; __device__ __forceinline__ void xcd_barrier(const XcdBarrier& b) {
;     asm volatile("s_waitcnt vmcnt(0)" ::: "memory");
;     __syncthreads();
;     if (threadIdx.x == 0) {
;         unsigned* bar = b.bar;
;         __builtin_amdgcn_s_waitcnt(0);
;         unsigned nloc = b.st[0], nx = b.st[1];
;         if (nloc == 0u) { xcd_barrier_complete(bar, b.x, nloc, nx); b.st[0] = nloc; b.st[1] = nx; }
;         const unsigned old = xb_add(&bar[XB_XSUB(b.x)], 1u);
.LBB0_784:
	s_and_saveexec_b64 s[0:1], s[96:97]
	s_cbranch_execz .LBB0_787
	s_mov_b64 s[2:3], exec
	v_mbcnt_lo_u32_b32 v1, s2, 0
	v_mbcnt_hi_u32_b32 v1, s3, v1
	v_cmp_eq_u32_e32 vcc, 0, v1
	s_and_b64 s[4:5], exec, vcc
	s_mov_b64 exec, s[4:5]
	s_cbranch_execz .LBB0_787
	s_bcnt1_i32_b64 s2, s[2:3]
	v_mov_b32_e32 v1, 0x1000
	v_mov_b32_e32 v2, s2
.LBB0_787:
	s_or_b64 exec, exec, s[0:1]
	v_readlane_b32 s8, v255, 4
	v_readlane_b32 s9, v255, 5
	v_readlane_b32 s76, v255, 39
	s_cmp_lt_i32 s9, 13
	v_readlane_b32 s77, v255, 40
	v_readlane_b32 s78, v255, 41
	v_readlane_b32 s79, v255, 42
	v_readlane_b32 s10, v255, 6
	v_readlane_b32 s11, v255, 7
	v_readlane_b32 s80, v255, 43
	v_readlane_b32 s81, v255, 44
	v_readlane_b32 s82, v255, 45
	v_readlane_b32 s83, v255, 46
	s_cbranch_scc1 .LBB0_837
	s_waitcnt vmcnt(0)
	s_waitcnt vmcnt(0)
	s_barrier
	s_and_saveexec_b64 s[0:1], s[96:97]
	s_cbranch_execz .LBB0_836
	v_readlane_b32 s2, v255, 10
	s_waitcnt vmcnt(0) expcnt(0) lgkmcnt(0)
	s_nop 0
	v_mov_b32_e32 v1, s2
	ds_read_b32 v3, v1
	ds_read_b32 v1, v1 offset:4
	s_waitcnt lgkmcnt(1)
	v_cmp_ne_u32_e32 vcc, 0, v3
	s_cbranch_vccnz .LBB0_804
	v_readlane_b32 s2, v255, 0
	v_readlane_b32 s3, v255, 1
	s_load_dwordx2 s[6:7], s[2:3], 0x4
	v_readlane_b32 s8, v255, 8
	v_readlane_b32 s9, v255, 9
	s_add_u32 s2, s8, 0x1000
	s_addc_u32 s3, s9, 0
	s_add_u32 s4, s8, 0x1100
	s_addc_u32 s5, s9, 0
	s_waitcnt lgkmcnt(0)
	s_mul_i32 s16, s6, s93
	s_add_u32 s6, s8, 0x1200
	s_mul_i32 s16, s16, s7
	s_addc_u32 s7, s9, 0
	s_add_u32 s8, s8, 0x1300
	s_addc_u32 s9, s9, 0
	s_mov_b32 s17, 1
	v_mov_b32_e32 v17, 0
	s_branch .LBB0_792

; __device__ __forceinline__ unsigned xb_add(unsigned* p, unsigned v) { return __hip_atomic_fetch_add(p, v, __ATOMIC_RELAXED, __HIP_MEMORY_SCOPE_AGENT); }
; __device__ __forceinline__ void xcd_barrier(const XcdBarrier& b) {
;     asm volatile("s_waitcnt vmcnt(0)" ::: "memory");
;     __syncthreads();
;     if (threadIdx.x == 0) {
;         unsigned* bar = b.bar;
;         __builtin_amdgcn_s_waitcnt(0);
;         unsigned nloc = b.st[0], nx = b.st[1];
;         if (nloc == 0u) { xcd_barrier_complete(bar, b.x, nloc, nx); b.st[0] = nloc; b.st[1] = nx; }
;         const unsigned old = xb_add(&bar[XB_XSUB(b.x)], 1u);
.LBB0_872:
	s_and_saveexec_b64 s[0:1], s[96:97]
	s_cbranch_execz .LBB0_875
	s_mov_b64 s[2:3], exec
	v_mbcnt_lo_u32_b32 v1, s2, 0
	v_mbcnt_hi_u32_b32 v1, s3, v1
	v_cmp_eq_u32_e32 vcc, 0, v1
	s_and_b64 s[4:5], exec, vcc
	s_mov_b64 exec, s[4:5]
	s_cbranch_execz .LBB0_875
	s_bcnt1_i32_b64 s2, s[2:3]
	v_mov_b32_e32 v1, 0x1000
	v_mov_b32_e32 v2, s2
.LBB0_875:
	s_or_b64 exec, exec, s[0:1]
	v_readlane_b32 s8, v255, 4
	v_readlane_b32 s9, v255, 5
	s_cmp_lt_i32 s9, 14
	v_readlane_b32 s10, v255, 6
	v_readlane_b32 s11, v255, 7
	s_cbranch_scc1 .LBB0_925
	s_waitcnt vmcnt(0)
	s_waitcnt vmcnt(0)
	s_barrier
	s_and_saveexec_b64 s[0:1], s[96:97]
	s_cbranch_execz .LBB0_924
	v_readlane_b32 s2, v255, 10
	s_waitcnt vmcnt(0) expcnt(0) lgkmcnt(0)
	s_nop 0
	v_mov_b32_e32 v1, s2
	ds_read_b32 v3, v1
	ds_read_b32 v1, v1 offset:4
	s_waitcnt lgkmcnt(1)
	v_cmp_ne_u32_e32 vcc, 0, v3
	s_cbranch_vccnz .LBB0_892
	v_readlane_b32 s2, v255, 0
	v_readlane_b32 s3, v255, 1
	s_load_dwordx2 s[6:7], s[2:3], 0x4
	v_readlane_b32 s8, v255, 8
	v_readlane_b32 s9, v255, 9
	s_add_u32 s2, s8, 0x1000
	s_addc_u32 s3, s9, 0
	s_add_u32 s4, s8, 0x1100
	s_addc_u32 s5, s9, 0
	s_waitcnt lgkmcnt(0)
	s_mul_i32 s16, s6, s93
	s_add_u32 s6, s8, 0x1200
	s_mul_i32 s16, s16, s7
	s_addc_u32 s7, s9, 0
	s_add_u32 s8, s8, 0x1300
	s_addc_u32 s9, s9, 0
	s_mov_b32 s17, 1
	v_mov_b32_e32 v17, 0
	s_branch .LBB0_880

; __device__ __forceinline__ unsigned xb_add(unsigned* p, unsigned v) { return __hip_atomic_fetch_add(p, v, __ATOMIC_RELAXED, __HIP_MEMORY_SCOPE_AGENT); }
; __device__ __forceinline__ void xcd_barrier(const XcdBarrier& b) {
;     asm volatile("s_waitcnt vmcnt(0)" ::: "memory");
;     __syncthreads();
;     if (threadIdx.x == 0) {
;         unsigned* bar = b.bar;
;         __builtin_amdgcn_s_waitcnt(0);
;         unsigned nloc = b.st[0], nx = b.st[1];
;         if (nloc == 0u) { xcd_barrier_complete(bar, b.x, nloc, nx); b.st[0] = nloc; b.st[1] = nx; }
;         const unsigned old = xb_add(&bar[XB_XSUB(b.x)], 1u);
.LBB0_943:
	s_and_saveexec_b64 s[0:1], s[96:97]
	s_cbranch_execz .LBB0_946
	s_mov_b64 s[2:3], exec
	v_mbcnt_lo_u32_b32 v1, s2, 0
	v_mbcnt_hi_u32_b32 v1, s3, v1
	v_cmp_eq_u32_e32 vcc, 0, v1
	s_and_b64 s[4:5], exec, vcc
	s_mov_b64 exec, s[4:5]
	s_cbranch_execz .LBB0_946
	s_bcnt1_i32_b64 s2, s[2:3]
	v_mov_b32_e32 v1, 0x1000
	v_mov_b32_e32 v2, s2
.LBB0_946:
	s_or_b64 exec, exec, s[0:1]
	v_readlane_b32 s8, v255, 4
	v_readlane_b32 s9, v255, 5
	s_cmp_lt_i32 s9, 15
	v_readlane_b32 s10, v255, 6
	v_readlane_b32 s11, v255, 7
	s_cbranch_scc1 .LBB0_996
	s_waitcnt vmcnt(0)
	s_barrier
	s_and_saveexec_b64 s[0:1], s[96:97]
	s_cbranch_execz .LBB0_995
	v_readlane_b32 s2, v255, 10
	s_waitcnt vmcnt(0) expcnt(0) lgkmcnt(0)
	s_nop 0
	v_mov_b32_e32 v1, s2
	ds_read_b32 v3, v1
	ds_read_b32 v1, v1 offset:4
	s_waitcnt lgkmcnt(1)
	v_cmp_ne_u32_e32 vcc, 0, v3
	s_cbranch_vccnz .LBB0_963
	v_readlane_b32 s2, v255, 0
	v_readlane_b32 s3, v255, 1
	s_load_dwordx2 s[6:7], s[2:3], 0x4
	v_readlane_b32 s8, v255, 8
	v_readlane_b32 s9, v255, 9
	s_add_u32 s2, s8, 0x1000
	s_addc_u32 s3, s9, 0
	s_add_u32 s4, s8, 0x1100
	s_addc_u32 s5, s9, 0
	s_waitcnt lgkmcnt(0)
	s_mul_i32 s16, s6, s93
	s_add_u32 s6, s8, 0x1200
	s_mul_i32 s16, s16, s7
	s_addc_u32 s7, s9, 0
	s_add_u32 s8, s8, 0x1300
	s_addc_u32 s9, s9, 0
	s_mov_b32 s17, 1
	v_mov_b32_e32 v17, 0
	s_branch .LBB0_951

; __device__ __forceinline__ unsigned xb_add(unsigned* p, unsigned v) { return __hip_atomic_fetch_add(p, v, __ATOMIC_RELAXED, __HIP_MEMORY_SCOPE_AGENT); }
; __device__ __forceinline__ void xcd_barrier(const XcdBarrier& b) {
;     asm volatile("s_waitcnt vmcnt(0)" ::: "memory");
;     __syncthreads();
;     if (threadIdx.x == 0) {
;         unsigned* bar = b.bar;
;         __builtin_amdgcn_s_waitcnt(0);
;         unsigned nloc = b.st[0], nx = b.st[1];
;         if (nloc == 0u) { xcd_barrier_complete(bar, b.x, nloc, nx); b.st[0] = nloc; b.st[1] = nx; }
;         const unsigned old = xb_add(&bar[XB_XSUB(b.x)], 1u);
.LBB0_1070:
	s_mov_b64 s[2:3], exec
	v_mbcnt_lo_u32_b32 v1, s2, 0
	v_mbcnt_hi_u32_b32 v1, s3, v1
	v_cmp_eq_u32_e32 vcc, 0, v1
	s_and_b64 s[4:5], exec, vcc
	s_mov_b64 exec, s[4:5]
	s_cbranch_execz .LBB0_1072
	s_bcnt1_i32_b64 s2, s[2:3]
	v_mov_b32_e32 v1, 0x1000
	v_mov_b32_e32 v2, s2
.LBB0_1072:
	s_or_b64 exec, exec, s[0:1]
	v_readlane_b32 s8, v255, 4
	v_readlane_b32 s9, v255, 5
	s_cmp_lt_i32 s9, 17
	v_readlane_b32 s10, v255, 6
	v_readlane_b32 s11, v255, 7
	s_cbranch_scc1 .LBB0_1122
	s_waitcnt vmcnt(0)
	s_waitcnt vmcnt(0)
	s_barrier
	s_and_saveexec_b64 s[0:1], s[96:97]
	s_cbranch_execz .LBB0_1121
	v_readlane_b32 s2, v255, 10
	s_waitcnt vmcnt(0) expcnt(0) lgkmcnt(0)
	s_nop 0
	v_mov_b32_e32 v1, s2
	ds_read_b32 v3, v1
	ds_read_b32 v1, v1 offset:4
	s_waitcnt lgkmcnt(1)
	v_cmp_ne_u32_e32 vcc, 0, v3
	s_cbranch_vccnz .LBB0_1089
	v_readlane_b32 s2, v255, 0
	v_readlane_b32 s3, v255, 1
	s_load_dwordx2 s[6:7], s[2:3], 0x4
	v_readlane_b32 s8, v255, 8
	v_readlane_b32 s9, v255, 9
	s_add_u32 s2, s8, 0x1000
	s_addc_u32 s3, s9, 0
	s_add_u32 s4, s8, 0x1100
	s_addc_u32 s5, s9, 0
	s_waitcnt lgkmcnt(0)
	s_mul_i32 s16, s6, s93
	s_add_u32 s6, s8, 0x1200
	s_mul_i32 s16, s16, s7
	s_addc_u32 s7, s9, 0
	s_add_u32 s8, s8, 0x1300
	s_addc_u32 s9, s9, 0
	s_mov_b32 s17, 1
	v_mov_b32_e32 v17, 0
	s_branch .LBB0_1077

; __device__ __forceinline__ unsigned xb_add(unsigned* p, unsigned v) { return __hip_atomic_fetch_add(p, v, __ATOMIC_RELAXED, __HIP_MEMORY_SCOPE_AGENT); }
; __device__ __forceinline__ void xcd_barrier(const XcdBarrier& b) {
;     asm volatile("s_waitcnt vmcnt(0)" ::: "memory");
;     __syncthreads();
;     if (threadIdx.x == 0) {
;         unsigned* bar = b.bar;
;         __builtin_amdgcn_s_waitcnt(0);
;         unsigned nloc = b.st[0], nx = b.st[1];
;         if (nloc == 0u) { xcd_barrier_complete(bar, b.x, nloc, nx); b.st[0] = nloc; b.st[1] = nx; }
;         const unsigned old = xb_add(&bar[XB_XSUB(b.x)], 1u);
.LBB0_1151:
	s_and_saveexec_b64 s[0:1], s[96:97]
	v_readlane_b32 s88, v255, 24
	v_readlane_b32 s89, v255, 25
	v_readlane_b32 s90, v255, 26
	v_readlane_b32 s91, v255, 27
	s_cbranch_execz .LBB0_1154
	s_mov_b64 s[2:3], exec
	v_mbcnt_lo_u32_b32 v1, s2, 0
	v_mbcnt_hi_u32_b32 v1, s3, v1
	v_cmp_eq_u32_e32 vcc, 0, v1
	s_and_b64 s[4:5], exec, vcc
	s_mov_b64 exec, s[4:5]
	s_cbranch_execz .LBB0_1154
	s_bcnt1_i32_b64 s2, s[2:3]
	v_mov_b32_e32 v1, 0x2000
	v_mov_b32_e32 v2, s2
.LBB0_1154:
	s_or_b64 exec, exec, s[0:1]
	v_readlane_b32 s8, v255, 4
	v_readlane_b32 s9, v255, 5
	s_cmp_lt_i32 s9, 19
	v_readlane_b32 s92, v255, 47
	v_readlane_b32 s10, v255, 6
	v_readlane_b32 s11, v255, 7
	s_cbranch_scc1 .LBB0_1204
	s_waitcnt vmcnt(0)
	s_barrier
	s_and_saveexec_b64 s[0:1], s[96:97]
	s_cbranch_execz .LBB0_1203
	v_readlane_b32 s2, v255, 10
	s_waitcnt vmcnt(0) expcnt(0) lgkmcnt(0)
	s_nop 0
	v_mov_b32_e32 v1, s2
	ds_read_b32 v3, v1
	ds_read_b32 v1, v1 offset:4
	s_waitcnt lgkmcnt(1)
	v_cmp_ne_u32_e32 vcc, 0, v3
	s_cbranch_vccnz .LBB0_1171
	v_readlane_b32 s2, v255, 0
	v_readlane_b32 s3, v255, 1
	s_load_dwordx2 s[6:7], s[2:3], 0x4
	v_readlane_b32 s8, v255, 8
	v_readlane_b32 s9, v255, 9
	s_add_u32 s2, s8, 0x1000
	s_addc_u32 s3, s9, 0
	s_add_u32 s4, s8, 0x1100
	s_addc_u32 s5, s9, 0
	s_waitcnt lgkmcnt(0)
	s_mul_i32 s16, s6, s93
	s_add_u32 s6, s8, 0x1200
	s_mul_i32 s16, s16, s7
	s_addc_u32 s7, s9, 0
	s_add_u32 s8, s8, 0x1300
	s_addc_u32 s9, s9, 0
	s_mov_b32 s17, 1
	v_mov_b32_e32 v17, 0
	s_branch .LBB0_1159

; __device__ __forceinline__ unsigned xb_add(unsigned* p, unsigned v) { return __hip_atomic_fetch_add(p, v, __ATOMIC_RELAXED, __HIP_MEMORY_SCOPE_AGENT); }
; __device__ __forceinline__ void xcd_barrier(const XcdBarrier& b) {
;     asm volatile("s_waitcnt vmcnt(0)" ::: "memory");
;     __syncthreads();
;     if (threadIdx.x == 0) {
;         unsigned* bar = b.bar;
;         __builtin_amdgcn_s_waitcnt(0);
;         unsigned nloc = b.st[0], nx = b.st[1];
;         if (nloc == 0u) { xcd_barrier_complete(bar, b.x, nloc, nx); b.st[0] = nloc; b.st[1] = nx; }
;         const unsigned old = xb_add(&bar[XB_XSUB(b.x)], 1u);
.LBB0_1244:
	s_mov_b64 s[2:3], exec
	v_mbcnt_lo_u32_b32 v1, s2, 0
	v_mbcnt_hi_u32_b32 v1, s3, v1
	v_cmp_eq_u32_e32 vcc, 0, v1
	s_and_b64 s[4:5], exec, vcc
	s_mov_b64 exec, s[4:5]
	s_cbranch_execz .LBB0_1246
	s_bcnt1_i32_b64 s2, s[2:3]
	v_mov_b32_e32 v1, 0x2000
	v_mov_b32_e32 v2, s2
.LBB0_1246:
	s_or_b64 exec, exec, s[0:1]
	v_readlane_b32 s8, v255, 4
	v_readlane_b32 s9, v255, 5
	s_cmp_lt_i32 s9, 21
	v_readlane_b32 s10, v255, 6
	v_readlane_b32 s11, v255, 7
	s_cbranch_scc1 .LBB0_1296
	s_waitcnt vmcnt(0)
	s_waitcnt vmcnt(0)
	s_barrier
	s_and_saveexec_b64 s[0:1], s[96:97]
	s_cbranch_execz .LBB0_1295
	v_readlane_b32 s2, v255, 10
	s_waitcnt vmcnt(0) expcnt(0) lgkmcnt(0)
	s_nop 0
	v_mov_b32_e32 v1, s2
	ds_read_b32 v3, v1
	ds_read_b32 v1, v1 offset:4
	s_waitcnt lgkmcnt(1)
	v_cmp_ne_u32_e32 vcc, 0, v3
	s_cbranch_vccnz .LBB0_1263
	v_readlane_b32 s2, v255, 0
	v_readlane_b32 s3, v255, 1
	s_load_dwordx2 s[6:7], s[2:3], 0x4
	v_readlane_b32 s8, v255, 8
	v_readlane_b32 s9, v255, 9
	s_add_u32 s2, s8, 0x1000
	s_addc_u32 s3, s9, 0
	s_add_u32 s4, s8, 0x1100
	s_addc_u32 s5, s9, 0
	s_waitcnt lgkmcnt(0)
	s_mul_i32 s16, s6, s93
	s_add_u32 s6, s8, 0x1200
	s_mul_i32 s16, s16, s7
	s_addc_u32 s7, s9, 0
	s_add_u32 s8, s8, 0x1300
	s_addc_u32 s9, s9, 0
	s_mov_b32 s17, 1
	v_mov_b32_e32 v17, 0
	s_branch .LBB0_1251

; #define LAS __attribute__((address_space(3)))
; __device__ __forceinline__ void phase_nrr(const Frame& F, const Args& a, int l, const bf16_t* XA, const float* g, const float* modl, unsigned char* XN8) {
;     ...
;         __syncthreads();
; #pragma unroll
;         for (int rb = 0; rb < 4; ++rb) *(LAS f32x4*)(Pl + (size_t)((kq * 64 + 16 * rb + fr) * NE + 16 * eb + 4 * fq)) = acc[rb];
;         __syncthreads();
;         const float bias = rbias[lane];
; #pragma unroll
;         for (int i = 0; i < 8; ++i) { const int t = tb + i;
;             const float lg = Pl[(w * 8 + i) * NE + lane] + Pl[(64 + w * 8 + i) * NE + lane]; const float sc = 1.f / (1.f + __expf(-lg)); const float bb = sc + bias;
;             float m1 = bb; m1 = fmaxf(m1, __shfl_xor(m1, 1)); m1 = fmaxf(m1, __shfl_xor(m1, 2)); m1 = fmaxf(m1, __shfl_xor(m1, 4));
;             const unsigned long long eq = __ballot(bb == m1); const int gbase = lane & ~7; const unsigned grpmask = (unsigned)((eq >> gbase) & 0xffull);
;             const int first = gbase + __builtin_ctz(grpmask);
;             float m2 = (lane == first) ? -INFINITY : bb; m2 = fmaxf(m2, __shfl_xor(m2, 1)); m2 = fmaxf(m2, __shfl_xor(m2, 2)); m2 = fmaxf(m2, __shfl_xor(m2, 4));
;             const float gsum = m1 + m2; const int gq = lane >> 3;
;             int grank = 0;
; #pragma unroll
;             for (int g2 = 0; g2 < 8; ++g2) { const float v = __int_as_float(__builtin_amdgcn_readlane(__float_as_int(gsum), g2 * 8)); grank += (v > gsum || (v == gsum && g2 < gq)) ? 1 : 0; }
;             const bool keep = grank < 4; const float val = keep ? bb : -INFINITY;
;             int rank = 0;
; #pragma unroll 8
;             for (int e2 = 0; e2 < 64; ++e2) { const float v = __int_as_float(__builtin_amdgcn_readlane(__float_as_int(val), e2)); rank += (v > val || (v == val && e2 < lane)) ? 1 : 0; }
.LBB0_1308:
	s_barrier
	ds_write_b128 v242, v[110:113]
	ds_write_b128 v242, v[118:121] offset:4096
	s_nop 0
	ds_write_b128 v242, v[126:129] offset:8192
	s_nop 1
	ds_write_b128 v242, v[130:133] offset:12288
	s_waitcnt lgkmcnt(0)
	s_barrier
	global_load_dword v3, v[198:199], off offset:256
	s_waitcnt vmcnt(15)
	v_add_u32_e32 v4, s33, v226
	ds_read2st64_b32 v[6:7], v4 offset1:64
	s_mov_b32 s3, 0
	s_waitcnt lgkmcnt(0)
	v_add_f32_e32 v2, v6, v7
	v_mul_f32_e32 v2, 0xbfb8aa3b, v2
	v_exp_f32_e32 v2, v2
	s_nop 0
	v_add_f32_e32 v2, 1.0, v2
	v_div_scale_f32 v5, s[20:21], v2, v2, 1.0
	v_rcp_f32_e32 v6, v5
	s_nop 0
	v_fma_f32 v7, -v5, v6, 1.0
	v_fmac_f32_e32 v6, v7, v6
	v_div_scale_f32 v7, vcc, 1.0, v2, 1.0
	v_mul_f32_e32 v8, v7, v6
	v_fma_f32 v9, -v5, v8, v7
	v_fmac_f32_e32 v8, v9, v6
	v_fma_f32 v5, -v5, v8, v7
	v_div_fmas_f32 v5, v5, v6, v8
	v_div_fixup_f32 v2, v5, v2, 1.0
	s_waitcnt vmcnt(0)
	v_add_f32_e32 v5, v3, v2
	s_nop 1
	s_waitcnt lgkmcnt(0)
	v_max_f32_dpp v6, v5, v5 quad_perm:[1,0,3,2] row_mask:0xf bank_mask:0xf
	s_nop 1
	s_waitcnt lgkmcnt(0)
	v_max_f32_dpp v6, v6, v6 quad_perm:[2,3,0,1] row_mask:0xf bank_mask:0xf
	s_nop 1
	s_waitcnt lgkmcnt(0)
	v_max_f32_dpp v8, v6, v6 row_half_mirror row_mask:0xf bank_mask:0xf
	v_cmp_eq_f32_e32 vcc, v5, v8
	s_nop 1
	v_lshrrev_b64 v[6:7], v200, vcc
	v_ffbl_b32_sdwa v6, v6 dst_sel:DWORD dst_unused:UNUSED_PAD src0_sel:BYTE_0
	v_add_u32_e32 v6, v6, v200
	v_cmp_ne_u32_e32 vcc, v230, v6
	s_nop 1
	v_cndmask_b32_e32 v6, v245, v5, vcc
	s_nop 1
	s_waitcnt lgkmcnt(0)
	v_max_f32_dpp v6, v6, v6 quad_perm:[1,0,3,2] row_mask:0xf bank_mask:0xf
	s_nop 1
	s_waitcnt lgkmcnt(0)
	v_max_f32_dpp v6, v6, v6 quad_perm:[2,3,0,1] row_mask:0xf bank_mask:0xf
	s_nop 1
	s_waitcnt lgkmcnt(0)
	v_max_f32_dpp v6, v6, v6 row_half_mirror row_mask:0xf bank_mask:0xf
	v_add_f32_e32 v6, v8, v6
	s_nop 0
	v_readlane_b32 s5, v6, 0
	s_nop 1
	v_cmp_eq_f32_e64 s[20:21], s5, v6
	v_cmp_gt_f32_e32 vcc, s5, v6
	s_and_b64 s[20:21], s[0:1], s[20:21]
	s_or_b64 s[20:21], vcc, s[20:21]
	v_readlane_b32 s5, v6, 8
	v_cndmask_b32_e64 v7, 0, 1, s[20:21]
	s_nop 0
	v_cmp_eq_f32_e64 s[20:21], s5, v6
	v_cmp_gt_f32_e32 vcc, s5, v6
	s_and_b64 s[20:21], s[6:7], s[20:21]
	s_or_b64 s[20:21], vcc, s[20:21]
	v_readlane_b32 s5, v6, 16
	v_cndmask_b32_e64 v8, 0, 1, s[20:21]
	s_nop 0
	v_cmp_eq_f32_e64 s[20:21], s5, v6
	v_cmp_gt_f32_e32 vcc, s5, v6
	s_and_b64 s[20:21], s[8:9], s[20:21]
	s_or_b64 s[20:21], vcc, s[20:21]
	v_readlane_b32 s5, v6, 24
	v_cndmask_b32_e64 v9, 0, 1, s[20:21]
	s_nop 0
	v_cmp_eq_f32_e64 s[20:21], s5, v6
	v_cmp_gt_f32_e32 vcc, s5, v6
	s_and_b64 s[20:21], s[10:11], s[20:21]
	s_or_b64 s[20:21], vcc, s[20:21]
	v_readlane_b32 s5, v6, 32
	v_cndmask_b32_e64 v10, 0, 1, s[20:21]
	s_nop 0
	v_cmp_eq_f32_e64 s[20:21], s5, v6
	v_cmp_gt_f32_e32 vcc, s5, v6
	s_and_b64 s[20:21], s[12:13], s[20:21]
	s_or_b64 s[20:21], vcc, s[20:21]
	v_readlane_b32 s5, v6, 40
	v_cndmask_b32_e64 v11, 0, 1, s[20:21]
	s_nop 0
	v_cmp_eq_f32_e64 s[20:21], s5, v6
	v_cmp_gt_f32_e32 vcc, s5, v6
	s_and_b64 s[20:21], s[14:15], s[20:21]
	s_or_b64 s[20:21], vcc, s[20:21]
	v_readlane_b32 s5, v6, 48
	v_cndmask_b32_e64 v12, 0, 1, s[20:21]
	s_nop 0
	v_cmp_eq_f32_e64 s[20:21], s5, v6
	v_cmp_gt_f32_e32 vcc, s5, v6
	s_and_b64 s[20:21], s[16:17], s[20:21]
	v_readlane_b32 s5, v6, 56
	s_or_b64 s[20:21], vcc, s[20:21]
	v_cndmask_b32_e64 v13, 0, 1, s[20:21]
	v_cmp_gt_f32_e32 vcc, s5, v6
	s_nop 1
	v_cndmask_b32_e64 v6, 0, 1, vcc
	v_add_u32_e32 v6, v8, v6
	v_add3_u32 v6, v6, v7, v9
	v_add3_u32 v6, v6, v10, v11
	v_add3_u32 v6, v6, v12, v13
	v_cmp_gt_u32_e32 vcc, 4, v6
	v_mov_b32_e32 v6, 0
	s_nop 0
	v_cndmask_b32_e32 v5, v245, v5, vcc
	v_ashrrev_i32_e32 v9, 31, v5
	v_sub_u32_e32 v8, 63, v230
	v_and_b32_e32 v9, 0x7fffffff, v9
	v_xor_b32_e32 v9, v5, v9
	s_nop 0
	v_readlane_b32 s23, v9, 0
	s_movk_i32 s22, 63
	v_readlane_b32 s21, v9, 1
	s_movk_i32 s20, 62
	v_cmp_gt_i64_e32 vcc, s[22:23], v[8:9]
	v_readlane_b32 s23, v9, 2
	s_movk_i32 s22, 61
	v_addc_co_u32_e32 v6, vcc, 0, v6, vcc
	v_cmp_gt_i64_e32 vcc, s[20:21], v[8:9]
	v_readlane_b32 s21, v9, 3
	s_movk_i32 s20, 60
	v_addc_co_u32_e32 v6, vcc, 0, v6, vcc
	v_cmp_gt_i64_e32 vcc, s[22:23], v[8:9]
	v_readlane_b32 s23, v9, 4
	s_movk_i32 s22, 59
	v_addc_co_u32_e32 v6, vcc, 0, v6, vcc
	v_cmp_gt_i64_e32 vcc, s[20:21], v[8:9]
	v_readlane_b32 s21, v9, 5
	s_movk_i32 s20, 58
	v_addc_co_u32_e32 v6, vcc, 0, v6, vcc
	v_cmp_gt_i64_e32 vcc, s[22:23], v[8:9]
	v_readlane_b32 s23, v9, 6
	s_movk_i32 s22, 57
	v_addc_co_u32_e32 v6, vcc, 0, v6, vcc
	v_cmp_gt_i64_e32 vcc, s[20:21], v[8:9]
	v_readlane_b32 s21, v9, 7
	s_movk_i32 s20, 56
	v_addc_co_u32_e32 v6, vcc, 0, v6, vcc
	v_cmp_gt_i64_e32 vcc, s[22:23], v[8:9]
	v_readlane_b32 s23, v9, 8
	s_movk_i32 s22, 55
	v_addc_co_u32_e32 v6, vcc, 0, v6, vcc
	v_cmp_gt_i64_e32 vcc, s[20:21], v[8:9]
	v_readlane_b32 s21, v9, 9
	s_movk_i32 s20, 54
	v_addc_co_u32_e32 v6, vcc, 0, v6, vcc
	v_cmp_gt_i64_e32 vcc, s[22:23], v[8:9]
	v_readlane_b32 s23, v9, 10
	s_movk_i32 s22, 53
	v_addc_co_u32_e32 v6, vcc, 0, v6, vcc
	v_cmp_gt_i64_e32 vcc, s[20:21], v[8:9]
	v_readlane_b32 s21, v9, 11
	s_movk_i32 s20, 52
	v_addc_co_u32_e32 v6, vcc, 0, v6, vcc
	v_cmp_gt_i64_e32 vcc, s[22:23], v[8:9]
	v_readlane_b32 s23, v9, 12
	s_movk_i32 s22, 51
	v_addc_co_u32_e32 v6, vcc, 0, v6, vcc
	v_cmp_gt_i64_e32 vcc, s[20:21], v[8:9]
	v_readlane_b32 s21, v9, 13
	s_movk_i32 s20, 50
	v_addc_co_u32_e32 v6, vcc, 0, v6, vcc
	v_cmp_gt_i64_e32 vcc, s[22:23], v[8:9]
	v_readlane_b32 s23, v9, 14
	s_movk_i32 s22, 49
	v_addc_co_u32_e32 v6, vcc, 0, v6, vcc
	v_cmp_gt_i64_e32 vcc, s[20:21], v[8:9]
	v_readlane_b32 s21, v9, 15
	s_movk_i32 s20, 48
	v_addc_co_u32_e32 v6, vcc, 0, v6, vcc
	v_cmp_gt_i64_e32 vcc, s[22:23], v[8:9]
; __device__ __forceinline__ void phase_nrr(const Frame& F, const Args& a, int l, const bf16_t* XA, const float* g, const float* modl, unsigned char* XN8) {
;     ...
;             int rank = 0;
; #pragma unroll 8
;             for (int e2 = 0; e2 < 64; ++e2) { const float v = __int_as_float(__builtin_amdgcn_readlane(__float_as_int(val), e2)); rank += (v > val || (v == val && e2 < lane)) ? 1 : 0; }
;             const bool sel = rank < TOPK;
;             const float ssum = wave_sum(sel ? sc : 0.f);
	v_readlane_b32 s23, v9, 16
	s_movk_i32 s22, 47
	v_addc_co_u32_e32 v6, vcc, 0, v6, vcc
	v_cmp_gt_i64_e32 vcc, s[20:21], v[8:9]
	v_readlane_b32 s21, v9, 17
	s_movk_i32 s20, 46
	v_addc_co_u32_e32 v6, vcc, 0, v6, vcc
	v_cmp_gt_i64_e32 vcc, s[22:23], v[8:9]
	v_readlane_b32 s23, v9, 18
	s_movk_i32 s22, 45
	v_addc_co_u32_e32 v6, vcc, 0, v6, vcc
	v_cmp_gt_i64_e32 vcc, s[20:21], v[8:9]
	v_readlane_b32 s21, v9, 19
	s_movk_i32 s20, 44
	v_addc_co_u32_e32 v6, vcc, 0, v6, vcc
	v_cmp_gt_i64_e32 vcc, s[22:23], v[8:9]
	v_readlane_b32 s23, v9, 20
	s_movk_i32 s22, 43
	v_addc_co_u32_e32 v6, vcc, 0, v6, vcc
	v_cmp_gt_i64_e32 vcc, s[20:21], v[8:9]
	v_readlane_b32 s21, v9, 21
	s_movk_i32 s20, 42
	v_addc_co_u32_e32 v6, vcc, 0, v6, vcc
	v_cmp_gt_i64_e32 vcc, s[22:23], v[8:9]
	v_readlane_b32 s23, v9, 22
	s_movk_i32 s22, 41
	v_addc_co_u32_e32 v6, vcc, 0, v6, vcc
	v_cmp_gt_i64_e32 vcc, s[20:21], v[8:9]
	v_readlane_b32 s21, v9, 23
	s_movk_i32 s20, 40
	v_addc_co_u32_e32 v6, vcc, 0, v6, vcc
	v_cmp_gt_i64_e32 vcc, s[22:23], v[8:9]
	v_readlane_b32 s23, v9, 24
	s_movk_i32 s22, 39
	v_addc_co_u32_e32 v6, vcc, 0, v6, vcc
	v_cmp_gt_i64_e32 vcc, s[20:21], v[8:9]
	v_readlane_b32 s21, v9, 25
	s_movk_i32 s20, 38
	v_addc_co_u32_e32 v6, vcc, 0, v6, vcc
	v_cmp_gt_i64_e32 vcc, s[22:23], v[8:9]
	v_readlane_b32 s23, v9, 26
	s_movk_i32 s22, 37
	v_addc_co_u32_e32 v6, vcc, 0, v6, vcc
	v_cmp_gt_i64_e32 vcc, s[20:21], v[8:9]
	v_readlane_b32 s21, v9, 27
	s_movk_i32 s20, 36
	v_addc_co_u32_e32 v6, vcc, 0, v6, vcc
	v_cmp_gt_i64_e32 vcc, s[22:23], v[8:9]
	v_readlane_b32 s23, v9, 28
	s_movk_i32 s22, 35
	v_addc_co_u32_e32 v6, vcc, 0, v6, vcc
	v_cmp_gt_i64_e32 vcc, s[20:21], v[8:9]
	v_readlane_b32 s21, v9, 29
	s_movk_i32 s20, 34
	v_addc_co_u32_e32 v6, vcc, 0, v6, vcc
	v_cmp_gt_i64_e32 vcc, s[22:23], v[8:9]
	v_readlane_b32 s23, v9, 30
	s_movk_i32 s22, 33
	v_addc_co_u32_e32 v6, vcc, 0, v6, vcc
	v_cmp_gt_i64_e32 vcc, s[20:21], v[8:9]
	v_readlane_b32 s21, v9, 31
	s_movk_i32 s20, 32
	v_addc_co_u32_e32 v6, vcc, 0, v6, vcc
	v_cmp_gt_i64_e32 vcc, s[22:23], v[8:9]
	v_readlane_b32 s23, v9, 32
	s_movk_i32 s22, 31
	v_addc_co_u32_e32 v6, vcc, 0, v6, vcc
	v_cmp_gt_i64_e32 vcc, s[20:21], v[8:9]
	v_readlane_b32 s21, v9, 33
	s_movk_i32 s20, 30
	v_addc_co_u32_e32 v6, vcc, 0, v6, vcc
	v_cmp_gt_i64_e32 vcc, s[22:23], v[8:9]
	v_readlane_b32 s23, v9, 34
	s_movk_i32 s22, 29
	v_addc_co_u32_e32 v6, vcc, 0, v6, vcc
	v_cmp_gt_i64_e32 vcc, s[20:21], v[8:9]
	v_readlane_b32 s21, v9, 35
	s_movk_i32 s20, 28
	v_addc_co_u32_e32 v6, vcc, 0, v6, vcc
	v_cmp_gt_i64_e32 vcc, s[22:23], v[8:9]
	v_readlane_b32 s23, v9, 36
	s_movk_i32 s22, 27
	v_addc_co_u32_e32 v6, vcc, 0, v6, vcc
	v_cmp_gt_i64_e32 vcc, s[20:21], v[8:9]
	v_readlane_b32 s21, v9, 37
	s_movk_i32 s20, 26
	v_addc_co_u32_e32 v6, vcc, 0, v6, vcc
	v_cmp_gt_i64_e32 vcc, s[22:23], v[8:9]
	v_readlane_b32 s23, v9, 38
	s_movk_i32 s22, 25
	v_addc_co_u32_e32 v6, vcc, 0, v6, vcc
	v_cmp_gt_i64_e32 vcc, s[20:21], v[8:9]
	v_readlane_b32 s21, v9, 39
	s_movk_i32 s20, 24
	v_addc_co_u32_e32 v6, vcc, 0, v6, vcc
	v_cmp_gt_i64_e32 vcc, s[22:23], v[8:9]
	v_readlane_b32 s23, v9, 40
	s_movk_i32 s22, 23
	v_addc_co_u32_e32 v6, vcc, 0, v6, vcc
	v_cmp_gt_i64_e32 vcc, s[20:21], v[8:9]
	v_readlane_b32 s21, v9, 41
	s_movk_i32 s20, 22
	v_addc_co_u32_e32 v6, vcc, 0, v6, vcc
	v_cmp_gt_i64_e32 vcc, s[22:23], v[8:9]
	v_readlane_b32 s23, v9, 42
	s_movk_i32 s22, 21
	v_addc_co_u32_e32 v6, vcc, 0, v6, vcc
	v_cmp_gt_i64_e32 vcc, s[20:21], v[8:9]
	v_readlane_b32 s21, v9, 43
	s_movk_i32 s20, 20
	v_addc_co_u32_e32 v6, vcc, 0, v6, vcc
	v_cmp_gt_i64_e32 vcc, s[22:23], v[8:9]
	v_readlane_b32 s23, v9, 44
	s_movk_i32 s22, 19
	v_addc_co_u32_e32 v6, vcc, 0, v6, vcc
	v_cmp_gt_i64_e32 vcc, s[20:21], v[8:9]
	v_readlane_b32 s21, v9, 45
	s_movk_i32 s20, 18
	v_addc_co_u32_e32 v6, vcc, 0, v6, vcc
	v_cmp_gt_i64_e32 vcc, s[22:23], v[8:9]
	v_readlane_b32 s23, v9, 46
	s_movk_i32 s22, 17
	v_addc_co_u32_e32 v6, vcc, 0, v6, vcc
	v_cmp_gt_i64_e32 vcc, s[20:21], v[8:9]
	v_readlane_b32 s21, v9, 47
	s_movk_i32 s20, 16
	v_addc_co_u32_e32 v6, vcc, 0, v6, vcc
	v_cmp_gt_i64_e32 vcc, s[22:23], v[8:9]
	v_readlane_b32 s23, v9, 48
	s_movk_i32 s22, 15
	v_addc_co_u32_e32 v6, vcc, 0, v6, vcc
	v_cmp_gt_i64_e32 vcc, s[20:21], v[8:9]
	v_readlane_b32 s21, v9, 49
	s_movk_i32 s20, 14
	v_addc_co_u32_e32 v6, vcc, 0, v6, vcc
	v_cmp_gt_i64_e32 vcc, s[22:23], v[8:9]
	v_readlane_b32 s23, v9, 50
	s_movk_i32 s22, 13
	v_addc_co_u32_e32 v6, vcc, 0, v6, vcc
	v_cmp_gt_i64_e32 vcc, s[20:21], v[8:9]
	v_readlane_b32 s21, v9, 51
	s_movk_i32 s20, 12
	v_addc_co_u32_e32 v6, vcc, 0, v6, vcc
	v_cmp_gt_i64_e32 vcc, s[22:23], v[8:9]
	v_readlane_b32 s23, v9, 52
	s_movk_i32 s22, 11
	v_addc_co_u32_e32 v6, vcc, 0, v6, vcc
	v_cmp_gt_i64_e32 vcc, s[20:21], v[8:9]
	v_readlane_b32 s21, v9, 53
	s_movk_i32 s20, 10
	v_addc_co_u32_e32 v6, vcc, 0, v6, vcc
	v_cmp_gt_i64_e32 vcc, s[22:23], v[8:9]
	v_readlane_b32 s23, v9, 54
	s_movk_i32 s22, 9
	v_addc_co_u32_e32 v6, vcc, 0, v6, vcc
	v_cmp_gt_i64_e32 vcc, s[20:21], v[8:9]
	v_readlane_b32 s21, v9, 55
	s_movk_i32 s20, 8
	v_addc_co_u32_e32 v6, vcc, 0, v6, vcc
	v_cmp_gt_i64_e32 vcc, s[22:23], v[8:9]
	v_readlane_b32 s23, v9, 56
	s_movk_i32 s22, 7
	v_addc_co_u32_e32 v6, vcc, 0, v6, vcc
	v_cmp_gt_i64_e32 vcc, s[20:21], v[8:9]
	v_readlane_b32 s21, v9, 57
	s_movk_i32 s20, 6
	v_addc_co_u32_e32 v6, vcc, 0, v6, vcc
	v_cmp_gt_i64_e32 vcc, s[22:23], v[8:9]
	v_readlane_b32 s23, v9, 58
	s_movk_i32 s22, 5
	v_addc_co_u32_e32 v6, vcc, 0, v6, vcc
	v_cmp_gt_i64_e32 vcc, s[20:21], v[8:9]
	v_readlane_b32 s21, v9, 59
	s_movk_i32 s20, 4
	v_addc_co_u32_e32 v6, vcc, 0, v6, vcc
	v_cmp_gt_i64_e32 vcc, s[22:23], v[8:9]
	v_readlane_b32 s23, v9, 60
	s_movk_i32 s22, 3
	v_addc_co_u32_e32 v6, vcc, 0, v6, vcc
	v_cmp_gt_i64_e32 vcc, s[20:21], v[8:9]
	v_readlane_b32 s21, v9, 61
	s_movk_i32 s20, 2
	v_addc_co_u32_e32 v6, vcc, 0, v6, vcc
	v_cmp_gt_i64_e32 vcc, s[22:23], v[8:9]
	v_readlane_b32 s23, v9, 62
	s_movk_i32 s22, 1
	v_addc_co_u32_e32 v6, vcc, 0, v6, vcc
	v_cmp_gt_i64_e32 vcc, s[20:21], v[8:9]
	v_readlane_b32 s21, v9, 63
	s_movk_i32 s20, 0
	v_addc_co_u32_e32 v6, vcc, 0, v6, vcc
	v_cmp_gt_i64_e32 vcc, s[22:23], v[8:9]
	s_nop 1
	v_addc_co_u32_e32 v6, vcc, 0, v6, vcc
	v_cmp_gt_i64_e32 vcc, s[20:21], v[8:9]
	s_nop 1
	v_addc_co_u32_e32 v6, vcc, 0, v6, vcc
	v_cmp_gt_u32_e32 vcc, 6, v6
	s_mul_i32 s50, s24, 6
	s_nop 0
	v_cndmask_b32_e32 v5, 0, v2, vcc
	s_nop 1
	v_add_f32_dpp v5, v5, v5 quad_perm:[1,0,3,2] row_mask:0xf bank_mask:0xf
	s_nop 1
	v_add_f32_dpp v5, v5, v5 quad_perm:[2,3,0,1] row_mask:0xf bank_mask:0xf
	s_nop 1
	v_add_f32_dpp v5, v5, v5 row_half_mirror row_mask:0xf bank_mask:0xf
	s_nop 1
	v_add_f32_dpp v5, v5, v5 row_mirror row_mask:0xf bank_mask:0xf
	s_nop 0
	ds_bpermute_b32 v7, v222, v5
	s_waitcnt lgkmcnt(0)
	v_add_f32_e32 v5, v5, v7
	v_mov_b32_e32 v7, v5
	s_nop 1
	v_permlane32_swap_b32_e32 v7, v5
	s_and_saveexec_b64 s[20:21], vcc
	s_cbranch_execz .LBB0_1312
; __device__ __forceinline__ void phase_nrr(const Frame& F, const Args& a, int l, const bf16_t* XA, const float* g, const float* modl, unsigned char* XN8) {
;     ...
;             const float lg = Pl[(w * 8 + i) * NE + lane] + Pl[(64 + w * 8 + i) * NE + lane]; const float sc = 1.f / (1.f + __expf(-lg)); const float bb = sc + bias;
;             float m1 = bb; m1 = fmaxf(m1, __shfl_xor(m1, 1)); m1 = fmaxf(m1, __shfl_xor(m1, 2)); m1 = fmaxf(m1, __shfl_xor(m1, 4));
;             const unsigned long long eq = __ballot(bb == m1); const int gbase = lane & ~7; const unsigned grpmask = (unsigned)((eq >> gbase) & 0xffull);
;             const int first = gbase + __builtin_ctz(grpmask);
;             float m2 = (lane == first) ? -INFINITY : bb; m2 = fmaxf(m2, __shfl_xor(m2, 1)); m2 = fmaxf(m2, __shfl_xor(m2, 2)); m2 = fmaxf(m2, __shfl_xor(m2, 4));
;             const float gsum = m1 + m2; const int gq = lane >> 3;
;             int grank = 0;
; #pragma unroll
;             for (int g2 = 0; g2 < 8; ++g2) { const float v = __int_as_float(__builtin_amdgcn_readlane(__float_as_int(gsum), g2 * 8)); grank += (v > gsum || (v == gsum && g2 < gq)) ? 1 : 0; }
;             const bool keep = grank < 4; const float val = keep ? bb : -INFINITY;
;             int rank = 0;
; #pragma unroll 8
;             for (int e2 = 0; e2 < 64; ++e2) { const float v = __int_as_float(__builtin_amdgcn_readlane(__float_as_int(val), e2)); rank += (v > val || (v == val && e2 < lane)) ? 1 : 0; }
;     ...
;             if (sel) { const int p = atomicAdd((int*)(hist + lane), 1); top_e[t * TOPK + rank] = lane; gate[t * TOPK + rank] = sc / ssum * 2.5f; lpos[t * TOPK + rank] = p; }
	s_waitcnt lgkmcnt(0)
	v_add_f32_e32 v5, v5, v7
	v_div_scale_f32 v11, s[22:23], v5, v5, v2
	v_or_b32_e32 v6, s50, v6
	v_rcp_f32_e32 v12, v11
	v_ashrrev_i32_e32 v7, 31, v6
	v_lshlrev_b64 v[6:7], 2, v[6:7]
	v_lshl_add_u64 v[8:9], s[42:43], 0, v[6:7]
	ds_add_rtn_u32 v10, v227, v243
	global_store_dword v[8:9], v230, off
	v_fma_f32 v8, -v11, v12, 1.0
	v_fmac_f32_e32 v12, v8, v12
	v_div_scale_f32 v8, vcc, v2, v5, v2
	v_mul_f32_e32 v9, v8, v12
	v_fma_f32 v13, -v11, v9, v8
	v_fmac_f32_e32 v9, v13, v12
	v_fma_f32 v8, -v11, v9, v8
	v_div_fmas_f32 v8, v8, v12, v9
	v_div_fixup_f32 v2, v8, v5, v2
	v_mul_f32_e32 v2, 0x40200000, v2
	v_lshl_add_u64 v[8:9], s[44:45], 0, v[6:7]
	v_lshl_add_u64 v[6:7], s[46:47], 0, v[6:7]
	global_store_dword v[8:9], v2, off
	s_waitcnt lgkmcnt(0)
	global_store_dword v[6:7], v10, off
.LBB0_1312:
	s_or_b64 exec, exec, s[20:21]
	v_add_u32_e32 v2, s76, v226
	ds_read_b32 v2, v2
	ds_read_b32 v5, v4 offset:16640
	s_mov_b32 s3, 0
	s_waitcnt lgkmcnt(0)
	v_add_f32_e32 v2, v2, v5
	v_mul_f32_e32 v2, 0xbfb8aa3b, v2
	v_exp_f32_e32 v2, v2
	s_nop 0
	v_add_f32_e32 v2, 1.0, v2
	v_div_scale_f32 v5, s[20:21], v2, v2, 1.0
	v_rcp_f32_e32 v6, v5
	v_div_scale_f32 v7, vcc, 1.0, v2, 1.0
	v_fma_f32 v8, -v5, v6, 1.0
	v_fmac_f32_e32 v6, v8, v6
	v_mul_f32_e32 v8, v7, v6
	v_fma_f32 v9, -v5, v8, v7
	v_fmac_f32_e32 v8, v9, v6
	v_fma_f32 v5, -v5, v8, v7
	v_div_fmas_f32 v5, v5, v6, v8
	v_div_fixup_f32 v5, v5, v2, 1.0
	v_add_f32_e32 v2, v3, v5
	s_nop 1
	s_waitcnt lgkmcnt(0)
	v_max_f32_dpp v6, v2, v2 quad_perm:[1,0,3,2] row_mask:0xf bank_mask:0xf
	s_nop 1
	s_waitcnt lgkmcnt(0)
	v_max_f32_dpp v6, v6, v6 quad_perm:[2,3,0,1] row_mask:0xf bank_mask:0xf
	s_nop 1
	s_waitcnt lgkmcnt(0)
	v_max_f32_dpp v8, v6, v6 row_half_mirror row_mask:0xf bank_mask:0xf
	v_cmp_eq_f32_e32 vcc, v2, v8
	s_nop 1
	v_lshrrev_b64 v[6:7], v200, vcc
	v_ffbl_b32_sdwa v6, v6 dst_sel:DWORD dst_unused:UNUSED_PAD src0_sel:BYTE_0
	v_add_u32_e32 v6, v6, v200
	v_cmp_ne_u32_e32 vcc, v230, v6
	s_nop 1
	v_cndmask_b32_e32 v6, v245, v2, vcc
	s_nop 1
	s_waitcnt lgkmcnt(0)
	v_max_f32_dpp v6, v6, v6 quad_perm:[1,0,3,2] row_mask:0xf bank_mask:0xf
	s_nop 1
	s_waitcnt lgkmcnt(0)
	v_max_f32_dpp v6, v6, v6 quad_perm:[2,3,0,1] row_mask:0xf bank_mask:0xf
	s_nop 1
	s_waitcnt lgkmcnt(0)
	v_max_f32_dpp v6, v6, v6 row_half_mirror row_mask:0xf bank_mask:0xf
	v_add_f32_e32 v6, v8, v6
	s_nop 0
	v_readlane_b32 s5, v6, 0
	v_readlane_b32 s24, v6, 8
	v_readlane_b32 s28, v6, 16
	v_cmp_eq_f32_e64 s[20:21], s5, v6
	v_cmp_gt_f32_e32 vcc, s5, v6
	v_cmp_gt_f32_e64 s[22:23], s24, v6
	v_cmp_eq_f32_e64 s[24:25], s24, v6
	s_and_b64 s[20:21], s[0:1], s[20:21]
	v_readlane_b32 s34, v6, 24
	v_cmp_gt_f32_e64 s[26:27], s28, v6
	v_cmp_eq_f32_e64 s[28:29], s28, v6
	s_and_b64 s[24:25], s[6:7], s[24:25]
	s_or_b64 s[20:21], vcc, s[20:21]
	v_readlane_b32 s40, v6, 32
	v_cmp_gt_f32_e64 s[30:31], s34, v6
	v_cmp_eq_f32_e64 s[34:35], s34, v6
	s_and_b64 s[28:29], s[8:9], s[28:29]
	v_cndmask_b32_e64 v7, 0, 1, s[20:21]
	s_or_b64 s[20:21], s[22:23], s[24:25]
	v_cmp_gt_f32_e64 s[36:37], s40, v6
	v_cmp_eq_f32_e64 s[40:41], s40, v6
	s_and_b64 s[34:35], s[10:11], s[34:35]
	v_cndmask_b32_e64 v8, 0, 1, s[20:21]
	s_or_b64 s[20:21], s[26:27], s[28:29]
	s_and_b64 s[40:41], s[12:13], s[40:41]
	v_cndmask_b32_e64 v9, 0, 1, s[20:21]
	s_or_b64 s[20:21], s[30:31], s[34:35]
	v_readlane_b32 s55, v6, 40
	v_cndmask_b32_e64 v10, 0, 1, s[20:21]
	s_or_b64 s[20:21], s[36:37], s[40:41]
	v_cndmask_b32_e64 v11, 0, 1, s[20:21]
	v_cmp_eq_f32_e64 s[20:21], s55, v6
	v_cmp_gt_f32_e32 vcc, s55, v6
	s_and_b64 s[20:21], s[14:15], s[20:21]
	s_or_b64 s[20:21], vcc, s[20:21]
	v_readlane_b32 s5, v6, 48
	v_cndmask_b32_e64 v12, 0, 1, s[20:21]
	s_nop 0
	v_cmp_eq_f32_e64 s[20:21], s5, v6
	v_cmp_gt_f32_e32 vcc, s5, v6
	s_and_b64 s[20:21], s[16:17], s[20:21]
	v_readlane_b32 s5, v6, 56
	s_or_b64 s[20:21], vcc, s[20:21]
	v_cndmask_b32_e64 v13, 0, 1, s[20:21]
	v_cmp_gt_f32_e32 vcc, s5, v6
	s_nop 1
	v_cndmask_b32_e64 v6, 0, 1, vcc
	v_add_u32_e32 v6, v8, v6
	v_add3_u32 v6, v6, v7, v9
	v_add3_u32 v6, v6, v10, v11
	v_add3_u32 v6, v6, v12, v13
	v_cmp_gt_u32_e32 vcc, 4, v6
	s_nop 1
	v_cndmask_b32_e32 v6, v245, v2, vcc
	v_mov_b32_e32 v2, 0
	v_ashrrev_i32_e32 v9, 31, v6
	v_sub_u32_e32 v8, 63, v230
	v_and_b32_e32 v9, 0x7fffffff, v9
	v_xor_b32_e32 v9, v6, v9
	s_nop 0
	v_readlane_b32 s23, v9, 0
	s_movk_i32 s22, 63
	v_readlane_b32 s21, v9, 1
	s_movk_i32 s20, 62
	v_cmp_gt_i64_e32 vcc, s[22:23], v[8:9]
	v_readlane_b32 s23, v9, 2
	s_movk_i32 s22, 61
	v_addc_co_u32_e32 v2, vcc, 0, v2, vcc
	v_cmp_gt_i64_e32 vcc, s[20:21], v[8:9]
	v_readlane_b32 s21, v9, 3
	s_movk_i32 s20, 60
	v_addc_co_u32_e32 v2, vcc, 0, v2, vcc
	v_cmp_gt_i64_e32 vcc, s[22:23], v[8:9]
	v_readlane_b32 s23, v9, 4
	s_movk_i32 s22, 59
	v_addc_co_u32_e32 v2, vcc, 0, v2, vcc
	v_cmp_gt_i64_e32 vcc, s[20:21], v[8:9]
	v_readlane_b32 s21, v9, 5
	s_movk_i32 s20, 58
	v_addc_co_u32_e32 v2, vcc, 0, v2, vcc
	v_cmp_gt_i64_e32 vcc, s[22:23], v[8:9]
	v_readlane_b32 s23, v9, 6
	s_movk_i32 s22, 57
	v_addc_co_u32_e32 v2, vcc, 0, v2, vcc
	v_cmp_gt_i64_e32 vcc, s[20:21], v[8:9]
	v_readlane_b32 s21, v9, 7
	s_movk_i32 s20, 56
	v_addc_co_u32_e32 v2, vcc, 0, v2, vcc
	v_cmp_gt_i64_e32 vcc, s[22:23], v[8:9]
	v_readlane_b32 s23, v9, 8
	s_movk_i32 s22, 55
	v_addc_co_u32_e32 v2, vcc, 0, v2, vcc
	v_cmp_gt_i64_e32 vcc, s[20:21], v[8:9]
	v_readlane_b32 s21, v9, 9
	s_movk_i32 s20, 54
	v_addc_co_u32_e32 v2, vcc, 0, v2, vcc
	v_cmp_gt_i64_e32 vcc, s[22:23], v[8:9]
	v_readlane_b32 s23, v9, 10
	s_movk_i32 s22, 53
	v_addc_co_u32_e32 v2, vcc, 0, v2, vcc
	v_cmp_gt_i64_e32 vcc, s[20:21], v[8:9]
	v_readlane_b32 s21, v9, 11
	s_movk_i32 s20, 52
	v_addc_co_u32_e32 v2, vcc, 0, v2, vcc
; __device__ __forceinline__ void phase_nrr(const Frame& F, const Args& a, int l, const bf16_t* XA, const float* g, const float* modl, unsigned char* XN8) {
;     ...
;             int rank = 0;
; #pragma unroll 8
;             for (int e2 = 0; e2 < 64; ++e2) { const float v = __int_as_float(__builtin_amdgcn_readlane(__float_as_int(val), e2)); rank += (v > val || (v == val && e2 < lane)) ? 1 : 0; }
	v_cmp_gt_i64_e32 vcc, s[22:23], v[8:9]
	v_readlane_b32 s23, v9, 12
	s_movk_i32 s22, 51
	v_addc_co_u32_e32 v2, vcc, 0, v2, vcc
	v_cmp_gt_i64_e32 vcc, s[20:21], v[8:9]
	v_readlane_b32 s21, v9, 13
	s_movk_i32 s20, 50
	v_addc_co_u32_e32 v2, vcc, 0, v2, vcc
	v_cmp_gt_i64_e32 vcc, s[22:23], v[8:9]
	v_readlane_b32 s23, v9, 14
	s_movk_i32 s22, 49
	v_addc_co_u32_e32 v2, vcc, 0, v2, vcc
	v_cmp_gt_i64_e32 vcc, s[20:21], v[8:9]
	v_readlane_b32 s21, v9, 15
	s_movk_i32 s20, 48
	v_addc_co_u32_e32 v2, vcc, 0, v2, vcc
	v_cmp_gt_i64_e32 vcc, s[22:23], v[8:9]
	v_readlane_b32 s23, v9, 16
	s_movk_i32 s22, 47
	v_addc_co_u32_e32 v2, vcc, 0, v2, vcc
	v_cmp_gt_i64_e32 vcc, s[20:21], v[8:9]
	v_readlane_b32 s21, v9, 17
	s_movk_i32 s20, 46
	v_addc_co_u32_e32 v2, vcc, 0, v2, vcc
	v_cmp_gt_i64_e32 vcc, s[22:23], v[8:9]
	v_readlane_b32 s23, v9, 18
	s_movk_i32 s22, 45
	v_addc_co_u32_e32 v2, vcc, 0, v2, vcc
	v_cmp_gt_i64_e32 vcc, s[20:21], v[8:9]
	v_readlane_b32 s21, v9, 19
	s_movk_i32 s20, 44
	v_addc_co_u32_e32 v2, vcc, 0, v2, vcc
	v_cmp_gt_i64_e32 vcc, s[22:23], v[8:9]
	v_readlane_b32 s23, v9, 20
	s_movk_i32 s22, 43
	v_addc_co_u32_e32 v2, vcc, 0, v2, vcc
	v_cmp_gt_i64_e32 vcc, s[20:21], v[8:9]
	v_readlane_b32 s21, v9, 21
	s_movk_i32 s20, 42
	v_addc_co_u32_e32 v2, vcc, 0, v2, vcc
	v_cmp_gt_i64_e32 vcc, s[22:23], v[8:9]
	v_readlane_b32 s23, v9, 22
	s_movk_i32 s22, 41
	v_addc_co_u32_e32 v2, vcc, 0, v2, vcc
	v_cmp_gt_i64_e32 vcc, s[20:21], v[8:9]
	v_readlane_b32 s21, v9, 23
	s_movk_i32 s20, 40
	v_addc_co_u32_e32 v2, vcc, 0, v2, vcc
	v_cmp_gt_i64_e32 vcc, s[22:23], v[8:9]
	v_readlane_b32 s23, v9, 24
	s_movk_i32 s22, 39
	v_addc_co_u32_e32 v2, vcc, 0, v2, vcc
	v_cmp_gt_i64_e32 vcc, s[20:21], v[8:9]
	v_readlane_b32 s21, v9, 25
	s_movk_i32 s20, 38
	v_addc_co_u32_e32 v2, vcc, 0, v2, vcc
	v_cmp_gt_i64_e32 vcc, s[22:23], v[8:9]
	v_readlane_b32 s23, v9, 26
	s_movk_i32 s22, 37
	v_addc_co_u32_e32 v2, vcc, 0, v2, vcc
	v_cmp_gt_i64_e32 vcc, s[20:21], v[8:9]
	v_readlane_b32 s21, v9, 27
	s_movk_i32 s20, 36
	v_addc_co_u32_e32 v2, vcc, 0, v2, vcc
	v_cmp_gt_i64_e32 vcc, s[22:23], v[8:9]
	v_readlane_b32 s23, v9, 28
	s_movk_i32 s22, 35
	v_addc_co_u32_e32 v2, vcc, 0, v2, vcc
	v_cmp_gt_i64_e32 vcc, s[20:21], v[8:9]
	v_readlane_b32 s21, v9, 29
	s_movk_i32 s20, 34
	v_addc_co_u32_e32 v2, vcc, 0, v2, vcc
	v_cmp_gt_i64_e32 vcc, s[22:23], v[8:9]
	v_readlane_b32 s23, v9, 30
	s_movk_i32 s22, 33
	v_addc_co_u32_e32 v2, vcc, 0, v2, vcc
	v_cmp_gt_i64_e32 vcc, s[20:21], v[8:9]
	v_readlane_b32 s21, v9, 31
	s_movk_i32 s20, 32
	v_addc_co_u32_e32 v2, vcc, 0, v2, vcc
	v_cmp_gt_i64_e32 vcc, s[22:23], v[8:9]
	v_readlane_b32 s23, v9, 32
	s_movk_i32 s22, 31
	v_addc_co_u32_e32 v2, vcc, 0, v2, vcc
	v_cmp_gt_i64_e32 vcc, s[20:21], v[8:9]
	v_readlane_b32 s21, v9, 33
	s_movk_i32 s20, 30
	v_addc_co_u32_e32 v2, vcc, 0, v2, vcc
	v_cmp_gt_i64_e32 vcc, s[22:23], v[8:9]
	v_readlane_b32 s23, v9, 34
	s_movk_i32 s22, 29
	v_addc_co_u32_e32 v2, vcc, 0, v2, vcc
	v_cmp_gt_i64_e32 vcc, s[20:21], v[8:9]
	v_readlane_b32 s21, v9, 35
	s_movk_i32 s20, 28
	v_addc_co_u32_e32 v2, vcc, 0, v2, vcc
	v_cmp_gt_i64_e32 vcc, s[22:23], v[8:9]
	v_readlane_b32 s23, v9, 36
	s_movk_i32 s22, 27
	v_addc_co_u32_e32 v2, vcc, 0, v2, vcc
	v_cmp_gt_i64_e32 vcc, s[20:21], v[8:9]
	v_readlane_b32 s21, v9, 37
	s_movk_i32 s20, 26
	v_addc_co_u32_e32 v2, vcc, 0, v2, vcc
	v_cmp_gt_i64_e32 vcc, s[22:23], v[8:9]
	v_readlane_b32 s23, v9, 38
	s_movk_i32 s22, 25
	v_addc_co_u32_e32 v2, vcc, 0, v2, vcc
	v_cmp_gt_i64_e32 vcc, s[20:21], v[8:9]
	v_readlane_b32 s21, v9, 39
	s_movk_i32 s20, 24
	v_addc_co_u32_e32 v2, vcc, 0, v2, vcc
	v_cmp_gt_i64_e32 vcc, s[22:23], v[8:9]
	v_readlane_b32 s23, v9, 40
	s_movk_i32 s22, 23
	v_addc_co_u32_e32 v2, vcc, 0, v2, vcc
	v_cmp_gt_i64_e32 vcc, s[20:21], v[8:9]
	v_readlane_b32 s21, v9, 41
	s_movk_i32 s20, 22
	v_addc_co_u32_e32 v2, vcc, 0, v2, vcc
	v_cmp_gt_i64_e32 vcc, s[22:23], v[8:9]
	v_readlane_b32 s23, v9, 42
	s_movk_i32 s22, 21
	v_addc_co_u32_e32 v2, vcc, 0, v2, vcc
	v_cmp_gt_i64_e32 vcc, s[20:21], v[8:9]
	v_readlane_b32 s21, v9, 43
	s_movk_i32 s20, 20
	v_addc_co_u32_e32 v2, vcc, 0, v2, vcc
	v_cmp_gt_i64_e32 vcc, s[22:23], v[8:9]
	v_readlane_b32 s23, v9, 44
	s_movk_i32 s22, 19
	v_addc_co_u32_e32 v2, vcc, 0, v2, vcc
	v_cmp_gt_i64_e32 vcc, s[20:21], v[8:9]
	v_readlane_b32 s21, v9, 45
	s_movk_i32 s20, 18
	v_addc_co_u32_e32 v2, vcc, 0, v2, vcc
	v_cmp_gt_i64_e32 vcc, s[22:23], v[8:9]
	v_readlane_b32 s23, v9, 46
	s_movk_i32 s22, 17
	v_addc_co_u32_e32 v2, vcc, 0, v2, vcc
	v_cmp_gt_i64_e32 vcc, s[20:21], v[8:9]
	v_readlane_b32 s21, v9, 47
	s_movk_i32 s20, 16
	v_addc_co_u32_e32 v2, vcc, 0, v2, vcc
	v_cmp_gt_i64_e32 vcc, s[22:23], v[8:9]
	v_readlane_b32 s23, v9, 48
	s_movk_i32 s22, 15
	v_addc_co_u32_e32 v2, vcc, 0, v2, vcc
	v_cmp_gt_i64_e32 vcc, s[20:21], v[8:9]
	v_readlane_b32 s21, v9, 49
	s_movk_i32 s20, 14
	v_addc_co_u32_e32 v2, vcc, 0, v2, vcc
	v_cmp_gt_i64_e32 vcc, s[22:23], v[8:9]
	v_readlane_b32 s23, v9, 50
	s_movk_i32 s22, 13
	v_addc_co_u32_e32 v2, vcc, 0, v2, vcc
	v_cmp_gt_i64_e32 vcc, s[20:21], v[8:9]
	v_readlane_b32 s21, v9, 51
	s_movk_i32 s20, 12
	v_addc_co_u32_e32 v2, vcc, 0, v2, vcc
	v_cmp_gt_i64_e32 vcc, s[22:23], v[8:9]
	v_readlane_b32 s23, v9, 52
	s_movk_i32 s22, 11
	v_addc_co_u32_e32 v2, vcc, 0, v2, vcc
	v_cmp_gt_i64_e32 vcc, s[20:21], v[8:9]
	v_readlane_b32 s21, v9, 53
	s_movk_i32 s20, 10
	v_addc_co_u32_e32 v2, vcc, 0, v2, vcc
	v_cmp_gt_i64_e32 vcc, s[22:23], v[8:9]
	v_readlane_b32 s23, v9, 54
	s_movk_i32 s22, 9
	v_addc_co_u32_e32 v2, vcc, 0, v2, vcc
	v_cmp_gt_i64_e32 vcc, s[20:21], v[8:9]
	v_readlane_b32 s21, v9, 55
	s_movk_i32 s20, 8
	v_addc_co_u32_e32 v2, vcc, 0, v2, vcc
	v_cmp_gt_i64_e32 vcc, s[22:23], v[8:9]
; __device__ __forceinline__ void phase_nrr(const Frame& F, const Args& a, int l, const bf16_t* XA, const float* g, const float* modl, unsigned char* XN8) {
;     ...
;             const float lg = Pl[(w * 8 + i) * NE + lane] + Pl[(64 + w * 8 + i) * NE + lane]; const float sc = 1.f / (1.f + __expf(-lg)); const float bb = sc + bias;
;             float m1 = bb; m1 = fmaxf(m1, __shfl_xor(m1, 1)); m1 = fmaxf(m1, __shfl_xor(m1, 2)); m1 = fmaxf(m1, __shfl_xor(m1, 4));
;             const unsigned long long eq = __ballot(bb == m1); const int gbase = lane & ~7; const unsigned grpmask = (unsigned)((eq >> gbase) & 0xffull);
;             const int first = gbase + __builtin_ctz(grpmask);
;             float m2 = (lane == first) ? -INFINITY : bb; m2 = fmaxf(m2, __shfl_xor(m2, 1)); m2 = fmaxf(m2, __shfl_xor(m2, 2)); m2 = fmaxf(m2, __shfl_xor(m2, 4));
;             const float gsum = m1 + m2; const int gq = lane >> 3;
;             int grank = 0;
; #pragma unroll
;             for (int g2 = 0; g2 < 8; ++g2) { const float v = __int_as_float(__builtin_amdgcn_readlane(__float_as_int(gsum), g2 * 8)); grank += (v > gsum || (v == gsum && g2 < gq)) ? 1 : 0; }
;     ...
;             int rank = 0;
; #pragma unroll 8
;             for (int e2 = 0; e2 < 64; ++e2) { const float v = __int_as_float(__builtin_amdgcn_readlane(__float_as_int(val), e2)); rank += (v > val || (v == val && e2 < lane)) ? 1 : 0; }
;             const bool sel = rank < TOPK;
;             const float ssum = wave_sum(sel ? sc : 0.f);
;             if (sel) { const int p = atomicAdd((int*)(hist + lane), 1); top_e[t * TOPK + rank] = lane; gate[t * TOPK + rank] = sc / ssum * 2.5f; lpos[t * TOPK + rank] = p; }
	v_readlane_b32 s23, v9, 56
	s_movk_i32 s22, 7
	v_addc_co_u32_e32 v2, vcc, 0, v2, vcc
	v_cmp_gt_i64_e32 vcc, s[20:21], v[8:9]
	v_readlane_b32 s21, v9, 57
	s_movk_i32 s20, 6
	v_addc_co_u32_e32 v2, vcc, 0, v2, vcc
	v_cmp_gt_i64_e32 vcc, s[22:23], v[8:9]
	v_readlane_b32 s23, v9, 58
	s_movk_i32 s22, 5
	v_addc_co_u32_e32 v2, vcc, 0, v2, vcc
	v_cmp_gt_i64_e32 vcc, s[20:21], v[8:9]
	v_readlane_b32 s21, v9, 59
	s_movk_i32 s20, 4
	v_addc_co_u32_e32 v2, vcc, 0, v2, vcc
	v_cmp_gt_i64_e32 vcc, s[22:23], v[8:9]
	v_readlane_b32 s23, v9, 60
	s_movk_i32 s22, 3
	v_addc_co_u32_e32 v2, vcc, 0, v2, vcc
	v_cmp_gt_i64_e32 vcc, s[20:21], v[8:9]
	v_readlane_b32 s21, v9, 61
	s_movk_i32 s20, 2
	v_addc_co_u32_e32 v2, vcc, 0, v2, vcc
	v_cmp_gt_i64_e32 vcc, s[22:23], v[8:9]
	v_readlane_b32 s23, v9, 62
	s_movk_i32 s22, 1
	v_addc_co_u32_e32 v2, vcc, 0, v2, vcc
	v_cmp_gt_i64_e32 vcc, s[20:21], v[8:9]
	v_readlane_b32 s21, v9, 63
	s_movk_i32 s20, 0
	v_addc_co_u32_e32 v2, vcc, 0, v2, vcc
	v_cmp_gt_i64_e32 vcc, s[22:23], v[8:9]
	s_nop 1
	v_addc_co_u32_e32 v2, vcc, 0, v2, vcc
	v_cmp_gt_i64_e32 vcc, s[20:21], v[8:9]
	s_nop 1
	v_addc_co_u32_e32 v2, vcc, 0, v2, vcc
	v_cmp_gt_u32_e32 vcc, 6, v2
	s_nop 1
	v_cndmask_b32_e32 v6, 0, v5, vcc
	s_nop 1
	v_add_f32_dpp v6, v6, v6 quad_perm:[1,0,3,2] row_mask:0xf bank_mask:0xf
	s_nop 1
	v_add_f32_dpp v6, v6, v6 quad_perm:[2,3,0,1] row_mask:0xf bank_mask:0xf
	s_nop 1
	v_add_f32_dpp v6, v6, v6 row_half_mirror row_mask:0xf bank_mask:0xf
	s_nop 1
	v_add_f32_dpp v6, v6, v6 row_mirror row_mask:0xf bank_mask:0xf
	s_nop 0
	ds_bpermute_b32 v7, v222, v6
	s_waitcnt lgkmcnt(0)
	v_add_f32_e32 v6, v6, v7
	v_mov_b32_e32 v7, v6
	s_nop 1
	v_permlane32_swap_b32_e32 v7, v6
	s_and_saveexec_b64 s[20:21], vcc
	s_cbranch_execz .LBB0_1316
	s_waitcnt lgkmcnt(0)
	v_add_f32_e32 v10, v6, v7
	v_mad_u64_u32 v[6:7], s[22:23], s56, 6, v[2:3]
	v_div_scale_f32 v2, s[22:23], v10, v10, v5
	v_rcp_f32_e32 v12, v2
	v_ashrrev_i32_e32 v7, 31, v6
	v_lshlrev_b64 v[6:7], 2, v[6:7]
	v_lshl_add_u64 v[8:9], s[42:43], 0, v[6:7]
	ds_add_rtn_u32 v11, v227, v243
	global_store_dword v[8:9], v230, off
	v_fma_f32 v8, -v2, v12, 1.0
	v_fmac_f32_e32 v12, v8, v12
	v_div_scale_f32 v8, vcc, v5, v10, v5
	v_mul_f32_e32 v9, v8, v12
	v_fma_f32 v13, -v2, v9, v8
	v_fmac_f32_e32 v9, v13, v12
	v_fma_f32 v2, -v2, v9, v8
	v_div_fmas_f32 v2, v2, v12, v9
	v_div_fixup_f32 v2, v2, v10, v5
	v_mul_f32_e32 v2, 0x40200000, v2
	v_lshl_add_u64 v[8:9], s[44:45], 0, v[6:7]
	v_lshl_add_u64 v[6:7], s[46:47], 0, v[6:7]
	global_store_dword v[8:9], v2, off
	s_waitcnt lgkmcnt(0)
	global_store_dword v[6:7], v11, off
.LBB0_1316:
	s_or_b64 exec, exec, s[20:21]
	v_add_u32_e32 v2, s77, v226
	ds_read_b32 v2, v2
	ds_read_b32 v5, v4 offset:16896
	s_mov_b32 s3, 0
	s_waitcnt lgkmcnt(0)
	v_add_f32_e32 v2, v2, v5
	v_mul_f32_e32 v2, 0xbfb8aa3b, v2
	v_exp_f32_e32 v2, v2
	s_nop 0
	v_add_f32_e32 v2, 1.0, v2
	v_div_scale_f32 v5, s[20:21], v2, v2, 1.0
	v_rcp_f32_e32 v6, v5
	v_div_scale_f32 v7, vcc, 1.0, v2, 1.0
	v_fma_f32 v8, -v5, v6, 1.0
	v_fmac_f32_e32 v6, v8, v6
	v_mul_f32_e32 v8, v7, v6
	v_fma_f32 v9, -v5, v8, v7
	v_fmac_f32_e32 v8, v9, v6
	v_fma_f32 v5, -v5, v8, v7
	v_div_fmas_f32 v5, v5, v6, v8
	v_div_fixup_f32 v5, v5, v2, 1.0
	v_add_f32_e32 v2, v3, v5
	s_nop 1
	s_waitcnt lgkmcnt(0)
	v_max_f32_dpp v6, v2, v2 quad_perm:[1,0,3,2] row_mask:0xf bank_mask:0xf
	s_nop 1
	s_waitcnt lgkmcnt(0)
	v_max_f32_dpp v6, v6, v6 quad_perm:[2,3,0,1] row_mask:0xf bank_mask:0xf
	s_nop 1
	s_waitcnt lgkmcnt(0)
	v_max_f32_dpp v8, v6, v6 row_half_mirror row_mask:0xf bank_mask:0xf
	v_cmp_eq_f32_e32 vcc, v2, v8
	s_nop 1
	v_lshrrev_b64 v[6:7], v200, vcc
	v_ffbl_b32_sdwa v6, v6 dst_sel:DWORD dst_unused:UNUSED_PAD src0_sel:BYTE_0
	v_add_u32_e32 v6, v6, v200
	v_cmp_ne_u32_e32 vcc, v230, v6
	s_nop 1
	v_cndmask_b32_e32 v6, v245, v2, vcc
	s_nop 1
	s_waitcnt lgkmcnt(0)
	v_max_f32_dpp v6, v6, v6 quad_perm:[1,0,3,2] row_mask:0xf bank_mask:0xf
	s_nop 1
	s_waitcnt lgkmcnt(0)
	v_max_f32_dpp v6, v6, v6 quad_perm:[2,3,0,1] row_mask:0xf bank_mask:0xf
	s_nop 1
	s_waitcnt lgkmcnt(0)
	v_max_f32_dpp v6, v6, v6 row_half_mirror row_mask:0xf bank_mask:0xf
	v_add_f32_e32 v6, v8, v6
	s_nop 0
	v_readlane_b32 s5, v6, 0
	v_readlane_b32 s24, v6, 8
	v_readlane_b32 s28, v6, 16
	v_cmp_eq_f32_e64 s[20:21], s5, v6
	v_cmp_gt_f32_e32 vcc, s5, v6
	v_cmp_gt_f32_e64 s[22:23], s24, v6
	v_cmp_eq_f32_e64 s[24:25], s24, v6
	s_and_b64 s[20:21], s[0:1], s[20:21]
	v_readlane_b32 s34, v6, 24
	v_cmp_gt_f32_e64 s[26:27], s28, v6
	v_cmp_eq_f32_e64 s[28:29], s28, v6
	s_and_b64 s[24:25], s[6:7], s[24:25]
	s_or_b64 s[20:21], vcc, s[20:21]
	v_readlane_b32 s40, v6, 32
	v_cmp_gt_f32_e64 s[30:31], s34, v6
	v_cmp_eq_f32_e64 s[34:35], s34, v6
	s_and_b64 s[28:29], s[8:9], s[28:29]
	v_cndmask_b32_e64 v7, 0, 1, s[20:21]
	s_or_b64 s[20:21], s[22:23], s[24:25]
	v_cmp_gt_f32_e64 s[36:37], s40, v6
	v_cmp_eq_f32_e64 s[40:41], s40, v6
	s_and_b64 s[34:35], s[10:11], s[34:35]
	v_cndmask_b32_e64 v8, 0, 1, s[20:21]
	s_or_b64 s[20:21], s[26:27], s[28:29]
	s_and_b64 s[40:41], s[12:13], s[40:41]
	v_cndmask_b32_e64 v9, 0, 1, s[20:21]
	s_or_b64 s[20:21], s[30:31], s[34:35]
	v_readlane_b32 s55, v6, 40
	v_cndmask_b32_e64 v10, 0, 1, s[20:21]
	s_or_b64 s[20:21], s[36:37], s[40:41]
	v_cndmask_b32_e64 v11, 0, 1, s[20:21]
	v_cmp_eq_f32_e64 s[20:21], s55, v6
	v_cmp_gt_f32_e32 vcc, s55, v6
	s_and_b64 s[20:21], s[14:15], s[20:21]
	s_or_b64 s[20:21], vcc, s[20:21]
	v_readlane_b32 s5, v6, 48
	v_cndmask_b32_e64 v12, 0, 1, s[20:21]
	s_nop 0
	v_cmp_eq_f32_e64 s[20:21], s5, v6
	v_cmp_gt_f32_e32 vcc, s5, v6
	s_and_b64 s[20:21], s[16:17], s[20:21]
	v_readlane_b32 s5, v6, 56
	s_or_b64 s[20:21], vcc, s[20:21]
	v_cndmask_b32_e64 v13, 0, 1, s[20:21]
; __device__ __forceinline__ void phase_nrr(const Frame& F, const Args& a, int l, const bf16_t* XA, const float* g, const float* modl, unsigned char* XN8) {
;     ...
;             int grank = 0;
; #pragma unroll
;             for (int g2 = 0; g2 < 8; ++g2) { const float v = __int_as_float(__builtin_amdgcn_readlane(__float_as_int(gsum), g2 * 8)); grank += (v > gsum || (v == gsum && g2 < gq)) ? 1 : 0; }
;             const bool keep = grank < 4; const float val = keep ? bb : -INFINITY;
;             int rank = 0;
; #pragma unroll 8
;             for (int e2 = 0; e2 < 64; ++e2) { const float v = __int_as_float(__builtin_amdgcn_readlane(__float_as_int(val), e2)); rank += (v > val || (v == val && e2 < lane)) ? 1 : 0; }
	v_cmp_gt_f32_e32 vcc, s5, v6
	s_nop 1
	v_cndmask_b32_e64 v6, 0, 1, vcc
	v_add_u32_e32 v6, v8, v6
	v_add3_u32 v6, v6, v7, v9
	v_add3_u32 v6, v6, v10, v11
	v_add3_u32 v6, v6, v12, v13
	v_cmp_gt_u32_e32 vcc, 4, v6
	s_nop 1
	v_cndmask_b32_e32 v6, v245, v2, vcc
	v_mov_b32_e32 v2, 0
	v_ashrrev_i32_e32 v9, 31, v6
	v_sub_u32_e32 v8, 63, v230
	v_and_b32_e32 v9, 0x7fffffff, v9
	v_xor_b32_e32 v9, v6, v9
	s_nop 0
	v_readlane_b32 s23, v9, 0
	s_movk_i32 s22, 63
	v_readlane_b32 s21, v9, 1
	s_movk_i32 s20, 62
	v_cmp_gt_i64_e32 vcc, s[22:23], v[8:9]
	v_readlane_b32 s23, v9, 2
	s_movk_i32 s22, 61
	v_addc_co_u32_e32 v2, vcc, 0, v2, vcc
	v_cmp_gt_i64_e32 vcc, s[20:21], v[8:9]
	v_readlane_b32 s21, v9, 3
	s_movk_i32 s20, 60
	v_addc_co_u32_e32 v2, vcc, 0, v2, vcc
	v_cmp_gt_i64_e32 vcc, s[22:23], v[8:9]
	v_readlane_b32 s23, v9, 4
	s_movk_i32 s22, 59
	v_addc_co_u32_e32 v2, vcc, 0, v2, vcc
	v_cmp_gt_i64_e32 vcc, s[20:21], v[8:9]
	v_readlane_b32 s21, v9, 5
	s_movk_i32 s20, 58
	v_addc_co_u32_e32 v2, vcc, 0, v2, vcc
	v_cmp_gt_i64_e32 vcc, s[22:23], v[8:9]
	v_readlane_b32 s23, v9, 6
	s_movk_i32 s22, 57
	v_addc_co_u32_e32 v2, vcc, 0, v2, vcc
	v_cmp_gt_i64_e32 vcc, s[20:21], v[8:9]
	v_readlane_b32 s21, v9, 7
	s_movk_i32 s20, 56
	v_addc_co_u32_e32 v2, vcc, 0, v2, vcc
	v_cmp_gt_i64_e32 vcc, s[22:23], v[8:9]
	v_readlane_b32 s23, v9, 8
	s_movk_i32 s22, 55
	v_addc_co_u32_e32 v2, vcc, 0, v2, vcc
	v_cmp_gt_i64_e32 vcc, s[20:21], v[8:9]
	v_readlane_b32 s21, v9, 9
	s_movk_i32 s20, 54
	v_addc_co_u32_e32 v2, vcc, 0, v2, vcc
	v_cmp_gt_i64_e32 vcc, s[22:23], v[8:9]
	v_readlane_b32 s23, v9, 10
	s_movk_i32 s22, 53
	v_addc_co_u32_e32 v2, vcc, 0, v2, vcc
	v_cmp_gt_i64_e32 vcc, s[20:21], v[8:9]
	v_readlane_b32 s21, v9, 11
	s_movk_i32 s20, 52
	v_addc_co_u32_e32 v2, vcc, 0, v2, vcc
	v_cmp_gt_i64_e32 vcc, s[22:23], v[8:9]
	v_readlane_b32 s23, v9, 12
	s_movk_i32 s22, 51
	v_addc_co_u32_e32 v2, vcc, 0, v2, vcc
	v_cmp_gt_i64_e32 vcc, s[20:21], v[8:9]
	v_readlane_b32 s21, v9, 13
	s_movk_i32 s20, 50
	v_addc_co_u32_e32 v2, vcc, 0, v2, vcc
	v_cmp_gt_i64_e32 vcc, s[22:23], v[8:9]
	v_readlane_b32 s23, v9, 14
	s_movk_i32 s22, 49
	v_addc_co_u32_e32 v2, vcc, 0, v2, vcc
	v_cmp_gt_i64_e32 vcc, s[20:21], v[8:9]
	v_readlane_b32 s21, v9, 15
	s_movk_i32 s20, 48
	v_addc_co_u32_e32 v2, vcc, 0, v2, vcc
	v_cmp_gt_i64_e32 vcc, s[22:23], v[8:9]
	v_readlane_b32 s23, v9, 16
	s_movk_i32 s22, 47
	v_addc_co_u32_e32 v2, vcc, 0, v2, vcc
	v_cmp_gt_i64_e32 vcc, s[20:21], v[8:9]
	v_readlane_b32 s21, v9, 17
	s_movk_i32 s20, 46
	v_addc_co_u32_e32 v2, vcc, 0, v2, vcc
	v_cmp_gt_i64_e32 vcc, s[22:23], v[8:9]
	v_readlane_b32 s23, v9, 18
	s_movk_i32 s22, 45
	v_addc_co_u32_e32 v2, vcc, 0, v2, vcc
	v_cmp_gt_i64_e32 vcc, s[20:21], v[8:9]
	v_readlane_b32 s21, v9, 19
	s_movk_i32 s20, 44
	v_addc_co_u32_e32 v2, vcc, 0, v2, vcc
	v_cmp_gt_i64_e32 vcc, s[22:23], v[8:9]
	v_readlane_b32 s23, v9, 20
	s_movk_i32 s22, 43
	v_addc_co_u32_e32 v2, vcc, 0, v2, vcc
	v_cmp_gt_i64_e32 vcc, s[20:21], v[8:9]
	v_readlane_b32 s21, v9, 21
	s_movk_i32 s20, 42
	v_addc_co_u32_e32 v2, vcc, 0, v2, vcc
	v_cmp_gt_i64_e32 vcc, s[22:23], v[8:9]
	v_readlane_b32 s23, v9, 22
	s_movk_i32 s22, 41
	v_addc_co_u32_e32 v2, vcc, 0, v2, vcc
	v_cmp_gt_i64_e32 vcc, s[20:21], v[8:9]
	v_readlane_b32 s21, v9, 23
	s_movk_i32 s20, 40
	v_addc_co_u32_e32 v2, vcc, 0, v2, vcc
	v_cmp_gt_i64_e32 vcc, s[22:23], v[8:9]
	v_readlane_b32 s23, v9, 24
	s_movk_i32 s22, 39
	v_addc_co_u32_e32 v2, vcc, 0, v2, vcc
	v_cmp_gt_i64_e32 vcc, s[20:21], v[8:9]
	v_readlane_b32 s21, v9, 25
	s_movk_i32 s20, 38
	v_addc_co_u32_e32 v2, vcc, 0, v2, vcc
	v_cmp_gt_i64_e32 vcc, s[22:23], v[8:9]
	v_readlane_b32 s23, v9, 26
	s_movk_i32 s22, 37
	v_addc_co_u32_e32 v2, vcc, 0, v2, vcc
	v_cmp_gt_i64_e32 vcc, s[20:21], v[8:9]
	v_readlane_b32 s21, v9, 27
	s_movk_i32 s20, 36
	v_addc_co_u32_e32 v2, vcc, 0, v2, vcc
	v_cmp_gt_i64_e32 vcc, s[22:23], v[8:9]
	v_readlane_b32 s23, v9, 28
	s_movk_i32 s22, 35
	v_addc_co_u32_e32 v2, vcc, 0, v2, vcc
	v_cmp_gt_i64_e32 vcc, s[20:21], v[8:9]
	v_readlane_b32 s21, v9, 29
	s_movk_i32 s20, 34
	v_addc_co_u32_e32 v2, vcc, 0, v2, vcc
	v_cmp_gt_i64_e32 vcc, s[22:23], v[8:9]
	v_readlane_b32 s23, v9, 30
	s_movk_i32 s22, 33
	v_addc_co_u32_e32 v2, vcc, 0, v2, vcc
	v_cmp_gt_i64_e32 vcc, s[20:21], v[8:9]
	v_readlane_b32 s21, v9, 31
	s_movk_i32 s20, 32
	v_addc_co_u32_e32 v2, vcc, 0, v2, vcc
	v_cmp_gt_i64_e32 vcc, s[22:23], v[8:9]
	v_readlane_b32 s23, v9, 32
	s_movk_i32 s22, 31
	v_addc_co_u32_e32 v2, vcc, 0, v2, vcc
	v_cmp_gt_i64_e32 vcc, s[20:21], v[8:9]
	v_readlane_b32 s21, v9, 33
	s_movk_i32 s20, 30
	v_addc_co_u32_e32 v2, vcc, 0, v2, vcc
	v_cmp_gt_i64_e32 vcc, s[22:23], v[8:9]
	v_readlane_b32 s23, v9, 34
	s_movk_i32 s22, 29
	v_addc_co_u32_e32 v2, vcc, 0, v2, vcc
	v_cmp_gt_i64_e32 vcc, s[20:21], v[8:9]
	v_readlane_b32 s21, v9, 35
	s_movk_i32 s20, 28
	v_addc_co_u32_e32 v2, vcc, 0, v2, vcc
	v_cmp_gt_i64_e32 vcc, s[22:23], v[8:9]
	v_readlane_b32 s23, v9, 36
	s_movk_i32 s22, 27
	v_addc_co_u32_e32 v2, vcc, 0, v2, vcc
	v_cmp_gt_i64_e32 vcc, s[20:21], v[8:9]
	v_readlane_b32 s21, v9, 37
	s_movk_i32 s20, 26
	v_addc_co_u32_e32 v2, vcc, 0, v2, vcc
	v_cmp_gt_i64_e32 vcc, s[22:23], v[8:9]
	v_readlane_b32 s23, v9, 38
	s_movk_i32 s22, 25
	v_addc_co_u32_e32 v2, vcc, 0, v2, vcc
	v_cmp_gt_i64_e32 vcc, s[20:21], v[8:9]
	v_readlane_b32 s21, v9, 39
	s_movk_i32 s20, 24
	v_addc_co_u32_e32 v2, vcc, 0, v2, vcc
	v_cmp_gt_i64_e32 vcc, s[22:23], v[8:9]
	v_readlane_b32 s23, v9, 40
	s_movk_i32 s22, 23
	v_addc_co_u32_e32 v2, vcc, 0, v2, vcc
	v_cmp_gt_i64_e32 vcc, s[20:21], v[8:9]
	v_readlane_b32 s21, v9, 41
	s_movk_i32 s20, 22
	v_addc_co_u32_e32 v2, vcc, 0, v2, vcc
	v_cmp_gt_i64_e32 vcc, s[22:23], v[8:9]
	v_readlane_b32 s23, v9, 42
; __device__ __forceinline__ void phase_nrr(const Frame& F, const Args& a, int l, const bf16_t* XA, const float* g, const float* modl, unsigned char* XN8) {
;     ...
;             for (int e2 = 0; e2 < 64; ++e2) { const float v = __int_as_float(__builtin_amdgcn_readlane(__float_as_int(val), e2)); rank += (v > val || (v == val && e2 < lane)) ? 1 : 0; }
;             const bool sel = rank < TOPK;
;             const float ssum = wave_sum(sel ? sc : 0.f);
;             if (sel) { const int p = atomicAdd((int*)(hist + lane), 1); top_e[t * TOPK + rank] = lane; gate[t * TOPK + rank] = sc / ssum * 2.5f; lpos[t * TOPK + rank] = p; }
	s_movk_i32 s22, 21
	v_addc_co_u32_e32 v2, vcc, 0, v2, vcc
	v_cmp_gt_i64_e32 vcc, s[20:21], v[8:9]
	v_readlane_b32 s21, v9, 43
	s_movk_i32 s20, 20
	v_addc_co_u32_e32 v2, vcc, 0, v2, vcc
	v_cmp_gt_i64_e32 vcc, s[22:23], v[8:9]
	v_readlane_b32 s23, v9, 44
	s_movk_i32 s22, 19
	v_addc_co_u32_e32 v2, vcc, 0, v2, vcc
	v_cmp_gt_i64_e32 vcc, s[20:21], v[8:9]
	v_readlane_b32 s21, v9, 45
	s_movk_i32 s20, 18
	v_addc_co_u32_e32 v2, vcc, 0, v2, vcc
	v_cmp_gt_i64_e32 vcc, s[22:23], v[8:9]
	v_readlane_b32 s23, v9, 46
	s_movk_i32 s22, 17
	v_addc_co_u32_e32 v2, vcc, 0, v2, vcc
	v_cmp_gt_i64_e32 vcc, s[20:21], v[8:9]
	v_readlane_b32 s21, v9, 47
	s_movk_i32 s20, 16
	v_addc_co_u32_e32 v2, vcc, 0, v2, vcc
	v_cmp_gt_i64_e32 vcc, s[22:23], v[8:9]
	v_readlane_b32 s23, v9, 48
	s_movk_i32 s22, 15
	v_addc_co_u32_e32 v2, vcc, 0, v2, vcc
	v_cmp_gt_i64_e32 vcc, s[20:21], v[8:9]
	v_readlane_b32 s21, v9, 49
	s_movk_i32 s20, 14
	v_addc_co_u32_e32 v2, vcc, 0, v2, vcc
	v_cmp_gt_i64_e32 vcc, s[22:23], v[8:9]
	v_readlane_b32 s23, v9, 50
	s_movk_i32 s22, 13
	v_addc_co_u32_e32 v2, vcc, 0, v2, vcc
	v_cmp_gt_i64_e32 vcc, s[20:21], v[8:9]
	v_readlane_b32 s21, v9, 51
	s_movk_i32 s20, 12
	v_addc_co_u32_e32 v2, vcc, 0, v2, vcc
	v_cmp_gt_i64_e32 vcc, s[22:23], v[8:9]
	v_readlane_b32 s23, v9, 52
	s_movk_i32 s22, 11
	v_addc_co_u32_e32 v2, vcc, 0, v2, vcc
	v_cmp_gt_i64_e32 vcc, s[20:21], v[8:9]
	v_readlane_b32 s21, v9, 53
	s_movk_i32 s20, 10
	v_addc_co_u32_e32 v2, vcc, 0, v2, vcc
	v_cmp_gt_i64_e32 vcc, s[22:23], v[8:9]
	v_readlane_b32 s23, v9, 54
	s_movk_i32 s22, 9
	v_addc_co_u32_e32 v2, vcc, 0, v2, vcc
	v_cmp_gt_i64_e32 vcc, s[20:21], v[8:9]
	v_readlane_b32 s21, v9, 55
	s_movk_i32 s20, 8
	v_addc_co_u32_e32 v2, vcc, 0, v2, vcc
	v_cmp_gt_i64_e32 vcc, s[22:23], v[8:9]
	v_readlane_b32 s23, v9, 56
	s_movk_i32 s22, 7
	v_addc_co_u32_e32 v2, vcc, 0, v2, vcc
	v_cmp_gt_i64_e32 vcc, s[20:21], v[8:9]
	v_readlane_b32 s21, v9, 57
	s_movk_i32 s20, 6
	v_addc_co_u32_e32 v2, vcc, 0, v2, vcc
	v_cmp_gt_i64_e32 vcc, s[22:23], v[8:9]
	v_readlane_b32 s23, v9, 58
	s_movk_i32 s22, 5
	v_addc_co_u32_e32 v2, vcc, 0, v2, vcc
	v_cmp_gt_i64_e32 vcc, s[20:21], v[8:9]
	v_readlane_b32 s21, v9, 59
	s_movk_i32 s20, 4
	v_addc_co_u32_e32 v2, vcc, 0, v2, vcc
	v_cmp_gt_i64_e32 vcc, s[22:23], v[8:9]
	v_readlane_b32 s23, v9, 60
	s_movk_i32 s22, 3
	v_addc_co_u32_e32 v2, vcc, 0, v2, vcc
	v_cmp_gt_i64_e32 vcc, s[20:21], v[8:9]
	v_readlane_b32 s21, v9, 61
	s_movk_i32 s20, 2
	v_addc_co_u32_e32 v2, vcc, 0, v2, vcc
	v_cmp_gt_i64_e32 vcc, s[22:23], v[8:9]
	v_readlane_b32 s23, v9, 62
	s_movk_i32 s22, 1
	v_addc_co_u32_e32 v2, vcc, 0, v2, vcc
	v_cmp_gt_i64_e32 vcc, s[20:21], v[8:9]
	v_readlane_b32 s21, v9, 63
	s_movk_i32 s20, 0
	v_addc_co_u32_e32 v2, vcc, 0, v2, vcc
	v_cmp_gt_i64_e32 vcc, s[22:23], v[8:9]
	s_nop 1
	v_addc_co_u32_e32 v2, vcc, 0, v2, vcc
	v_cmp_gt_i64_e32 vcc, s[20:21], v[8:9]
	s_nop 1
	v_addc_co_u32_e32 v2, vcc, 0, v2, vcc
	v_cmp_gt_u32_e32 vcc, 6, v2
	s_nop 1
	v_cndmask_b32_e32 v6, 0, v5, vcc
	s_nop 1
	v_add_f32_dpp v6, v6, v6 quad_perm:[1,0,3,2] row_mask:0xf bank_mask:0xf
	s_nop 1
	v_add_f32_dpp v6, v6, v6 quad_perm:[2,3,0,1] row_mask:0xf bank_mask:0xf
	s_nop 1
	v_add_f32_dpp v6, v6, v6 row_half_mirror row_mask:0xf bank_mask:0xf
	s_nop 1
	v_add_f32_dpp v6, v6, v6 row_mirror row_mask:0xf bank_mask:0xf
	s_nop 0
	ds_bpermute_b32 v7, v222, v6
	s_waitcnt lgkmcnt(0)
	v_add_f32_e32 v6, v6, v7
	v_mov_b32_e32 v7, v6
	s_nop 1
	v_permlane32_swap_b32_e32 v7, v6
	s_and_saveexec_b64 s[20:21], vcc
	s_cbranch_execz .LBB0_1320
	s_waitcnt lgkmcnt(0)
	v_add_f32_e32 v10, v6, v7
	v_mad_u64_u32 v[6:7], s[22:23], s54, 6, v[2:3]
	v_div_scale_f32 v2, s[22:23], v10, v10, v5
	v_rcp_f32_e32 v12, v2
	v_ashrrev_i32_e32 v7, 31, v6
	v_lshlrev_b64 v[6:7], 2, v[6:7]
	v_lshl_add_u64 v[8:9], s[42:43], 0, v[6:7]
	ds_add_rtn_u32 v11, v227, v243
	global_store_dword v[8:9], v230, off
	v_fma_f32 v8, -v2, v12, 1.0
	v_fmac_f32_e32 v12, v8, v12
	v_div_scale_f32 v8, vcc, v5, v10, v5
	v_mul_f32_e32 v9, v8, v12
	v_fma_f32 v13, -v2, v9, v8
	v_fmac_f32_e32 v9, v13, v12
	v_fma_f32 v2, -v2, v9, v8
	v_div_fmas_f32 v2, v2, v12, v9
	v_div_fixup_f32 v2, v2, v10, v5
	v_mul_f32_e32 v2, 0x40200000, v2
	v_lshl_add_u64 v[8:9], s[44:45], 0, v[6:7]
	v_lshl_add_u64 v[6:7], s[46:47], 0, v[6:7]
	global_store_dword v[8:9], v2, off
	s_waitcnt lgkmcnt(0)
	global_store_dword v[6:7], v11, off
; __device__ __forceinline__ void phase_nrr(const Frame& F, const Args& a, int l, const bf16_t* XA, const float* g, const float* modl, unsigned char* XN8) {
;     ...
;             const float lg = Pl[(w * 8 + i) * NE + lane] + Pl[(64 + w * 8 + i) * NE + lane]; const float sc = 1.f / (1.f + __expf(-lg)); const float bb = sc + bias;
;             float m1 = bb; m1 = fmaxf(m1, __shfl_xor(m1, 1)); m1 = fmaxf(m1, __shfl_xor(m1, 2)); m1 = fmaxf(m1, __shfl_xor(m1, 4));
;             const unsigned long long eq = __ballot(bb == m1); const int gbase = lane & ~7; const unsigned grpmask = (unsigned)((eq >> gbase) & 0xffull);
;             const int first = gbase + __builtin_ctz(grpmask);
;             float m2 = (lane == first) ? -INFINITY : bb; m2 = fmaxf(m2, __shfl_xor(m2, 1)); m2 = fmaxf(m2, __shfl_xor(m2, 2)); m2 = fmaxf(m2, __shfl_xor(m2, 4));
;             const float gsum = m1 + m2; const int gq = lane >> 3;
;             int grank = 0;
; #pragma unroll
;             for (int g2 = 0; g2 < 8; ++g2) { const float v = __int_as_float(__builtin_amdgcn_readlane(__float_as_int(gsum), g2 * 8)); grank += (v > gsum || (v == gsum && g2 < gq)) ? 1 : 0; }
;             const bool keep = grank < 4; const float val = keep ? bb : -INFINITY;
;             int rank = 0;
; #pragma unroll 8
;             for (int e2 = 0; e2 < 64; ++e2) { const float v = __int_as_float(__builtin_amdgcn_readlane(__float_as_int(val), e2)); rank += (v > val || (v == val && e2 < lane)) ? 1 : 0; }
.LBB0_1320:
	s_or_b64 exec, exec, s[20:21]
	v_add_u32_e32 v2, s78, v226
	ds_read_b32 v2, v2
	ds_read_b32 v5, v4 offset:17152
	s_mov_b32 s3, 0
	s_waitcnt lgkmcnt(0)
	v_add_f32_e32 v2, v2, v5
	v_mul_f32_e32 v2, 0xbfb8aa3b, v2
	v_exp_f32_e32 v2, v2
	s_nop 0
	v_add_f32_e32 v2, 1.0, v2
	v_div_scale_f32 v5, s[20:21], v2, v2, 1.0
	v_rcp_f32_e32 v6, v5
	v_div_scale_f32 v7, vcc, 1.0, v2, 1.0
	v_fma_f32 v8, -v5, v6, 1.0
	v_fmac_f32_e32 v6, v8, v6
	v_mul_f32_e32 v8, v7, v6
	v_fma_f32 v9, -v5, v8, v7
	v_fmac_f32_e32 v8, v9, v6
	v_fma_f32 v5, -v5, v8, v7
	v_div_fmas_f32 v5, v5, v6, v8
	v_div_fixup_f32 v5, v5, v2, 1.0
	v_add_f32_e32 v2, v3, v5
	s_nop 1
	s_waitcnt lgkmcnt(0)
	v_max_f32_dpp v6, v2, v2 quad_perm:[1,0,3,2] row_mask:0xf bank_mask:0xf
	s_nop 1
	s_waitcnt lgkmcnt(0)
	v_max_f32_dpp v6, v6, v6 quad_perm:[2,3,0,1] row_mask:0xf bank_mask:0xf
	s_nop 1
	s_waitcnt lgkmcnt(0)
	v_max_f32_dpp v8, v6, v6 row_half_mirror row_mask:0xf bank_mask:0xf
	v_cmp_eq_f32_e32 vcc, v2, v8
	s_nop 1
	v_lshrrev_b64 v[6:7], v200, vcc
	v_ffbl_b32_sdwa v6, v6 dst_sel:DWORD dst_unused:UNUSED_PAD src0_sel:BYTE_0
	v_add_u32_e32 v6, v6, v200
	v_cmp_ne_u32_e32 vcc, v230, v6
	s_nop 1
	v_cndmask_b32_e32 v6, v245, v2, vcc
	s_nop 1
	s_waitcnt lgkmcnt(0)
	v_max_f32_dpp v6, v6, v6 quad_perm:[1,0,3,2] row_mask:0xf bank_mask:0xf
	s_nop 1
	s_waitcnt lgkmcnt(0)
	v_max_f32_dpp v6, v6, v6 quad_perm:[2,3,0,1] row_mask:0xf bank_mask:0xf
	s_nop 1
	s_waitcnt lgkmcnt(0)
	v_max_f32_dpp v6, v6, v6 row_half_mirror row_mask:0xf bank_mask:0xf
	v_add_f32_e32 v6, v8, v6
	s_nop 0
	v_readlane_b32 s5, v6, 0
	v_readlane_b32 s24, v6, 8
	v_readlane_b32 s28, v6, 16
	v_cmp_eq_f32_e64 s[20:21], s5, v6
	v_cmp_gt_f32_e32 vcc, s5, v6
	v_cmp_gt_f32_e64 s[22:23], s24, v6
	v_cmp_eq_f32_e64 s[24:25], s24, v6
	s_and_b64 s[20:21], s[0:1], s[20:21]
	v_readlane_b32 s34, v6, 24
	v_cmp_gt_f32_e64 s[26:27], s28, v6
	v_cmp_eq_f32_e64 s[28:29], s28, v6
	s_and_b64 s[24:25], s[6:7], s[24:25]
	s_or_b64 s[20:21], vcc, s[20:21]
	v_readlane_b32 s40, v6, 32
	v_cmp_gt_f32_e64 s[30:31], s34, v6
	v_cmp_eq_f32_e64 s[34:35], s34, v6
	s_and_b64 s[28:29], s[8:9], s[28:29]
	v_cndmask_b32_e64 v7, 0, 1, s[20:21]
	s_or_b64 s[20:21], s[22:23], s[24:25]
	v_cmp_gt_f32_e64 s[36:37], s40, v6
	v_cmp_eq_f32_e64 s[40:41], s40, v6
	s_and_b64 s[34:35], s[10:11], s[34:35]
	v_cndmask_b32_e64 v8, 0, 1, s[20:21]
	s_or_b64 s[20:21], s[26:27], s[28:29]
	s_and_b64 s[40:41], s[12:13], s[40:41]
	v_cndmask_b32_e64 v9, 0, 1, s[20:21]
	s_or_b64 s[20:21], s[30:31], s[34:35]
	v_readlane_b32 s54, v6, 40
	v_cndmask_b32_e64 v10, 0, 1, s[20:21]
	s_or_b64 s[20:21], s[36:37], s[40:41]
	v_cndmask_b32_e64 v11, 0, 1, s[20:21]
	v_cmp_eq_f32_e64 s[20:21], s54, v6
	v_cmp_gt_f32_e32 vcc, s54, v6
	s_and_b64 s[20:21], s[14:15], s[20:21]
	s_or_b64 s[20:21], vcc, s[20:21]
	v_readlane_b32 s5, v6, 48
	v_cndmask_b32_e64 v12, 0, 1, s[20:21]
	s_nop 0
	v_cmp_eq_f32_e64 s[20:21], s5, v6
	v_cmp_gt_f32_e32 vcc, s5, v6
	s_and_b64 s[20:21], s[16:17], s[20:21]
	v_readlane_b32 s5, v6, 56
	s_or_b64 s[20:21], vcc, s[20:21]
	v_cndmask_b32_e64 v13, 0, 1, s[20:21]
	v_cmp_gt_f32_e32 vcc, s5, v6
	s_nop 1
	v_cndmask_b32_e64 v6, 0, 1, vcc
	v_add_u32_e32 v6, v8, v6
	v_add3_u32 v6, v6, v7, v9
	v_add3_u32 v6, v6, v10, v11
	v_add3_u32 v6, v6, v12, v13
	v_cmp_gt_u32_e32 vcc, 4, v6
	s_nop 1
	v_cndmask_b32_e32 v6, v245, v2, vcc
	v_mov_b32_e32 v2, 0
	v_ashrrev_i32_e32 v9, 31, v6
	v_sub_u32_e32 v8, 63, v230
	v_and_b32_e32 v9, 0x7fffffff, v9
	v_xor_b32_e32 v9, v6, v9
	s_nop 0
	v_readlane_b32 s23, v9, 0
	s_movk_i32 s22, 63
	v_readlane_b32 s21, v9, 1
	s_movk_i32 s20, 62
	v_cmp_gt_i64_e32 vcc, s[22:23], v[8:9]
	v_readlane_b32 s23, v9, 2
	s_movk_i32 s22, 61
	v_addc_co_u32_e32 v2, vcc, 0, v2, vcc
	v_cmp_gt_i64_e32 vcc, s[20:21], v[8:9]
	v_readlane_b32 s21, v9, 3
	s_movk_i32 s20, 60
	v_addc_co_u32_e32 v2, vcc, 0, v2, vcc
	v_cmp_gt_i64_e32 vcc, s[22:23], v[8:9]
	v_readlane_b32 s23, v9, 4
	s_movk_i32 s22, 59
	v_addc_co_u32_e32 v2, vcc, 0, v2, vcc
	v_cmp_gt_i64_e32 vcc, s[20:21], v[8:9]
	v_readlane_b32 s21, v9, 5
	s_movk_i32 s20, 58
	v_addc_co_u32_e32 v2, vcc, 0, v2, vcc
	v_cmp_gt_i64_e32 vcc, s[22:23], v[8:9]
	v_readlane_b32 s23, v9, 6
	s_movk_i32 s22, 57
	v_addc_co_u32_e32 v2, vcc, 0, v2, vcc
	v_cmp_gt_i64_e32 vcc, s[20:21], v[8:9]
	v_readlane_b32 s21, v9, 7
	s_movk_i32 s20, 56
	v_addc_co_u32_e32 v2, vcc, 0, v2, vcc
	v_cmp_gt_i64_e32 vcc, s[22:23], v[8:9]
	v_readlane_b32 s23, v9, 8
	s_movk_i32 s22, 55
	v_addc_co_u32_e32 v2, vcc, 0, v2, vcc
	v_cmp_gt_i64_e32 vcc, s[20:21], v[8:9]
	v_readlane_b32 s21, v9, 9
	s_movk_i32 s20, 54
	v_addc_co_u32_e32 v2, vcc, 0, v2, vcc
	v_cmp_gt_i64_e32 vcc, s[22:23], v[8:9]
	v_readlane_b32 s23, v9, 10
	s_movk_i32 s22, 53
	v_addc_co_u32_e32 v2, vcc, 0, v2, vcc
	v_cmp_gt_i64_e32 vcc, s[20:21], v[8:9]
	v_readlane_b32 s21, v9, 11
	s_movk_i32 s20, 52
	v_addc_co_u32_e32 v2, vcc, 0, v2, vcc
	v_cmp_gt_i64_e32 vcc, s[22:23], v[8:9]
	v_readlane_b32 s23, v9, 12
	s_movk_i32 s22, 51
	v_addc_co_u32_e32 v2, vcc, 0, v2, vcc
	v_cmp_gt_i64_e32 vcc, s[20:21], v[8:9]
	v_readlane_b32 s21, v9, 13
	s_movk_i32 s20, 50
	v_addc_co_u32_e32 v2, vcc, 0, v2, vcc
	v_cmp_gt_i64_e32 vcc, s[22:23], v[8:9]
	v_readlane_b32 s23, v9, 14
	s_movk_i32 s22, 49
	v_addc_co_u32_e32 v2, vcc, 0, v2, vcc
	v_cmp_gt_i64_e32 vcc, s[20:21], v[8:9]
	v_readlane_b32 s21, v9, 15
	s_movk_i32 s20, 48
	v_addc_co_u32_e32 v2, vcc, 0, v2, vcc
	v_cmp_gt_i64_e32 vcc, s[22:23], v[8:9]
	v_readlane_b32 s23, v9, 16
	s_movk_i32 s22, 47
	v_addc_co_u32_e32 v2, vcc, 0, v2, vcc
	v_cmp_gt_i64_e32 vcc, s[20:21], v[8:9]
	v_readlane_b32 s21, v9, 17
	s_movk_i32 s20, 46
	v_addc_co_u32_e32 v2, vcc, 0, v2, vcc
	v_cmp_gt_i64_e32 vcc, s[22:23], v[8:9]
	v_readlane_b32 s23, v9, 18
; __device__ __forceinline__ void phase_nrr(const Frame& F, const Args& a, int l, const bf16_t* XA, const float* g, const float* modl, unsigned char* XN8) {
;     ...
;             int rank = 0;
; #pragma unroll 8
;             for (int e2 = 0; e2 < 64; ++e2) { const float v = __int_as_float(__builtin_amdgcn_readlane(__float_as_int(val), e2)); rank += (v > val || (v == val && e2 < lane)) ? 1 : 0; }
;             const bool sel = rank < TOPK;
;             const float ssum = wave_sum(sel ? sc : 0.f);
	s_movk_i32 s22, 45
	v_addc_co_u32_e32 v2, vcc, 0, v2, vcc
	v_cmp_gt_i64_e32 vcc, s[20:21], v[8:9]
	v_readlane_b32 s21, v9, 19
	s_movk_i32 s20, 44
	v_addc_co_u32_e32 v2, vcc, 0, v2, vcc
	v_cmp_gt_i64_e32 vcc, s[22:23], v[8:9]
	v_readlane_b32 s23, v9, 20
	s_movk_i32 s22, 43
	v_addc_co_u32_e32 v2, vcc, 0, v2, vcc
	v_cmp_gt_i64_e32 vcc, s[20:21], v[8:9]
	v_readlane_b32 s21, v9, 21
	s_movk_i32 s20, 42
	v_addc_co_u32_e32 v2, vcc, 0, v2, vcc
	v_cmp_gt_i64_e32 vcc, s[22:23], v[8:9]
	v_readlane_b32 s23, v9, 22
	s_movk_i32 s22, 41
	v_addc_co_u32_e32 v2, vcc, 0, v2, vcc
	v_cmp_gt_i64_e32 vcc, s[20:21], v[8:9]
	v_readlane_b32 s21, v9, 23
	s_movk_i32 s20, 40
	v_addc_co_u32_e32 v2, vcc, 0, v2, vcc
	v_cmp_gt_i64_e32 vcc, s[22:23], v[8:9]
	v_readlane_b32 s23, v9, 24
	s_movk_i32 s22, 39
	v_addc_co_u32_e32 v2, vcc, 0, v2, vcc
	v_cmp_gt_i64_e32 vcc, s[20:21], v[8:9]
	v_readlane_b32 s21, v9, 25
	s_movk_i32 s20, 38
	v_addc_co_u32_e32 v2, vcc, 0, v2, vcc
	v_cmp_gt_i64_e32 vcc, s[22:23], v[8:9]
	v_readlane_b32 s23, v9, 26
	s_movk_i32 s22, 37
	v_addc_co_u32_e32 v2, vcc, 0, v2, vcc
	v_cmp_gt_i64_e32 vcc, s[20:21], v[8:9]
	v_readlane_b32 s21, v9, 27
	s_movk_i32 s20, 36
	v_addc_co_u32_e32 v2, vcc, 0, v2, vcc
	v_cmp_gt_i64_e32 vcc, s[22:23], v[8:9]
	v_readlane_b32 s23, v9, 28
	s_movk_i32 s22, 35
	v_addc_co_u32_e32 v2, vcc, 0, v2, vcc
	v_cmp_gt_i64_e32 vcc, s[20:21], v[8:9]
	v_readlane_b32 s21, v9, 29
	s_movk_i32 s20, 34
	v_addc_co_u32_e32 v2, vcc, 0, v2, vcc
	v_cmp_gt_i64_e32 vcc, s[22:23], v[8:9]
	v_readlane_b32 s23, v9, 30
	s_movk_i32 s22, 33
	v_addc_co_u32_e32 v2, vcc, 0, v2, vcc
	v_cmp_gt_i64_e32 vcc, s[20:21], v[8:9]
	v_readlane_b32 s21, v9, 31
	s_movk_i32 s20, 32
	v_addc_co_u32_e32 v2, vcc, 0, v2, vcc
	v_cmp_gt_i64_e32 vcc, s[22:23], v[8:9]
	v_readlane_b32 s23, v9, 32
	s_movk_i32 s22, 31
	v_addc_co_u32_e32 v2, vcc, 0, v2, vcc
	v_cmp_gt_i64_e32 vcc, s[20:21], v[8:9]
	v_readlane_b32 s21, v9, 33
	s_movk_i32 s20, 30
	v_addc_co_u32_e32 v2, vcc, 0, v2, vcc
	v_cmp_gt_i64_e32 vcc, s[22:23], v[8:9]
	v_readlane_b32 s23, v9, 34
	s_movk_i32 s22, 29
	v_addc_co_u32_e32 v2, vcc, 0, v2, vcc
	v_cmp_gt_i64_e32 vcc, s[20:21], v[8:9]
	v_readlane_b32 s21, v9, 35
	s_movk_i32 s20, 28
	v_addc_co_u32_e32 v2, vcc, 0, v2, vcc
	v_cmp_gt_i64_e32 vcc, s[22:23], v[8:9]
	v_readlane_b32 s23, v9, 36
	s_movk_i32 s22, 27
	v_addc_co_u32_e32 v2, vcc, 0, v2, vcc
	v_cmp_gt_i64_e32 vcc, s[20:21], v[8:9]
	v_readlane_b32 s21, v9, 37
	s_movk_i32 s20, 26
	v_addc_co_u32_e32 v2, vcc, 0, v2, vcc
	v_cmp_gt_i64_e32 vcc, s[22:23], v[8:9]
	v_readlane_b32 s23, v9, 38
	s_movk_i32 s22, 25
	v_addc_co_u32_e32 v2, vcc, 0, v2, vcc
	v_cmp_gt_i64_e32 vcc, s[20:21], v[8:9]
	v_readlane_b32 s21, v9, 39
	s_movk_i32 s20, 24
	v_addc_co_u32_e32 v2, vcc, 0, v2, vcc
	v_cmp_gt_i64_e32 vcc, s[22:23], v[8:9]
	v_readlane_b32 s23, v9, 40
	s_movk_i32 s22, 23
	v_addc_co_u32_e32 v2, vcc, 0, v2, vcc
	v_cmp_gt_i64_e32 vcc, s[20:21], v[8:9]
	v_readlane_b32 s21, v9, 41
	s_movk_i32 s20, 22
	v_addc_co_u32_e32 v2, vcc, 0, v2, vcc
	v_cmp_gt_i64_e32 vcc, s[22:23], v[8:9]
	v_readlane_b32 s23, v9, 42
	s_movk_i32 s22, 21
	v_addc_co_u32_e32 v2, vcc, 0, v2, vcc
	v_cmp_gt_i64_e32 vcc, s[20:21], v[8:9]
	v_readlane_b32 s21, v9, 43
	s_movk_i32 s20, 20
	v_addc_co_u32_e32 v2, vcc, 0, v2, vcc
	v_cmp_gt_i64_e32 vcc, s[22:23], v[8:9]
	v_readlane_b32 s23, v9, 44
	s_movk_i32 s22, 19
	v_addc_co_u32_e32 v2, vcc, 0, v2, vcc
	v_cmp_gt_i64_e32 vcc, s[20:21], v[8:9]
	v_readlane_b32 s21, v9, 45
	s_movk_i32 s20, 18
	v_addc_co_u32_e32 v2, vcc, 0, v2, vcc
	v_cmp_gt_i64_e32 vcc, s[22:23], v[8:9]
	v_readlane_b32 s23, v9, 46
	s_movk_i32 s22, 17
	v_addc_co_u32_e32 v2, vcc, 0, v2, vcc
	v_cmp_gt_i64_e32 vcc, s[20:21], v[8:9]
	v_readlane_b32 s21, v9, 47
	s_movk_i32 s20, 16
	v_addc_co_u32_e32 v2, vcc, 0, v2, vcc
	v_cmp_gt_i64_e32 vcc, s[22:23], v[8:9]
	v_readlane_b32 s23, v9, 48
	s_movk_i32 s22, 15
	v_addc_co_u32_e32 v2, vcc, 0, v2, vcc
	v_cmp_gt_i64_e32 vcc, s[20:21], v[8:9]
	v_readlane_b32 s21, v9, 49
	s_movk_i32 s20, 14
	v_addc_co_u32_e32 v2, vcc, 0, v2, vcc
	v_cmp_gt_i64_e32 vcc, s[22:23], v[8:9]
	v_readlane_b32 s23, v9, 50
	s_movk_i32 s22, 13
	v_addc_co_u32_e32 v2, vcc, 0, v2, vcc
	v_cmp_gt_i64_e32 vcc, s[20:21], v[8:9]
	v_readlane_b32 s21, v9, 51
	s_movk_i32 s20, 12
	v_addc_co_u32_e32 v2, vcc, 0, v2, vcc
	v_cmp_gt_i64_e32 vcc, s[22:23], v[8:9]
	v_readlane_b32 s23, v9, 52
	s_movk_i32 s22, 11
	v_addc_co_u32_e32 v2, vcc, 0, v2, vcc
	v_cmp_gt_i64_e32 vcc, s[20:21], v[8:9]
	v_readlane_b32 s21, v9, 53
	s_movk_i32 s20, 10
	v_addc_co_u32_e32 v2, vcc, 0, v2, vcc
	v_cmp_gt_i64_e32 vcc, s[22:23], v[8:9]
	v_readlane_b32 s23, v9, 54
	s_movk_i32 s22, 9
	v_addc_co_u32_e32 v2, vcc, 0, v2, vcc
	v_cmp_gt_i64_e32 vcc, s[20:21], v[8:9]
	v_readlane_b32 s21, v9, 55
	s_movk_i32 s20, 8
	v_addc_co_u32_e32 v2, vcc, 0, v2, vcc
	v_cmp_gt_i64_e32 vcc, s[22:23], v[8:9]
	v_readlane_b32 s23, v9, 56
	s_movk_i32 s22, 7
	v_addc_co_u32_e32 v2, vcc, 0, v2, vcc
	v_cmp_gt_i64_e32 vcc, s[20:21], v[8:9]
	v_readlane_b32 s21, v9, 57
	s_movk_i32 s20, 6
	v_addc_co_u32_e32 v2, vcc, 0, v2, vcc
	v_cmp_gt_i64_e32 vcc, s[22:23], v[8:9]
	v_readlane_b32 s23, v9, 58
	s_movk_i32 s22, 5
	v_addc_co_u32_e32 v2, vcc, 0, v2, vcc
	v_cmp_gt_i64_e32 vcc, s[20:21], v[8:9]
	v_readlane_b32 s21, v9, 59
	s_movk_i32 s20, 4
	v_addc_co_u32_e32 v2, vcc, 0, v2, vcc
	v_cmp_gt_i64_e32 vcc, s[22:23], v[8:9]
	v_readlane_b32 s23, v9, 60
	s_movk_i32 s22, 3
	v_addc_co_u32_e32 v2, vcc, 0, v2, vcc
	v_cmp_gt_i64_e32 vcc, s[20:21], v[8:9]
	v_readlane_b32 s21, v9, 61
	s_movk_i32 s20, 2
	v_addc_co_u32_e32 v2, vcc, 0, v2, vcc
	v_cmp_gt_i64_e32 vcc, s[22:23], v[8:9]
	v_readlane_b32 s23, v9, 62
	s_movk_i32 s22, 1
	v_addc_co_u32_e32 v2, vcc, 0, v2, vcc
	v_cmp_gt_i64_e32 vcc, s[20:21], v[8:9]
	v_readlane_b32 s21, v9, 63
	s_movk_i32 s20, 0
	v_addc_co_u32_e32 v2, vcc, 0, v2, vcc
	v_cmp_gt_i64_e32 vcc, s[22:23], v[8:9]
	s_nop 1
	v_addc_co_u32_e32 v2, vcc, 0, v2, vcc
	v_cmp_gt_i64_e32 vcc, s[20:21], v[8:9]
	s_nop 1
	v_addc_co_u32_e32 v2, vcc, 0, v2, vcc
	v_cmp_gt_u32_e32 vcc, 6, v2
	s_nop 1
	v_cndmask_b32_e32 v6, 0, v5, vcc
	s_nop 1
	v_add_f32_dpp v6, v6, v6 quad_perm:[1,0,3,2] row_mask:0xf bank_mask:0xf
	s_nop 1
	v_add_f32_dpp v6, v6, v6 quad_perm:[2,3,0,1] row_mask:0xf bank_mask:0xf
	s_nop 1
	v_add_f32_dpp v6, v6, v6 row_half_mirror row_mask:0xf bank_mask:0xf
	s_nop 1
	v_add_f32_dpp v6, v6, v6 row_mirror row_mask:0xf bank_mask:0xf
	s_nop 0
	ds_bpermute_b32 v7, v222, v6
	s_waitcnt lgkmcnt(0)
	v_add_f32_e32 v6, v6, v7
	v_mov_b32_e32 v7, v6
	s_nop 1
	v_permlane32_swap_b32_e32 v7, v6
	s_and_saveexec_b64 s[20:21], vcc
	s_cbranch_execz .LBB0_1324
; __device__ __forceinline__ void phase_nrr(const Frame& F, const Args& a, int l, const bf16_t* XA, const float* g, const float* modl, unsigned char* XN8) {
;     ...
;             const float lg = Pl[(w * 8 + i) * NE + lane] + Pl[(64 + w * 8 + i) * NE + lane]; const float sc = 1.f / (1.f + __expf(-lg)); const float bb = sc + bias;
;             float m1 = bb; m1 = fmaxf(m1, __shfl_xor(m1, 1)); m1 = fmaxf(m1, __shfl_xor(m1, 2)); m1 = fmaxf(m1, __shfl_xor(m1, 4));
;             const unsigned long long eq = __ballot(bb == m1); const int gbase = lane & ~7; const unsigned grpmask = (unsigned)((eq >> gbase) & 0xffull);
;             const int first = gbase + __builtin_ctz(grpmask);
;             float m2 = (lane == first) ? -INFINITY : bb; m2 = fmaxf(m2, __shfl_xor(m2, 1)); m2 = fmaxf(m2, __shfl_xor(m2, 2)); m2 = fmaxf(m2, __shfl_xor(m2, 4));
;             const float gsum = m1 + m2; const int gq = lane >> 3;
;             int grank = 0;
; #pragma unroll
;             for (int g2 = 0; g2 < 8; ++g2) { const float v = __int_as_float(__builtin_amdgcn_readlane(__float_as_int(gsum), g2 * 8)); grank += (v > gsum || (v == gsum && g2 < gq)) ? 1 : 0; }
;             const bool keep = grank < 4; const float val = keep ? bb : -INFINITY;
;             int rank = 0;
; #pragma unroll 8
;             for (int e2 = 0; e2 < 64; ++e2) { const float v = __int_as_float(__builtin_amdgcn_readlane(__float_as_int(val), e2)); rank += (v > val || (v == val && e2 < lane)) ? 1 : 0; }
;     ...
;             if (sel) { const int p = atomicAdd((int*)(hist + lane), 1); top_e[t * TOPK + rank] = lane; gate[t * TOPK + rank] = sc / ssum * 2.5f; lpos[t * TOPK + rank] = p; }
	s_waitcnt lgkmcnt(0)
	v_add_f32_e32 v10, v6, v7
	v_mad_u64_u32 v[6:7], s[4:5], s4, 6, v[2:3]
	v_div_scale_f32 v2, s[4:5], v10, v10, v5
	v_rcp_f32_e32 v12, v2
	v_ashrrev_i32_e32 v7, 31, v6
	v_lshlrev_b64 v[6:7], 2, v[6:7]
	v_lshl_add_u64 v[8:9], s[42:43], 0, v[6:7]
	ds_add_rtn_u32 v11, v227, v243
	global_store_dword v[8:9], v230, off
	v_fma_f32 v8, -v2, v12, 1.0
	v_fmac_f32_e32 v12, v8, v12
	v_div_scale_f32 v8, vcc, v5, v10, v5
	v_mul_f32_e32 v9, v8, v12
	v_fma_f32 v13, -v2, v9, v8
	v_fmac_f32_e32 v9, v13, v12
	v_fma_f32 v2, -v2, v9, v8
	v_div_fmas_f32 v2, v2, v12, v9
	v_div_fixup_f32 v2, v2, v10, v5
	v_mul_f32_e32 v2, 0x40200000, v2
	v_lshl_add_u64 v[8:9], s[44:45], 0, v[6:7]
	v_lshl_add_u64 v[6:7], s[46:47], 0, v[6:7]
	global_store_dword v[8:9], v2, off
	s_waitcnt lgkmcnt(0)
	global_store_dword v[6:7], v11, off
.LBB0_1324:
	s_or_b64 exec, exec, s[20:21]
	v_add_u32_e32 v2, s79, v226
	ds_read_b32 v2, v2
	ds_read_b32 v5, v4 offset:17408
	s_mov_b32 s3, 0
	s_waitcnt lgkmcnt(0)
	v_add_f32_e32 v2, v2, v5
	v_mul_f32_e32 v2, 0xbfb8aa3b, v2
	v_exp_f32_e32 v2, v2
	s_nop 0
	v_add_f32_e32 v2, 1.0, v2
	v_div_scale_f32 v5, s[4:5], v2, v2, 1.0
	v_rcp_f32_e32 v6, v5
	v_div_scale_f32 v7, vcc, 1.0, v2, 1.0
	v_fma_f32 v8, -v5, v6, 1.0
	v_fmac_f32_e32 v6, v8, v6
	v_mul_f32_e32 v8, v7, v6
	v_fma_f32 v9, -v5, v8, v7
	v_fmac_f32_e32 v8, v9, v6
	v_fma_f32 v5, -v5, v8, v7
	v_div_fmas_f32 v5, v5, v6, v8
	v_div_fixup_f32 v2, v5, v2, 1.0
	v_add_f32_e32 v5, v3, v2
	s_nop 1
	s_waitcnt lgkmcnt(0)
	v_max_f32_dpp v6, v5, v5 quad_perm:[1,0,3,2] row_mask:0xf bank_mask:0xf
	s_nop 1
	s_waitcnt lgkmcnt(0)
	v_max_f32_dpp v6, v6, v6 quad_perm:[2,3,0,1] row_mask:0xf bank_mask:0xf
	s_nop 1
	s_waitcnt lgkmcnt(0)
	v_max_f32_dpp v8, v6, v6 row_half_mirror row_mask:0xf bank_mask:0xf
	v_cmp_eq_f32_e32 vcc, v5, v8
	s_nop 1
	v_lshrrev_b64 v[6:7], v200, vcc
	v_ffbl_b32_sdwa v6, v6 dst_sel:DWORD dst_unused:UNUSED_PAD src0_sel:BYTE_0
	v_add_u32_e32 v6, v6, v200
	v_cmp_ne_u32_e32 vcc, v230, v6
	s_nop 1
	v_cndmask_b32_e32 v6, v245, v5, vcc
	s_nop 1
	s_waitcnt lgkmcnt(0)
	v_max_f32_dpp v6, v6, v6 quad_perm:[1,0,3,2] row_mask:0xf bank_mask:0xf
	s_nop 1
	s_waitcnt lgkmcnt(0)
	v_max_f32_dpp v6, v6, v6 quad_perm:[2,3,0,1] row_mask:0xf bank_mask:0xf
	s_nop 1
	s_waitcnt lgkmcnt(0)
	v_max_f32_dpp v6, v6, v6 row_half_mirror row_mask:0xf bank_mask:0xf
	v_add_f32_e32 v6, v8, v6
	s_nop 0
	v_readlane_b32 s4, v6, 0
	v_readlane_b32 s5, v6, 8
	v_readlane_b32 s28, v6, 16
	v_cmp_eq_f32_e64 s[20:21], s4, v6
	v_cmp_gt_f32_e32 vcc, s4, v6
	v_cmp_gt_f32_e64 s[22:23], s5, v6
	v_cmp_eq_f32_e64 s[24:25], s5, v6
	s_and_b64 s[4:5], s[0:1], s[20:21]
	v_readlane_b32 s34, v6, 24
	v_cmp_gt_f32_e64 s[26:27], s28, v6
	v_cmp_eq_f32_e64 s[28:29], s28, v6
	s_and_b64 s[20:21], s[6:7], s[24:25]
	s_or_b64 s[4:5], vcc, s[4:5]
	v_readlane_b32 s40, v6, 32
	v_cmp_gt_f32_e64 s[30:31], s34, v6
	v_cmp_eq_f32_e64 s[34:35], s34, v6
	s_and_b64 s[24:25], s[8:9], s[28:29]
	v_cndmask_b32_e64 v7, 0, 1, s[4:5]
	s_or_b64 s[4:5], s[22:23], s[20:21]
	v_cmp_gt_f32_e64 s[36:37], s40, v6
	v_cmp_eq_f32_e64 s[40:41], s40, v6
	s_and_b64 s[28:29], s[10:11], s[34:35]
	v_cndmask_b32_e64 v8, 0, 1, s[4:5]
	s_or_b64 s[4:5], s[26:27], s[24:25]
	v_readlane_b32 s54, v6, 40
	s_and_b64 s[34:35], s[12:13], s[40:41]
	v_cndmask_b32_e64 v9, 0, 1, s[4:5]
	s_or_b64 s[4:5], s[30:31], s[28:29]
	v_cndmask_b32_e64 v10, 0, 1, s[4:5]
	s_or_b64 s[4:5], s[36:37], s[34:35]
	v_cmp_eq_f32_e64 s[20:21], s54, v6
	v_cndmask_b32_e64 v11, 0, 1, s[4:5]
	v_cmp_gt_f32_e32 vcc, s54, v6
	s_and_b64 s[4:5], s[14:15], s[20:21]
	s_or_b64 s[4:5], vcc, s[4:5]
	v_cndmask_b32_e64 v12, 0, 1, s[4:5]
	v_readlane_b32 s4, v6, 48
	s_nop 1
	v_cmp_eq_f32_e64 s[20:21], s4, v6
	v_cmp_gt_f32_e32 vcc, s4, v6
	s_and_b64 s[4:5], s[16:17], s[20:21]
	s_or_b64 s[4:5], vcc, s[4:5]
	v_cndmask_b32_e64 v13, 0, 1, s[4:5]
	v_readlane_b32 s4, v6, 56
	s_nop 1
	v_cmp_gt_f32_e32 vcc, s4, v6
	s_nop 1
	v_cndmask_b32_e64 v6, 0, 1, vcc
	v_add_u32_e32 v6, v8, v6
	v_add3_u32 v6, v6, v7, v9
	v_add3_u32 v6, v6, v10, v11
	v_add3_u32 v6, v6, v12, v13
	v_cmp_gt_u32_e32 vcc, 4, v6
	v_mov_b32_e32 v6, 0
	s_nop 0
	v_cndmask_b32_e32 v5, v245, v5, vcc
	v_ashrrev_i32_e32 v9, 31, v5
	v_sub_u32_e32 v8, 63, v230
	v_and_b32_e32 v9, 0x7fffffff, v9
	v_xor_b32_e32 v9, v5, v9
	s_nop 0
	v_readlane_b32 s23, v9, 0
	s_movk_i32 s22, 63
	v_readlane_b32 s21, v9, 1
	s_movk_i32 s20, 62
	v_cmp_gt_i64_e32 vcc, s[22:23], v[8:9]
	v_readlane_b32 s23, v9, 2
	s_movk_i32 s22, 61
	v_addc_co_u32_e32 v6, vcc, 0, v6, vcc
	v_cmp_gt_i64_e32 vcc, s[20:21], v[8:9]
	v_readlane_b32 s21, v9, 3
	s_movk_i32 s20, 60
	v_addc_co_u32_e32 v6, vcc, 0, v6, vcc
	v_cmp_gt_i64_e32 vcc, s[22:23], v[8:9]
	v_readlane_b32 s23, v9, 4
	s_movk_i32 s22, 59
	v_addc_co_u32_e32 v6, vcc, 0, v6, vcc
	v_cmp_gt_i64_e32 vcc, s[20:21], v[8:9]
	v_readlane_b32 s21, v9, 5
	s_movk_i32 s20, 58
	v_addc_co_u32_e32 v6, vcc, 0, v6, vcc
	v_cmp_gt_i64_e32 vcc, s[22:23], v[8:9]
	v_readlane_b32 s23, v9, 6
	s_movk_i32 s22, 57
	v_addc_co_u32_e32 v6, vcc, 0, v6, vcc
	v_cmp_gt_i64_e32 vcc, s[20:21], v[8:9]
	v_readlane_b32 s21, v9, 7
	s_movk_i32 s20, 56
	v_addc_co_u32_e32 v6, vcc, 0, v6, vcc
	v_cmp_gt_i64_e32 vcc, s[22:23], v[8:9]
	v_readlane_b32 s23, v9, 8
	s_movk_i32 s22, 55
	v_addc_co_u32_e32 v6, vcc, 0, v6, vcc
	v_cmp_gt_i64_e32 vcc, s[20:21], v[8:9]
	v_readlane_b32 s21, v9, 9
	s_movk_i32 s20, 54
	v_addc_co_u32_e32 v6, vcc, 0, v6, vcc
	v_cmp_gt_i64_e32 vcc, s[22:23], v[8:9]
	v_readlane_b32 s23, v9, 10
	s_movk_i32 s22, 53
	v_addc_co_u32_e32 v6, vcc, 0, v6, vcc
	v_cmp_gt_i64_e32 vcc, s[20:21], v[8:9]
	v_readlane_b32 s21, v9, 11
	s_movk_i32 s20, 52
	v_addc_co_u32_e32 v6, vcc, 0, v6, vcc
	v_cmp_gt_i64_e32 vcc, s[22:23], v[8:9]
; __device__ __forceinline__ void phase_nrr(const Frame& F, const Args& a, int l, const bf16_t* XA, const float* g, const float* modl, unsigned char* XN8) {
;     ...
;             int rank = 0;
; #pragma unroll 8
;             for (int e2 = 0; e2 < 64; ++e2) { const float v = __int_as_float(__builtin_amdgcn_readlane(__float_as_int(val), e2)); rank += (v > val || (v == val && e2 < lane)) ? 1 : 0; }
	v_readlane_b32 s23, v9, 12
	s_movk_i32 s22, 51
	v_addc_co_u32_e32 v6, vcc, 0, v6, vcc
	v_cmp_gt_i64_e32 vcc, s[20:21], v[8:9]
	v_readlane_b32 s21, v9, 13
	s_movk_i32 s20, 50
	v_addc_co_u32_e32 v6, vcc, 0, v6, vcc
	v_cmp_gt_i64_e32 vcc, s[22:23], v[8:9]
	v_readlane_b32 s23, v9, 14
	s_movk_i32 s22, 49
	v_addc_co_u32_e32 v6, vcc, 0, v6, vcc
	v_cmp_gt_i64_e32 vcc, s[20:21], v[8:9]
	v_readlane_b32 s21, v9, 15
	s_movk_i32 s20, 48
	v_addc_co_u32_e32 v6, vcc, 0, v6, vcc
	v_cmp_gt_i64_e32 vcc, s[22:23], v[8:9]
	v_readlane_b32 s23, v9, 16
	s_movk_i32 s22, 47
	v_addc_co_u32_e32 v6, vcc, 0, v6, vcc
	v_cmp_gt_i64_e32 vcc, s[20:21], v[8:9]
	v_readlane_b32 s21, v9, 17
	s_movk_i32 s20, 46
	v_addc_co_u32_e32 v6, vcc, 0, v6, vcc
	v_cmp_gt_i64_e32 vcc, s[22:23], v[8:9]
	v_readlane_b32 s23, v9, 18
	s_movk_i32 s22, 45
	v_addc_co_u32_e32 v6, vcc, 0, v6, vcc
	v_cmp_gt_i64_e32 vcc, s[20:21], v[8:9]
	v_readlane_b32 s21, v9, 19
	s_movk_i32 s20, 44
	v_addc_co_u32_e32 v6, vcc, 0, v6, vcc
	v_cmp_gt_i64_e32 vcc, s[22:23], v[8:9]
	v_readlane_b32 s23, v9, 20
	s_movk_i32 s22, 43
	v_addc_co_u32_e32 v6, vcc, 0, v6, vcc
	v_cmp_gt_i64_e32 vcc, s[20:21], v[8:9]
	v_readlane_b32 s21, v9, 21
	s_movk_i32 s20, 42
	v_addc_co_u32_e32 v6, vcc, 0, v6, vcc
	v_cmp_gt_i64_e32 vcc, s[22:23], v[8:9]
	v_readlane_b32 s23, v9, 22
	s_movk_i32 s22, 41
	v_addc_co_u32_e32 v6, vcc, 0, v6, vcc
	v_cmp_gt_i64_e32 vcc, s[20:21], v[8:9]
	v_readlane_b32 s21, v9, 23
	s_movk_i32 s20, 40
	v_addc_co_u32_e32 v6, vcc, 0, v6, vcc
	v_cmp_gt_i64_e32 vcc, s[22:23], v[8:9]
	v_readlane_b32 s23, v9, 24
	s_movk_i32 s22, 39
	v_addc_co_u32_e32 v6, vcc, 0, v6, vcc
	v_cmp_gt_i64_e32 vcc, s[20:21], v[8:9]
	v_readlane_b32 s21, v9, 25
	s_movk_i32 s20, 38
	v_addc_co_u32_e32 v6, vcc, 0, v6, vcc
	v_cmp_gt_i64_e32 vcc, s[22:23], v[8:9]
	v_readlane_b32 s23, v9, 26
	s_movk_i32 s22, 37
	v_addc_co_u32_e32 v6, vcc, 0, v6, vcc
	v_cmp_gt_i64_e32 vcc, s[20:21], v[8:9]
	v_readlane_b32 s21, v9, 27
	s_movk_i32 s20, 36
	v_addc_co_u32_e32 v6, vcc, 0, v6, vcc
	v_cmp_gt_i64_e32 vcc, s[22:23], v[8:9]
	v_readlane_b32 s23, v9, 28
	s_movk_i32 s22, 35
	v_addc_co_u32_e32 v6, vcc, 0, v6, vcc
	v_cmp_gt_i64_e32 vcc, s[20:21], v[8:9]
	v_readlane_b32 s21, v9, 29
	s_movk_i32 s20, 34
	v_addc_co_u32_e32 v6, vcc, 0, v6, vcc
	v_cmp_gt_i64_e32 vcc, s[22:23], v[8:9]
	v_readlane_b32 s23, v9, 30
	s_movk_i32 s22, 33
	v_addc_co_u32_e32 v6, vcc, 0, v6, vcc
	v_cmp_gt_i64_e32 vcc, s[20:21], v[8:9]
	v_readlane_b32 s21, v9, 31
	s_movk_i32 s20, 32
	v_addc_co_u32_e32 v6, vcc, 0, v6, vcc
	v_cmp_gt_i64_e32 vcc, s[22:23], v[8:9]
	v_readlane_b32 s23, v9, 32
	s_movk_i32 s22, 31
	v_addc_co_u32_e32 v6, vcc, 0, v6, vcc
	v_cmp_gt_i64_e32 vcc, s[20:21], v[8:9]
	v_readlane_b32 s21, v9, 33
	s_movk_i32 s20, 30
	v_addc_co_u32_e32 v6, vcc, 0, v6, vcc
	v_cmp_gt_i64_e32 vcc, s[22:23], v[8:9]
	v_readlane_b32 s23, v9, 34
	s_movk_i32 s22, 29
	v_addc_co_u32_e32 v6, vcc, 0, v6, vcc
	v_cmp_gt_i64_e32 vcc, s[20:21], v[8:9]
	v_readlane_b32 s21, v9, 35
	s_movk_i32 s20, 28
	v_addc_co_u32_e32 v6, vcc, 0, v6, vcc
	v_cmp_gt_i64_e32 vcc, s[22:23], v[8:9]
	v_readlane_b32 s23, v9, 36
	s_movk_i32 s22, 27
	v_addc_co_u32_e32 v6, vcc, 0, v6, vcc
	v_cmp_gt_i64_e32 vcc, s[20:21], v[8:9]
	v_readlane_b32 s21, v9, 37
	s_movk_i32 s20, 26
	v_addc_co_u32_e32 v6, vcc, 0, v6, vcc
	v_cmp_gt_i64_e32 vcc, s[22:23], v[8:9]
	v_readlane_b32 s23, v9, 38
	s_movk_i32 s22, 25
	v_addc_co_u32_e32 v6, vcc, 0, v6, vcc
	v_cmp_gt_i64_e32 vcc, s[20:21], v[8:9]
	v_readlane_b32 s21, v9, 39
	s_movk_i32 s20, 24
	v_addc_co_u32_e32 v6, vcc, 0, v6, vcc
	v_cmp_gt_i64_e32 vcc, s[22:23], v[8:9]
	v_readlane_b32 s23, v9, 40
	s_movk_i32 s22, 23
	v_addc_co_u32_e32 v6, vcc, 0, v6, vcc
	v_cmp_gt_i64_e32 vcc, s[20:21], v[8:9]
	v_readlane_b32 s21, v9, 41
	s_movk_i32 s20, 22
	v_addc_co_u32_e32 v6, vcc, 0, v6, vcc
	v_cmp_gt_i64_e32 vcc, s[22:23], v[8:9]
	v_readlane_b32 s23, v9, 42
	s_movk_i32 s22, 21
	v_addc_co_u32_e32 v6, vcc, 0, v6, vcc
	v_cmp_gt_i64_e32 vcc, s[20:21], v[8:9]
	v_readlane_b32 s21, v9, 43
	s_movk_i32 s20, 20
	v_addc_co_u32_e32 v6, vcc, 0, v6, vcc
	v_cmp_gt_i64_e32 vcc, s[22:23], v[8:9]
	v_readlane_b32 s23, v9, 44
	s_movk_i32 s22, 19
	v_addc_co_u32_e32 v6, vcc, 0, v6, vcc
	v_cmp_gt_i64_e32 vcc, s[20:21], v[8:9]
	v_readlane_b32 s21, v9, 45
	s_movk_i32 s20, 18
	v_addc_co_u32_e32 v6, vcc, 0, v6, vcc
	v_cmp_gt_i64_e32 vcc, s[22:23], v[8:9]
	v_readlane_b32 s23, v9, 46
	s_movk_i32 s22, 17
	v_addc_co_u32_e32 v6, vcc, 0, v6, vcc
	v_cmp_gt_i64_e32 vcc, s[20:21], v[8:9]
	v_readlane_b32 s21, v9, 47
	s_movk_i32 s20, 16
	v_addc_co_u32_e32 v6, vcc, 0, v6, vcc
	v_cmp_gt_i64_e32 vcc, s[22:23], v[8:9]
	v_readlane_b32 s23, v9, 48
	s_movk_i32 s22, 15
	v_addc_co_u32_e32 v6, vcc, 0, v6, vcc
	v_cmp_gt_i64_e32 vcc, s[20:21], v[8:9]
	v_readlane_b32 s21, v9, 49
	s_movk_i32 s20, 14
	v_addc_co_u32_e32 v6, vcc, 0, v6, vcc
	v_cmp_gt_i64_e32 vcc, s[22:23], v[8:9]
	v_readlane_b32 s23, v9, 50
	s_movk_i32 s22, 13
	v_addc_co_u32_e32 v6, vcc, 0, v6, vcc
	v_cmp_gt_i64_e32 vcc, s[20:21], v[8:9]
	v_readlane_b32 s21, v9, 51
	s_movk_i32 s20, 12
	v_addc_co_u32_e32 v6, vcc, 0, v6, vcc
	v_cmp_gt_i64_e32 vcc, s[22:23], v[8:9]
	v_readlane_b32 s23, v9, 52
	s_movk_i32 s22, 11
	v_addc_co_u32_e32 v6, vcc, 0, v6, vcc
	v_cmp_gt_i64_e32 vcc, s[20:21], v[8:9]
	v_readlane_b32 s21, v9, 53
	s_movk_i32 s20, 10
	v_addc_co_u32_e32 v6, vcc, 0, v6, vcc
	v_cmp_gt_i64_e32 vcc, s[22:23], v[8:9]
	v_readlane_b32 s23, v9, 54
	s_movk_i32 s22, 9
	v_addc_co_u32_e32 v6, vcc, 0, v6, vcc
	v_cmp_gt_i64_e32 vcc, s[20:21], v[8:9]
	v_readlane_b32 s21, v9, 55
	s_movk_i32 s20, 8
	v_addc_co_u32_e32 v6, vcc, 0, v6, vcc
	v_cmp_gt_i64_e32 vcc, s[22:23], v[8:9]
	v_readlane_b32 s23, v9, 56
	s_movk_i32 s22, 7
; __device__ __forceinline__ void phase_nrr(const Frame& F, const Args& a, int l, const bf16_t* XA, const float* g, const float* modl, unsigned char* XN8) {
;     ...
;             const float lg = Pl[(w * 8 + i) * NE + lane] + Pl[(64 + w * 8 + i) * NE + lane]; const float sc = 1.f / (1.f + __expf(-lg)); const float bb = sc + bias;
;             float m1 = bb; m1 = fmaxf(m1, __shfl_xor(m1, 1)); m1 = fmaxf(m1, __shfl_xor(m1, 2)); m1 = fmaxf(m1, __shfl_xor(m1, 4));
;             const unsigned long long eq = __ballot(bb == m1); const int gbase = lane & ~7; const unsigned grpmask = (unsigned)((eq >> gbase) & 0xffull);
;             const int first = gbase + __builtin_ctz(grpmask);
;             float m2 = (lane == first) ? -INFINITY : bb; m2 = fmaxf(m2, __shfl_xor(m2, 1)); m2 = fmaxf(m2, __shfl_xor(m2, 2)); m2 = fmaxf(m2, __shfl_xor(m2, 4));
;             const float gsum = m1 + m2; const int gq = lane >> 3;
;             int grank = 0;
; #pragma unroll
;             for (int g2 = 0; g2 < 8; ++g2) { const float v = __int_as_float(__builtin_amdgcn_readlane(__float_as_int(gsum), g2 * 8)); grank += (v > gsum || (v == gsum && g2 < gq)) ? 1 : 0; }
;             const bool keep = grank < 4; const float val = keep ? bb : -INFINITY;
;             int rank = 0;
; #pragma unroll 8
;             for (int e2 = 0; e2 < 64; ++e2) { const float v = __int_as_float(__builtin_amdgcn_readlane(__float_as_int(val), e2)); rank += (v > val || (v == val && e2 < lane)) ? 1 : 0; }
;             const bool sel = rank < TOPK;
;             const float ssum = wave_sum(sel ? sc : 0.f);
;             if (sel) { const int p = atomicAdd((int*)(hist + lane), 1); top_e[t * TOPK + rank] = lane; gate[t * TOPK + rank] = sc / ssum * 2.5f; lpos[t * TOPK + rank] = p; }
	v_addc_co_u32_e32 v6, vcc, 0, v6, vcc
	v_cmp_gt_i64_e32 vcc, s[20:21], v[8:9]
	v_readlane_b32 s21, v9, 57
	s_movk_i32 s20, 6
	v_addc_co_u32_e32 v6, vcc, 0, v6, vcc
	v_cmp_gt_i64_e32 vcc, s[22:23], v[8:9]
	v_readlane_b32 s23, v9, 58
	s_movk_i32 s22, 5
	v_addc_co_u32_e32 v6, vcc, 0, v6, vcc
	v_cmp_gt_i64_e32 vcc, s[20:21], v[8:9]
	v_readlane_b32 s21, v9, 59
	s_movk_i32 s20, 4
	v_addc_co_u32_e32 v6, vcc, 0, v6, vcc
	v_cmp_gt_i64_e32 vcc, s[22:23], v[8:9]
	v_readlane_b32 s23, v9, 60
	s_movk_i32 s22, 3
	v_addc_co_u32_e32 v6, vcc, 0, v6, vcc
	v_cmp_gt_i64_e32 vcc, s[20:21], v[8:9]
	v_readlane_b32 s21, v9, 61
	s_movk_i32 s20, 2
	v_addc_co_u32_e32 v6, vcc, 0, v6, vcc
	v_cmp_gt_i64_e32 vcc, s[22:23], v[8:9]
	v_readlane_b32 s23, v9, 62
	s_movk_i32 s22, 1
	v_addc_co_u32_e32 v6, vcc, 0, v6, vcc
	v_cmp_gt_i64_e32 vcc, s[20:21], v[8:9]
	v_readlane_b32 s21, v9, 63
	s_movk_i32 s20, 0
	v_addc_co_u32_e32 v6, vcc, 0, v6, vcc
	v_cmp_gt_i64_e32 vcc, s[22:23], v[8:9]
	s_nop 1
	v_addc_co_u32_e32 v6, vcc, 0, v6, vcc
	v_cmp_gt_i64_e32 vcc, s[20:21], v[8:9]
	s_nop 1
	v_addc_co_u32_e32 v6, vcc, 0, v6, vcc
	v_cmp_gt_u32_e32 vcc, 6, v6
	s_nop 1
	v_cndmask_b32_e32 v5, 0, v2, vcc
	s_nop 1
	v_add_f32_dpp v5, v5, v5 quad_perm:[1,0,3,2] row_mask:0xf bank_mask:0xf
	s_nop 1
	v_add_f32_dpp v5, v5, v5 quad_perm:[2,3,0,1] row_mask:0xf bank_mask:0xf
	s_nop 1
	v_add_f32_dpp v5, v5, v5 row_half_mirror row_mask:0xf bank_mask:0xf
	s_nop 1
	v_add_f32_dpp v5, v5, v5 row_mirror row_mask:0xf bank_mask:0xf
	s_nop 0
	ds_bpermute_b32 v7, v222, v5
	s_waitcnt lgkmcnt(0)
	v_add_f32_e32 v5, v5, v7
	v_mov_b32_e32 v7, v5
	s_nop 1
	v_permlane32_swap_b32_e32 v7, v5
	s_and_saveexec_b64 s[4:5], vcc
	s_cbranch_execz .LBB0_1328
	s_waitcnt lgkmcnt(0)
	v_add_f32_e32 v5, v5, v7
	s_mul_i32 s2, s2, 6
	v_or_b32_e32 v6, s2, v6
	v_div_scale_f32 v11, s[2:3], v5, v5, v2
	v_rcp_f32_e32 v12, v11
	v_ashrrev_i32_e32 v7, 31, v6
	v_lshlrev_b64 v[6:7], 2, v[6:7]
	v_lshl_add_u64 v[8:9], s[42:43], 0, v[6:7]
	ds_add_rtn_u32 v10, v227, v243
	global_store_dword v[8:9], v230, off
	v_fma_f32 v8, -v11, v12, 1.0
	v_fmac_f32_e32 v12, v8, v12
	v_div_scale_f32 v8, vcc, v2, v5, v2
	v_mul_f32_e32 v9, v8, v12
	v_fma_f32 v13, -v11, v9, v8
	v_fmac_f32_e32 v9, v13, v12
	v_fma_f32 v8, -v11, v9, v8
	v_div_fmas_f32 v8, v8, v12, v9
	v_div_fixup_f32 v2, v8, v5, v2
	v_mul_f32_e32 v2, 0x40200000, v2
	v_lshl_add_u64 v[8:9], s[44:45], 0, v[6:7]
	v_lshl_add_u64 v[6:7], s[46:47], 0, v[6:7]
	global_store_dword v[8:9], v2, off
	s_waitcnt lgkmcnt(0)
	global_store_dword v[6:7], v10, off
.LBB0_1328:
	s_or_b64 exec, exec, s[4:5]
	v_add_u32_e32 v2, s80, v226
	ds_read_b32 v2, v2
	ds_read_b32 v5, v4 offset:17664
	s_waitcnt lgkmcnt(0)
	v_add_f32_e32 v2, v2, v5
	v_mul_f32_e32 v2, 0xbfb8aa3b, v2
	v_exp_f32_e32 v2, v2
	s_nop 0
	v_add_f32_e32 v2, 1.0, v2
	v_div_scale_f32 v5, s[2:3], v2, v2, 1.0
	v_rcp_f32_e32 v6, v5
	v_div_scale_f32 v7, vcc, 1.0, v2, 1.0
	s_mov_b32 s2, 0
	v_fma_f32 v8, -v5, v6, 1.0
	v_fmac_f32_e32 v6, v8, v6
	v_mul_f32_e32 v8, v7, v6
	v_fma_f32 v9, -v5, v8, v7
	v_fmac_f32_e32 v8, v9, v6
	v_fma_f32 v5, -v5, v8, v7
	v_div_fmas_f32 v5, v5, v6, v8
	v_div_fixup_f32 v2, v5, v2, 1.0
	v_add_f32_e32 v5, v3, v2
	s_nop 1
	s_waitcnt lgkmcnt(0)
	v_max_f32_dpp v6, v5, v5 quad_perm:[1,0,3,2] row_mask:0xf bank_mask:0xf
	s_nop 1
	s_waitcnt lgkmcnt(0)
	v_max_f32_dpp v6, v6, v6 quad_perm:[2,3,0,1] row_mask:0xf bank_mask:0xf
	s_nop 1
	s_waitcnt lgkmcnt(0)
	v_max_f32_dpp v8, v6, v6 row_half_mirror row_mask:0xf bank_mask:0xf
	v_cmp_eq_f32_e32 vcc, v5, v8
	s_nop 1
	v_lshrrev_b64 v[6:7], v200, vcc
	v_ffbl_b32_sdwa v6, v6 dst_sel:DWORD dst_unused:UNUSED_PAD src0_sel:BYTE_0
	v_add_u32_e32 v6, v6, v200
	v_cmp_ne_u32_e32 vcc, v230, v6
	s_nop 1
	v_cndmask_b32_e32 v6, v245, v5, vcc
	s_nop 1
	s_waitcnt lgkmcnt(0)
	v_max_f32_dpp v6, v6, v6 quad_perm:[1,0,3,2] row_mask:0xf bank_mask:0xf
	s_nop 1
	s_waitcnt lgkmcnt(0)
	v_max_f32_dpp v6, v6, v6 quad_perm:[2,3,0,1] row_mask:0xf bank_mask:0xf
	s_nop 1
	s_waitcnt lgkmcnt(0)
	v_max_f32_dpp v6, v6, v6 row_half_mirror row_mask:0xf bank_mask:0xf
	v_add_f32_e32 v6, v8, v6
	s_nop 0
	v_readlane_b32 s3, v6, 0
	v_readlane_b32 s4, v6, 8
	v_readlane_b32 s5, v6, 16
	v_cmp_eq_f32_e64 s[20:21], s3, v6
	v_cmp_gt_f32_e32 vcc, s3, v6
	v_cmp_gt_f32_e64 s[22:23], s4, v6
	v_cmp_eq_f32_e64 s[24:25], s4, v6
	v_cmp_gt_f32_e64 s[26:27], s5, v6
	v_cmp_eq_f32_e64 s[28:29], s5, v6
	s_and_b64 s[4:5], s[0:1], s[20:21]
	v_readlane_b32 s34, v6, 24
	s_and_b64 s[20:21], s[6:7], s[24:25]
	s_or_b64 s[4:5], vcc, s[4:5]
	v_readlane_b32 s40, v6, 32
	v_cmp_gt_f32_e64 s[30:31], s34, v6
	v_cmp_eq_f32_e64 s[34:35], s34, v6
	s_and_b64 s[24:25], s[8:9], s[28:29]
	v_cndmask_b32_e64 v7, 0, 1, s[4:5]
	s_or_b64 s[4:5], s[22:23], s[20:21]
	v_cmp_gt_f32_e64 s[36:37], s40, v6
	v_cmp_eq_f32_e64 s[40:41], s40, v6
	s_and_b64 s[28:29], s[10:11], s[34:35]
	v_cndmask_b32_e64 v8, 0, 1, s[4:5]
	s_or_b64 s[4:5], s[26:27], s[24:25]
	v_readlane_b32 s54, v6, 40
	s_and_b64 s[34:35], s[12:13], s[40:41]
	v_cndmask_b32_e64 v9, 0, 1, s[4:5]
	s_or_b64 s[4:5], s[30:31], s[28:29]
	v_cndmask_b32_e64 v10, 0, 1, s[4:5]
	s_or_b64 s[4:5], s[36:37], s[34:35]
	v_cmp_eq_f32_e64 s[20:21], s54, v6
	v_cndmask_b32_e64 v11, 0, 1, s[4:5]
	v_cmp_gt_f32_e32 vcc, s54, v6
	s_and_b64 s[4:5], s[14:15], s[20:21]
	v_readlane_b32 s3, v6, 48
	s_or_b64 s[4:5], vcc, s[4:5]
	v_cndmask_b32_e64 v12, 0, 1, s[4:5]
	v_cmp_eq_f32_e64 s[20:21], s3, v6
	v_cmp_gt_f32_e32 vcc, s3, v6
	s_and_b64 s[4:5], s[16:17], s[20:21]
	v_readlane_b32 s3, v6, 56
	s_or_b64 s[4:5], vcc, s[4:5]
	v_cndmask_b32_e64 v13, 0, 1, s[4:5]
	v_cmp_gt_f32_e32 vcc, s3, v6
	s_nop 1
	v_cndmask_b32_e64 v6, 0, 1, vcc
	v_add_u32_e32 v6, v8, v6
	v_add3_u32 v6, v6, v7, v9
; __device__ __forceinline__ void phase_nrr(const Frame& F, const Args& a, int l, const bf16_t* XA, const float* g, const float* modl, unsigned char* XN8) {
;     ...
;             int grank = 0;
; #pragma unroll
;             for (int g2 = 0; g2 < 8; ++g2) { const float v = __int_as_float(__builtin_amdgcn_readlane(__float_as_int(gsum), g2 * 8)); grank += (v > gsum || (v == gsum && g2 < gq)) ? 1 : 0; }
;             const bool keep = grank < 4; const float val = keep ? bb : -INFINITY;
;             int rank = 0;
; #pragma unroll 8
;             for (int e2 = 0; e2 < 64; ++e2) { const float v = __int_as_float(__builtin_amdgcn_readlane(__float_as_int(val), e2)); rank += (v > val || (v == val && e2 < lane)) ? 1 : 0; }
	v_add3_u32 v6, v6, v10, v11
	v_add3_u32 v6, v6, v12, v13
	v_cmp_gt_u32_e32 vcc, 4, v6
	v_mov_b32_e32 v6, 0
	s_nop 0
	v_cndmask_b32_e32 v5, v245, v5, vcc
	v_ashrrev_i32_e32 v9, 31, v5
	v_sub_u32_e32 v8, 63, v230
	v_and_b32_e32 v9, 0x7fffffff, v9
	v_xor_b32_e32 v9, v5, v9
	s_nop 0
	v_readlane_b32 s23, v9, 0
	s_movk_i32 s22, 63
	v_readlane_b32 s21, v9, 1
	s_movk_i32 s20, 62
	v_cmp_gt_i64_e32 vcc, s[22:23], v[8:9]
	v_readlane_b32 s23, v9, 2
	s_movk_i32 s22, 61
	v_addc_co_u32_e32 v6, vcc, 0, v6, vcc
	v_cmp_gt_i64_e32 vcc, s[20:21], v[8:9]
	v_readlane_b32 s21, v9, 3
	s_movk_i32 s20, 60
	v_addc_co_u32_e32 v6, vcc, 0, v6, vcc
	v_cmp_gt_i64_e32 vcc, s[22:23], v[8:9]
	v_readlane_b32 s23, v9, 4
	s_movk_i32 s22, 59
	v_addc_co_u32_e32 v6, vcc, 0, v6, vcc
	v_cmp_gt_i64_e32 vcc, s[20:21], v[8:9]
	v_readlane_b32 s21, v9, 5
	s_movk_i32 s20, 58
	v_addc_co_u32_e32 v6, vcc, 0, v6, vcc
	v_cmp_gt_i64_e32 vcc, s[22:23], v[8:9]
	v_readlane_b32 s23, v9, 6
	s_movk_i32 s22, 57
	v_addc_co_u32_e32 v6, vcc, 0, v6, vcc
	v_cmp_gt_i64_e32 vcc, s[20:21], v[8:9]
	v_readlane_b32 s21, v9, 7
	s_movk_i32 s20, 56
	v_addc_co_u32_e32 v6, vcc, 0, v6, vcc
	v_cmp_gt_i64_e32 vcc, s[22:23], v[8:9]
	v_readlane_b32 s23, v9, 8
	s_movk_i32 s22, 55
	v_addc_co_u32_e32 v6, vcc, 0, v6, vcc
	v_cmp_gt_i64_e32 vcc, s[20:21], v[8:9]
	v_readlane_b32 s21, v9, 9
	s_movk_i32 s20, 54
	v_addc_co_u32_e32 v6, vcc, 0, v6, vcc
	v_cmp_gt_i64_e32 vcc, s[22:23], v[8:9]
	v_readlane_b32 s23, v9, 10
	s_movk_i32 s22, 53
	v_addc_co_u32_e32 v6, vcc, 0, v6, vcc
	v_cmp_gt_i64_e32 vcc, s[20:21], v[8:9]
	v_readlane_b32 s21, v9, 11
	s_movk_i32 s20, 52
	v_addc_co_u32_e32 v6, vcc, 0, v6, vcc
	v_cmp_gt_i64_e32 vcc, s[22:23], v[8:9]
	v_readlane_b32 s23, v9, 12
	s_movk_i32 s22, 51
	v_addc_co_u32_e32 v6, vcc, 0, v6, vcc
	v_cmp_gt_i64_e32 vcc, s[20:21], v[8:9]
	v_readlane_b32 s21, v9, 13
	s_movk_i32 s20, 50
	v_addc_co_u32_e32 v6, vcc, 0, v6, vcc
	v_cmp_gt_i64_e32 vcc, s[22:23], v[8:9]
	v_readlane_b32 s23, v9, 14
	s_movk_i32 s22, 49
	v_addc_co_u32_e32 v6, vcc, 0, v6, vcc
	v_cmp_gt_i64_e32 vcc, s[20:21], v[8:9]
	v_readlane_b32 s21, v9, 15
	s_movk_i32 s20, 48
	v_addc_co_u32_e32 v6, vcc, 0, v6, vcc
	v_cmp_gt_i64_e32 vcc, s[22:23], v[8:9]
	v_readlane_b32 s23, v9, 16
	s_movk_i32 s22, 47
	v_addc_co_u32_e32 v6, vcc, 0, v6, vcc
	v_cmp_gt_i64_e32 vcc, s[20:21], v[8:9]
	v_readlane_b32 s21, v9, 17
	s_movk_i32 s20, 46
	v_addc_co_u32_e32 v6, vcc, 0, v6, vcc
	v_cmp_gt_i64_e32 vcc, s[22:23], v[8:9]
	v_readlane_b32 s23, v9, 18
	s_movk_i32 s22, 45
	v_addc_co_u32_e32 v6, vcc, 0, v6, vcc
	v_cmp_gt_i64_e32 vcc, s[20:21], v[8:9]
	v_readlane_b32 s21, v9, 19
	s_movk_i32 s20, 44
	v_addc_co_u32_e32 v6, vcc, 0, v6, vcc
	v_cmp_gt_i64_e32 vcc, s[22:23], v[8:9]
	v_readlane_b32 s23, v9, 20
	s_movk_i32 s22, 43
	v_addc_co_u32_e32 v6, vcc, 0, v6, vcc
	v_cmp_gt_i64_e32 vcc, s[20:21], v[8:9]
	v_readlane_b32 s21, v9, 21
	s_movk_i32 s20, 42
	v_addc_co_u32_e32 v6, vcc, 0, v6, vcc
	v_cmp_gt_i64_e32 vcc, s[22:23], v[8:9]
	v_readlane_b32 s23, v9, 22
	s_movk_i32 s22, 41
	v_addc_co_u32_e32 v6, vcc, 0, v6, vcc
	v_cmp_gt_i64_e32 vcc, s[20:21], v[8:9]
	v_readlane_b32 s21, v9, 23
	s_movk_i32 s20, 40
	v_addc_co_u32_e32 v6, vcc, 0, v6, vcc
	v_cmp_gt_i64_e32 vcc, s[22:23], v[8:9]
	v_readlane_b32 s23, v9, 24
	s_movk_i32 s22, 39
	v_addc_co_u32_e32 v6, vcc, 0, v6, vcc
	v_cmp_gt_i64_e32 vcc, s[20:21], v[8:9]
	v_readlane_b32 s21, v9, 25
	s_movk_i32 s20, 38
	v_addc_co_u32_e32 v6, vcc, 0, v6, vcc
	v_cmp_gt_i64_e32 vcc, s[22:23], v[8:9]
	v_readlane_b32 s23, v9, 26
	s_movk_i32 s22, 37
	v_addc_co_u32_e32 v6, vcc, 0, v6, vcc
	v_cmp_gt_i64_e32 vcc, s[20:21], v[8:9]
	v_readlane_b32 s21, v9, 27
	s_movk_i32 s20, 36
	v_addc_co_u32_e32 v6, vcc, 0, v6, vcc
	v_cmp_gt_i64_e32 vcc, s[22:23], v[8:9]
	v_readlane_b32 s23, v9, 28
	s_movk_i32 s22, 35
	v_addc_co_u32_e32 v6, vcc, 0, v6, vcc
	v_cmp_gt_i64_e32 vcc, s[20:21], v[8:9]
	v_readlane_b32 s21, v9, 29
	s_movk_i32 s20, 34
	v_addc_co_u32_e32 v6, vcc, 0, v6, vcc
	v_cmp_gt_i64_e32 vcc, s[22:23], v[8:9]
	v_readlane_b32 s23, v9, 30
	s_movk_i32 s22, 33
	v_addc_co_u32_e32 v6, vcc, 0, v6, vcc
	v_cmp_gt_i64_e32 vcc, s[20:21], v[8:9]
	v_readlane_b32 s21, v9, 31
	s_movk_i32 s20, 32
	v_addc_co_u32_e32 v6, vcc, 0, v6, vcc
	v_cmp_gt_i64_e32 vcc, s[22:23], v[8:9]
	v_readlane_b32 s23, v9, 32
	s_movk_i32 s22, 31
	v_addc_co_u32_e32 v6, vcc, 0, v6, vcc
	v_cmp_gt_i64_e32 vcc, s[20:21], v[8:9]
	v_readlane_b32 s21, v9, 33
	s_movk_i32 s20, 30
	v_addc_co_u32_e32 v6, vcc, 0, v6, vcc
	v_cmp_gt_i64_e32 vcc, s[22:23], v[8:9]
	v_readlane_b32 s23, v9, 34
	s_movk_i32 s22, 29
	v_addc_co_u32_e32 v6, vcc, 0, v6, vcc
	v_cmp_gt_i64_e32 vcc, s[20:21], v[8:9]
	v_readlane_b32 s21, v9, 35
	s_movk_i32 s20, 28
	v_addc_co_u32_e32 v6, vcc, 0, v6, vcc
	v_cmp_gt_i64_e32 vcc, s[22:23], v[8:9]
	v_readlane_b32 s23, v9, 36
	s_movk_i32 s22, 27
	v_addc_co_u32_e32 v6, vcc, 0, v6, vcc
	v_cmp_gt_i64_e32 vcc, s[20:21], v[8:9]
	v_readlane_b32 s21, v9, 37
	s_movk_i32 s20, 26
	v_addc_co_u32_e32 v6, vcc, 0, v6, vcc
	v_cmp_gt_i64_e32 vcc, s[22:23], v[8:9]
	v_readlane_b32 s23, v9, 38
	s_movk_i32 s22, 25
	v_addc_co_u32_e32 v6, vcc, 0, v6, vcc
	v_cmp_gt_i64_e32 vcc, s[20:21], v[8:9]
	v_readlane_b32 s21, v9, 39
	s_movk_i32 s20, 24
	v_addc_co_u32_e32 v6, vcc, 0, v6, vcc
	v_cmp_gt_i64_e32 vcc, s[22:23], v[8:9]
	v_readlane_b32 s23, v9, 40
	s_movk_i32 s22, 23
	v_addc_co_u32_e32 v6, vcc, 0, v6, vcc
	v_cmp_gt_i64_e32 vcc, s[20:21], v[8:9]
	v_readlane_b32 s21, v9, 41
	s_movk_i32 s20, 22
	v_addc_co_u32_e32 v6, vcc, 0, v6, vcc
	v_cmp_gt_i64_e32 vcc, s[22:23], v[8:9]
	v_readlane_b32 s23, v9, 42
	s_movk_i32 s22, 21
	v_addc_co_u32_e32 v6, vcc, 0, v6, vcc
	v_cmp_gt_i64_e32 vcc, s[20:21], v[8:9]
	v_readlane_b32 s21, v9, 43
; __device__ __forceinline__ void phase_nrr(const Frame& F, const Args& a, int l, const bf16_t* XA, const float* g, const float* modl, unsigned char* XN8) {
;     ...
;             const float lg = Pl[(w * 8 + i) * NE + lane] + Pl[(64 + w * 8 + i) * NE + lane]; const float sc = 1.f / (1.f + __expf(-lg)); const float bb = sc + bias;
;             float m1 = bb; m1 = fmaxf(m1, __shfl_xor(m1, 1)); m1 = fmaxf(m1, __shfl_xor(m1, 2)); m1 = fmaxf(m1, __shfl_xor(m1, 4));
;             const unsigned long long eq = __ballot(bb == m1); const int gbase = lane & ~7; const unsigned grpmask = (unsigned)((eq >> gbase) & 0xffull);
;             const int first = gbase + __builtin_ctz(grpmask);
;             float m2 = (lane == first) ? -INFINITY : bb; m2 = fmaxf(m2, __shfl_xor(m2, 1)); m2 = fmaxf(m2, __shfl_xor(m2, 2)); m2 = fmaxf(m2, __shfl_xor(m2, 4));
;             const float gsum = m1 + m2; const int gq = lane >> 3;
;             int grank = 0;
; #pragma unroll
;             for (int g2 = 0; g2 < 8; ++g2) { const float v = __int_as_float(__builtin_amdgcn_readlane(__float_as_int(gsum), g2 * 8)); grank += (v > gsum || (v == gsum && g2 < gq)) ? 1 : 0; }
;     ...
;             int rank = 0;
; #pragma unroll 8
;             for (int e2 = 0; e2 < 64; ++e2) { const float v = __int_as_float(__builtin_amdgcn_readlane(__float_as_int(val), e2)); rank += (v > val || (v == val && e2 < lane)) ? 1 : 0; }
;             const bool sel = rank < TOPK;
;             const float ssum = wave_sum(sel ? sc : 0.f);
;             if (sel) { const int p = atomicAdd((int*)(hist + lane), 1); top_e[t * TOPK + rank] = lane; gate[t * TOPK + rank] = sc / ssum * 2.5f; lpos[t * TOPK + rank] = p; }
	s_movk_i32 s20, 20
	v_addc_co_u32_e32 v6, vcc, 0, v6, vcc
	v_cmp_gt_i64_e32 vcc, s[22:23], v[8:9]
	v_readlane_b32 s23, v9, 44
	s_movk_i32 s22, 19
	v_addc_co_u32_e32 v6, vcc, 0, v6, vcc
	v_cmp_gt_i64_e32 vcc, s[20:21], v[8:9]
	v_readlane_b32 s21, v9, 45
	s_movk_i32 s20, 18
	v_addc_co_u32_e32 v6, vcc, 0, v6, vcc
	v_cmp_gt_i64_e32 vcc, s[22:23], v[8:9]
	v_readlane_b32 s23, v9, 46
	s_movk_i32 s22, 17
	v_addc_co_u32_e32 v6, vcc, 0, v6, vcc
	v_cmp_gt_i64_e32 vcc, s[20:21], v[8:9]
	v_readlane_b32 s21, v9, 47
	s_movk_i32 s20, 16
	v_addc_co_u32_e32 v6, vcc, 0, v6, vcc
	v_cmp_gt_i64_e32 vcc, s[22:23], v[8:9]
	v_readlane_b32 s23, v9, 48
	s_movk_i32 s22, 15
	v_addc_co_u32_e32 v6, vcc, 0, v6, vcc
	v_cmp_gt_i64_e32 vcc, s[20:21], v[8:9]
	v_readlane_b32 s21, v9, 49
	s_movk_i32 s20, 14
	v_addc_co_u32_e32 v6, vcc, 0, v6, vcc
	v_cmp_gt_i64_e32 vcc, s[22:23], v[8:9]
	v_readlane_b32 s23, v9, 50
	s_movk_i32 s22, 13
	v_addc_co_u32_e32 v6, vcc, 0, v6, vcc
	v_cmp_gt_i64_e32 vcc, s[20:21], v[8:9]
	v_readlane_b32 s21, v9, 51
	s_movk_i32 s20, 12
	v_addc_co_u32_e32 v6, vcc, 0, v6, vcc
	v_cmp_gt_i64_e32 vcc, s[22:23], v[8:9]
	v_readlane_b32 s23, v9, 52
	s_movk_i32 s22, 11
	v_addc_co_u32_e32 v6, vcc, 0, v6, vcc
	v_cmp_gt_i64_e32 vcc, s[20:21], v[8:9]
	v_readlane_b32 s21, v9, 53
	s_movk_i32 s20, 10
	v_addc_co_u32_e32 v6, vcc, 0, v6, vcc
	v_cmp_gt_i64_e32 vcc, s[22:23], v[8:9]
	v_readlane_b32 s23, v9, 54
	s_movk_i32 s22, 9
	v_addc_co_u32_e32 v6, vcc, 0, v6, vcc
	v_cmp_gt_i64_e32 vcc, s[20:21], v[8:9]
	v_readlane_b32 s21, v9, 55
	s_movk_i32 s20, 8
	v_addc_co_u32_e32 v6, vcc, 0, v6, vcc
	v_cmp_gt_i64_e32 vcc, s[22:23], v[8:9]
	v_readlane_b32 s23, v9, 56
	s_movk_i32 s22, 7
	v_addc_co_u32_e32 v6, vcc, 0, v6, vcc
	v_cmp_gt_i64_e32 vcc, s[20:21], v[8:9]
	v_readlane_b32 s21, v9, 57
	s_movk_i32 s20, 6
	v_addc_co_u32_e32 v6, vcc, 0, v6, vcc
	v_cmp_gt_i64_e32 vcc, s[22:23], v[8:9]
	v_readlane_b32 s23, v9, 58
	s_movk_i32 s22, 5
	v_addc_co_u32_e32 v6, vcc, 0, v6, vcc
	v_cmp_gt_i64_e32 vcc, s[20:21], v[8:9]
	v_readlane_b32 s21, v9, 59
	s_movk_i32 s20, 4
	v_addc_co_u32_e32 v6, vcc, 0, v6, vcc
	v_cmp_gt_i64_e32 vcc, s[22:23], v[8:9]
	v_readlane_b32 s23, v9, 60
	s_movk_i32 s22, 3
	v_addc_co_u32_e32 v6, vcc, 0, v6, vcc
	v_cmp_gt_i64_e32 vcc, s[20:21], v[8:9]
	v_readlane_b32 s21, v9, 61
	s_movk_i32 s20, 2
	v_addc_co_u32_e32 v6, vcc, 0, v6, vcc
	v_cmp_gt_i64_e32 vcc, s[22:23], v[8:9]
	v_readlane_b32 s23, v9, 62
	s_movk_i32 s22, 1
	v_addc_co_u32_e32 v6, vcc, 0, v6, vcc
	v_cmp_gt_i64_e32 vcc, s[20:21], v[8:9]
	v_readlane_b32 s21, v9, 63
	s_movk_i32 s20, 0
	v_addc_co_u32_e32 v6, vcc, 0, v6, vcc
	v_cmp_gt_i64_e32 vcc, s[22:23], v[8:9]
	s_nop 1
	v_addc_co_u32_e32 v6, vcc, 0, v6, vcc
	v_cmp_gt_i64_e32 vcc, s[20:21], v[8:9]
	s_nop 1
	v_addc_co_u32_e32 v6, vcc, 0, v6, vcc
	v_cmp_gt_u32_e32 vcc, 6, v6
	s_nop 1
	v_cndmask_b32_e32 v5, 0, v2, vcc
	s_nop 1
	v_add_f32_dpp v5, v5, v5 quad_perm:[1,0,3,2] row_mask:0xf bank_mask:0xf
	s_nop 1
	v_add_f32_dpp v5, v5, v5 quad_perm:[2,3,0,1] row_mask:0xf bank_mask:0xf
	s_nop 1
	v_add_f32_dpp v5, v5, v5 row_half_mirror row_mask:0xf bank_mask:0xf
	s_nop 1
	v_add_f32_dpp v5, v5, v5 row_mirror row_mask:0xf bank_mask:0xf
	s_nop 0
	ds_bpermute_b32 v7, v222, v5
	s_waitcnt lgkmcnt(0)
	v_add_f32_e32 v5, v5, v7
	v_mov_b32_e32 v7, v5
	s_nop 1
	v_permlane32_swap_b32_e32 v7, v5
	s_and_saveexec_b64 s[2:3], vcc
	s_cbranch_execz .LBB0_1332
	s_waitcnt lgkmcnt(0)
	v_add_f32_e32 v5, v5, v7
	v_div_scale_f32 v11, s[4:5], v5, v5, v2
	v_add3_u32 v6, s50, 30, v6
	v_rcp_f32_e32 v12, v11
	v_ashrrev_i32_e32 v7, 31, v6
	v_lshlrev_b64 v[6:7], 2, v[6:7]
	v_lshl_add_u64 v[8:9], s[42:43], 0, v[6:7]
	ds_add_rtn_u32 v10, v227, v243
	global_store_dword v[8:9], v230, off
	v_fma_f32 v8, -v11, v12, 1.0
	v_fmac_f32_e32 v12, v8, v12
	v_div_scale_f32 v8, vcc, v2, v5, v2
	v_mul_f32_e32 v9, v8, v12
	v_fma_f32 v13, -v11, v9, v8
	v_fmac_f32_e32 v9, v13, v12
	v_fma_f32 v8, -v11, v9, v8
	v_div_fmas_f32 v8, v8, v12, v9
	v_div_fixup_f32 v2, v8, v5, v2
	v_mul_f32_e32 v2, 0x40200000, v2
	v_lshl_add_u64 v[8:9], s[44:45], 0, v[6:7]
	v_lshl_add_u64 v[6:7], s[46:47], 0, v[6:7]
	global_store_dword v[8:9], v2, off
	s_waitcnt lgkmcnt(0)
	global_store_dword v[6:7], v10, off
.LBB0_1332:
	s_or_b64 exec, exec, s[2:3]
	v_add_u32_e32 v2, s81, v226
	ds_read_b32 v2, v2
	ds_read_b32 v5, v4 offset:17920
	s_waitcnt lgkmcnt(0)
	v_add_f32_e32 v2, v2, v5
	v_mul_f32_e32 v2, 0xbfb8aa3b, v2
	v_exp_f32_e32 v2, v2
	s_nop 0
	v_add_f32_e32 v2, 1.0, v2
	v_div_scale_f32 v5, s[2:3], v2, v2, 1.0
	v_rcp_f32_e32 v6, v5
	v_div_scale_f32 v7, vcc, 1.0, v2, 1.0
	s_mov_b32 s2, 0
	v_fma_f32 v8, -v5, v6, 1.0
	v_fmac_f32_e32 v6, v8, v6
	v_mul_f32_e32 v8, v7, v6
	v_fma_f32 v9, -v5, v8, v7
	v_fmac_f32_e32 v8, v9, v6
	v_fma_f32 v5, -v5, v8, v7
	v_div_fmas_f32 v5, v5, v6, v8
	v_div_fixup_f32 v2, v5, v2, 1.0
	v_add_f32_e32 v5, v3, v2
	s_nop 1
	s_waitcnt lgkmcnt(0)
	v_max_f32_dpp v6, v5, v5 quad_perm:[1,0,3,2] row_mask:0xf bank_mask:0xf
	s_nop 1
	s_waitcnt lgkmcnt(0)
	v_max_f32_dpp v6, v6, v6 quad_perm:[2,3,0,1] row_mask:0xf bank_mask:0xf
	s_nop 1
	s_waitcnt lgkmcnt(0)
	v_max_f32_dpp v8, v6, v6 row_half_mirror row_mask:0xf bank_mask:0xf
	v_cmp_eq_f32_e32 vcc, v5, v8
	s_nop 1
	v_lshrrev_b64 v[6:7], v200, vcc
	v_ffbl_b32_sdwa v6, v6 dst_sel:DWORD dst_unused:UNUSED_PAD src0_sel:BYTE_0
	v_add_u32_e32 v6, v6, v200
	v_cmp_ne_u32_e32 vcc, v230, v6
	s_nop 1
	v_cndmask_b32_e32 v6, v245, v5, vcc
	s_nop 1
	s_waitcnt lgkmcnt(0)
	v_max_f32_dpp v6, v6, v6 quad_perm:[1,0,3,2] row_mask:0xf bank_mask:0xf
	s_nop 1
	s_waitcnt lgkmcnt(0)
	v_max_f32_dpp v6, v6, v6 quad_perm:[2,3,0,1] row_mask:0xf bank_mask:0xf
	s_nop 1
	s_waitcnt lgkmcnt(0)
; __device__ __forceinline__ void phase_nrr(const Frame& F, const Args& a, int l, const bf16_t* XA, const float* g, const float* modl, unsigned char* XN8) {
;     ...
;             int grank = 0;
; #pragma unroll
;             for (int g2 = 0; g2 < 8; ++g2) { const float v = __int_as_float(__builtin_amdgcn_readlane(__float_as_int(gsum), g2 * 8)); grank += (v > gsum || (v == gsum && g2 < gq)) ? 1 : 0; }
;             const bool keep = grank < 4; const float val = keep ? bb : -INFINITY;
;             int rank = 0;
; #pragma unroll 8
;             for (int e2 = 0; e2 < 64; ++e2) { const float v = __int_as_float(__builtin_amdgcn_readlane(__float_as_int(val), e2)); rank += (v > val || (v == val && e2 < lane)) ? 1 : 0; }
	v_max_f32_dpp v6, v6, v6 row_half_mirror row_mask:0xf bank_mask:0xf
	v_add_f32_e32 v6, v8, v6
	s_nop 0
	v_readlane_b32 s3, v6, 0
	v_readlane_b32 s4, v6, 8
	v_readlane_b32 s5, v6, 16
	v_cmp_eq_f32_e64 s[20:21], s3, v6
	v_cmp_gt_f32_e32 vcc, s3, v6
	v_cmp_gt_f32_e64 s[22:23], s4, v6
	v_cmp_eq_f32_e64 s[24:25], s4, v6
	v_cmp_gt_f32_e64 s[26:27], s5, v6
	v_cmp_eq_f32_e64 s[28:29], s5, v6
	s_and_b64 s[4:5], s[0:1], s[20:21]
	v_readlane_b32 s34, v6, 24
	s_and_b64 s[20:21], s[6:7], s[24:25]
	s_or_b64 s[4:5], vcc, s[4:5]
	v_readlane_b32 s40, v6, 32
	v_cmp_gt_f32_e64 s[30:31], s34, v6
	v_cmp_eq_f32_e64 s[34:35], s34, v6
	s_and_b64 s[24:25], s[8:9], s[28:29]
	v_cndmask_b32_e64 v7, 0, 1, s[4:5]
	s_or_b64 s[4:5], s[22:23], s[20:21]
	v_cmp_gt_f32_e64 s[36:37], s40, v6
	v_cmp_eq_f32_e64 s[40:41], s40, v6
	s_and_b64 s[28:29], s[10:11], s[34:35]
	v_cndmask_b32_e64 v8, 0, 1, s[4:5]
	s_or_b64 s[4:5], s[26:27], s[24:25]
	v_readlane_b32 s54, v6, 40
	s_and_b64 s[34:35], s[12:13], s[40:41]
	v_cndmask_b32_e64 v9, 0, 1, s[4:5]
	s_or_b64 s[4:5], s[30:31], s[28:29]
	v_cndmask_b32_e64 v10, 0, 1, s[4:5]
	s_or_b64 s[4:5], s[36:37], s[34:35]
	v_cmp_eq_f32_e64 s[20:21], s54, v6
	v_cndmask_b32_e64 v11, 0, 1, s[4:5]
	v_cmp_gt_f32_e32 vcc, s54, v6
	s_and_b64 s[4:5], s[14:15], s[20:21]
	v_readlane_b32 s3, v6, 48
	s_or_b64 s[4:5], vcc, s[4:5]
	v_cndmask_b32_e64 v12, 0, 1, s[4:5]
	v_cmp_eq_f32_e64 s[20:21], s3, v6
	v_cmp_gt_f32_e32 vcc, s3, v6
	s_and_b64 s[4:5], s[16:17], s[20:21]
	v_readlane_b32 s3, v6, 56
	s_or_b64 s[4:5], vcc, s[4:5]
	v_cndmask_b32_e64 v13, 0, 1, s[4:5]
	v_cmp_gt_f32_e32 vcc, s3, v6
	s_nop 1
	v_cndmask_b32_e64 v6, 0, 1, vcc
	v_add_u32_e32 v6, v8, v6
	v_add3_u32 v6, v6, v7, v9
	v_add3_u32 v6, v6, v10, v11
	v_add3_u32 v6, v6, v12, v13
	v_cmp_gt_u32_e32 vcc, 4, v6
	v_mov_b32_e32 v6, 0
	s_nop 0
	v_cndmask_b32_e32 v5, v245, v5, vcc
	v_ashrrev_i32_e32 v9, 31, v5
	v_sub_u32_e32 v8, 63, v230
	v_and_b32_e32 v9, 0x7fffffff, v9
	v_xor_b32_e32 v9, v5, v9
	s_nop 0
	v_readlane_b32 s23, v9, 0
	s_movk_i32 s22, 63
	v_readlane_b32 s21, v9, 1
	s_movk_i32 s20, 62
	v_cmp_gt_i64_e32 vcc, s[22:23], v[8:9]
	v_readlane_b32 s23, v9, 2
	s_movk_i32 s22, 61
	v_addc_co_u32_e32 v6, vcc, 0, v6, vcc
	v_cmp_gt_i64_e32 vcc, s[20:21], v[8:9]
	v_readlane_b32 s21, v9, 3
	s_movk_i32 s20, 60
	v_addc_co_u32_e32 v6, vcc, 0, v6, vcc
	v_cmp_gt_i64_e32 vcc, s[22:23], v[8:9]
	v_readlane_b32 s23, v9, 4
	s_movk_i32 s22, 59
	v_addc_co_u32_e32 v6, vcc, 0, v6, vcc
	v_cmp_gt_i64_e32 vcc, s[20:21], v[8:9]
	v_readlane_b32 s21, v9, 5
	s_movk_i32 s20, 58
	v_addc_co_u32_e32 v6, vcc, 0, v6, vcc
	v_cmp_gt_i64_e32 vcc, s[22:23], v[8:9]
	v_readlane_b32 s23, v9, 6
	s_movk_i32 s22, 57
	v_addc_co_u32_e32 v6, vcc, 0, v6, vcc
	v_cmp_gt_i64_e32 vcc, s[20:21], v[8:9]
	v_readlane_b32 s21, v9, 7
	s_movk_i32 s20, 56
	v_addc_co_u32_e32 v6, vcc, 0, v6, vcc
	v_cmp_gt_i64_e32 vcc, s[22:23], v[8:9]
	v_readlane_b32 s23, v9, 8
	s_movk_i32 s22, 55
	v_addc_co_u32_e32 v6, vcc, 0, v6, vcc
	v_cmp_gt_i64_e32 vcc, s[20:21], v[8:9]
	v_readlane_b32 s21, v9, 9
	s_movk_i32 s20, 54
	v_addc_co_u32_e32 v6, vcc, 0, v6, vcc
	v_cmp_gt_i64_e32 vcc, s[22:23], v[8:9]
	v_readlane_b32 s23, v9, 10
	s_movk_i32 s22, 53
	v_addc_co_u32_e32 v6, vcc, 0, v6, vcc
	v_cmp_gt_i64_e32 vcc, s[20:21], v[8:9]
	v_readlane_b32 s21, v9, 11
	s_movk_i32 s20, 52
	v_addc_co_u32_e32 v6, vcc, 0, v6, vcc
	v_cmp_gt_i64_e32 vcc, s[22:23], v[8:9]
	v_readlane_b32 s23, v9, 12
	s_movk_i32 s22, 51
	v_addc_co_u32_e32 v6, vcc, 0, v6, vcc
	v_cmp_gt_i64_e32 vcc, s[20:21], v[8:9]
	v_readlane_b32 s21, v9, 13
	s_movk_i32 s20, 50
	v_addc_co_u32_e32 v6, vcc, 0, v6, vcc
	v_cmp_gt_i64_e32 vcc, s[22:23], v[8:9]
	v_readlane_b32 s23, v9, 14
	s_movk_i32 s22, 49
	v_addc_co_u32_e32 v6, vcc, 0, v6, vcc
	v_cmp_gt_i64_e32 vcc, s[20:21], v[8:9]
	v_readlane_b32 s21, v9, 15
	s_movk_i32 s20, 48
	v_addc_co_u32_e32 v6, vcc, 0, v6, vcc
	v_cmp_gt_i64_e32 vcc, s[22:23], v[8:9]
	v_readlane_b32 s23, v9, 16
	s_movk_i32 s22, 47
	v_addc_co_u32_e32 v6, vcc, 0, v6, vcc
	v_cmp_gt_i64_e32 vcc, s[20:21], v[8:9]
	v_readlane_b32 s21, v9, 17
	s_movk_i32 s20, 46
	v_addc_co_u32_e32 v6, vcc, 0, v6, vcc
	v_cmp_gt_i64_e32 vcc, s[22:23], v[8:9]
	v_readlane_b32 s23, v9, 18
	s_movk_i32 s22, 45
	v_addc_co_u32_e32 v6, vcc, 0, v6, vcc
	v_cmp_gt_i64_e32 vcc, s[20:21], v[8:9]
	v_readlane_b32 s21, v9, 19
	s_movk_i32 s20, 44
	v_addc_co_u32_e32 v6, vcc, 0, v6, vcc
	v_cmp_gt_i64_e32 vcc, s[22:23], v[8:9]
	v_readlane_b32 s23, v9, 20
	s_movk_i32 s22, 43
	v_addc_co_u32_e32 v6, vcc, 0, v6, vcc
	v_cmp_gt_i64_e32 vcc, s[20:21], v[8:9]
	v_readlane_b32 s21, v9, 21
	s_movk_i32 s20, 42
	v_addc_co_u32_e32 v6, vcc, 0, v6, vcc
	v_cmp_gt_i64_e32 vcc, s[22:23], v[8:9]
	v_readlane_b32 s23, v9, 22
	s_movk_i32 s22, 41
	v_addc_co_u32_e32 v6, vcc, 0, v6, vcc
	v_cmp_gt_i64_e32 vcc, s[20:21], v[8:9]
	v_readlane_b32 s21, v9, 23
	s_movk_i32 s20, 40
	v_addc_co_u32_e32 v6, vcc, 0, v6, vcc
	v_cmp_gt_i64_e32 vcc, s[22:23], v[8:9]
	v_readlane_b32 s23, v9, 24
	s_movk_i32 s22, 39
	v_addc_co_u32_e32 v6, vcc, 0, v6, vcc
	v_cmp_gt_i64_e32 vcc, s[20:21], v[8:9]
	v_readlane_b32 s21, v9, 25
	s_movk_i32 s20, 38
	v_addc_co_u32_e32 v6, vcc, 0, v6, vcc
	v_cmp_gt_i64_e32 vcc, s[22:23], v[8:9]
	v_readlane_b32 s23, v9, 26
	s_movk_i32 s22, 37
	v_addc_co_u32_e32 v6, vcc, 0, v6, vcc
	v_cmp_gt_i64_e32 vcc, s[20:21], v[8:9]
	v_readlane_b32 s21, v9, 27
	s_movk_i32 s20, 36
	v_addc_co_u32_e32 v6, vcc, 0, v6, vcc
	v_cmp_gt_i64_e32 vcc, s[22:23], v[8:9]
	v_readlane_b32 s23, v9, 28
	s_movk_i32 s22, 35
	v_addc_co_u32_e32 v6, vcc, 0, v6, vcc
	v_cmp_gt_i64_e32 vcc, s[20:21], v[8:9]
	v_readlane_b32 s21, v9, 29
	s_movk_i32 s20, 34
	v_addc_co_u32_e32 v6, vcc, 0, v6, vcc
	v_cmp_gt_i64_e32 vcc, s[22:23], v[8:9]
; __device__ __forceinline__ void phase_nrr(const Frame& F, const Args& a, int l, const bf16_t* XA, const float* g, const float* modl, unsigned char* XN8) {
;     ...
;             int rank = 0;
; #pragma unroll 8
;             for (int e2 = 0; e2 < 64; ++e2) { const float v = __int_as_float(__builtin_amdgcn_readlane(__float_as_int(val), e2)); rank += (v > val || (v == val && e2 < lane)) ? 1 : 0; }
;             const bool sel = rank < TOPK;
;             const float ssum = wave_sum(sel ? sc : 0.f);
;             if (sel) { const int p = atomicAdd((int*)(hist + lane), 1); top_e[t * TOPK + rank] = lane; gate[t * TOPK + rank] = sc / ssum * 2.5f; lpos[t * TOPK + rank] = p; }
	v_readlane_b32 s23, v9, 30
	s_movk_i32 s22, 33
	v_addc_co_u32_e32 v6, vcc, 0, v6, vcc
	v_cmp_gt_i64_e32 vcc, s[20:21], v[8:9]
	v_readlane_b32 s21, v9, 31
	s_movk_i32 s20, 32
	v_addc_co_u32_e32 v6, vcc, 0, v6, vcc
	v_cmp_gt_i64_e32 vcc, s[22:23], v[8:9]
	v_readlane_b32 s23, v9, 32
	s_movk_i32 s22, 31
	v_addc_co_u32_e32 v6, vcc, 0, v6, vcc
	v_cmp_gt_i64_e32 vcc, s[20:21], v[8:9]
	v_readlane_b32 s21, v9, 33
	s_movk_i32 s20, 30
	v_addc_co_u32_e32 v6, vcc, 0, v6, vcc
	v_cmp_gt_i64_e32 vcc, s[22:23], v[8:9]
	v_readlane_b32 s23, v9, 34
	s_movk_i32 s22, 29
	v_addc_co_u32_e32 v6, vcc, 0, v6, vcc
	v_cmp_gt_i64_e32 vcc, s[20:21], v[8:9]
	v_readlane_b32 s21, v9, 35
	s_movk_i32 s20, 28
	v_addc_co_u32_e32 v6, vcc, 0, v6, vcc
	v_cmp_gt_i64_e32 vcc, s[22:23], v[8:9]
	v_readlane_b32 s23, v9, 36
	s_movk_i32 s22, 27
	v_addc_co_u32_e32 v6, vcc, 0, v6, vcc
	v_cmp_gt_i64_e32 vcc, s[20:21], v[8:9]
	v_readlane_b32 s21, v9, 37
	s_movk_i32 s20, 26
	v_addc_co_u32_e32 v6, vcc, 0, v6, vcc
	v_cmp_gt_i64_e32 vcc, s[22:23], v[8:9]
	v_readlane_b32 s23, v9, 38
	s_movk_i32 s22, 25
	v_addc_co_u32_e32 v6, vcc, 0, v6, vcc
	v_cmp_gt_i64_e32 vcc, s[20:21], v[8:9]
	v_readlane_b32 s21, v9, 39
	s_movk_i32 s20, 24
	v_addc_co_u32_e32 v6, vcc, 0, v6, vcc
	v_cmp_gt_i64_e32 vcc, s[22:23], v[8:9]
	v_readlane_b32 s23, v9, 40
	s_movk_i32 s22, 23
	v_addc_co_u32_e32 v6, vcc, 0, v6, vcc
	v_cmp_gt_i64_e32 vcc, s[20:21], v[8:9]
	v_readlane_b32 s21, v9, 41
	s_movk_i32 s20, 22
	v_addc_co_u32_e32 v6, vcc, 0, v6, vcc
	v_cmp_gt_i64_e32 vcc, s[22:23], v[8:9]
	v_readlane_b32 s23, v9, 42
	s_movk_i32 s22, 21
	v_addc_co_u32_e32 v6, vcc, 0, v6, vcc
	v_cmp_gt_i64_e32 vcc, s[20:21], v[8:9]
	v_readlane_b32 s21, v9, 43
	s_movk_i32 s20, 20
	v_addc_co_u32_e32 v6, vcc, 0, v6, vcc
	v_cmp_gt_i64_e32 vcc, s[22:23], v[8:9]
	v_readlane_b32 s23, v9, 44
	s_movk_i32 s22, 19
	v_addc_co_u32_e32 v6, vcc, 0, v6, vcc
	v_cmp_gt_i64_e32 vcc, s[20:21], v[8:9]
	v_readlane_b32 s21, v9, 45
	s_movk_i32 s20, 18
	v_addc_co_u32_e32 v6, vcc, 0, v6, vcc
	v_cmp_gt_i64_e32 vcc, s[22:23], v[8:9]
	v_readlane_b32 s23, v9, 46
	s_movk_i32 s22, 17
	v_addc_co_u32_e32 v6, vcc, 0, v6, vcc
	v_cmp_gt_i64_e32 vcc, s[20:21], v[8:9]
	v_readlane_b32 s21, v9, 47
	s_movk_i32 s20, 16
	v_addc_co_u32_e32 v6, vcc, 0, v6, vcc
	v_cmp_gt_i64_e32 vcc, s[22:23], v[8:9]
	v_readlane_b32 s23, v9, 48
	s_movk_i32 s22, 15
	v_addc_co_u32_e32 v6, vcc, 0, v6, vcc
	v_cmp_gt_i64_e32 vcc, s[20:21], v[8:9]
	v_readlane_b32 s21, v9, 49
	s_movk_i32 s20, 14
	v_addc_co_u32_e32 v6, vcc, 0, v6, vcc
	v_cmp_gt_i64_e32 vcc, s[22:23], v[8:9]
	v_readlane_b32 s23, v9, 50
	s_movk_i32 s22, 13
	v_addc_co_u32_e32 v6, vcc, 0, v6, vcc
	v_cmp_gt_i64_e32 vcc, s[20:21], v[8:9]
	v_readlane_b32 s21, v9, 51
	s_movk_i32 s20, 12
	v_addc_co_u32_e32 v6, vcc, 0, v6, vcc
	v_cmp_gt_i64_e32 vcc, s[22:23], v[8:9]
	v_readlane_b32 s23, v9, 52
	s_movk_i32 s22, 11
	v_addc_co_u32_e32 v6, vcc, 0, v6, vcc
	v_cmp_gt_i64_e32 vcc, s[20:21], v[8:9]
	v_readlane_b32 s21, v9, 53
	s_movk_i32 s20, 10
	v_addc_co_u32_e32 v6, vcc, 0, v6, vcc
	v_cmp_gt_i64_e32 vcc, s[22:23], v[8:9]
	v_readlane_b32 s23, v9, 54
	s_movk_i32 s22, 9
	v_addc_co_u32_e32 v6, vcc, 0, v6, vcc
	v_cmp_gt_i64_e32 vcc, s[20:21], v[8:9]
	v_readlane_b32 s21, v9, 55
	s_movk_i32 s20, 8
	v_addc_co_u32_e32 v6, vcc, 0, v6, vcc
	v_cmp_gt_i64_e32 vcc, s[22:23], v[8:9]
	v_readlane_b32 s23, v9, 56
	s_movk_i32 s22, 7
	v_addc_co_u32_e32 v6, vcc, 0, v6, vcc
	v_cmp_gt_i64_e32 vcc, s[20:21], v[8:9]
	v_readlane_b32 s21, v9, 57
	s_movk_i32 s20, 6
	v_addc_co_u32_e32 v6, vcc, 0, v6, vcc
	v_cmp_gt_i64_e32 vcc, s[22:23], v[8:9]
	v_readlane_b32 s23, v9, 58
	s_movk_i32 s22, 5
	v_addc_co_u32_e32 v6, vcc, 0, v6, vcc
	v_cmp_gt_i64_e32 vcc, s[20:21], v[8:9]
	v_readlane_b32 s21, v9, 59
	s_movk_i32 s20, 4
	v_addc_co_u32_e32 v6, vcc, 0, v6, vcc
	v_cmp_gt_i64_e32 vcc, s[22:23], v[8:9]
	v_readlane_b32 s23, v9, 60
	s_movk_i32 s22, 3
	v_addc_co_u32_e32 v6, vcc, 0, v6, vcc
	v_cmp_gt_i64_e32 vcc, s[20:21], v[8:9]
	v_readlane_b32 s21, v9, 61
	s_movk_i32 s20, 2
	v_addc_co_u32_e32 v6, vcc, 0, v6, vcc
	v_cmp_gt_i64_e32 vcc, s[22:23], v[8:9]
	v_readlane_b32 s23, v9, 62
	s_movk_i32 s22, 1
	v_addc_co_u32_e32 v6, vcc, 0, v6, vcc
	v_cmp_gt_i64_e32 vcc, s[20:21], v[8:9]
	v_readlane_b32 s21, v9, 63
	s_movk_i32 s20, 0
	v_addc_co_u32_e32 v6, vcc, 0, v6, vcc
	v_cmp_gt_i64_e32 vcc, s[22:23], v[8:9]
	s_nop 1
	v_addc_co_u32_e32 v6, vcc, 0, v6, vcc
	v_cmp_gt_i64_e32 vcc, s[20:21], v[8:9]
	s_nop 1
	v_addc_co_u32_e32 v6, vcc, 0, v6, vcc
	v_cmp_gt_u32_e32 vcc, 6, v6
	s_nop 1
	v_cndmask_b32_e32 v5, 0, v2, vcc
	s_nop 1
	v_add_f32_dpp v5, v5, v5 quad_perm:[1,0,3,2] row_mask:0xf bank_mask:0xf
	s_nop 1
	v_add_f32_dpp v5, v5, v5 quad_perm:[2,3,0,1] row_mask:0xf bank_mask:0xf
	s_nop 1
	v_add_f32_dpp v5, v5, v5 row_half_mirror row_mask:0xf bank_mask:0xf
	s_nop 1
	v_add_f32_dpp v5, v5, v5 row_mirror row_mask:0xf bank_mask:0xf
	s_nop 0
	ds_bpermute_b32 v7, v222, v5
	s_waitcnt lgkmcnt(0)
	v_add_f32_e32 v5, v5, v7
	v_mov_b32_e32 v7, v5
	s_nop 1
	v_permlane32_swap_b32_e32 v7, v5
	s_and_saveexec_b64 s[2:3], vcc
	s_cbranch_execz .LBB0_1336
	s_waitcnt lgkmcnt(0)
	v_add_f32_e32 v5, v5, v7
	v_div_scale_f32 v11, s[4:5], v5, v5, v2
	v_add3_u32 v6, s50, 36, v6
	v_rcp_f32_e32 v12, v11
	v_ashrrev_i32_e32 v7, 31, v6
	v_lshlrev_b64 v[6:7], 2, v[6:7]
	v_lshl_add_u64 v[8:9], s[42:43], 0, v[6:7]
	ds_add_rtn_u32 v10, v227, v243
	global_store_dword v[8:9], v230, off
	v_fma_f32 v8, -v11, v12, 1.0
	v_fmac_f32_e32 v12, v8, v12
	v_div_scale_f32 v8, vcc, v2, v5, v2
	v_mul_f32_e32 v9, v8, v12
	v_fma_f32 v13, -v11, v9, v8
	v_fmac_f32_e32 v9, v13, v12
	v_fma_f32 v8, -v11, v9, v8
	v_div_fmas_f32 v8, v8, v12, v9
	v_div_fixup_f32 v2, v8, v5, v2
	v_mul_f32_e32 v2, 0x40200000, v2
	v_lshl_add_u64 v[8:9], s[44:45], 0, v[6:7]
	v_lshl_add_u64 v[6:7], s[46:47], 0, v[6:7]
	global_store_dword v[8:9], v2, off
	s_waitcnt lgkmcnt(0)
	global_store_dword v[6:7], v10, off
; __device__ __forceinline__ void phase_nrr(const Frame& F, const Args& a, int l, const bf16_t* XA, const float* g, const float* modl, unsigned char* XN8) {
;     ...
;             const float lg = Pl[(w * 8 + i) * NE + lane] + Pl[(64 + w * 8 + i) * NE + lane]; const float sc = 1.f / (1.f + __expf(-lg)); const float bb = sc + bias;
;             float m1 = bb; m1 = fmaxf(m1, __shfl_xor(m1, 1)); m1 = fmaxf(m1, __shfl_xor(m1, 2)); m1 = fmaxf(m1, __shfl_xor(m1, 4));
;             const unsigned long long eq = __ballot(bb == m1); const int gbase = lane & ~7; const unsigned grpmask = (unsigned)((eq >> gbase) & 0xffull);
;             const int first = gbase + __builtin_ctz(grpmask);
;             float m2 = (lane == first) ? -INFINITY : bb; m2 = fmaxf(m2, __shfl_xor(m2, 1)); m2 = fmaxf(m2, __shfl_xor(m2, 2)); m2 = fmaxf(m2, __shfl_xor(m2, 4));
;             const float gsum = m1 + m2; const int gq = lane >> 3;
;             int grank = 0;
; #pragma unroll
;             for (int g2 = 0; g2 < 8; ++g2) { const float v = __int_as_float(__builtin_amdgcn_readlane(__float_as_int(gsum), g2 * 8)); grank += (v > gsum || (v == gsum && g2 < gq)) ? 1 : 0; }
;             const bool keep = grank < 4; const float val = keep ? bb : -INFINITY;
;             int rank = 0;
; #pragma unroll 8
;             for (int e2 = 0; e2 < 64; ++e2) { const float v = __int_as_float(__builtin_amdgcn_readlane(__float_as_int(val), e2)); rank += (v > val || (v == val && e2 < lane)) ? 1 : 0; }
.LBB0_1336:
	s_or_b64 exec, exec, s[2:3]
	v_add_u32_e32 v2, s82, v226
	ds_read_b32 v2, v2
	ds_read_b32 v4, v4 offset:18176
	s_waitcnt lgkmcnt(0)
	v_add_f32_e32 v2, v2, v4
	v_mul_f32_e32 v2, 0xbfb8aa3b, v2
	v_exp_f32_e32 v2, v2
	s_nop 0
	v_add_f32_e32 v2, 1.0, v2
	v_div_scale_f32 v4, s[2:3], v2, v2, 1.0
	v_rcp_f32_e32 v5, v4
	v_div_scale_f32 v6, vcc, 1.0, v2, 1.0
	s_mov_b32 s2, 0
	v_fma_f32 v7, -v4, v5, 1.0
	v_fmac_f32_e32 v5, v7, v5
	v_mul_f32_e32 v7, v6, v5
	v_fma_f32 v8, -v4, v7, v6
	v_fmac_f32_e32 v7, v8, v5
	v_fma_f32 v4, -v4, v7, v6
	v_div_fmas_f32 v4, v4, v5, v7
	v_div_fixup_f32 v2, v4, v2, 1.0
	v_add_f32_e32 v3, v3, v2
	s_nop 1
	s_waitcnt lgkmcnt(0)
	v_max_f32_dpp v4, v3, v3 quad_perm:[1,0,3,2] row_mask:0xf bank_mask:0xf
	s_nop 1
	s_waitcnt lgkmcnt(0)
	v_max_f32_dpp v4, v4, v4 quad_perm:[2,3,0,1] row_mask:0xf bank_mask:0xf
	s_nop 1
	s_waitcnt lgkmcnt(0)
	v_max_f32_dpp v6, v4, v4 row_half_mirror row_mask:0xf bank_mask:0xf
	v_cmp_eq_f32_e32 vcc, v3, v6
	s_nop 1
	v_lshrrev_b64 v[4:5], v200, vcc
	v_ffbl_b32_sdwa v4, v4 dst_sel:DWORD dst_unused:UNUSED_PAD src0_sel:BYTE_0
	v_add_u32_e32 v4, v4, v200
	v_cmp_ne_u32_e32 vcc, v230, v4
	s_nop 1
	v_cndmask_b32_e32 v4, v245, v3, vcc
	s_nop 1
	s_waitcnt lgkmcnt(0)
	v_max_f32_dpp v4, v4, v4 quad_perm:[1,0,3,2] row_mask:0xf bank_mask:0xf
	s_nop 1
	s_waitcnt lgkmcnt(0)
	v_max_f32_dpp v4, v4, v4 quad_perm:[2,3,0,1] row_mask:0xf bank_mask:0xf
	s_nop 1
	s_waitcnt lgkmcnt(0)
	v_max_f32_dpp v4, v4, v4 row_half_mirror row_mask:0xf bank_mask:0xf
	v_add_f32_e32 v4, v6, v4
	s_nop 0
	v_readlane_b32 s3, v4, 0
	v_readlane_b32 s4, v4, 8
	v_readlane_b32 s5, v4, 16
	v_cmp_eq_f32_e64 s[20:21], s3, v4
	v_cmp_gt_f32_e32 vcc, s3, v4
	v_cmp_gt_f32_e64 s[22:23], s4, v4
	v_cmp_eq_f32_e64 s[24:25], s4, v4
	v_cmp_gt_f32_e64 s[26:27], s5, v4
	v_cmp_eq_f32_e64 s[28:29], s5, v4
	s_and_b64 s[4:5], s[0:1], s[20:21]
	v_readlane_b32 s34, v4, 24
	s_and_b64 s[20:21], s[6:7], s[24:25]
	s_or_b64 s[4:5], vcc, s[4:5]
	v_readlane_b32 s40, v4, 32
	v_cmp_gt_f32_e64 s[30:31], s34, v4
	v_cmp_eq_f32_e64 s[34:35], s34, v4
	s_and_b64 s[24:25], s[8:9], s[28:29]
	v_cndmask_b32_e64 v5, 0, 1, s[4:5]
	s_or_b64 s[4:5], s[22:23], s[20:21]
	v_cmp_gt_f32_e64 s[36:37], s40, v4
	v_cmp_eq_f32_e64 s[40:41], s40, v4
	s_and_b64 s[28:29], s[10:11], s[34:35]
	v_cndmask_b32_e64 v6, 0, 1, s[4:5]
	s_or_b64 s[4:5], s[26:27], s[24:25]
	v_readlane_b32 s54, v4, 40
	s_and_b64 s[34:35], s[12:13], s[40:41]
	v_cndmask_b32_e64 v7, 0, 1, s[4:5]
	s_or_b64 s[4:5], s[30:31], s[28:29]
	v_cndmask_b32_e64 v8, 0, 1, s[4:5]
	s_or_b64 s[4:5], s[36:37], s[34:35]
	v_cmp_eq_f32_e64 s[20:21], s54, v4
	v_cndmask_b32_e64 v9, 0, 1, s[4:5]
	v_cmp_gt_f32_e32 vcc, s54, v4
	s_and_b64 s[4:5], s[14:15], s[20:21]
	v_readlane_b32 s3, v4, 48
	s_or_b64 s[4:5], vcc, s[4:5]
	v_cndmask_b32_e64 v10, 0, 1, s[4:5]
	v_cmp_eq_f32_e64 s[20:21], s3, v4
	v_cmp_gt_f32_e32 vcc, s3, v4
	s_and_b64 s[4:5], s[16:17], s[20:21]
	v_readlane_b32 s3, v4, 56
	s_or_b64 s[4:5], vcc, s[4:5]
	v_cndmask_b32_e64 v11, 0, 1, s[4:5]
	v_cmp_gt_f32_e32 vcc, s3, v4
	s_nop 1
	v_cndmask_b32_e64 v4, 0, 1, vcc
	v_add_u32_e32 v4, v6, v4
	v_add3_u32 v4, v4, v5, v7
	v_add3_u32 v4, v4, v8, v9
	v_add3_u32 v4, v4, v10, v11
	v_cmp_gt_u32_e32 vcc, 4, v4
	v_mov_b32_e32 v4, 0
	s_nop 0
	v_cndmask_b32_e32 v3, v245, v3, vcc
	v_ashrrev_i32_e32 v9, 31, v3
	v_sub_u32_e32 v8, 63, v230
	v_and_b32_e32 v9, 0x7fffffff, v9
	v_xor_b32_e32 v9, v3, v9
	s_nop 0
	v_readlane_b32 s23, v9, 0
	s_movk_i32 s22, 63
	v_readlane_b32 s21, v9, 1
	s_movk_i32 s20, 62
	v_cmp_gt_i64_e32 vcc, s[22:23], v[8:9]
	v_readlane_b32 s23, v9, 2
	s_movk_i32 s22, 61
	v_addc_co_u32_e32 v4, vcc, 0, v4, vcc
	v_cmp_gt_i64_e32 vcc, s[20:21], v[8:9]
	v_readlane_b32 s21, v9, 3
	s_movk_i32 s20, 60
	v_addc_co_u32_e32 v4, vcc, 0, v4, vcc
	v_cmp_gt_i64_e32 vcc, s[22:23], v[8:9]
	v_readlane_b32 s23, v9, 4
	s_movk_i32 s22, 59
	v_addc_co_u32_e32 v4, vcc, 0, v4, vcc
	v_cmp_gt_i64_e32 vcc, s[20:21], v[8:9]
	v_readlane_b32 s21, v9, 5
	s_movk_i32 s20, 58
	v_addc_co_u32_e32 v4, vcc, 0, v4, vcc
	v_cmp_gt_i64_e32 vcc, s[22:23], v[8:9]
	v_readlane_b32 s23, v9, 6
	s_movk_i32 s22, 57
	v_addc_co_u32_e32 v4, vcc, 0, v4, vcc
	v_cmp_gt_i64_e32 vcc, s[20:21], v[8:9]
	v_readlane_b32 s21, v9, 7
	s_movk_i32 s20, 56
	v_addc_co_u32_e32 v4, vcc, 0, v4, vcc
	v_cmp_gt_i64_e32 vcc, s[22:23], v[8:9]
	v_readlane_b32 s23, v9, 8
	s_movk_i32 s22, 55
	v_addc_co_u32_e32 v4, vcc, 0, v4, vcc
	v_cmp_gt_i64_e32 vcc, s[20:21], v[8:9]
	v_readlane_b32 s21, v9, 9
	s_movk_i32 s20, 54
	v_addc_co_u32_e32 v4, vcc, 0, v4, vcc
	v_cmp_gt_i64_e32 vcc, s[22:23], v[8:9]
	v_readlane_b32 s23, v9, 10
	s_movk_i32 s22, 53
	v_addc_co_u32_e32 v4, vcc, 0, v4, vcc
	v_cmp_gt_i64_e32 vcc, s[20:21], v[8:9]
	v_readlane_b32 s21, v9, 11
	s_movk_i32 s20, 52
	v_addc_co_u32_e32 v4, vcc, 0, v4, vcc
	v_cmp_gt_i64_e32 vcc, s[22:23], v[8:9]
	v_readlane_b32 s23, v9, 12
	s_movk_i32 s22, 51
	v_addc_co_u32_e32 v4, vcc, 0, v4, vcc
	v_cmp_gt_i64_e32 vcc, s[20:21], v[8:9]
	v_readlane_b32 s21, v9, 13
	s_movk_i32 s20, 50
	v_addc_co_u32_e32 v4, vcc, 0, v4, vcc
	v_cmp_gt_i64_e32 vcc, s[22:23], v[8:9]
	v_readlane_b32 s23, v9, 14
	s_movk_i32 s22, 49
	v_addc_co_u32_e32 v4, vcc, 0, v4, vcc
	v_cmp_gt_i64_e32 vcc, s[20:21], v[8:9]
	v_readlane_b32 s21, v9, 15
	s_movk_i32 s20, 48
	v_addc_co_u32_e32 v4, vcc, 0, v4, vcc
	v_cmp_gt_i64_e32 vcc, s[22:23], v[8:9]
	v_readlane_b32 s23, v9, 16
	s_movk_i32 s22, 47
	v_addc_co_u32_e32 v4, vcc, 0, v4, vcc
	v_cmp_gt_i64_e32 vcc, s[20:21], v[8:9]
	v_readlane_b32 s21, v9, 17
	s_movk_i32 s20, 46
	v_addc_co_u32_e32 v4, vcc, 0, v4, vcc
	v_cmp_gt_i64_e32 vcc, s[22:23], v[8:9]
	v_readlane_b32 s23, v9, 18
	s_movk_i32 s22, 45
	v_addc_co_u32_e32 v4, vcc, 0, v4, vcc
; __device__ __forceinline__ void phase_nrr(const Frame& F, const Args& a, int l, const bf16_t* XA, const float* g, const float* modl, unsigned char* XN8) {
;     ...
;             int rank = 0;
; #pragma unroll 8
;             for (int e2 = 0; e2 < 64; ++e2) { const float v = __int_as_float(__builtin_amdgcn_readlane(__float_as_int(val), e2)); rank += (v > val || (v == val && e2 < lane)) ? 1 : 0; }
;             const bool sel = rank < TOPK;
;             const float ssum = wave_sum(sel ? sc : 0.f);
	v_cmp_gt_i64_e32 vcc, s[20:21], v[8:9]
	v_readlane_b32 s21, v9, 19
	s_movk_i32 s20, 44
	v_addc_co_u32_e32 v4, vcc, 0, v4, vcc
	v_cmp_gt_i64_e32 vcc, s[22:23], v[8:9]
	v_readlane_b32 s23, v9, 20
	s_movk_i32 s22, 43
	v_addc_co_u32_e32 v4, vcc, 0, v4, vcc
	v_cmp_gt_i64_e32 vcc, s[20:21], v[8:9]
	v_readlane_b32 s21, v9, 21
	s_movk_i32 s20, 42
	v_addc_co_u32_e32 v4, vcc, 0, v4, vcc
	v_cmp_gt_i64_e32 vcc, s[22:23], v[8:9]
	v_readlane_b32 s23, v9, 22
	s_movk_i32 s22, 41
	v_addc_co_u32_e32 v4, vcc, 0, v4, vcc
	v_cmp_gt_i64_e32 vcc, s[20:21], v[8:9]
	v_readlane_b32 s21, v9, 23
	s_movk_i32 s20, 40
	v_addc_co_u32_e32 v4, vcc, 0, v4, vcc
	v_cmp_gt_i64_e32 vcc, s[22:23], v[8:9]
	v_readlane_b32 s23, v9, 24
	s_movk_i32 s22, 39
	v_addc_co_u32_e32 v4, vcc, 0, v4, vcc
	v_cmp_gt_i64_e32 vcc, s[20:21], v[8:9]
	v_readlane_b32 s21, v9, 25
	s_movk_i32 s20, 38
	v_addc_co_u32_e32 v4, vcc, 0, v4, vcc
	v_cmp_gt_i64_e32 vcc, s[22:23], v[8:9]
	v_readlane_b32 s23, v9, 26
	s_movk_i32 s22, 37
	v_addc_co_u32_e32 v4, vcc, 0, v4, vcc
	v_cmp_gt_i64_e32 vcc, s[20:21], v[8:9]
	v_readlane_b32 s21, v9, 27
	s_movk_i32 s20, 36
	v_addc_co_u32_e32 v4, vcc, 0, v4, vcc
	v_cmp_gt_i64_e32 vcc, s[22:23], v[8:9]
	v_readlane_b32 s23, v9, 28
	s_movk_i32 s22, 35
	v_addc_co_u32_e32 v4, vcc, 0, v4, vcc
	v_cmp_gt_i64_e32 vcc, s[20:21], v[8:9]
	v_readlane_b32 s21, v9, 29
	s_movk_i32 s20, 34
	v_addc_co_u32_e32 v4, vcc, 0, v4, vcc
	v_cmp_gt_i64_e32 vcc, s[22:23], v[8:9]
	v_readlane_b32 s23, v9, 30
	s_movk_i32 s22, 33
	v_addc_co_u32_e32 v4, vcc, 0, v4, vcc
	v_cmp_gt_i64_e32 vcc, s[20:21], v[8:9]
	v_readlane_b32 s21, v9, 31
	s_movk_i32 s20, 32
	v_addc_co_u32_e32 v4, vcc, 0, v4, vcc
	v_cmp_gt_i64_e32 vcc, s[22:23], v[8:9]
	v_readlane_b32 s23, v9, 32
	s_movk_i32 s22, 31
	v_addc_co_u32_e32 v4, vcc, 0, v4, vcc
	v_cmp_gt_i64_e32 vcc, s[20:21], v[8:9]
	v_readlane_b32 s21, v9, 33
	s_movk_i32 s20, 30
	v_addc_co_u32_e32 v4, vcc, 0, v4, vcc
	v_cmp_gt_i64_e32 vcc, s[22:23], v[8:9]
	v_readlane_b32 s23, v9, 34
	s_movk_i32 s22, 29
	v_addc_co_u32_e32 v4, vcc, 0, v4, vcc
	v_cmp_gt_i64_e32 vcc, s[20:21], v[8:9]
	v_readlane_b32 s21, v9, 35
	s_movk_i32 s20, 28
	v_addc_co_u32_e32 v4, vcc, 0, v4, vcc
	v_cmp_gt_i64_e32 vcc, s[22:23], v[8:9]
	v_readlane_b32 s23, v9, 36
	s_movk_i32 s22, 27
	v_addc_co_u32_e32 v4, vcc, 0, v4, vcc
	v_cmp_gt_i64_e32 vcc, s[20:21], v[8:9]
	v_readlane_b32 s21, v9, 37
	s_movk_i32 s20, 26
	v_addc_co_u32_e32 v4, vcc, 0, v4, vcc
	v_cmp_gt_i64_e32 vcc, s[22:23], v[8:9]
	v_readlane_b32 s23, v9, 38
	s_movk_i32 s22, 25
	v_addc_co_u32_e32 v4, vcc, 0, v4, vcc
	v_cmp_gt_i64_e32 vcc, s[20:21], v[8:9]
	v_readlane_b32 s21, v9, 39
	s_movk_i32 s20, 24
	v_addc_co_u32_e32 v4, vcc, 0, v4, vcc
	v_cmp_gt_i64_e32 vcc, s[22:23], v[8:9]
	v_readlane_b32 s23, v9, 40
	s_movk_i32 s22, 23
	v_addc_co_u32_e32 v4, vcc, 0, v4, vcc
	v_cmp_gt_i64_e32 vcc, s[20:21], v[8:9]
	v_readlane_b32 s21, v9, 41
	s_movk_i32 s20, 22
	v_addc_co_u32_e32 v4, vcc, 0, v4, vcc
	v_cmp_gt_i64_e32 vcc, s[22:23], v[8:9]
	v_readlane_b32 s23, v9, 42
	s_movk_i32 s22, 21
	v_addc_co_u32_e32 v4, vcc, 0, v4, vcc
	v_cmp_gt_i64_e32 vcc, s[20:21], v[8:9]
	v_readlane_b32 s21, v9, 43
	s_movk_i32 s20, 20
	v_addc_co_u32_e32 v4, vcc, 0, v4, vcc
	v_cmp_gt_i64_e32 vcc, s[22:23], v[8:9]
	v_readlane_b32 s23, v9, 44
	s_movk_i32 s22, 19
	v_addc_co_u32_e32 v4, vcc, 0, v4, vcc
	v_cmp_gt_i64_e32 vcc, s[20:21], v[8:9]
	v_readlane_b32 s21, v9, 45
	s_movk_i32 s20, 18
	v_addc_co_u32_e32 v4, vcc, 0, v4, vcc
	v_cmp_gt_i64_e32 vcc, s[22:23], v[8:9]
	v_readlane_b32 s23, v9, 46
	s_movk_i32 s22, 17
	v_addc_co_u32_e32 v4, vcc, 0, v4, vcc
	v_cmp_gt_i64_e32 vcc, s[20:21], v[8:9]
	v_readlane_b32 s21, v9, 47
	s_movk_i32 s20, 16
	v_addc_co_u32_e32 v4, vcc, 0, v4, vcc
	v_cmp_gt_i64_e32 vcc, s[22:23], v[8:9]
	v_readlane_b32 s23, v9, 48
	s_movk_i32 s22, 15
	v_addc_co_u32_e32 v4, vcc, 0, v4, vcc
	v_cmp_gt_i64_e32 vcc, s[20:21], v[8:9]
	v_readlane_b32 s21, v9, 49
	s_movk_i32 s20, 14
	v_addc_co_u32_e32 v4, vcc, 0, v4, vcc
	v_cmp_gt_i64_e32 vcc, s[22:23], v[8:9]
	v_readlane_b32 s23, v9, 50
	s_movk_i32 s22, 13
	v_addc_co_u32_e32 v4, vcc, 0, v4, vcc
	v_cmp_gt_i64_e32 vcc, s[20:21], v[8:9]
	v_readlane_b32 s21, v9, 51
	s_movk_i32 s20, 12
	v_addc_co_u32_e32 v4, vcc, 0, v4, vcc
	v_cmp_gt_i64_e32 vcc, s[22:23], v[8:9]
	v_readlane_b32 s23, v9, 52
	s_movk_i32 s22, 11
	v_addc_co_u32_e32 v4, vcc, 0, v4, vcc
	v_cmp_gt_i64_e32 vcc, s[20:21], v[8:9]
	v_readlane_b32 s21, v9, 53
	s_movk_i32 s20, 10
	v_addc_co_u32_e32 v4, vcc, 0, v4, vcc
	v_cmp_gt_i64_e32 vcc, s[22:23], v[8:9]
	v_readlane_b32 s23, v9, 54
	s_movk_i32 s22, 9
	v_addc_co_u32_e32 v4, vcc, 0, v4, vcc
	v_cmp_gt_i64_e32 vcc, s[20:21], v[8:9]
	v_readlane_b32 s21, v9, 55
	s_movk_i32 s20, 8
	v_addc_co_u32_e32 v4, vcc, 0, v4, vcc
	v_cmp_gt_i64_e32 vcc, s[22:23], v[8:9]
	v_readlane_b32 s23, v9, 56
	s_movk_i32 s22, 7
	v_addc_co_u32_e32 v4, vcc, 0, v4, vcc
	v_cmp_gt_i64_e32 vcc, s[20:21], v[8:9]
	v_readlane_b32 s21, v9, 57
	s_movk_i32 s20, 6
	v_addc_co_u32_e32 v4, vcc, 0, v4, vcc
	v_cmp_gt_i64_e32 vcc, s[22:23], v[8:9]
	v_readlane_b32 s23, v9, 58
	s_movk_i32 s22, 5
	v_addc_co_u32_e32 v4, vcc, 0, v4, vcc
	v_cmp_gt_i64_e32 vcc, s[20:21], v[8:9]
	v_readlane_b32 s21, v9, 59
	s_movk_i32 s20, 4
	v_addc_co_u32_e32 v4, vcc, 0, v4, vcc
	v_cmp_gt_i64_e32 vcc, s[22:23], v[8:9]
	v_readlane_b32 s23, v9, 60
	s_movk_i32 s22, 3
	v_addc_co_u32_e32 v4, vcc, 0, v4, vcc
	v_cmp_gt_i64_e32 vcc, s[20:21], v[8:9]
	v_readlane_b32 s21, v9, 61
	s_movk_i32 s20, 2
	v_addc_co_u32_e32 v4, vcc, 0, v4, vcc
	v_cmp_gt_i64_e32 vcc, s[22:23], v[8:9]
	v_readlane_b32 s23, v9, 62
	s_movk_i32 s22, 1
	v_addc_co_u32_e32 v4, vcc, 0, v4, vcc
	v_cmp_gt_i64_e32 vcc, s[20:21], v[8:9]
	v_readlane_b32 s21, v9, 63
	s_movk_i32 s20, 0
	v_addc_co_u32_e32 v4, vcc, 0, v4, vcc
	v_cmp_gt_i64_e32 vcc, s[22:23], v[8:9]
	s_nop 1
	v_addc_co_u32_e32 v4, vcc, 0, v4, vcc
	v_cmp_gt_i64_e32 vcc, s[20:21], v[8:9]
	s_nop 1
	v_addc_co_u32_e32 v4, vcc, 0, v4, vcc
	v_cmp_gt_u32_e32 vcc, 6, v4
	s_nop 1
	v_cndmask_b32_e32 v3, 0, v2, vcc
	s_nop 1
	v_add_f32_dpp v3, v3, v3 quad_perm:[1,0,3,2] row_mask:0xf bank_mask:0xf
	s_nop 1
	v_add_f32_dpp v3, v3, v3 quad_perm:[2,3,0,1] row_mask:0xf bank_mask:0xf
	s_nop 1
	v_add_f32_dpp v3, v3, v3 row_half_mirror row_mask:0xf bank_mask:0xf
	s_nop 1
	v_add_f32_dpp v3, v3, v3 row_mirror row_mask:0xf bank_mask:0xf
	s_nop 0
	ds_bpermute_b32 v5, v222, v3
	s_waitcnt lgkmcnt(0)
	v_add_f32_e32 v3, v3, v5
	v_mov_b32_e32 v5, v3
	s_nop 1
	v_permlane32_swap_b32_e32 v5, v3
	s_and_saveexec_b64 s[2:3], vcc
	s_cbranch_execz .LBB0_1340
; __device__ __forceinline__ void phase_nrr(const Frame& F, const Args& a, int l, const bf16_t* XA, const float* g, const float* modl, unsigned char* XN8) {
;     ...
;             if (sel) { const int p = atomicAdd((int*)(hist + lane), 1); top_e[t * TOPK + rank] = lane; gate[t * TOPK + rank] = sc / ssum * 2.5f; lpos[t * TOPK + rank] = p; }
	s_waitcnt lgkmcnt(0)
	v_add_f32_e32 v3, v3, v5
	v_div_scale_f32 v9, s[4:5], v3, v3, v2
	v_add3_u32 v4, s50, 42, v4
	v_rcp_f32_e32 v10, v9
	v_ashrrev_i32_e32 v5, 31, v4
	v_lshlrev_b64 v[4:5], 2, v[4:5]
	v_lshl_add_u64 v[6:7], s[42:43], 0, v[4:5]
	ds_add_rtn_u32 v8, v227, v243
	global_store_dword v[6:7], v230, off
	v_fma_f32 v6, -v9, v10, 1.0
	v_fmac_f32_e32 v10, v6, v10
	v_div_scale_f32 v6, vcc, v2, v3, v2
	v_mul_f32_e32 v7, v6, v10
	v_fma_f32 v11, -v9, v7, v6
	v_fmac_f32_e32 v7, v11, v10
	v_fma_f32 v6, -v9, v7, v6
	v_div_fmas_f32 v6, v6, v10, v7
	v_div_fixup_f32 v2, v6, v3, v2
	v_mul_f32_e32 v6, 0x40200000, v2
	v_lshl_add_u64 v[2:3], s[44:45], 0, v[4:5]
	global_store_dword v[2:3], v6, off
	v_lshl_add_u64 v[2:3], s[46:47], 0, v[4:5]
	s_waitcnt lgkmcnt(0)
	global_store_dword v[2:3], v8, off

; __device__ __forceinline__ void xcd_barrier(const XcdBarrier& b) {
;     asm volatile("s_waitcnt vmcnt(0)" ::: "memory");
;     __syncthreads();
;     if (threadIdx.x == 0) {
;         unsigned* bar = b.bar;
;         __builtin_amdgcn_s_waitcnt(0);
;         unsigned nloc = b.st[0], nx = b.st[1];
;         if (nloc == 0u) { xcd_barrier_complete(bar, b.x, nloc, nx); b.st[0] = nloc; b.st[1] = nx; }
.LBB0_1342:
	s_and_saveexec_b64 s[0:1], s[96:97]
	s_cbranch_execz .LBB0_1345
	s_mov_b64 s[2:3], exec
	v_mbcnt_lo_u32_b32 v1, s2, 0
	v_mbcnt_hi_u32_b32 v1, s3, v1
	v_cmp_eq_u32_e32 vcc, 0, v1
	s_and_b64 s[4:5], exec, vcc
	s_mov_b64 exec, s[4:5]
	s_cbranch_execz .LBB0_1345
	s_bcnt1_i32_b64 s2, s[2:3]
	v_mov_b32_e32 v1, 0x2000
	v_mov_b32_e32 v2, s2
.LBB0_1345:
	s_or_b64 exec, exec, s[0:1]
	v_readlane_b32 s8, v255, 4
	v_readlane_b32 s9, v255, 5
	s_cmp_lt_i32 s9, 22
	v_readlane_b32 s10, v255, 6
	v_readlane_b32 s11, v255, 7
	s_cbranch_scc1 .LBB0_1395
	s_waitcnt vmcnt(0)
	s_waitcnt vmcnt(0)
	s_barrier
	s_and_saveexec_b64 s[0:1], s[96:97]
	v_readlane_b32 s18, v255, 10
	s_cbranch_execz .LBB0_1394
	s_nop 0
	v_mov_b32_e32 v1, s18
	s_waitcnt vmcnt(0) expcnt(0) lgkmcnt(0)
	ds_read_b32 v3, v1
	ds_read_b32 v1, v1 offset:4
	s_waitcnt lgkmcnt(1)
	v_cmp_ne_u32_e32 vcc, 0, v3
	s_cbranch_vccnz .LBB0_1362
	v_readlane_b32 s2, v255, 0
	v_readlane_b32 s3, v255, 1
	s_load_dwordx2 s[6:7], s[2:3], 0x4
	v_readlane_b32 s8, v255, 8
	v_readlane_b32 s9, v255, 9
	s_add_u32 s2, s8, 0x1000
	s_addc_u32 s3, s9, 0
	s_add_u32 s4, s8, 0x1100
	s_addc_u32 s5, s9, 0
	s_waitcnt lgkmcnt(0)
	s_mul_i32 s16, s6, s93
	s_add_u32 s6, s8, 0x1200
	s_mul_i32 s16, s16, s7
	s_addc_u32 s7, s9, 0
	s_add_u32 s8, s8, 0x1300
	s_addc_u32 s9, s9, 0
	s_mov_b32 s17, 1
	v_mov_b32_e32 v17, 0
	s_branch .LBB0_1350

; __device__ __forceinline__ void xcd_barrier(const XcdBarrier& b) {
;     asm volatile("s_waitcnt vmcnt(0)" ::: "memory");
;     __syncthreads();
;     if (threadIdx.x == 0) {
;         unsigned* bar = b.bar;
;         __builtin_amdgcn_s_waitcnt(0);
;         unsigned nloc = b.st[0], nx = b.st[1];
;         if (nloc == 0u) { xcd_barrier_complete(bar, b.x, nloc, nx); b.st[0] = nloc; b.st[1] = nx; }
.LBB0_1451:
	s_and_saveexec_b64 s[0:1], s[96:97]
	s_cbranch_execz .LBB0_1454
	s_mov_b64 s[2:3], exec
	v_mbcnt_lo_u32_b32 v1, s2, 0
	v_mbcnt_hi_u32_b32 v1, s3, v1
	v_cmp_eq_u32_e32 vcc, 0, v1
	s_and_b64 s[4:5], exec, vcc
	s_mov_b64 exec, s[4:5]
	s_cbranch_execz .LBB0_1454
	s_bcnt1_i32_b64 s2, s[2:3]
	v_mov_b32_e32 v1, 0x2000
	v_mov_b32_e32 v2, s2
.LBB0_1454:
	s_or_b64 exec, exec, s[0:1]
	v_readlane_b32 s8, v255, 4
	v_readlane_b32 s9, v255, 5
	s_cmp_lt_i32 s9, 25
	v_readlane_b32 s10, v255, 6
	v_readlane_b32 s11, v255, 7
	s_cbranch_scc1 .LBB0_1504
	s_waitcnt vmcnt(0)
	s_barrier
	s_and_saveexec_b64 s[0:1], s[96:97]
	s_cbranch_execz .LBB0_1503
	v_mov_b32_e32 v1, s81
	s_waitcnt vmcnt(0) expcnt(0) lgkmcnt(0)
	ds_read_b32 v3, v1
	ds_read_b32 v1, v1 offset:4
	s_waitcnt lgkmcnt(1)
	v_cmp_ne_u32_e32 vcc, 0, v3
	s_cbranch_vccnz .LBB0_1471
	v_readlane_b32 s2, v255, 0
	v_readlane_b32 s3, v255, 1
	s_load_dwordx2 s[6:7], s[2:3], 0x4
	v_readlane_b32 s8, v255, 8
	v_readlane_b32 s9, v255, 9
	s_add_u32 s2, s8, 0x1000
	s_addc_u32 s3, s9, 0
	s_add_u32 s4, s8, 0x1100
	s_addc_u32 s5, s9, 0
	s_waitcnt lgkmcnt(0)
	s_mul_i32 s16, s6, s93
	s_add_u32 s6, s8, 0x1200
	s_mul_i32 s16, s16, s7
	s_addc_u32 s7, s9, 0
	s_add_u32 s8, s8, 0x1300
	s_addc_u32 s9, s9, 0
	s_mov_b32 s17, 1
	v_mov_b32_e32 v17, 0
	s_branch .LBB0_1459

; __device__ __forceinline__ void xcd_barrier(const XcdBarrier& b) {
;     asm volatile("s_waitcnt vmcnt(0)" ::: "memory");
;     __syncthreads();
;     if (threadIdx.x == 0) {
;         unsigned* bar = b.bar;
;         __builtin_amdgcn_s_waitcnt(0);
;         unsigned nloc = b.st[0], nx = b.st[1];
;         if (nloc == 0u) { xcd_barrier_complete(bar, b.x, nloc, nx); b.st[0] = nloc; b.st[1] = nx; }
.LBB0_1557:
	s_and_saveexec_b64 s[0:1], s[96:97]
	s_cbranch_execz .LBB0_1560
	s_mov_b64 s[2:3], exec
	v_mbcnt_lo_u32_b32 v1, s2, 0
	v_mbcnt_hi_u32_b32 v1, s3, v1
	v_cmp_eq_u32_e32 vcc, 0, v1
	s_and_b64 s[4:5], exec, vcc
	s_mov_b64 exec, s[4:5]
	s_cbranch_execz .LBB0_1560
	s_bcnt1_i32_b64 s2, s[2:3]
	v_mov_b32_e32 v1, 0x2000
	v_mov_b32_e32 v2, s2
.LBB0_1560:
	s_or_b64 exec, exec, s[0:1]
	v_readlane_b32 s8, v255, 4
	v_readlane_b32 s9, v255, 5
	s_cmp_lt_i32 s9, 26
	v_readlane_b32 s10, v255, 6
	v_readlane_b32 s11, v255, 7
	s_cbranch_scc1 .LBB0_1610
	s_waitcnt vmcnt(0)
	s_waitcnt vmcnt(0)
	s_barrier
	s_and_saveexec_b64 s[0:1], s[96:97]
	s_cbranch_execz .LBB0_1609
	v_mov_b32_e32 v1, s81
	s_waitcnt vmcnt(0) expcnt(0) lgkmcnt(0)
	ds_read_b32 v3, v1
	ds_read_b32 v1, v1 offset:4
	s_waitcnt lgkmcnt(1)
	v_cmp_ne_u32_e32 vcc, 0, v3
	s_cbranch_vccnz .LBB0_1577
	v_readlane_b32 s2, v255, 0
	v_readlane_b32 s3, v255, 1
	s_load_dwordx2 s[6:7], s[2:3], 0x4
	v_readlane_b32 s8, v255, 8
	v_readlane_b32 s9, v255, 9
	s_add_u32 s2, s8, 0x1000
	s_addc_u32 s3, s9, 0
	s_add_u32 s4, s8, 0x1100
	s_addc_u32 s5, s9, 0
	s_waitcnt lgkmcnt(0)
	s_mul_i32 s16, s6, s93
	s_add_u32 s6, s8, 0x1200
	s_mul_i32 s16, s16, s7
	s_addc_u32 s7, s9, 0
	s_add_u32 s8, s8, 0x1300
	s_addc_u32 s9, s9, 0
	s_mov_b32 s17, 1
	v_mov_b32_e32 v17, 0
	s_branch .LBB0_1565

; __device__ __forceinline__ void xcd_barrier(const XcdBarrier& b) {
;     asm volatile("s_waitcnt vmcnt(0)" ::: "memory");
;     __syncthreads();
;     if (threadIdx.x == 0) {
;         unsigned* bar = b.bar;
;         __builtin_amdgcn_s_waitcnt(0);
;         unsigned nloc = b.st[0], nx = b.st[1];
;         if (nloc == 0u) { xcd_barrier_complete(bar, b.x, nloc, nx); b.st[0] = nloc; b.st[1] = nx; }
.LBB0_1645:
	s_and_saveexec_b64 s[0:1], s[96:97]
	s_cbranch_execz .LBB0_1648
	s_mov_b64 s[2:3], exec
	v_mbcnt_lo_u32_b32 v0, s2, 0
	v_mbcnt_hi_u32_b32 v0, s3, v0
	v_cmp_eq_u32_e32 vcc, 0, v0
	s_and_b64 s[4:5], exec, vcc
	s_mov_b64 exec, s[4:5]
	s_cbranch_execz .LBB0_1648
	s_bcnt1_i32_b64 s2, s[2:3]
	v_mov_b32_e32 v0, 0x2000
	v_mov_b32_e32 v1, s2
.LBB0_1648:
	s_or_b64 exec, exec, s[0:1]
	v_readlane_b32 s8, v255, 4
	v_readlane_b32 s9, v255, 5
	s_cmp_lt_i32 s9, 27
	v_readlane_b32 s10, v255, 6
	v_readlane_b32 s11, v255, 7
	s_cbranch_scc1 .LBB0_1698
	s_waitcnt vmcnt(0)
	s_waitcnt vmcnt(0)
	s_barrier
	s_and_saveexec_b64 s[0:1], s[96:97]
	s_cbranch_execz .LBB0_1697
	v_mov_b32_e32 v0, s81
	s_waitcnt vmcnt(0) expcnt(0) lgkmcnt(0)
	ds_read_b32 v2, v0
	ds_read_b32 v0, v0 offset:4
	s_waitcnt lgkmcnt(1)
	v_cmp_ne_u32_e32 vcc, 0, v2
	s_cbranch_vccnz .LBB0_1665
	v_readlane_b32 s2, v255, 0
	v_readlane_b32 s3, v255, 1
	s_load_dwordx2 s[6:7], s[2:3], 0x4
	v_readlane_b32 s8, v255, 8
	v_readlane_b32 s9, v255, 9
	s_add_u32 s2, s8, 0x1000
	s_addc_u32 s3, s9, 0
	s_add_u32 s4, s8, 0x1100
	s_addc_u32 s5, s9, 0
	s_waitcnt lgkmcnt(0)
	s_mul_i32 s16, s6, s93
	s_add_u32 s6, s8, 0x1200
	s_mul_i32 s16, s16, s7
	s_addc_u32 s7, s9, 0
	s_add_u32 s8, s8, 0x1300
	s_addc_u32 s9, s9, 0
	s_mov_b32 s17, 1
	v_mov_b32_e32 v16, 0
	s_branch .LBB0_1653

; __device__ __forceinline__ void xcd_barrier(const XcdBarrier& b) {
;     asm volatile("s_waitcnt vmcnt(0)" ::: "memory");
;     __syncthreads();
;     if (threadIdx.x == 0) {
;         unsigned* bar = b.bar;
;         __builtin_amdgcn_s_waitcnt(0);
;         unsigned nloc = b.st[0], nx = b.st[1];
;         if (nloc == 0u) { xcd_barrier_complete(bar, b.x, nloc, nx); b.st[0] = nloc; b.st[1] = nx; }
.LBB0_1706:
	s_and_saveexec_b64 s[0:1], s[96:97]
	s_cbranch_execz .LBB0_1709
	s_mov_b64 s[2:3], exec
	v_mbcnt_lo_u32_b32 v0, s2, 0
	v_mbcnt_hi_u32_b32 v0, s3, v0
	v_cmp_eq_u32_e32 vcc, 0, v0
	s_and_b64 s[4:5], exec, vcc
	s_mov_b64 exec, s[4:5]
	s_cbranch_execz .LBB0_1709
	s_bcnt1_i32_b64 s2, s[2:3]
	v_mov_b32_e32 v0, 0x2000
	v_mov_b32_e32 v1, s2
.LBB0_1709:
	s_or_b64 exec, exec, s[0:1]
	v_readlane_b32 s0, v255, 4
	v_readlane_b32 s1, v255, 5
	s_cmp_lt_i32 s1, 28
	v_readlane_b32 s2, v255, 6
	v_readlane_b32 s3, v255, 7
	s_cbranch_scc1 .LBB0_1759
	s_waitcnt vmcnt(0)
	s_waitcnt vmcnt(0)
	s_barrier
	s_and_saveexec_b64 s[0:1], s[96:97]
	s_cbranch_execz .LBB0_1758
	v_mov_b32_e32 v0, s81
	s_waitcnt vmcnt(0) expcnt(0) lgkmcnt(0)
	ds_read_b32 v2, v0
	ds_read_b32 v0, v0 offset:4
	s_waitcnt lgkmcnt(1)
	v_cmp_ne_u32_e32 vcc, 0, v2
	s_cbranch_vccnz .LBB0_1726
	v_readlane_b32 s2, v255, 0
	v_readlane_b32 s3, v255, 1
	s_load_dwordx2 s[6:7], s[2:3], 0x4
	v_readlane_b32 s8, v255, 8
	v_readlane_b32 s9, v255, 9
	s_add_u32 s2, s8, 0x1000
	s_addc_u32 s3, s9, 0
	s_add_u32 s4, s8, 0x1100
	s_addc_u32 s5, s9, 0
	s_waitcnt lgkmcnt(0)
	s_mul_i32 s16, s6, s93
	s_add_u32 s6, s8, 0x1200
	s_mul_i32 s16, s16, s7
	s_addc_u32 s7, s9, 0
	s_add_u32 s8, s8, 0x1300
	s_addc_u32 s9, s9, 0
	s_mov_b32 s17, 1
	v_mov_b32_e32 v16, 0
	s_branch .LBB0_1714
